# speedup vs baseline: 1.0077x; 1.0077x over previous
_Z12gemm8_kernelPKDF16_S0_PDF16_S1_:
	s_load_dwordx8 s[4:11], s[0:1], 0x0
	s_and_b32 s12, s2, 7
	s_lshr_b32 s13, s2, 3
	v_lshrrev_b32_e32 v1, 6, v0
	v_and_b32_e32 v28, 63, v0
	v_and_b32_e32 v29, 15, v28
	v_lshrrev_b32_e32 v30, 4, v28
	v_readfirstlane_b32 s14, v1
	v_lshrrev_b32_e32 v2, 3, v0
	v_lshlrev_b32_e32 v2, 11, v2
	v_and_b32_e32 v3, 7, v0
	v_bfe_u32 v4, v0, 4, 3
	v_xor_b32_e32 v3, v3, v4
	v_lshl_or_b32 v2, v3, 4, v2
	v_bfe_u32 v6, v0, 3, 4
	v_lshrrev_b32_e32 v7, 2, v6
	v_lshlrev_b32_e32 v7, 3, v7
	v_and_b32_e32 v4, 3, v6
	v_or_b32_e32 v7, v7, v4
	v_bfe_u32 v4, v0, 7, 1
	v_lshl_or_b32 v7, v4, 2, v7
	v_bfe_u32 v4, v0, 8, 1
	v_lshl_or_b32 v7, v4, 5, v7
	v_lshlrev_b32_e32 v7, 11, v7
	v_lshl_or_b32 v6, v3, 4, v7
	v_add_u32_e32 v7, 0x20000, v6
	v_add_u32_e32 v3, 0x20000, v2
	v_add_u32_e32 v4, 0x40000, v2
	v_add_u32_e32 v5, 0x60000, v2
	v_lshrrev_b32_e32 v31, 1, v29
	v_xor_b32_e32 v31, v30, v31
	v_lshlrev_b32_e32 v31, 4, v31
	v_lshl_or_b32 v31, v29, 7, v31
	s_lshr_b32 s15, s14, 1
	s_and_b32 s36, s14, 1
	s_lshl_b32 s37, s15, 13
	s_lshl_b32 s38, s36, 13
	v_add_u32_e32 v8, s37, v31
	v_add_u32_e32 v9, s38, v31
	v_xor_b32_e32 v10, 64, v8
	v_xor_b32_e32 v11, 64, v9
	v_add_u32_e32 v12, 0xc000, v8
	v_add_u32_e32 v13, 0xc000, v9
	v_add_u32_e32 v14, 0xc000, v10
	v_add_u32_e32 v15, 0xc000, v11
	v_add_u32_e32 v16, 0x18000, v8
	v_add_u32_e32 v17, 0x18000, v9
	v_add_u32_e32 v18, 0x18000, v10
	v_add_u32_e32 v19, 0x18000, v11
	s_lshl_b32 s39, s15, 6
	s_lshl_b32 s40, s36, 7
	v_add_u32_e32 v28, s39, v29
	v_lshl_add_u32 v30, v30, 4, s40
	v_lshl_add_u32 v20, v28, 12, v30
	v_lshl_add_u32 v24, v28, 13, v30
	v_add_u32_e32 v21, 0x10000, v20
	v_add_u32_e32 v25, 0x20000, v24
	v_add_u32_e32 v22, 0x20000, v20
	v_add_u32_e32 v26, 0x40000, v24
	v_add_u32_e32 v23, 0x30000, v20
	v_add_u32_e32 v27, 0x60000, v24
	s_lshl_b32 s14, s14, 10
	s_mov_b32 s50, 0x3d000000
	s_lshr_b32 s41, s12, 1
	s_lshl_b32 s41, s41, 3
	s_and_b32 s42, s13, 7
	s_add_u32 s41, s41, s42
	s_and_b32 s43, s12, 1
	s_lshl_b32 s43, s43, 2
	s_lshr_b32 s44, s13, 3
	s_add_u32 s43, s43, s44
	s_lshl_b32 s45, s12, 2
	s_add_u32 s45, s45, s44
	s_waitcnt lgkmcnt(0)
	s_lshl_b32 s46, s41, 19
	s_add_u32 s16, s4, s46
	s_addc_u32 s17, s5, 0
	s_lshl_b32 s46, s42, 19
	s_add_u32 s46, s46, 0x400000
	s_add_u32 s18, s6, s46
	s_addc_u32 s19, s7, 0
	s_lshl_b32 s46, s43, 19
	s_add_u32 s20, s6, s46
	s_addc_u32 s21, s7, 0
	s_add_u32 s22, s20, 0x40000
	s_addc_u32 s23, s21, 0
	s_lshl_b32 s46, s45, 19
	s_add_u32 s24, s4, s46
	s_addc_u32 s25, s5, 0
	s_add_u32 s26, s24, 0x40000
	s_addc_u32 s27, s25, 0
	s_lshl_b32 s46, s41, 20
	s_lshl_b32 s47, s43, 9
	s_add_u32 s46, s46, s47
	s_add_u32 s32, s8, s46
	s_addc_u32 s33, s9, 0
	s_lshr_b32 s46, s45, 4
	s_lshl_b32 s46, s46, 24
	s_lshl_b32 s47, s42, 21
	s_add_u32 s46, s46, s47
	s_and_b32 s47, s45, 15
	s_lshl_b32 s47, s47, 9
	s_add_u32 s46, s46, s47
	s_add_u32 s34, s10, s46
	s_addc_u32 s35, s11, 0
	s_mov_b64 s[28:29], s[16:17]
	s_mov_b64 s[30:31], s[20:21]
	s_add_u32 m0, s14, 0x0
	s_nop 0
	global_load_lds_dwordx4 v2, s[28:29]
	s_add_u32 m0, s14, 0x2000
	s_nop 0
	global_load_lds_dwordx4 v3, s[28:29]
	s_add_u32 m0, s14, 0x4000
	s_nop 0
	global_load_lds_dwordx4 v4, s[28:29]
	s_add_u32 m0, s14, 0x6000
	s_nop 0
	global_load_lds_dwordx4 v5, s[28:29]
	s_add_u32 m0, s14, 0x8000
	s_nop 0
	global_load_lds_dwordx4 v6, s[30:31]
	s_add_u32 m0, s14, 0xa000
	s_nop 0
	global_load_lds_dwordx4 v7, s[30:31]
	s_add_u32 s28, s28, 0x80
	s_addc_u32 s29, s29, 0
	s_add_u32 s30, s30, 0x80
	s_addc_u32 s31, s31, 0
	s_add_u32 m0, s14, 0xc000
	s_nop 0
	global_load_lds_dwordx4 v2, s[28:29]
	s_add_u32 m0, s14, 0xe000
	s_nop 0
	global_load_lds_dwordx4 v3, s[28:29]
	s_add_u32 m0, s14, 0x10000
	s_nop 0
	global_load_lds_dwordx4 v4, s[28:29]
	s_add_u32 m0, s14, 0x12000
	s_nop 0
	global_load_lds_dwordx4 v5, s[28:29]
	s_add_u32 m0, s14, 0x14000
	s_nop 0
	global_load_lds_dwordx4 v6, s[30:31]
	s_add_u32 m0, s14, 0x16000
	s_nop 0
	global_load_lds_dwordx4 v7, s[30:31]
	s_add_u32 s28, s28, 0x80
	s_addc_u32 s29, s29, 0
	s_add_u32 s30, s30, 0x80
	s_addc_u32 s31, s31, 0
	s_add_u32 m0, s14, 0x18000
	s_nop 0
	global_load_lds_dwordx4 v2, s[28:29]
	s_add_u32 m0, s14, 0x1a000
	s_nop 0
	global_load_lds_dwordx4 v3, s[28:29]
	s_add_u32 m0, s14, 0x1c000
	s_nop 0
	global_load_lds_dwordx4 v4, s[28:29]
	s_add_u32 m0, s14, 0x1e000
	s_nop 0
	global_load_lds_dwordx4 v5, s[28:29]
	s_add_u32 m0, s14, 0x20000
	s_nop 0
	global_load_lds_dwordx4 v6, s[30:31]
	s_add_u32 m0, s14, 0x22000
	s_nop 0
	global_load_lds_dwordx4 v7, s[30:31]
	s_waitcnt vmcnt(12)
	s_barrier
	ds_read_b128 v[96:99], v8
	ds_read_b128 v[112:115], v9 offset:32768
	ds_read_b128 v[116:119], v9 offset:34816
	ds_read_b128 v[120:123], v9 offset:36864
	ds_read_b128 v[124:127], v9 offset:38912
	ds_read_b128 v[100:103], v8 offset:2048
	ds_read_b128 v[104:107], v8 offset:4096
	ds_read_b128 v[108:111], v8 offset:6144
	s_waitcnt lgkmcnt(0)
	v_mfma_f32_16x16x32_f16 v[32:35], v[112:115], v[96:99], 0
	ds_read_b128 v[128:131], v10
	v_mfma_f32_16x16x32_f16 v[36:39], v[116:119], v[96:99], 0
	ds_read_b128 v[144:147], v11 offset:32768
	v_mfma_f32_16x16x32_f16 v[40:43], v[120:123], v[96:99], 0
	ds_read_b128 v[148:151], v11 offset:34816
	v_mfma_f32_16x16x32_f16 v[44:47], v[124:127], v[96:99], 0
	ds_read_b128 v[152:155], v11 offset:36864
	v_mfma_f32_16x16x32_f16 v[48:51], v[112:115], v[100:103], 0
	ds_read_b128 v[156:159], v11 offset:38912
	v_mfma_f32_16x16x32_f16 v[52:55], v[116:119], v[100:103], 0
	ds_read_b128 v[132:135], v10 offset:2048
	v_mfma_f32_16x16x32_f16 v[56:59], v[120:123], v[100:103], 0
	ds_read_b128 v[136:139], v10 offset:4096
	v_mfma_f32_16x16x32_f16 v[60:63], v[124:127], v[100:103], 0
	ds_read_b128 v[140:143], v10 offset:6144
	v_mfma_f32_16x16x32_f16 v[64:67], v[112:115], v[104:107], 0
	v_mfma_f32_16x16x32_f16 v[68:71], v[116:119], v[104:107], 0
	v_mfma_f32_16x16x32_f16 v[72:75], v[120:123], v[104:107], 0
	v_mfma_f32_16x16x32_f16 v[76:79], v[124:127], v[104:107], 0
	v_mfma_f32_16x16x32_f16 v[80:83], v[112:115], v[108:111], 0
	v_mfma_f32_16x16x32_f16 v[84:87], v[116:119], v[108:111], 0
	v_mfma_f32_16x16x32_f16 v[88:91], v[120:123], v[108:111], 0
	v_mfma_f32_16x16x32_f16 v[92:95], v[124:127], v[108:111], 0
	s_waitcnt vmcnt(6) lgkmcnt(0)
	s_barrier
	s_add_u32 s28, s28, 0x80
	s_addc_u32 s29, s29, 0
	s_add_u32 s30, s30, 0x80
	s_addc_u32 s31, s31, 0
	s_waitcnt lgkmcnt(0)
	v_mfma_f32_16x16x32_f16 v[32:35], v[144:147], v[128:131], v[32:35]
	ds_read_b128 v[96:99], v12
	v_mfma_f32_16x16x32_f16 v[36:39], v[148:151], v[128:131], v[36:39]
	ds_read_b128 v[112:115], v13 offset:32768
	v_mfma_f32_16x16x32_f16 v[40:43], v[152:155], v[128:131], v[40:43]
	ds_read_b128 v[116:119], v13 offset:34816
	v_mfma_f32_16x16x32_f16 v[44:47], v[156:159], v[128:131], v[44:47]
	ds_read_b128 v[120:123], v13 offset:36864
	v_mfma_f32_16x16x32_f16 v[48:51], v[144:147], v[132:135], v[48:51]
	ds_read_b128 v[124:127], v13 offset:38912
	v_mfma_f32_16x16x32_f16 v[52:55], v[148:151], v[132:135], v[52:55]
	ds_read_b128 v[100:103], v12 offset:2048
	v_mfma_f32_16x16x32_f16 v[56:59], v[152:155], v[132:135], v[56:59]
	ds_read_b128 v[104:107], v12 offset:4096
	v_mfma_f32_16x16x32_f16 v[60:63], v[156:159], v[132:135], v[60:63]
	ds_read_b128 v[108:111], v12 offset:6144
	v_mfma_f32_16x16x32_f16 v[64:67], v[144:147], v[136:139], v[64:67]
	v_mfma_f32_16x16x32_f16 v[68:71], v[148:151], v[136:139], v[68:71]
	v_mfma_f32_16x16x32_f16 v[72:75], v[152:155], v[136:139], v[72:75]
	s_add_u32 m0, s14, 0x0
	s_nop 0
	global_load_lds_dwordx4 v2, s[28:29]
	v_mfma_f32_16x16x32_f16 v[76:79], v[156:159], v[136:139], v[76:79]
	v_mfma_f32_16x16x32_f16 v[80:83], v[144:147], v[140:143], v[80:83]
	s_add_u32 m0, s14, 0x2000
	s_nop 0
	global_load_lds_dwordx4 v3, s[28:29]
	v_mfma_f32_16x16x32_f16 v[84:87], v[148:151], v[140:143], v[84:87]
	v_mfma_f32_16x16x32_f16 v[88:91], v[152:155], v[140:143], v[88:91]
	s_add_u32 m0, s14, 0x4000
	s_nop 0
	global_load_lds_dwordx4 v4, s[28:29]
	v_mfma_f32_16x16x32_f16 v[92:95], v[156:159], v[140:143], v[92:95]
	s_waitcnt lgkmcnt(0)
	v_mfma_f32_16x16x32_f16 v[32:35], v[112:115], v[96:99], v[32:35]
	ds_read_b128 v[128:131], v14
	v_mfma_f32_16x16x32_f16 v[36:39], v[116:119], v[96:99], v[36:39]
	ds_read_b128 v[144:147], v15 offset:32768
	v_mfma_f32_16x16x32_f16 v[40:43], v[120:123], v[96:99], v[40:43]
	ds_read_b128 v[148:151], v15 offset:34816
	v_mfma_f32_16x16x32_f16 v[44:47], v[124:127], v[96:99], v[44:47]
	ds_read_b128 v[152:155], v15 offset:36864
	v_mfma_f32_16x16x32_f16 v[48:51], v[112:115], v[100:103], v[48:51]
	ds_read_b128 v[156:159], v15 offset:38912
	v_mfma_f32_16x16x32_f16 v[52:55], v[116:119], v[100:103], v[52:55]
	ds_read_b128 v[132:135], v14 offset:2048
	v_mfma_f32_16x16x32_f16 v[56:59], v[120:123], v[100:103], v[56:59]
	ds_read_b128 v[136:139], v14 offset:4096
	v_mfma_f32_16x16x32_f16 v[60:63], v[124:127], v[100:103], v[60:63]
	ds_read_b128 v[140:143], v14 offset:6144
	v_mfma_f32_16x16x32_f16 v[64:67], v[112:115], v[104:107], v[64:67]
	v_mfma_f32_16x16x32_f16 v[68:71], v[116:119], v[104:107], v[68:71]
	v_mfma_f32_16x16x32_f16 v[72:75], v[120:123], v[104:107], v[72:75]
	s_add_u32 m0, s14, 0x6000
	s_nop 0
	global_load_lds_dwordx4 v5, s[28:29]
	v_mfma_f32_16x16x32_f16 v[76:79], v[124:127], v[104:107], v[76:79]
	v_mfma_f32_16x16x32_f16 v[80:83], v[112:115], v[108:111], v[80:83]
	s_add_u32 m0, s14, 0x8000
	s_nop 0
	global_load_lds_dwordx4 v6, s[30:31]
	v_mfma_f32_16x16x32_f16 v[84:87], v[116:119], v[108:111], v[84:87]
	v_mfma_f32_16x16x32_f16 v[88:91], v[120:123], v[108:111], v[88:91]
	s_add_u32 m0, s14, 0xa000
	s_nop 0
	global_load_lds_dwordx4 v7, s[30:31]
	v_mfma_f32_16x16x32_f16 v[92:95], v[124:127], v[108:111], v[92:95]
	s_waitcnt vmcnt(6) lgkmcnt(0)
	s_barrier
	s_add_u32 s28, s28, 0x80
	s_addc_u32 s29, s29, 0
	s_add_u32 s30, s30, 0x80
	s_addc_u32 s31, s31, 0
	s_waitcnt lgkmcnt(0)
	v_mfma_f32_16x16x32_f16 v[32:35], v[144:147], v[128:131], v[32:35]
	ds_read_b128 v[96:99], v16
	v_mfma_f32_16x16x32_f16 v[36:39], v[148:151], v[128:131], v[36:39]
	ds_read_b128 v[112:115], v17 offset:32768
	v_mfma_f32_16x16x32_f16 v[40:43], v[152:155], v[128:131], v[40:43]
	ds_read_b128 v[116:119], v17 offset:34816
	v_mfma_f32_16x16x32_f16 v[44:47], v[156:159], v[128:131], v[44:47]
	ds_read_b128 v[120:123], v17 offset:36864
	v_mfma_f32_16x16x32_f16 v[48:51], v[144:147], v[132:135], v[48:51]
	ds_read_b128 v[124:127], v17 offset:38912
	v_mfma_f32_16x16x32_f16 v[52:55], v[148:151], v[132:135], v[52:55]
	ds_read_b128 v[100:103], v16 offset:2048
	v_mfma_f32_16x16x32_f16 v[56:59], v[152:155], v[132:135], v[56:59]
	ds_read_b128 v[104:107], v16 offset:4096
	v_mfma_f32_16x16x32_f16 v[60:63], v[156:159], v[132:135], v[60:63]
	ds_read_b128 v[108:111], v16 offset:6144
	v_mfma_f32_16x16x32_f16 v[64:67], v[144:147], v[136:139], v[64:67]
	v_mfma_f32_16x16x32_f16 v[68:71], v[148:151], v[136:139], v[68:71]
	v_mfma_f32_16x16x32_f16 v[72:75], v[152:155], v[136:139], v[72:75]
	s_add_u32 m0, s14, 0xc000
	s_nop 0
	global_load_lds_dwordx4 v2, s[28:29]
	v_mfma_f32_16x16x32_f16 v[76:79], v[156:159], v[136:139], v[76:79]
	v_mfma_f32_16x16x32_f16 v[80:83], v[144:147], v[140:143], v[80:83]
	s_add_u32 m0, s14, 0xe000
	s_nop 0
	global_load_lds_dwordx4 v3, s[28:29]
	v_mfma_f32_16x16x32_f16 v[84:87], v[148:151], v[140:143], v[84:87]
	v_mfma_f32_16x16x32_f16 v[88:91], v[152:155], v[140:143], v[88:91]
	s_add_u32 m0, s14, 0x10000
	s_nop 0
	global_load_lds_dwordx4 v4, s[28:29]
	v_mfma_f32_16x16x32_f16 v[92:95], v[156:159], v[140:143], v[92:95]
	s_waitcnt lgkmcnt(0)
	v_mfma_f32_16x16x32_f16 v[32:35], v[112:115], v[96:99], v[32:35]
	ds_read_b128 v[128:131], v18
	v_mfma_f32_16x16x32_f16 v[36:39], v[116:119], v[96:99], v[36:39]
	ds_read_b128 v[144:147], v19 offset:32768
	v_mfma_f32_16x16x32_f16 v[40:43], v[120:123], v[96:99], v[40:43]
	ds_read_b128 v[148:151], v19 offset:34816
	v_mfma_f32_16x16x32_f16 v[44:47], v[124:127], v[96:99], v[44:47]
	ds_read_b128 v[152:155], v19 offset:36864
	v_mfma_f32_16x16x32_f16 v[48:51], v[112:115], v[100:103], v[48:51]
	ds_read_b128 v[156:159], v19 offset:38912
	v_mfma_f32_16x16x32_f16 v[52:55], v[116:119], v[100:103], v[52:55]
	ds_read_b128 v[132:135], v18 offset:2048
	v_mfma_f32_16x16x32_f16 v[56:59], v[120:123], v[100:103], v[56:59]
	ds_read_b128 v[136:139], v18 offset:4096
	v_mfma_f32_16x16x32_f16 v[60:63], v[124:127], v[100:103], v[60:63]
	ds_read_b128 v[140:143], v18 offset:6144
	v_mfma_f32_16x16x32_f16 v[64:67], v[112:115], v[104:107], v[64:67]
	v_mfma_f32_16x16x32_f16 v[68:71], v[116:119], v[104:107], v[68:71]
	v_mfma_f32_16x16x32_f16 v[72:75], v[120:123], v[104:107], v[72:75]
	s_add_u32 m0, s14, 0x12000
	s_nop 0
	global_load_lds_dwordx4 v5, s[28:29]
	v_mfma_f32_16x16x32_f16 v[76:79], v[124:127], v[104:107], v[76:79]
	v_mfma_f32_16x16x32_f16 v[80:83], v[112:115], v[108:111], v[80:83]
	s_add_u32 m0, s14, 0x14000
	s_nop 0
	global_load_lds_dwordx4 v6, s[30:31]
	v_mfma_f32_16x16x32_f16 v[84:87], v[116:119], v[108:111], v[84:87]
	v_mfma_f32_16x16x32_f16 v[88:91], v[120:123], v[108:111], v[88:91]
	s_add_u32 m0, s14, 0x16000
	s_nop 0
	global_load_lds_dwordx4 v7, s[30:31]
	v_mfma_f32_16x16x32_f16 v[92:95], v[124:127], v[108:111], v[92:95]
	s_waitcnt vmcnt(6) lgkmcnt(0)
	s_barrier
	s_add_u32 s28, s28, 0x80
	s_addc_u32 s29, s29, 0
	s_add_u32 s30, s30, 0x80
	s_addc_u32 s31, s31, 0
	s_waitcnt lgkmcnt(0)
	v_mfma_f32_16x16x32_f16 v[32:35], v[144:147], v[128:131], v[32:35]
	ds_read_b128 v[96:99], v8
	v_mfma_f32_16x16x32_f16 v[36:39], v[148:151], v[128:131], v[36:39]
	ds_read_b128 v[112:115], v9 offset:32768
	v_mfma_f32_16x16x32_f16 v[40:43], v[152:155], v[128:131], v[40:43]
	ds_read_b128 v[116:119], v9 offset:34816
	v_mfma_f32_16x16x32_f16 v[44:47], v[156:159], v[128:131], v[44:47]
	ds_read_b128 v[120:123], v9 offset:36864
	v_mfma_f32_16x16x32_f16 v[48:51], v[144:147], v[132:135], v[48:51]
	ds_read_b128 v[124:127], v9 offset:38912
	v_mfma_f32_16x16x32_f16 v[52:55], v[148:151], v[132:135], v[52:55]
	ds_read_b128 v[100:103], v8 offset:2048
	v_mfma_f32_16x16x32_f16 v[56:59], v[152:155], v[132:135], v[56:59]
	ds_read_b128 v[104:107], v8 offset:4096
	v_mfma_f32_16x16x32_f16 v[60:63], v[156:159], v[132:135], v[60:63]
	ds_read_b128 v[108:111], v8 offset:6144
	v_mfma_f32_16x16x32_f16 v[64:67], v[144:147], v[136:139], v[64:67]
	v_mfma_f32_16x16x32_f16 v[68:71], v[148:151], v[136:139], v[68:71]
	v_mfma_f32_16x16x32_f16 v[72:75], v[152:155], v[136:139], v[72:75]
	s_add_u32 m0, s14, 0x18000
	s_nop 0
	global_load_lds_dwordx4 v2, s[28:29]
	v_mfma_f32_16x16x32_f16 v[76:79], v[156:159], v[136:139], v[76:79]
	v_mfma_f32_16x16x32_f16 v[80:83], v[144:147], v[140:143], v[80:83]
	s_add_u32 m0, s14, 0x1a000
	s_nop 0
	global_load_lds_dwordx4 v3, s[28:29]
	v_mfma_f32_16x16x32_f16 v[84:87], v[148:151], v[140:143], v[84:87]
	v_mfma_f32_16x16x32_f16 v[88:91], v[152:155], v[140:143], v[88:91]
	s_add_u32 m0, s14, 0x1c000
	s_nop 0
	global_load_lds_dwordx4 v4, s[28:29]
	v_mfma_f32_16x16x32_f16 v[92:95], v[156:159], v[140:143], v[92:95]
	s_waitcnt lgkmcnt(0)
	v_mfma_f32_16x16x32_f16 v[32:35], v[112:115], v[96:99], v[32:35]
	ds_read_b128 v[128:131], v10
	v_mfma_f32_16x16x32_f16 v[36:39], v[116:119], v[96:99], v[36:39]
	ds_read_b128 v[144:147], v11 offset:32768
	v_mfma_f32_16x16x32_f16 v[40:43], v[120:123], v[96:99], v[40:43]
	ds_read_b128 v[148:151], v11 offset:34816
	v_mfma_f32_16x16x32_f16 v[44:47], v[124:127], v[96:99], v[44:47]
	ds_read_b128 v[152:155], v11 offset:36864
	v_mfma_f32_16x16x32_f16 v[48:51], v[112:115], v[100:103], v[48:51]
	ds_read_b128 v[156:159], v11 offset:38912
	v_mfma_f32_16x16x32_f16 v[52:55], v[116:119], v[100:103], v[52:55]
	ds_read_b128 v[132:135], v10 offset:2048
	v_mfma_f32_16x16x32_f16 v[56:59], v[120:123], v[100:103], v[56:59]
	ds_read_b128 v[136:139], v10 offset:4096
	v_mfma_f32_16x16x32_f16 v[60:63], v[124:127], v[100:103], v[60:63]
	ds_read_b128 v[140:143], v10 offset:6144
	v_mfma_f32_16x16x32_f16 v[64:67], v[112:115], v[104:107], v[64:67]
	v_mfma_f32_16x16x32_f16 v[68:71], v[116:119], v[104:107], v[68:71]
	v_mfma_f32_16x16x32_f16 v[72:75], v[120:123], v[104:107], v[72:75]
	s_add_u32 m0, s14, 0x1e000
	s_nop 0
	global_load_lds_dwordx4 v5, s[28:29]
	v_mfma_f32_16x16x32_f16 v[76:79], v[124:127], v[104:107], v[76:79]
	v_mfma_f32_16x16x32_f16 v[80:83], v[112:115], v[108:111], v[80:83]
	s_add_u32 m0, s14, 0x20000
	s_nop 0
	global_load_lds_dwordx4 v6, s[30:31]
	v_mfma_f32_16x16x32_f16 v[84:87], v[116:119], v[108:111], v[84:87]
	v_mfma_f32_16x16x32_f16 v[88:91], v[120:123], v[108:111], v[88:91]
	s_add_u32 m0, s14, 0x22000
	s_nop 0
	global_load_lds_dwordx4 v7, s[30:31]
	v_mfma_f32_16x16x32_f16 v[92:95], v[124:127], v[108:111], v[92:95]
	s_waitcnt vmcnt(6) lgkmcnt(0)
	s_barrier
	s_add_u32 s28, s28, 0x80
	s_addc_u32 s29, s29, 0
	s_add_u32 s30, s30, 0x80
	s_addc_u32 s31, s31, 0
	s_waitcnt lgkmcnt(0)
	v_mfma_f32_16x16x32_f16 v[32:35], v[144:147], v[128:131], v[32:35]
	ds_read_b128 v[96:99], v12
	v_mfma_f32_16x16x32_f16 v[36:39], v[148:151], v[128:131], v[36:39]
	ds_read_b128 v[112:115], v13 offset:32768
	v_mfma_f32_16x16x32_f16 v[40:43], v[152:155], v[128:131], v[40:43]
	ds_read_b128 v[116:119], v13 offset:34816
	v_mfma_f32_16x16x32_f16 v[44:47], v[156:159], v[128:131], v[44:47]
	ds_read_b128 v[120:123], v13 offset:36864
	v_mfma_f32_16x16x32_f16 v[48:51], v[144:147], v[132:135], v[48:51]
	ds_read_b128 v[124:127], v13 offset:38912
	v_mfma_f32_16x16x32_f16 v[52:55], v[148:151], v[132:135], v[52:55]
	ds_read_b128 v[100:103], v12 offset:2048
	v_mfma_f32_16x16x32_f16 v[56:59], v[152:155], v[132:135], v[56:59]
	ds_read_b128 v[104:107], v12 offset:4096
	v_mfma_f32_16x16x32_f16 v[60:63], v[156:159], v[132:135], v[60:63]
	ds_read_b128 v[108:111], v12 offset:6144
	v_mfma_f32_16x16x32_f16 v[64:67], v[144:147], v[136:139], v[64:67]
	v_mfma_f32_16x16x32_f16 v[68:71], v[148:151], v[136:139], v[68:71]
	v_mfma_f32_16x16x32_f16 v[72:75], v[152:155], v[136:139], v[72:75]
	s_add_u32 m0, s14, 0x0
	s_nop 0
	global_load_lds_dwordx4 v2, s[28:29]
	v_mfma_f32_16x16x32_f16 v[76:79], v[156:159], v[136:139], v[76:79]
	v_mfma_f32_16x16x32_f16 v[80:83], v[144:147], v[140:143], v[80:83]
	s_add_u32 m0, s14, 0x2000
	s_nop 0
	global_load_lds_dwordx4 v3, s[28:29]
	v_mfma_f32_16x16x32_f16 v[84:87], v[148:151], v[140:143], v[84:87]
	v_mfma_f32_16x16x32_f16 v[88:91], v[152:155], v[140:143], v[88:91]
	s_add_u32 m0, s14, 0x4000
	s_nop 0
	global_load_lds_dwordx4 v4, s[28:29]
	v_mfma_f32_16x16x32_f16 v[92:95], v[156:159], v[140:143], v[92:95]
	s_waitcnt lgkmcnt(0)
	v_mfma_f32_16x16x32_f16 v[32:35], v[112:115], v[96:99], v[32:35]
	ds_read_b128 v[128:131], v14
	v_mfma_f32_16x16x32_f16 v[36:39], v[116:119], v[96:99], v[36:39]
	ds_read_b128 v[144:147], v15 offset:32768
	v_mfma_f32_16x16x32_f16 v[40:43], v[120:123], v[96:99], v[40:43]
	ds_read_b128 v[148:151], v15 offset:34816
	v_mfma_f32_16x16x32_f16 v[44:47], v[124:127], v[96:99], v[44:47]
	ds_read_b128 v[152:155], v15 offset:36864
	v_mfma_f32_16x16x32_f16 v[48:51], v[112:115], v[100:103], v[48:51]
	ds_read_b128 v[156:159], v15 offset:38912
	v_mfma_f32_16x16x32_f16 v[52:55], v[116:119], v[100:103], v[52:55]
	ds_read_b128 v[132:135], v14 offset:2048
	v_mfma_f32_16x16x32_f16 v[56:59], v[120:123], v[100:103], v[56:59]
	ds_read_b128 v[136:139], v14 offset:4096
	v_mfma_f32_16x16x32_f16 v[60:63], v[124:127], v[100:103], v[60:63]
	ds_read_b128 v[140:143], v14 offset:6144
	v_mfma_f32_16x16x32_f16 v[64:67], v[112:115], v[104:107], v[64:67]
	v_mfma_f32_16x16x32_f16 v[68:71], v[116:119], v[104:107], v[68:71]
	v_mfma_f32_16x16x32_f16 v[72:75], v[120:123], v[104:107], v[72:75]
	s_add_u32 m0, s14, 0x6000
	s_nop 0
	global_load_lds_dwordx4 v5, s[28:29]
	v_mfma_f32_16x16x32_f16 v[76:79], v[124:127], v[104:107], v[76:79]
	v_mfma_f32_16x16x32_f16 v[80:83], v[112:115], v[108:111], v[80:83]
	s_add_u32 m0, s14, 0x8000
	s_nop 0
	global_load_lds_dwordx4 v6, s[30:31]
	v_mfma_f32_16x16x32_f16 v[84:87], v[116:119], v[108:111], v[84:87]
	v_mfma_f32_16x16x32_f16 v[88:91], v[120:123], v[108:111], v[88:91]
	s_add_u32 m0, s14, 0xa000
	s_nop 0
	global_load_lds_dwordx4 v7, s[30:31]
	v_mfma_f32_16x16x32_f16 v[92:95], v[124:127], v[108:111], v[92:95]
	s_waitcnt vmcnt(6) lgkmcnt(0)
	s_barrier
	s_add_u32 s28, s28, 0x80
	s_addc_u32 s29, s29, 0
	s_add_u32 s30, s30, 0x80
	s_addc_u32 s31, s31, 0
	s_waitcnt lgkmcnt(0)
	v_mfma_f32_16x16x32_f16 v[32:35], v[144:147], v[128:131], v[32:35]
	ds_read_b128 v[96:99], v16
	v_mfma_f32_16x16x32_f16 v[36:39], v[148:151], v[128:131], v[36:39]
	ds_read_b128 v[112:115], v17 offset:32768
	v_mfma_f32_16x16x32_f16 v[40:43], v[152:155], v[128:131], v[40:43]
	ds_read_b128 v[116:119], v17 offset:34816
	v_mfma_f32_16x16x32_f16 v[44:47], v[156:159], v[128:131], v[44:47]
	ds_read_b128 v[120:123], v17 offset:36864
	v_mfma_f32_16x16x32_f16 v[48:51], v[144:147], v[132:135], v[48:51]
	ds_read_b128 v[124:127], v17 offset:38912
	v_mfma_f32_16x16x32_f16 v[52:55], v[148:151], v[132:135], v[52:55]
	ds_read_b128 v[100:103], v16 offset:2048
	v_mfma_f32_16x16x32_f16 v[56:59], v[152:155], v[132:135], v[56:59]
	ds_read_b128 v[104:107], v16 offset:4096
	v_mfma_f32_16x16x32_f16 v[60:63], v[156:159], v[132:135], v[60:63]
	ds_read_b128 v[108:111], v16 offset:6144
	v_mfma_f32_16x16x32_f16 v[64:67], v[144:147], v[136:139], v[64:67]
	v_mfma_f32_16x16x32_f16 v[68:71], v[148:151], v[136:139], v[68:71]
	v_mfma_f32_16x16x32_f16 v[72:75], v[152:155], v[136:139], v[72:75]
	s_add_u32 m0, s14, 0xc000
	s_nop 0
	global_load_lds_dwordx4 v2, s[28:29]
	v_mfma_f32_16x16x32_f16 v[76:79], v[156:159], v[136:139], v[76:79]
	v_mfma_f32_16x16x32_f16 v[80:83], v[144:147], v[140:143], v[80:83]
	s_add_u32 m0, s14, 0xe000
	s_nop 0
	global_load_lds_dwordx4 v3, s[28:29]
	v_mfma_f32_16x16x32_f16 v[84:87], v[148:151], v[140:143], v[84:87]
	v_mfma_f32_16x16x32_f16 v[88:91], v[152:155], v[140:143], v[88:91]
	s_add_u32 m0, s14, 0x10000
	s_nop 0
	global_load_lds_dwordx4 v4, s[28:29]
	v_mfma_f32_16x16x32_f16 v[92:95], v[156:159], v[140:143], v[92:95]
	s_waitcnt lgkmcnt(0)
	v_mfma_f32_16x16x32_f16 v[32:35], v[112:115], v[96:99], v[32:35]
	ds_read_b128 v[128:131], v18
	v_mfma_f32_16x16x32_f16 v[36:39], v[116:119], v[96:99], v[36:39]
	ds_read_b128 v[144:147], v19 offset:32768
	v_mfma_f32_16x16x32_f16 v[40:43], v[120:123], v[96:99], v[40:43]
	ds_read_b128 v[148:151], v19 offset:34816
	v_mfma_f32_16x16x32_f16 v[44:47], v[124:127], v[96:99], v[44:47]
	ds_read_b128 v[152:155], v19 offset:36864
	v_mfma_f32_16x16x32_f16 v[48:51], v[112:115], v[100:103], v[48:51]
	ds_read_b128 v[156:159], v19 offset:38912
	v_mfma_f32_16x16x32_f16 v[52:55], v[116:119], v[100:103], v[52:55]
	ds_read_b128 v[132:135], v18 offset:2048
	v_mfma_f32_16x16x32_f16 v[56:59], v[120:123], v[100:103], v[56:59]
	ds_read_b128 v[136:139], v18 offset:4096
	v_mfma_f32_16x16x32_f16 v[60:63], v[124:127], v[100:103], v[60:63]
	ds_read_b128 v[140:143], v18 offset:6144
	v_mfma_f32_16x16x32_f16 v[64:67], v[112:115], v[104:107], v[64:67]
	v_mfma_f32_16x16x32_f16 v[68:71], v[116:119], v[104:107], v[68:71]
	v_mfma_f32_16x16x32_f16 v[72:75], v[120:123], v[104:107], v[72:75]
	s_add_u32 m0, s14, 0x12000
	s_nop 0
	global_load_lds_dwordx4 v5, s[28:29]
	v_mfma_f32_16x16x32_f16 v[76:79], v[124:127], v[104:107], v[76:79]
	v_mfma_f32_16x16x32_f16 v[80:83], v[112:115], v[108:111], v[80:83]
	s_add_u32 m0, s14, 0x14000
	s_nop 0
	global_load_lds_dwordx4 v6, s[30:31]
	v_mfma_f32_16x16x32_f16 v[84:87], v[116:119], v[108:111], v[84:87]
	v_mfma_f32_16x16x32_f16 v[88:91], v[120:123], v[108:111], v[88:91]
	s_add_u32 m0, s14, 0x16000
	s_nop 0
	global_load_lds_dwordx4 v7, s[30:31]
	v_mfma_f32_16x16x32_f16 v[92:95], v[124:127], v[108:111], v[92:95]
	s_waitcnt vmcnt(6) lgkmcnt(0)
	s_barrier
	s_add_u32 s28, s28, 0x80
	s_addc_u32 s29, s29, 0
	s_add_u32 s30, s30, 0x80
	s_addc_u32 s31, s31, 0
	s_waitcnt lgkmcnt(0)
	v_mfma_f32_16x16x32_f16 v[32:35], v[144:147], v[128:131], v[32:35]
	ds_read_b128 v[96:99], v8
	v_mfma_f32_16x16x32_f16 v[36:39], v[148:151], v[128:131], v[36:39]
	ds_read_b128 v[112:115], v9 offset:32768
	v_mfma_f32_16x16x32_f16 v[40:43], v[152:155], v[128:131], v[40:43]
	ds_read_b128 v[116:119], v9 offset:34816
	v_mfma_f32_16x16x32_f16 v[44:47], v[156:159], v[128:131], v[44:47]
	ds_read_b128 v[120:123], v9 offset:36864
	v_mfma_f32_16x16x32_f16 v[48:51], v[144:147], v[132:135], v[48:51]
	ds_read_b128 v[124:127], v9 offset:38912
	v_mfma_f32_16x16x32_f16 v[52:55], v[148:151], v[132:135], v[52:55]
	ds_read_b128 v[100:103], v8 offset:2048
	v_mfma_f32_16x16x32_f16 v[56:59], v[152:155], v[132:135], v[56:59]
	ds_read_b128 v[104:107], v8 offset:4096
	v_mfma_f32_16x16x32_f16 v[60:63], v[156:159], v[132:135], v[60:63]
	ds_read_b128 v[108:111], v8 offset:6144
	v_mfma_f32_16x16x32_f16 v[64:67], v[144:147], v[136:139], v[64:67]
	v_mfma_f32_16x16x32_f16 v[68:71], v[148:151], v[136:139], v[68:71]
	v_mfma_f32_16x16x32_f16 v[72:75], v[152:155], v[136:139], v[72:75]
	s_add_u32 m0, s14, 0x18000
	s_nop 0
	global_load_lds_dwordx4 v2, s[28:29]
	v_mfma_f32_16x16x32_f16 v[76:79], v[156:159], v[136:139], v[76:79]
	v_mfma_f32_16x16x32_f16 v[80:83], v[144:147], v[140:143], v[80:83]
	s_add_u32 m0, s14, 0x1a000
	s_nop 0
	global_load_lds_dwordx4 v3, s[28:29]
	v_mfma_f32_16x16x32_f16 v[84:87], v[148:151], v[140:143], v[84:87]
	v_mfma_f32_16x16x32_f16 v[88:91], v[152:155], v[140:143], v[88:91]
	s_add_u32 m0, s14, 0x1c000
	s_nop 0
	global_load_lds_dwordx4 v4, s[28:29]
	v_mfma_f32_16x16x32_f16 v[92:95], v[156:159], v[140:143], v[92:95]
	s_waitcnt lgkmcnt(0)
	v_mfma_f32_16x16x32_f16 v[32:35], v[112:115], v[96:99], v[32:35]
	ds_read_b128 v[128:131], v10
	v_mfma_f32_16x16x32_f16 v[36:39], v[116:119], v[96:99], v[36:39]
	ds_read_b128 v[144:147], v11 offset:32768
	v_mfma_f32_16x16x32_f16 v[40:43], v[120:123], v[96:99], v[40:43]
	ds_read_b128 v[148:151], v11 offset:34816
	v_mfma_f32_16x16x32_f16 v[44:47], v[124:127], v[96:99], v[44:47]
	ds_read_b128 v[152:155], v11 offset:36864
	v_mfma_f32_16x16x32_f16 v[48:51], v[112:115], v[100:103], v[48:51]
	ds_read_b128 v[156:159], v11 offset:38912
	v_mfma_f32_16x16x32_f16 v[52:55], v[116:119], v[100:103], v[52:55]
	ds_read_b128 v[132:135], v10 offset:2048
	v_mfma_f32_16x16x32_f16 v[56:59], v[120:123], v[100:103], v[56:59]
	ds_read_b128 v[136:139], v10 offset:4096
	v_mfma_f32_16x16x32_f16 v[60:63], v[124:127], v[100:103], v[60:63]
	ds_read_b128 v[140:143], v10 offset:6144
	v_mfma_f32_16x16x32_f16 v[64:67], v[112:115], v[104:107], v[64:67]
	v_mfma_f32_16x16x32_f16 v[68:71], v[116:119], v[104:107], v[68:71]
	v_mfma_f32_16x16x32_f16 v[72:75], v[120:123], v[104:107], v[72:75]
	s_add_u32 m0, s14, 0x1e000
	s_nop 0
	global_load_lds_dwordx4 v5, s[28:29]
	v_mfma_f32_16x16x32_f16 v[76:79], v[124:127], v[104:107], v[76:79]
	v_mfma_f32_16x16x32_f16 v[80:83], v[112:115], v[108:111], v[80:83]
	s_add_u32 m0, s14, 0x20000
	s_nop 0
	global_load_lds_dwordx4 v6, s[30:31]
	v_mfma_f32_16x16x32_f16 v[84:87], v[116:119], v[108:111], v[84:87]
	v_mfma_f32_16x16x32_f16 v[88:91], v[120:123], v[108:111], v[88:91]
	s_add_u32 m0, s14, 0x22000
	s_nop 0
	global_load_lds_dwordx4 v7, s[30:31]
	v_mfma_f32_16x16x32_f16 v[92:95], v[124:127], v[108:111], v[92:95]
	s_waitcnt vmcnt(6) lgkmcnt(0)
	s_barrier
	s_add_u32 s28, s28, 0x80
	s_addc_u32 s29, s29, 0
	s_add_u32 s30, s30, 0x80
	s_addc_u32 s31, s31, 0
	s_waitcnt lgkmcnt(0)
	v_mfma_f32_16x16x32_f16 v[32:35], v[144:147], v[128:131], v[32:35]
	ds_read_b128 v[96:99], v12
	v_mfma_f32_16x16x32_f16 v[36:39], v[148:151], v[128:131], v[36:39]
	ds_read_b128 v[112:115], v13 offset:32768
	v_mfma_f32_16x16x32_f16 v[40:43], v[152:155], v[128:131], v[40:43]
	ds_read_b128 v[116:119], v13 offset:34816
	v_mfma_f32_16x16x32_f16 v[44:47], v[156:159], v[128:131], v[44:47]
	ds_read_b128 v[120:123], v13 offset:36864
	v_mfma_f32_16x16x32_f16 v[48:51], v[144:147], v[132:135], v[48:51]
	ds_read_b128 v[124:127], v13 offset:38912
	v_mfma_f32_16x16x32_f16 v[52:55], v[148:151], v[132:135], v[52:55]
	ds_read_b128 v[100:103], v12 offset:2048
	v_mfma_f32_16x16x32_f16 v[56:59], v[152:155], v[132:135], v[56:59]
	ds_read_b128 v[104:107], v12 offset:4096
	v_mfma_f32_16x16x32_f16 v[60:63], v[156:159], v[132:135], v[60:63]
	ds_read_b128 v[108:111], v12 offset:6144
	v_mfma_f32_16x16x32_f16 v[64:67], v[144:147], v[136:139], v[64:67]
	v_mfma_f32_16x16x32_f16 v[68:71], v[148:151], v[136:139], v[68:71]
	v_mfma_f32_16x16x32_f16 v[72:75], v[152:155], v[136:139], v[72:75]
	s_add_u32 m0, s14, 0x0
	s_nop 0
	global_load_lds_dwordx4 v2, s[28:29]
	v_mfma_f32_16x16x32_f16 v[76:79], v[156:159], v[136:139], v[76:79]
	v_mfma_f32_16x16x32_f16 v[80:83], v[144:147], v[140:143], v[80:83]
	s_add_u32 m0, s14, 0x2000
	s_nop 0
	global_load_lds_dwordx4 v3, s[28:29]
	v_mfma_f32_16x16x32_f16 v[84:87], v[148:151], v[140:143], v[84:87]
	v_mfma_f32_16x16x32_f16 v[88:91], v[152:155], v[140:143], v[88:91]
	s_add_u32 m0, s14, 0x4000
	s_nop 0
	global_load_lds_dwordx4 v4, s[28:29]
	v_mfma_f32_16x16x32_f16 v[92:95], v[156:159], v[140:143], v[92:95]
	s_waitcnt lgkmcnt(0)
	v_mfma_f32_16x16x32_f16 v[32:35], v[112:115], v[96:99], v[32:35]
	ds_read_b128 v[128:131], v14
	v_mfma_f32_16x16x32_f16 v[36:39], v[116:119], v[96:99], v[36:39]
	ds_read_b128 v[144:147], v15 offset:32768
	v_mfma_f32_16x16x32_f16 v[40:43], v[120:123], v[96:99], v[40:43]
	ds_read_b128 v[148:151], v15 offset:34816
	v_mfma_f32_16x16x32_f16 v[44:47], v[124:127], v[96:99], v[44:47]
	ds_read_b128 v[152:155], v15 offset:36864
	v_mfma_f32_16x16x32_f16 v[48:51], v[112:115], v[100:103], v[48:51]
	ds_read_b128 v[156:159], v15 offset:38912
	v_mfma_f32_16x16x32_f16 v[52:55], v[116:119], v[100:103], v[52:55]
	ds_read_b128 v[132:135], v14 offset:2048
	v_mfma_f32_16x16x32_f16 v[56:59], v[120:123], v[100:103], v[56:59]
	ds_read_b128 v[136:139], v14 offset:4096
	v_mfma_f32_16x16x32_f16 v[60:63], v[124:127], v[100:103], v[60:63]
	ds_read_b128 v[140:143], v14 offset:6144
	v_mfma_f32_16x16x32_f16 v[64:67], v[112:115], v[104:107], v[64:67]
	v_mfma_f32_16x16x32_f16 v[68:71], v[116:119], v[104:107], v[68:71]
	v_mfma_f32_16x16x32_f16 v[72:75], v[120:123], v[104:107], v[72:75]
	s_add_u32 m0, s14, 0x6000
	s_nop 0
	global_load_lds_dwordx4 v5, s[28:29]
	v_mfma_f32_16x16x32_f16 v[76:79], v[124:127], v[104:107], v[76:79]
	v_mfma_f32_16x16x32_f16 v[80:83], v[112:115], v[108:111], v[80:83]
	s_add_u32 m0, s14, 0x8000
	s_nop 0
	global_load_lds_dwordx4 v6, s[30:31]
	v_mfma_f32_16x16x32_f16 v[84:87], v[116:119], v[108:111], v[84:87]
	v_mfma_f32_16x16x32_f16 v[88:91], v[120:123], v[108:111], v[88:91]
	s_add_u32 m0, s14, 0xa000
	s_nop 0
	global_load_lds_dwordx4 v7, s[30:31]
	v_mfma_f32_16x16x32_f16 v[92:95], v[124:127], v[108:111], v[92:95]
	s_waitcnt vmcnt(6) lgkmcnt(0)
	s_barrier
	s_add_u32 s28, s28, 0x80
	s_addc_u32 s29, s29, 0
	s_add_u32 s30, s30, 0x80
	s_addc_u32 s31, s31, 0
	s_waitcnt lgkmcnt(0)
	v_mfma_f32_16x16x32_f16 v[32:35], v[144:147], v[128:131], v[32:35]
	ds_read_b128 v[96:99], v16
	v_mfma_f32_16x16x32_f16 v[36:39], v[148:151], v[128:131], v[36:39]
	ds_read_b128 v[112:115], v17 offset:32768
	v_mfma_f32_16x16x32_f16 v[40:43], v[152:155], v[128:131], v[40:43]
	ds_read_b128 v[116:119], v17 offset:34816
	v_mfma_f32_16x16x32_f16 v[44:47], v[156:159], v[128:131], v[44:47]
	ds_read_b128 v[120:123], v17 offset:36864
	v_mfma_f32_16x16x32_f16 v[48:51], v[144:147], v[132:135], v[48:51]
	ds_read_b128 v[124:127], v17 offset:38912
	v_mfma_f32_16x16x32_f16 v[52:55], v[148:151], v[132:135], v[52:55]
	ds_read_b128 v[100:103], v16 offset:2048
	v_mfma_f32_16x16x32_f16 v[56:59], v[152:155], v[132:135], v[56:59]
	ds_read_b128 v[104:107], v16 offset:4096
	v_mfma_f32_16x16x32_f16 v[60:63], v[156:159], v[132:135], v[60:63]
	ds_read_b128 v[108:111], v16 offset:6144
	v_mfma_f32_16x16x32_f16 v[64:67], v[144:147], v[136:139], v[64:67]
	v_mfma_f32_16x16x32_f16 v[68:71], v[148:151], v[136:139], v[68:71]
	v_mfma_f32_16x16x32_f16 v[72:75], v[152:155], v[136:139], v[72:75]
	s_add_u32 m0, s14, 0xc000
	s_nop 0
	global_load_lds_dwordx4 v2, s[28:29]
	v_mfma_f32_16x16x32_f16 v[76:79], v[156:159], v[136:139], v[76:79]
	v_mfma_f32_16x16x32_f16 v[80:83], v[144:147], v[140:143], v[80:83]
	s_add_u32 m0, s14, 0xe000
	s_nop 0
	global_load_lds_dwordx4 v3, s[28:29]
	v_mfma_f32_16x16x32_f16 v[84:87], v[148:151], v[140:143], v[84:87]
	v_mfma_f32_16x16x32_f16 v[88:91], v[152:155], v[140:143], v[88:91]
	s_add_u32 m0, s14, 0x10000
	s_nop 0
	global_load_lds_dwordx4 v4, s[28:29]
	v_mfma_f32_16x16x32_f16 v[92:95], v[156:159], v[140:143], v[92:95]
	s_waitcnt lgkmcnt(0)
	v_mfma_f32_16x16x32_f16 v[32:35], v[112:115], v[96:99], v[32:35]
	ds_read_b128 v[128:131], v18
	v_mfma_f32_16x16x32_f16 v[36:39], v[116:119], v[96:99], v[36:39]
	ds_read_b128 v[144:147], v19 offset:32768
	v_mfma_f32_16x16x32_f16 v[40:43], v[120:123], v[96:99], v[40:43]
	ds_read_b128 v[148:151], v19 offset:34816
	v_mfma_f32_16x16x32_f16 v[44:47], v[124:127], v[96:99], v[44:47]
	ds_read_b128 v[152:155], v19 offset:36864
	v_mfma_f32_16x16x32_f16 v[48:51], v[112:115], v[100:103], v[48:51]
	ds_read_b128 v[156:159], v19 offset:38912
	v_mfma_f32_16x16x32_f16 v[52:55], v[116:119], v[100:103], v[52:55]
	ds_read_b128 v[132:135], v18 offset:2048
	v_mfma_f32_16x16x32_f16 v[56:59], v[120:123], v[100:103], v[56:59]
	ds_read_b128 v[136:139], v18 offset:4096
	v_mfma_f32_16x16x32_f16 v[60:63], v[124:127], v[100:103], v[60:63]
	ds_read_b128 v[140:143], v18 offset:6144
	v_mfma_f32_16x16x32_f16 v[64:67], v[112:115], v[104:107], v[64:67]
	v_mfma_f32_16x16x32_f16 v[68:71], v[116:119], v[104:107], v[68:71]
	v_mfma_f32_16x16x32_f16 v[72:75], v[120:123], v[104:107], v[72:75]
	s_add_u32 m0, s14, 0x12000
	s_nop 0
	global_load_lds_dwordx4 v5, s[28:29]
	v_mfma_f32_16x16x32_f16 v[76:79], v[124:127], v[104:107], v[76:79]
	v_mfma_f32_16x16x32_f16 v[80:83], v[112:115], v[108:111], v[80:83]
	s_add_u32 m0, s14, 0x14000
	s_nop 0
	global_load_lds_dwordx4 v6, s[30:31]
	v_mfma_f32_16x16x32_f16 v[84:87], v[116:119], v[108:111], v[84:87]
	v_mfma_f32_16x16x32_f16 v[88:91], v[120:123], v[108:111], v[88:91]
	s_add_u32 m0, s14, 0x16000
	s_nop 0
	global_load_lds_dwordx4 v7, s[30:31]
	v_mfma_f32_16x16x32_f16 v[92:95], v[124:127], v[108:111], v[92:95]
	s_waitcnt vmcnt(6) lgkmcnt(0)
	s_barrier
	s_add_u32 s28, s28, 0x80
	s_addc_u32 s29, s29, 0
	s_add_u32 s30, s30, 0x80
	s_addc_u32 s31, s31, 0
	s_waitcnt lgkmcnt(0)
	v_mfma_f32_16x16x32_f16 v[32:35], v[144:147], v[128:131], v[32:35]
	ds_read_b128 v[96:99], v8
	v_mfma_f32_16x16x32_f16 v[36:39], v[148:151], v[128:131], v[36:39]
	ds_read_b128 v[112:115], v9 offset:32768
	v_mfma_f32_16x16x32_f16 v[40:43], v[152:155], v[128:131], v[40:43]
	ds_read_b128 v[116:119], v9 offset:34816
	v_mfma_f32_16x16x32_f16 v[44:47], v[156:159], v[128:131], v[44:47]
	ds_read_b128 v[120:123], v9 offset:36864
	v_mfma_f32_16x16x32_f16 v[48:51], v[144:147], v[132:135], v[48:51]
	ds_read_b128 v[124:127], v9 offset:38912
	v_mfma_f32_16x16x32_f16 v[52:55], v[148:151], v[132:135], v[52:55]
	ds_read_b128 v[100:103], v8 offset:2048
	v_mfma_f32_16x16x32_f16 v[56:59], v[152:155], v[132:135], v[56:59]
	ds_read_b128 v[104:107], v8 offset:4096
	v_mfma_f32_16x16x32_f16 v[60:63], v[156:159], v[132:135], v[60:63]
	ds_read_b128 v[108:111], v8 offset:6144
	v_mfma_f32_16x16x32_f16 v[64:67], v[144:147], v[136:139], v[64:67]
	v_mfma_f32_16x16x32_f16 v[68:71], v[148:151], v[136:139], v[68:71]
	v_mfma_f32_16x16x32_f16 v[72:75], v[152:155], v[136:139], v[72:75]
	s_add_u32 m0, s14, 0x18000
	s_nop 0
	global_load_lds_dwordx4 v2, s[28:29]
	v_mfma_f32_16x16x32_f16 v[76:79], v[156:159], v[136:139], v[76:79]
	v_mfma_f32_16x16x32_f16 v[80:83], v[144:147], v[140:143], v[80:83]
	s_add_u32 m0, s14, 0x1a000
	s_nop 0
	global_load_lds_dwordx4 v3, s[28:29]
	v_mfma_f32_16x16x32_f16 v[84:87], v[148:151], v[140:143], v[84:87]
	v_mfma_f32_16x16x32_f16 v[88:91], v[152:155], v[140:143], v[88:91]
	s_add_u32 m0, s14, 0x1c000
	s_nop 0
	global_load_lds_dwordx4 v4, s[28:29]
	v_mfma_f32_16x16x32_f16 v[92:95], v[156:159], v[140:143], v[92:95]
	s_waitcnt lgkmcnt(0)
	v_mfma_f32_16x16x32_f16 v[32:35], v[112:115], v[96:99], v[32:35]
	ds_read_b128 v[128:131], v10
	v_mfma_f32_16x16x32_f16 v[36:39], v[116:119], v[96:99], v[36:39]
	ds_read_b128 v[144:147], v11 offset:32768
	v_mfma_f32_16x16x32_f16 v[40:43], v[120:123], v[96:99], v[40:43]
	ds_read_b128 v[148:151], v11 offset:34816
	v_mfma_f32_16x16x32_f16 v[44:47], v[124:127], v[96:99], v[44:47]
	ds_read_b128 v[152:155], v11 offset:36864
	v_mfma_f32_16x16x32_f16 v[48:51], v[112:115], v[100:103], v[48:51]
	ds_read_b128 v[156:159], v11 offset:38912
	v_mfma_f32_16x16x32_f16 v[52:55], v[116:119], v[100:103], v[52:55]
	ds_read_b128 v[132:135], v10 offset:2048
	v_mfma_f32_16x16x32_f16 v[56:59], v[120:123], v[100:103], v[56:59]
	ds_read_b128 v[136:139], v10 offset:4096
	v_mfma_f32_16x16x32_f16 v[60:63], v[124:127], v[100:103], v[60:63]
	ds_read_b128 v[140:143], v10 offset:6144
	v_mfma_f32_16x16x32_f16 v[64:67], v[112:115], v[104:107], v[64:67]
	v_mfma_f32_16x16x32_f16 v[68:71], v[116:119], v[104:107], v[68:71]
	v_mfma_f32_16x16x32_f16 v[72:75], v[120:123], v[104:107], v[72:75]
	s_add_u32 m0, s14, 0x1e000
	s_nop 0
	global_load_lds_dwordx4 v5, s[28:29]
	v_mfma_f32_16x16x32_f16 v[76:79], v[124:127], v[104:107], v[76:79]
	v_mfma_f32_16x16x32_f16 v[80:83], v[112:115], v[108:111], v[80:83]
	s_add_u32 m0, s14, 0x20000
	s_nop 0
	global_load_lds_dwordx4 v6, s[30:31]
	v_mfma_f32_16x16x32_f16 v[84:87], v[116:119], v[108:111], v[84:87]
	v_mfma_f32_16x16x32_f16 v[88:91], v[120:123], v[108:111], v[88:91]
	s_add_u32 m0, s14, 0x22000
	s_nop 0
	global_load_lds_dwordx4 v7, s[30:31]
	v_mfma_f32_16x16x32_f16 v[92:95], v[124:127], v[108:111], v[92:95]
	s_waitcnt vmcnt(6) lgkmcnt(0)
	s_barrier
	s_add_u32 s28, s28, 0x80
	s_addc_u32 s29, s29, 0
	s_add_u32 s30, s30, 0x80
	s_addc_u32 s31, s31, 0
	s_waitcnt lgkmcnt(0)
	v_mfma_f32_16x16x32_f16 v[32:35], v[144:147], v[128:131], v[32:35]
	ds_read_b128 v[96:99], v12
	v_mfma_f32_16x16x32_f16 v[36:39], v[148:151], v[128:131], v[36:39]
	ds_read_b128 v[112:115], v13 offset:32768
	v_mfma_f32_16x16x32_f16 v[40:43], v[152:155], v[128:131], v[40:43]
	ds_read_b128 v[116:119], v13 offset:34816
	v_mfma_f32_16x16x32_f16 v[44:47], v[156:159], v[128:131], v[44:47]
	ds_read_b128 v[120:123], v13 offset:36864
	v_mfma_f32_16x16x32_f16 v[48:51], v[144:147], v[132:135], v[48:51]
	ds_read_b128 v[124:127], v13 offset:38912
	v_mfma_f32_16x16x32_f16 v[52:55], v[148:151], v[132:135], v[52:55]
	ds_read_b128 v[100:103], v12 offset:2048
	v_mfma_f32_16x16x32_f16 v[56:59], v[152:155], v[132:135], v[56:59]
	ds_read_b128 v[104:107], v12 offset:4096
	v_mfma_f32_16x16x32_f16 v[60:63], v[156:159], v[132:135], v[60:63]
	ds_read_b128 v[108:111], v12 offset:6144
	v_mfma_f32_16x16x32_f16 v[64:67], v[144:147], v[136:139], v[64:67]
	v_mfma_f32_16x16x32_f16 v[68:71], v[148:151], v[136:139], v[68:71]
	v_mfma_f32_16x16x32_f16 v[72:75], v[152:155], v[136:139], v[72:75]
	s_add_u32 m0, s14, 0x0
	s_nop 0
	global_load_lds_dwordx4 v2, s[28:29]
	v_mfma_f32_16x16x32_f16 v[76:79], v[156:159], v[136:139], v[76:79]
	v_mfma_f32_16x16x32_f16 v[80:83], v[144:147], v[140:143], v[80:83]
	s_add_u32 m0, s14, 0x2000
	s_nop 0
	global_load_lds_dwordx4 v3, s[28:29]
	v_mfma_f32_16x16x32_f16 v[84:87], v[148:151], v[140:143], v[84:87]
	v_mfma_f32_16x16x32_f16 v[88:91], v[152:155], v[140:143], v[88:91]
	s_add_u32 m0, s14, 0x4000
	s_nop 0
	global_load_lds_dwordx4 v4, s[28:29]
	v_mfma_f32_16x16x32_f16 v[92:95], v[156:159], v[140:143], v[92:95]
	s_waitcnt lgkmcnt(0)
	v_mfma_f32_16x16x32_f16 v[32:35], v[112:115], v[96:99], v[32:35]
	ds_read_b128 v[128:131], v14
	v_mfma_f32_16x16x32_f16 v[36:39], v[116:119], v[96:99], v[36:39]
	ds_read_b128 v[144:147], v15 offset:32768
	v_mfma_f32_16x16x32_f16 v[40:43], v[120:123], v[96:99], v[40:43]
	ds_read_b128 v[148:151], v15 offset:34816
	v_mfma_f32_16x16x32_f16 v[44:47], v[124:127], v[96:99], v[44:47]
	ds_read_b128 v[152:155], v15 offset:36864
	v_mfma_f32_16x16x32_f16 v[48:51], v[112:115], v[100:103], v[48:51]
	ds_read_b128 v[156:159], v15 offset:38912
	v_mfma_f32_16x16x32_f16 v[52:55], v[116:119], v[100:103], v[52:55]
	ds_read_b128 v[132:135], v14 offset:2048
	v_mfma_f32_16x16x32_f16 v[56:59], v[120:123], v[100:103], v[56:59]
	ds_read_b128 v[136:139], v14 offset:4096
	v_mfma_f32_16x16x32_f16 v[60:63], v[124:127], v[100:103], v[60:63]
	ds_read_b128 v[140:143], v14 offset:6144
	v_mfma_f32_16x16x32_f16 v[64:67], v[112:115], v[104:107], v[64:67]
	v_mfma_f32_16x16x32_f16 v[68:71], v[116:119], v[104:107], v[68:71]
	v_mfma_f32_16x16x32_f16 v[72:75], v[120:123], v[104:107], v[72:75]
	s_add_u32 m0, s14, 0x6000
	s_nop 0
	global_load_lds_dwordx4 v5, s[28:29]
	v_mfma_f32_16x16x32_f16 v[76:79], v[124:127], v[104:107], v[76:79]
	v_mfma_f32_16x16x32_f16 v[80:83], v[112:115], v[108:111], v[80:83]
	s_add_u32 m0, s14, 0x8000
	s_nop 0
	global_load_lds_dwordx4 v6, s[30:31]
	v_mfma_f32_16x16x32_f16 v[84:87], v[116:119], v[108:111], v[84:87]
	v_mfma_f32_16x16x32_f16 v[88:91], v[120:123], v[108:111], v[88:91]
	s_add_u32 m0, s14, 0xa000
	s_nop 0
	global_load_lds_dwordx4 v7, s[30:31]
	v_mfma_f32_16x16x32_f16 v[92:95], v[124:127], v[108:111], v[92:95]
	s_waitcnt vmcnt(6) lgkmcnt(0)
	s_barrier
	s_add_u32 s28, s28, 0x80
	s_addc_u32 s29, s29, 0
	s_add_u32 s30, s30, 0x80
	s_addc_u32 s31, s31, 0
	s_waitcnt lgkmcnt(0)
	v_mfma_f32_16x16x32_f16 v[32:35], v[144:147], v[128:131], v[32:35]
	ds_read_b128 v[96:99], v16
	v_mfma_f32_16x16x32_f16 v[36:39], v[148:151], v[128:131], v[36:39]
	ds_read_b128 v[112:115], v17 offset:32768
	v_mfma_f32_16x16x32_f16 v[40:43], v[152:155], v[128:131], v[40:43]
	ds_read_b128 v[116:119], v17 offset:34816
	v_mfma_f32_16x16x32_f16 v[44:47], v[156:159], v[128:131], v[44:47]
	ds_read_b128 v[120:123], v17 offset:36864
	v_mfma_f32_16x16x32_f16 v[48:51], v[144:147], v[132:135], v[48:51]
	ds_read_b128 v[124:127], v17 offset:38912
	v_mfma_f32_16x16x32_f16 v[52:55], v[148:151], v[132:135], v[52:55]
	ds_read_b128 v[100:103], v16 offset:2048
	v_mfma_f32_16x16x32_f16 v[56:59], v[152:155], v[132:135], v[56:59]
	ds_read_b128 v[104:107], v16 offset:4096
	v_mfma_f32_16x16x32_f16 v[60:63], v[156:159], v[132:135], v[60:63]
	ds_read_b128 v[108:111], v16 offset:6144
	v_mfma_f32_16x16x32_f16 v[64:67], v[144:147], v[136:139], v[64:67]
	v_mfma_f32_16x16x32_f16 v[68:71], v[148:151], v[136:139], v[68:71]
	v_mfma_f32_16x16x32_f16 v[72:75], v[152:155], v[136:139], v[72:75]
	s_add_u32 m0, s14, 0xc000
	s_nop 0
	global_load_lds_dwordx4 v2, s[28:29]
	v_mfma_f32_16x16x32_f16 v[76:79], v[156:159], v[136:139], v[76:79]
	v_mfma_f32_16x16x32_f16 v[80:83], v[144:147], v[140:143], v[80:83]
	s_add_u32 m0, s14, 0xe000
	s_nop 0
	global_load_lds_dwordx4 v3, s[28:29]
	v_mfma_f32_16x16x32_f16 v[84:87], v[148:151], v[140:143], v[84:87]
	v_mfma_f32_16x16x32_f16 v[88:91], v[152:155], v[140:143], v[88:91]
	s_add_u32 m0, s14, 0x10000
	s_nop 0
	global_load_lds_dwordx4 v4, s[28:29]
	v_mfma_f32_16x16x32_f16 v[92:95], v[156:159], v[140:143], v[92:95]
	s_waitcnt lgkmcnt(0)
	v_mfma_f32_16x16x32_f16 v[32:35], v[112:115], v[96:99], v[32:35]
	ds_read_b128 v[128:131], v18
	v_mfma_f32_16x16x32_f16 v[36:39], v[116:119], v[96:99], v[36:39]
	ds_read_b128 v[144:147], v19 offset:32768
	v_mfma_f32_16x16x32_f16 v[40:43], v[120:123], v[96:99], v[40:43]
	ds_read_b128 v[148:151], v19 offset:34816
	v_mfma_f32_16x16x32_f16 v[44:47], v[124:127], v[96:99], v[44:47]
	ds_read_b128 v[152:155], v19 offset:36864
	v_mfma_f32_16x16x32_f16 v[48:51], v[112:115], v[100:103], v[48:51]
	ds_read_b128 v[156:159], v19 offset:38912
	v_mfma_f32_16x16x32_f16 v[52:55], v[116:119], v[100:103], v[52:55]
	ds_read_b128 v[132:135], v18 offset:2048
	v_mfma_f32_16x16x32_f16 v[56:59], v[120:123], v[100:103], v[56:59]
	ds_read_b128 v[136:139], v18 offset:4096
	v_mfma_f32_16x16x32_f16 v[60:63], v[124:127], v[100:103], v[60:63]
	ds_read_b128 v[140:143], v18 offset:6144
	v_mfma_f32_16x16x32_f16 v[64:67], v[112:115], v[104:107], v[64:67]
	v_mfma_f32_16x16x32_f16 v[68:71], v[116:119], v[104:107], v[68:71]
	v_mfma_f32_16x16x32_f16 v[72:75], v[120:123], v[104:107], v[72:75]
	s_add_u32 m0, s14, 0x12000
	s_nop 0
	global_load_lds_dwordx4 v5, s[28:29]
	v_mfma_f32_16x16x32_f16 v[76:79], v[124:127], v[104:107], v[76:79]
	v_mfma_f32_16x16x32_f16 v[80:83], v[112:115], v[108:111], v[80:83]
	s_add_u32 m0, s14, 0x14000
	s_nop 0
	global_load_lds_dwordx4 v6, s[30:31]
	v_mfma_f32_16x16x32_f16 v[84:87], v[116:119], v[108:111], v[84:87]
	v_mfma_f32_16x16x32_f16 v[88:91], v[120:123], v[108:111], v[88:91]
	s_add_u32 m0, s14, 0x16000
	s_nop 0
	global_load_lds_dwordx4 v7, s[30:31]
	v_mfma_f32_16x16x32_f16 v[92:95], v[124:127], v[108:111], v[92:95]
	s_waitcnt vmcnt(6) lgkmcnt(0)
	s_barrier
	s_add_u32 s28, s28, 0x80
	s_addc_u32 s29, s29, 0
	s_add_u32 s30, s30, 0x80
	s_addc_u32 s31, s31, 0
	s_waitcnt lgkmcnt(0)
	v_mfma_f32_16x16x32_f16 v[32:35], v[144:147], v[128:131], v[32:35]
	ds_read_b128 v[96:99], v8
	v_mfma_f32_16x16x32_f16 v[36:39], v[148:151], v[128:131], v[36:39]
	ds_read_b128 v[112:115], v9 offset:32768
	v_mfma_f32_16x16x32_f16 v[40:43], v[152:155], v[128:131], v[40:43]
	ds_read_b128 v[116:119], v9 offset:34816
	v_mfma_f32_16x16x32_f16 v[44:47], v[156:159], v[128:131], v[44:47]
	ds_read_b128 v[120:123], v9 offset:36864
	v_mfma_f32_16x16x32_f16 v[48:51], v[144:147], v[132:135], v[48:51]
	ds_read_b128 v[124:127], v9 offset:38912
	v_mfma_f32_16x16x32_f16 v[52:55], v[148:151], v[132:135], v[52:55]
	ds_read_b128 v[100:103], v8 offset:2048
	v_mfma_f32_16x16x32_f16 v[56:59], v[152:155], v[132:135], v[56:59]
	ds_read_b128 v[104:107], v8 offset:4096
	v_mfma_f32_16x16x32_f16 v[60:63], v[156:159], v[132:135], v[60:63]
	ds_read_b128 v[108:111], v8 offset:6144
	v_mfma_f32_16x16x32_f16 v[64:67], v[144:147], v[136:139], v[64:67]
	v_mfma_f32_16x16x32_f16 v[68:71], v[148:151], v[136:139], v[68:71]
	v_mfma_f32_16x16x32_f16 v[72:75], v[152:155], v[136:139], v[72:75]
	s_add_u32 m0, s14, 0x18000
	s_nop 0
	global_load_lds_dwordx4 v2, s[28:29]
	v_mfma_f32_16x16x32_f16 v[76:79], v[156:159], v[136:139], v[76:79]
	v_mfma_f32_16x16x32_f16 v[80:83], v[144:147], v[140:143], v[80:83]
	s_add_u32 m0, s14, 0x1a000
	s_nop 0
	global_load_lds_dwordx4 v3, s[28:29]
	v_mfma_f32_16x16x32_f16 v[84:87], v[148:151], v[140:143], v[84:87]
	v_mfma_f32_16x16x32_f16 v[88:91], v[152:155], v[140:143], v[88:91]
	s_add_u32 m0, s14, 0x1c000
	s_nop 0
	global_load_lds_dwordx4 v4, s[28:29]
	v_mfma_f32_16x16x32_f16 v[92:95], v[156:159], v[140:143], v[92:95]
	s_waitcnt lgkmcnt(0)
	v_mfma_f32_16x16x32_f16 v[32:35], v[112:115], v[96:99], v[32:35]
	ds_read_b128 v[128:131], v10
	v_mfma_f32_16x16x32_f16 v[36:39], v[116:119], v[96:99], v[36:39]
	ds_read_b128 v[144:147], v11 offset:32768
	v_mfma_f32_16x16x32_f16 v[40:43], v[120:123], v[96:99], v[40:43]
	ds_read_b128 v[148:151], v11 offset:34816
	v_mfma_f32_16x16x32_f16 v[44:47], v[124:127], v[96:99], v[44:47]
	ds_read_b128 v[152:155], v11 offset:36864
	v_mfma_f32_16x16x32_f16 v[48:51], v[112:115], v[100:103], v[48:51]
	ds_read_b128 v[156:159], v11 offset:38912
	v_mfma_f32_16x16x32_f16 v[52:55], v[116:119], v[100:103], v[52:55]
	ds_read_b128 v[132:135], v10 offset:2048
	v_mfma_f32_16x16x32_f16 v[56:59], v[120:123], v[100:103], v[56:59]
	ds_read_b128 v[136:139], v10 offset:4096
	v_mfma_f32_16x16x32_f16 v[60:63], v[124:127], v[100:103], v[60:63]
	ds_read_b128 v[140:143], v10 offset:6144
	v_mfma_f32_16x16x32_f16 v[64:67], v[112:115], v[104:107], v[64:67]
	v_mfma_f32_16x16x32_f16 v[68:71], v[116:119], v[104:107], v[68:71]
	v_mfma_f32_16x16x32_f16 v[72:75], v[120:123], v[104:107], v[72:75]
	s_add_u32 m0, s14, 0x1e000
	s_nop 0
	global_load_lds_dwordx4 v5, s[28:29]
	v_mfma_f32_16x16x32_f16 v[76:79], v[124:127], v[104:107], v[76:79]
	v_mfma_f32_16x16x32_f16 v[80:83], v[112:115], v[108:111], v[80:83]
	s_add_u32 m0, s14, 0x20000
	s_nop 0
	global_load_lds_dwordx4 v6, s[30:31]
	v_mfma_f32_16x16x32_f16 v[84:87], v[116:119], v[108:111], v[84:87]
	v_mfma_f32_16x16x32_f16 v[88:91], v[120:123], v[108:111], v[88:91]
	s_add_u32 m0, s14, 0x22000
	s_nop 0
	global_load_lds_dwordx4 v7, s[30:31]
	v_mfma_f32_16x16x32_f16 v[92:95], v[124:127], v[108:111], v[92:95]
	s_waitcnt vmcnt(6) lgkmcnt(0)
	s_barrier
	s_add_u32 s28, s28, 0x80
	s_addc_u32 s29, s29, 0
	s_add_u32 s30, s30, 0x80
	s_addc_u32 s31, s31, 0
	s_waitcnt lgkmcnt(0)
	v_mfma_f32_16x16x32_f16 v[32:35], v[144:147], v[128:131], v[32:35]
	ds_read_b128 v[96:99], v12
	v_mfma_f32_16x16x32_f16 v[36:39], v[148:151], v[128:131], v[36:39]
	ds_read_b128 v[112:115], v13 offset:32768
	v_mfma_f32_16x16x32_f16 v[40:43], v[152:155], v[128:131], v[40:43]
	ds_read_b128 v[116:119], v13 offset:34816
	v_mfma_f32_16x16x32_f16 v[44:47], v[156:159], v[128:131], v[44:47]
	ds_read_b128 v[120:123], v13 offset:36864
	v_mfma_f32_16x16x32_f16 v[48:51], v[144:147], v[132:135], v[48:51]
	ds_read_b128 v[124:127], v13 offset:38912
	v_mfma_f32_16x16x32_f16 v[52:55], v[148:151], v[132:135], v[52:55]
	ds_read_b128 v[100:103], v12 offset:2048
	v_mfma_f32_16x16x32_f16 v[56:59], v[152:155], v[132:135], v[56:59]
	ds_read_b128 v[104:107], v12 offset:4096
	v_mfma_f32_16x16x32_f16 v[60:63], v[156:159], v[132:135], v[60:63]
	ds_read_b128 v[108:111], v12 offset:6144
	v_mfma_f32_16x16x32_f16 v[64:67], v[144:147], v[136:139], v[64:67]
	v_mfma_f32_16x16x32_f16 v[68:71], v[148:151], v[136:139], v[68:71]
	v_mfma_f32_16x16x32_f16 v[72:75], v[152:155], v[136:139], v[72:75]
	s_add_u32 m0, s14, 0x0
	s_nop 0
	global_load_lds_dwordx4 v2, s[28:29]
	v_mfma_f32_16x16x32_f16 v[76:79], v[156:159], v[136:139], v[76:79]
	v_mfma_f32_16x16x32_f16 v[80:83], v[144:147], v[140:143], v[80:83]
	s_add_u32 m0, s14, 0x2000
	s_nop 0
	global_load_lds_dwordx4 v3, s[28:29]
	v_mfma_f32_16x16x32_f16 v[84:87], v[148:151], v[140:143], v[84:87]
	v_mfma_f32_16x16x32_f16 v[88:91], v[152:155], v[140:143], v[88:91]
	s_add_u32 m0, s14, 0x4000
	s_nop 0
	global_load_lds_dwordx4 v4, s[28:29]
	v_mfma_f32_16x16x32_f16 v[92:95], v[156:159], v[140:143], v[92:95]
	s_waitcnt lgkmcnt(0)
	v_mfma_f32_16x16x32_f16 v[32:35], v[112:115], v[96:99], v[32:35]
	ds_read_b128 v[128:131], v14
	v_mfma_f32_16x16x32_f16 v[36:39], v[116:119], v[96:99], v[36:39]
	ds_read_b128 v[144:147], v15 offset:32768
	v_mfma_f32_16x16x32_f16 v[40:43], v[120:123], v[96:99], v[40:43]
	ds_read_b128 v[148:151], v15 offset:34816
	v_mfma_f32_16x16x32_f16 v[44:47], v[124:127], v[96:99], v[44:47]
	ds_read_b128 v[152:155], v15 offset:36864
	v_mfma_f32_16x16x32_f16 v[48:51], v[112:115], v[100:103], v[48:51]
	ds_read_b128 v[156:159], v15 offset:38912
	v_mfma_f32_16x16x32_f16 v[52:55], v[116:119], v[100:103], v[52:55]
	ds_read_b128 v[132:135], v14 offset:2048
	v_mfma_f32_16x16x32_f16 v[56:59], v[120:123], v[100:103], v[56:59]
	ds_read_b128 v[136:139], v14 offset:4096
	v_mfma_f32_16x16x32_f16 v[60:63], v[124:127], v[100:103], v[60:63]
	ds_read_b128 v[140:143], v14 offset:6144
	v_mfma_f32_16x16x32_f16 v[64:67], v[112:115], v[104:107], v[64:67]
	v_mfma_f32_16x16x32_f16 v[68:71], v[116:119], v[104:107], v[68:71]
	v_mfma_f32_16x16x32_f16 v[72:75], v[120:123], v[104:107], v[72:75]
	s_add_u32 m0, s14, 0x6000
	s_nop 0
	global_load_lds_dwordx4 v5, s[28:29]
	v_mfma_f32_16x16x32_f16 v[76:79], v[124:127], v[104:107], v[76:79]
	v_mfma_f32_16x16x32_f16 v[80:83], v[112:115], v[108:111], v[80:83]
	s_add_u32 m0, s14, 0x8000
	s_nop 0
	global_load_lds_dwordx4 v6, s[30:31]
	v_mfma_f32_16x16x32_f16 v[84:87], v[116:119], v[108:111], v[84:87]
	v_mfma_f32_16x16x32_f16 v[88:91], v[120:123], v[108:111], v[88:91]
	s_add_u32 m0, s14, 0xa000
	s_nop 0
	global_load_lds_dwordx4 v7, s[30:31]
	v_mfma_f32_16x16x32_f16 v[92:95], v[124:127], v[108:111], v[92:95]
	s_waitcnt vmcnt(6) lgkmcnt(0)
	s_barrier
	s_mov_b64 s[28:29], s[16:17]
	s_mov_b64 s[30:31], s[22:23]
	s_waitcnt lgkmcnt(0)
	v_mfma_f32_16x16x32_f16 v[32:35], v[144:147], v[128:131], v[32:35]
	ds_read_b128 v[96:99], v16
	v_mfma_f32_16x16x32_f16 v[36:39], v[148:151], v[128:131], v[36:39]
	ds_read_b128 v[112:115], v17 offset:32768
	v_mfma_f32_16x16x32_f16 v[40:43], v[152:155], v[128:131], v[40:43]
	ds_read_b128 v[116:119], v17 offset:34816
	v_mfma_f32_16x16x32_f16 v[44:47], v[156:159], v[128:131], v[44:47]
	ds_read_b128 v[120:123], v17 offset:36864
	v_mfma_f32_16x16x32_f16 v[48:51], v[144:147], v[132:135], v[48:51]
	ds_read_b128 v[124:127], v17 offset:38912
	v_mfma_f32_16x16x32_f16 v[52:55], v[148:151], v[132:135], v[52:55]
	ds_read_b128 v[100:103], v16 offset:2048
	v_mfma_f32_16x16x32_f16 v[56:59], v[152:155], v[132:135], v[56:59]
	ds_read_b128 v[104:107], v16 offset:4096
	v_mfma_f32_16x16x32_f16 v[60:63], v[156:159], v[132:135], v[60:63]
	ds_read_b128 v[108:111], v16 offset:6144
	v_mfma_f32_16x16x32_f16 v[64:67], v[144:147], v[136:139], v[64:67]
	v_mfma_f32_16x16x32_f16 v[68:71], v[148:151], v[136:139], v[68:71]
	v_mfma_f32_16x16x32_f16 v[72:75], v[152:155], v[136:139], v[72:75]
	s_add_u32 m0, s14, 0xc000
	s_nop 0
	global_load_lds_dwordx4 v2, s[28:29]
	v_mfma_f32_16x16x32_f16 v[76:79], v[156:159], v[136:139], v[76:79]
	v_mfma_f32_16x16x32_f16 v[80:83], v[144:147], v[140:143], v[80:83]
	s_add_u32 m0, s14, 0xe000
	s_nop 0
	global_load_lds_dwordx4 v3, s[28:29]
	v_mfma_f32_16x16x32_f16 v[84:87], v[148:151], v[140:143], v[84:87]
	v_mfma_f32_16x16x32_f16 v[88:91], v[152:155], v[140:143], v[88:91]
	s_add_u32 m0, s14, 0x10000
	s_nop 0
	global_load_lds_dwordx4 v4, s[28:29]
	v_mfma_f32_16x16x32_f16 v[92:95], v[156:159], v[140:143], v[92:95]
	s_waitcnt lgkmcnt(0)
	v_mfma_f32_16x16x32_f16 v[32:35], v[112:115], v[96:99], v[32:35]
	ds_read_b128 v[128:131], v18
	v_mfma_f32_16x16x32_f16 v[36:39], v[116:119], v[96:99], v[36:39]
	ds_read_b128 v[144:147], v19 offset:32768
	v_mfma_f32_16x16x32_f16 v[40:43], v[120:123], v[96:99], v[40:43]
	ds_read_b128 v[148:151], v19 offset:34816
	v_mfma_f32_16x16x32_f16 v[44:47], v[124:127], v[96:99], v[44:47]
	ds_read_b128 v[152:155], v19 offset:36864
	v_mfma_f32_16x16x32_f16 v[48:51], v[112:115], v[100:103], v[48:51]
	ds_read_b128 v[156:159], v19 offset:38912
	v_mfma_f32_16x16x32_f16 v[52:55], v[116:119], v[100:103], v[52:55]
	ds_read_b128 v[132:135], v18 offset:2048
	v_mfma_f32_16x16x32_f16 v[56:59], v[120:123], v[100:103], v[56:59]
	ds_read_b128 v[136:139], v18 offset:4096
	v_mfma_f32_16x16x32_f16 v[60:63], v[124:127], v[100:103], v[60:63]
	ds_read_b128 v[140:143], v18 offset:6144
	v_mfma_f32_16x16x32_f16 v[64:67], v[112:115], v[104:107], v[64:67]
	v_mfma_f32_16x16x32_f16 v[68:71], v[116:119], v[104:107], v[68:71]
	v_mfma_f32_16x16x32_f16 v[72:75], v[120:123], v[104:107], v[72:75]
	s_add_u32 m0, s14, 0x12000
	s_nop 0
	global_load_lds_dwordx4 v5, s[28:29]
	v_mfma_f32_16x16x32_f16 v[76:79], v[124:127], v[104:107], v[76:79]
	v_mfma_f32_16x16x32_f16 v[80:83], v[112:115], v[108:111], v[80:83]
	s_add_u32 m0, s14, 0x14000
	s_nop 0
	global_load_lds_dwordx4 v6, s[30:31]
	v_mfma_f32_16x16x32_f16 v[84:87], v[116:119], v[108:111], v[84:87]
	v_mfma_f32_16x16x32_f16 v[88:91], v[120:123], v[108:111], v[88:91]
	s_add_u32 m0, s14, 0x16000
	s_nop 0
	global_load_lds_dwordx4 v7, s[30:31]
	v_mfma_f32_16x16x32_f16 v[92:95], v[124:127], v[108:111], v[92:95]
	s_waitcnt vmcnt(6) lgkmcnt(0)
	s_barrier
	s_add_u32 s28, s28, 0x80
	s_addc_u32 s29, s29, 0
	s_add_u32 s30, s30, 0x80
	s_addc_u32 s31, s31, 0
	s_waitcnt lgkmcnt(0)
	v_mfma_f32_16x16x32_f16 v[32:35], v[144:147], v[128:131], v[32:35]
	ds_read_b128 v[96:99], v8
	v_mfma_f32_16x16x32_f16 v[36:39], v[148:151], v[128:131], v[36:39]
	ds_read_b128 v[112:115], v9 offset:32768
	v_mfma_f32_16x16x32_f16 v[40:43], v[152:155], v[128:131], v[40:43]
	ds_read_b128 v[116:119], v9 offset:34816
	v_mfma_f32_16x16x32_f16 v[44:47], v[156:159], v[128:131], v[44:47]
	ds_read_b128 v[120:123], v9 offset:36864
	v_mfma_f32_16x16x32_f16 v[48:51], v[144:147], v[132:135], v[48:51]
	ds_read_b128 v[124:127], v9 offset:38912
	v_mfma_f32_16x16x32_f16 v[52:55], v[148:151], v[132:135], v[52:55]
	ds_read_b128 v[100:103], v8 offset:2048
	v_mfma_f32_16x16x32_f16 v[56:59], v[152:155], v[132:135], v[56:59]
	ds_read_b128 v[104:107], v8 offset:4096
	v_mfma_f32_16x16x32_f16 v[60:63], v[156:159], v[132:135], v[60:63]
	ds_read_b128 v[108:111], v8 offset:6144
	v_mfma_f32_16x16x32_f16 v[64:67], v[144:147], v[136:139], v[64:67]
	v_mfma_f32_16x16x32_f16 v[68:71], v[148:151], v[136:139], v[68:71]
	v_mfma_f32_16x16x32_f16 v[72:75], v[152:155], v[136:139], v[72:75]
	s_add_u32 m0, s14, 0x18000
	s_nop 0
	global_load_lds_dwordx4 v2, s[28:29]
	v_mfma_f32_16x16x32_f16 v[76:79], v[156:159], v[136:139], v[76:79]
	v_mfma_f32_16x16x32_f16 v[80:83], v[144:147], v[140:143], v[80:83]
	s_add_u32 m0, s14, 0x1a000
	s_nop 0
	global_load_lds_dwordx4 v3, s[28:29]
	v_mfma_f32_16x16x32_f16 v[84:87], v[148:151], v[140:143], v[84:87]
	v_mfma_f32_16x16x32_f16 v[88:91], v[152:155], v[140:143], v[88:91]
	s_add_u32 m0, s14, 0x1c000
	s_nop 0
	global_load_lds_dwordx4 v4, s[28:29]
	v_mfma_f32_16x16x32_f16 v[92:95], v[156:159], v[140:143], v[92:95]
	s_waitcnt lgkmcnt(0)
	v_mfma_f32_16x16x32_f16 v[32:35], v[112:115], v[96:99], v[32:35]
	ds_read_b128 v[128:131], v10
	v_mfma_f32_16x16x32_f16 v[36:39], v[116:119], v[96:99], v[36:39]
	ds_read_b128 v[144:147], v11 offset:32768
	v_mfma_f32_16x16x32_f16 v[40:43], v[120:123], v[96:99], v[40:43]
	ds_read_b128 v[148:151], v11 offset:34816
	v_mfma_f32_16x16x32_f16 v[44:47], v[124:127], v[96:99], v[44:47]
	ds_read_b128 v[152:155], v11 offset:36864
	v_mfma_f32_16x16x32_f16 v[48:51], v[112:115], v[100:103], v[48:51]
	ds_read_b128 v[156:159], v11 offset:38912
	v_mfma_f32_16x16x32_f16 v[52:55], v[116:119], v[100:103], v[52:55]
	ds_read_b128 v[132:135], v10 offset:2048
	v_mfma_f32_16x16x32_f16 v[56:59], v[120:123], v[100:103], v[56:59]
	ds_read_b128 v[136:139], v10 offset:4096
	v_mfma_f32_16x16x32_f16 v[60:63], v[124:127], v[100:103], v[60:63]
	ds_read_b128 v[140:143], v10 offset:6144
	v_mfma_f32_16x16x32_f16 v[64:67], v[112:115], v[104:107], v[64:67]
	v_mfma_f32_16x16x32_f16 v[68:71], v[116:119], v[104:107], v[68:71]
	v_mfma_f32_16x16x32_f16 v[72:75], v[120:123], v[104:107], v[72:75]
	s_add_u32 m0, s14, 0x1e000
	s_nop 0
	global_load_lds_dwordx4 v5, s[28:29]
	v_mfma_f32_16x16x32_f16 v[76:79], v[124:127], v[104:107], v[76:79]
	v_mfma_f32_16x16x32_f16 v[80:83], v[112:115], v[108:111], v[80:83]
	s_add_u32 m0, s14, 0x20000
	s_nop 0
	global_load_lds_dwordx4 v6, s[30:31]
	v_mfma_f32_16x16x32_f16 v[84:87], v[116:119], v[108:111], v[84:87]
	v_mfma_f32_16x16x32_f16 v[88:91], v[120:123], v[108:111], v[88:91]
	s_add_u32 m0, s14, 0x22000
	s_nop 0
	global_load_lds_dwordx4 v7, s[30:31]
	v_mfma_f32_16x16x32_f16 v[92:95], v[124:127], v[108:111], v[92:95]
	s_waitcnt vmcnt(6) lgkmcnt(0)
	s_barrier
	s_add_u32 s28, s28, 0x80
	s_addc_u32 s29, s29, 0
	s_add_u32 s30, s30, 0x80
	s_addc_u32 s31, s31, 0
	s_waitcnt lgkmcnt(0)
	v_mfma_f32_16x16x32_f16 v[32:35], v[144:147], v[128:131], v[32:35]
	ds_read_b128 v[96:99], v12
	v_mfma_f32_16x16x32_f16 v[36:39], v[148:151], v[128:131], v[36:39]
	ds_read_b128 v[112:115], v13 offset:32768
	v_mfma_f32_16x16x32_f16 v[40:43], v[152:155], v[128:131], v[40:43]
	ds_read_b128 v[116:119], v13 offset:34816
	v_mfma_f32_16x16x32_f16 v[44:47], v[156:159], v[128:131], v[44:47]
	ds_read_b128 v[120:123], v13 offset:36864
	v_mfma_f32_16x16x32_f16 v[48:51], v[144:147], v[132:135], v[48:51]
	ds_read_b128 v[124:127], v13 offset:38912
	v_mfma_f32_16x16x32_f16 v[52:55], v[148:151], v[132:135], v[52:55]
	ds_read_b128 v[100:103], v12 offset:2048
	v_mfma_f32_16x16x32_f16 v[56:59], v[152:155], v[132:135], v[56:59]
	ds_read_b128 v[104:107], v12 offset:4096
	v_mfma_f32_16x16x32_f16 v[60:63], v[156:159], v[132:135], v[60:63]
	ds_read_b128 v[108:111], v12 offset:6144
	v_mfma_f32_16x16x32_f16 v[64:67], v[144:147], v[136:139], v[64:67]
	v_mfma_f32_16x16x32_f16 v[68:71], v[148:151], v[136:139], v[68:71]
	v_mfma_f32_16x16x32_f16 v[72:75], v[152:155], v[136:139], v[72:75]
	s_add_u32 m0, s14, 0x0
	s_nop 0
	global_load_lds_dwordx4 v2, s[28:29]
	v_mfma_f32_16x16x32_f16 v[76:79], v[156:159], v[136:139], v[76:79]
	v_mfma_f32_16x16x32_f16 v[80:83], v[144:147], v[140:143], v[80:83]
	s_add_u32 m0, s14, 0x2000
	s_nop 0
	global_load_lds_dwordx4 v3, s[28:29]
	v_mfma_f32_16x16x32_f16 v[84:87], v[148:151], v[140:143], v[84:87]
	v_mfma_f32_16x16x32_f16 v[88:91], v[152:155], v[140:143], v[88:91]
	s_add_u32 m0, s14, 0x4000
	s_nop 0
	global_load_lds_dwordx4 v4, s[28:29]
	v_mfma_f32_16x16x32_f16 v[92:95], v[156:159], v[140:143], v[92:95]
	s_nop 7
	s_nop 1
	v_mul_f32_e32 v160, s50, v32
	v_mul_f32_e32 v161, s50, v33
	v_mul_f32_e32 v162, s50, v34
	v_mul_f32_e32 v163, s50, v35
	v_mul_f32_e32 v164, s50, v36
	v_mul_f32_e32 v165, s50, v37
	v_mul_f32_e32 v166, s50, v38
	v_mul_f32_e32 v167, s50, v39
	v_mul_f32_e32 v176, 0xbfb8aa3b, v160
	v_mul_f32_e32 v177, 0xbfb8aa3b, v161
	v_mul_f32_e32 v178, 0xbfb8aa3b, v162
	v_mul_f32_e32 v179, 0xbfb8aa3b, v163
	v_mul_f32_e32 v180, 0xbfb8aa3b, v164
	v_mul_f32_e32 v181, 0xbfb8aa3b, v165
	v_mul_f32_e32 v182, 0xbfb8aa3b, v166
	v_mul_f32_e32 v183, 0xbfb8aa3b, v167
	v_exp_f32_e32 v176, v176
	v_exp_f32_e32 v177, v177
	v_exp_f32_e32 v178, v178
	v_exp_f32_e32 v179, v179
	v_exp_f32_e32 v180, v180
	v_exp_f32_e32 v181, v181
	v_exp_f32_e32 v182, v182
	v_exp_f32_e32 v183, v183
	v_add_f32_e32 v176, 1.0, v176
	v_add_f32_e32 v177, 1.0, v177
	v_add_f32_e32 v178, 1.0, v178
	v_add_f32_e32 v179, 1.0, v179
	v_add_f32_e32 v180, 1.0, v180
	v_add_f32_e32 v181, 1.0, v181
	v_add_f32_e32 v182, 1.0, v182
	v_add_f32_e32 v183, 1.0, v183
	v_rcp_f32_e32 v176, v176
	v_rcp_f32_e32 v177, v177
	v_rcp_f32_e32 v178, v178
	v_rcp_f32_e32 v179, v179
	v_rcp_f32_e32 v180, v180
	v_rcp_f32_e32 v181, v181
	v_rcp_f32_e32 v182, v182
	v_rcp_f32_e32 v183, v183
	v_mul_f32_e32 v160, v160, v176
	v_mul_f32_e32 v161, v161, v177
	v_mul_f32_e32 v162, v162, v178
	v_mul_f32_e32 v163, v163, v179
	v_mul_f32_e32 v164, v164, v180
	v_mul_f32_e32 v165, v165, v181
	v_mul_f32_e32 v166, v166, v182
	v_mul_f32_e32 v167, v167, v183
	v_cvt_pk_f16_f32 v168, v160, v161
	v_cvt_pk_f16_f32 v169, v162, v163
	v_cvt_pk_f16_f32 v170, v164, v165
	v_cvt_pk_f16_f32 v171, v166, v167
	global_store_dwordx4 v20, v[168:171], s[32:33]
	v_mul_f32_e32 v160, s50, v40
	v_mul_f32_e32 v161, s50, v41
	v_mul_f32_e32 v162, s50, v42
	v_mul_f32_e32 v163, s50, v43
	v_mul_f32_e32 v164, s50, v44
	v_mul_f32_e32 v165, s50, v45
	v_mul_f32_e32 v166, s50, v46
	v_mul_f32_e32 v167, s50, v47
	v_mul_f32_e32 v176, 0xbfb8aa3b, v160
	v_mul_f32_e32 v177, 0xbfb8aa3b, v161
	v_mul_f32_e32 v178, 0xbfb8aa3b, v162
	v_mul_f32_e32 v179, 0xbfb8aa3b, v163
	v_mul_f32_e32 v180, 0xbfb8aa3b, v164
	v_mul_f32_e32 v181, 0xbfb8aa3b, v165
	v_mul_f32_e32 v182, 0xbfb8aa3b, v166
	v_mul_f32_e32 v183, 0xbfb8aa3b, v167
	v_exp_f32_e32 v176, v176
	v_exp_f32_e32 v177, v177
	v_exp_f32_e32 v178, v178
	v_exp_f32_e32 v179, v179
	v_exp_f32_e32 v180, v180
	v_exp_f32_e32 v181, v181
	v_exp_f32_e32 v182, v182
	v_exp_f32_e32 v183, v183
	v_add_f32_e32 v176, 1.0, v176
	v_add_f32_e32 v177, 1.0, v177
	v_add_f32_e32 v178, 1.0, v178
	v_add_f32_e32 v179, 1.0, v179
	v_add_f32_e32 v180, 1.0, v180
	v_add_f32_e32 v181, 1.0, v181
	v_add_f32_e32 v182, 1.0, v182
	v_add_f32_e32 v183, 1.0, v183
	v_rcp_f32_e32 v176, v176
	v_rcp_f32_e32 v177, v177
	v_rcp_f32_e32 v178, v178
	v_rcp_f32_e32 v179, v179
	v_rcp_f32_e32 v180, v180
	v_rcp_f32_e32 v181, v181
	v_rcp_f32_e32 v182, v182
	v_rcp_f32_e32 v183, v183
	v_mul_f32_e32 v160, v160, v176
	v_mul_f32_e32 v161, v161, v177
	v_mul_f32_e32 v162, v162, v178
	v_mul_f32_e32 v163, v163, v179
	v_mul_f32_e32 v164, v164, v180
	v_mul_f32_e32 v165, v165, v181
	v_mul_f32_e32 v166, v166, v182
	v_mul_f32_e32 v167, v167, v183
	v_cvt_pk_f16_f32 v172, v160, v161
	v_cvt_pk_f16_f32 v173, v162, v163
	v_cvt_pk_f16_f32 v174, v164, v165
	v_cvt_pk_f16_f32 v175, v166, v167
	global_store_dwordx4 v20, v[172:175], s[32:33] offset:64
	v_mul_f32_e32 v160, s50, v48
	v_mul_f32_e32 v161, s50, v49
	v_mul_f32_e32 v162, s50, v50
	v_mul_f32_e32 v163, s50, v51
	v_mul_f32_e32 v164, s50, v52
	v_mul_f32_e32 v165, s50, v53
	v_mul_f32_e32 v166, s50, v54
	v_mul_f32_e32 v167, s50, v55
	v_mul_f32_e32 v176, 0xbfb8aa3b, v160
	v_mul_f32_e32 v177, 0xbfb8aa3b, v161
	v_mul_f32_e32 v178, 0xbfb8aa3b, v162
	v_mul_f32_e32 v179, 0xbfb8aa3b, v163
	v_mul_f32_e32 v180, 0xbfb8aa3b, v164
	v_mul_f32_e32 v181, 0xbfb8aa3b, v165
	v_mul_f32_e32 v182, 0xbfb8aa3b, v166
	v_mul_f32_e32 v183, 0xbfb8aa3b, v167
	v_exp_f32_e32 v176, v176
	v_exp_f32_e32 v177, v177
	v_exp_f32_e32 v178, v178
	v_exp_f32_e32 v179, v179
	v_exp_f32_e32 v180, v180
	v_exp_f32_e32 v181, v181
	v_exp_f32_e32 v182, v182
	v_exp_f32_e32 v183, v183
	v_add_f32_e32 v176, 1.0, v176
	v_add_f32_e32 v177, 1.0, v177
	v_add_f32_e32 v178, 1.0, v178
	v_add_f32_e32 v179, 1.0, v179
	v_add_f32_e32 v180, 1.0, v180
	v_add_f32_e32 v181, 1.0, v181
	v_add_f32_e32 v182, 1.0, v182
	v_add_f32_e32 v183, 1.0, v183
	v_rcp_f32_e32 v176, v176
	v_rcp_f32_e32 v177, v177
	v_rcp_f32_e32 v178, v178
	v_rcp_f32_e32 v179, v179
	v_rcp_f32_e32 v180, v180
	v_rcp_f32_e32 v181, v181
	v_rcp_f32_e32 v182, v182
	v_rcp_f32_e32 v183, v183
	v_mul_f32_e32 v160, v160, v176
	v_mul_f32_e32 v161, v161, v177
	v_mul_f32_e32 v162, v162, v178
	v_mul_f32_e32 v163, v163, v179
	v_mul_f32_e32 v164, v164, v180
	v_mul_f32_e32 v165, v165, v181
	v_mul_f32_e32 v166, v166, v182
	v_mul_f32_e32 v167, v167, v183
	v_cvt_pk_f16_f32 v168, v160, v161
	v_cvt_pk_f16_f32 v169, v162, v163
	v_cvt_pk_f16_f32 v170, v164, v165
	v_cvt_pk_f16_f32 v171, v166, v167
	global_store_dwordx4 v21, v[168:171], s[32:33]
	v_mul_f32_e32 v160, s50, v56
	v_mul_f32_e32 v161, s50, v57
	v_mul_f32_e32 v162, s50, v58
	v_mul_f32_e32 v163, s50, v59
	v_mul_f32_e32 v164, s50, v60
	v_mul_f32_e32 v165, s50, v61
	v_mul_f32_e32 v166, s50, v62
	v_mul_f32_e32 v167, s50, v63
	v_mul_f32_e32 v176, 0xbfb8aa3b, v160
	v_mul_f32_e32 v177, 0xbfb8aa3b, v161
	v_mul_f32_e32 v178, 0xbfb8aa3b, v162
	v_mul_f32_e32 v179, 0xbfb8aa3b, v163
	v_mul_f32_e32 v180, 0xbfb8aa3b, v164
	v_mul_f32_e32 v181, 0xbfb8aa3b, v165
	v_mul_f32_e32 v182, 0xbfb8aa3b, v166
	v_mul_f32_e32 v183, 0xbfb8aa3b, v167
	v_exp_f32_e32 v176, v176
	v_exp_f32_e32 v177, v177
	v_exp_f32_e32 v178, v178
	v_exp_f32_e32 v179, v179
	v_exp_f32_e32 v180, v180
	v_exp_f32_e32 v181, v181
	v_exp_f32_e32 v182, v182
	v_exp_f32_e32 v183, v183
	v_add_f32_e32 v176, 1.0, v176
	v_add_f32_e32 v177, 1.0, v177
	v_add_f32_e32 v178, 1.0, v178
	v_add_f32_e32 v179, 1.0, v179
	v_add_f32_e32 v180, 1.0, v180
	v_add_f32_e32 v181, 1.0, v181
	v_add_f32_e32 v182, 1.0, v182
	v_add_f32_e32 v183, 1.0, v183
	v_rcp_f32_e32 v176, v176
	v_rcp_f32_e32 v177, v177
	v_rcp_f32_e32 v178, v178
	v_rcp_f32_e32 v179, v179
	v_rcp_f32_e32 v180, v180
	v_rcp_f32_e32 v181, v181
	v_rcp_f32_e32 v182, v182
	v_rcp_f32_e32 v183, v183
	v_mul_f32_e32 v160, v160, v176
	v_mul_f32_e32 v161, v161, v177
	v_mul_f32_e32 v162, v162, v178
	v_mul_f32_e32 v163, v163, v179
	v_mul_f32_e32 v164, v164, v180
	v_mul_f32_e32 v165, v165, v181
	v_mul_f32_e32 v166, v166, v182
	v_mul_f32_e32 v167, v167, v183
	v_cvt_pk_f16_f32 v172, v160, v161
	v_cvt_pk_f16_f32 v173, v162, v163
	v_cvt_pk_f16_f32 v174, v164, v165
	v_cvt_pk_f16_f32 v175, v166, v167
	global_store_dwordx4 v21, v[172:175], s[32:33] offset:64
	v_mul_f32_e32 v160, s50, v64
	v_mul_f32_e32 v161, s50, v65
	v_mul_f32_e32 v162, s50, v66
	v_mul_f32_e32 v163, s50, v67
	v_mul_f32_e32 v164, s50, v68
	v_mul_f32_e32 v165, s50, v69
	v_mul_f32_e32 v166, s50, v70
	v_mul_f32_e32 v167, s50, v71
	v_mul_f32_e32 v176, 0xbfb8aa3b, v160
	v_mul_f32_e32 v177, 0xbfb8aa3b, v161
	v_mul_f32_e32 v178, 0xbfb8aa3b, v162
	v_mul_f32_e32 v179, 0xbfb8aa3b, v163
	v_mul_f32_e32 v180, 0xbfb8aa3b, v164
	v_mul_f32_e32 v181, 0xbfb8aa3b, v165
	v_mul_f32_e32 v182, 0xbfb8aa3b, v166
	v_mul_f32_e32 v183, 0xbfb8aa3b, v167
	v_exp_f32_e32 v176, v176
	v_exp_f32_e32 v177, v177
	v_exp_f32_e32 v178, v178
	v_exp_f32_e32 v179, v179
	v_exp_f32_e32 v180, v180
	v_exp_f32_e32 v181, v181
	v_exp_f32_e32 v182, v182
	v_exp_f32_e32 v183, v183
	v_add_f32_e32 v176, 1.0, v176
	v_add_f32_e32 v177, 1.0, v177
	v_add_f32_e32 v178, 1.0, v178
	v_add_f32_e32 v179, 1.0, v179
	v_add_f32_e32 v180, 1.0, v180
	v_add_f32_e32 v181, 1.0, v181
	v_add_f32_e32 v182, 1.0, v182
	v_add_f32_e32 v183, 1.0, v183
	v_rcp_f32_e32 v176, v176
	v_rcp_f32_e32 v177, v177
	v_rcp_f32_e32 v178, v178
	v_rcp_f32_e32 v179, v179
	v_rcp_f32_e32 v180, v180
	v_rcp_f32_e32 v181, v181
	v_rcp_f32_e32 v182, v182
	v_rcp_f32_e32 v183, v183
	v_mul_f32_e32 v160, v160, v176
	v_mul_f32_e32 v161, v161, v177
	v_mul_f32_e32 v162, v162, v178
	v_mul_f32_e32 v163, v163, v179
	v_mul_f32_e32 v164, v164, v180
	v_mul_f32_e32 v165, v165, v181
	v_mul_f32_e32 v166, v166, v182
	v_mul_f32_e32 v167, v167, v183
	v_cvt_pk_f16_f32 v168, v160, v161
	v_cvt_pk_f16_f32 v169, v162, v163
	v_cvt_pk_f16_f32 v170, v164, v165
	v_cvt_pk_f16_f32 v171, v166, v167
	global_store_dwordx4 v22, v[168:171], s[32:33]
	v_mul_f32_e32 v160, s50, v72
	v_mul_f32_e32 v161, s50, v73
	v_mul_f32_e32 v162, s50, v74
	v_mul_f32_e32 v163, s50, v75
	v_mul_f32_e32 v164, s50, v76
	v_mul_f32_e32 v165, s50, v77
	v_mul_f32_e32 v166, s50, v78
	v_mul_f32_e32 v167, s50, v79
	v_mul_f32_e32 v176, 0xbfb8aa3b, v160
	v_mul_f32_e32 v177, 0xbfb8aa3b, v161
	v_mul_f32_e32 v178, 0xbfb8aa3b, v162
	v_mul_f32_e32 v179, 0xbfb8aa3b, v163
	v_mul_f32_e32 v180, 0xbfb8aa3b, v164
	v_mul_f32_e32 v181, 0xbfb8aa3b, v165
	v_mul_f32_e32 v182, 0xbfb8aa3b, v166
	v_mul_f32_e32 v183, 0xbfb8aa3b, v167
	v_exp_f32_e32 v176, v176
	v_exp_f32_e32 v177, v177
	v_exp_f32_e32 v178, v178
	v_exp_f32_e32 v179, v179
	v_exp_f32_e32 v180, v180
	v_exp_f32_e32 v181, v181
	v_exp_f32_e32 v182, v182
	v_exp_f32_e32 v183, v183
	v_add_f32_e32 v176, 1.0, v176
	v_add_f32_e32 v177, 1.0, v177
	v_add_f32_e32 v178, 1.0, v178
	v_add_f32_e32 v179, 1.0, v179
	v_add_f32_e32 v180, 1.0, v180
	v_add_f32_e32 v181, 1.0, v181
	v_add_f32_e32 v182, 1.0, v182
	v_add_f32_e32 v183, 1.0, v183
	v_rcp_f32_e32 v176, v176
	v_rcp_f32_e32 v177, v177
	v_rcp_f32_e32 v178, v178
	v_rcp_f32_e32 v179, v179
	v_rcp_f32_e32 v180, v180
	v_rcp_f32_e32 v181, v181
	v_rcp_f32_e32 v182, v182
	v_rcp_f32_e32 v183, v183
	v_mul_f32_e32 v160, v160, v176
	v_mul_f32_e32 v161, v161, v177
	v_mul_f32_e32 v162, v162, v178
	v_mul_f32_e32 v163, v163, v179
	v_mul_f32_e32 v164, v164, v180
	v_mul_f32_e32 v165, v165, v181
	v_mul_f32_e32 v166, v166, v182
	v_mul_f32_e32 v167, v167, v183
	v_cvt_pk_f16_f32 v172, v160, v161
	v_cvt_pk_f16_f32 v173, v162, v163
	v_cvt_pk_f16_f32 v174, v164, v165
	v_cvt_pk_f16_f32 v175, v166, v167
	global_store_dwordx4 v22, v[172:175], s[32:33] offset:64
	v_mul_f32_e32 v160, s50, v80
	v_mul_f32_e32 v161, s50, v81
	v_mul_f32_e32 v162, s50, v82
	v_mul_f32_e32 v163, s50, v83
	v_mul_f32_e32 v164, s50, v84
	v_mul_f32_e32 v165, s50, v85
	v_mul_f32_e32 v166, s50, v86
	v_mul_f32_e32 v167, s50, v87
	v_mul_f32_e32 v176, 0xbfb8aa3b, v160
	v_mul_f32_e32 v177, 0xbfb8aa3b, v161
	v_mul_f32_e32 v178, 0xbfb8aa3b, v162
	v_mul_f32_e32 v179, 0xbfb8aa3b, v163
	v_mul_f32_e32 v180, 0xbfb8aa3b, v164
	v_mul_f32_e32 v181, 0xbfb8aa3b, v165
	v_mul_f32_e32 v182, 0xbfb8aa3b, v166
	v_mul_f32_e32 v183, 0xbfb8aa3b, v167
	v_exp_f32_e32 v176, v176
	v_exp_f32_e32 v177, v177
	v_exp_f32_e32 v178, v178
	v_exp_f32_e32 v179, v179
	v_exp_f32_e32 v180, v180
	v_exp_f32_e32 v181, v181
	v_exp_f32_e32 v182, v182
	v_exp_f32_e32 v183, v183
	v_add_f32_e32 v176, 1.0, v176
	v_add_f32_e32 v177, 1.0, v177
	v_add_f32_e32 v178, 1.0, v178
	v_add_f32_e32 v179, 1.0, v179
	v_add_f32_e32 v180, 1.0, v180
	v_add_f32_e32 v181, 1.0, v181
	v_add_f32_e32 v182, 1.0, v182
	v_add_f32_e32 v183, 1.0, v183
	v_rcp_f32_e32 v176, v176
	v_rcp_f32_e32 v177, v177
	v_rcp_f32_e32 v178, v178
	v_rcp_f32_e32 v179, v179
	v_rcp_f32_e32 v180, v180
	v_rcp_f32_e32 v181, v181
	v_rcp_f32_e32 v182, v182
	v_rcp_f32_e32 v183, v183
	v_mul_f32_e32 v160, v160, v176
	v_mul_f32_e32 v161, v161, v177
	v_mul_f32_e32 v162, v162, v178
	v_mul_f32_e32 v163, v163, v179
	v_mul_f32_e32 v164, v164, v180
	v_mul_f32_e32 v165, v165, v181
	v_mul_f32_e32 v166, v166, v182
	v_mul_f32_e32 v167, v167, v183
	v_cvt_pk_f16_f32 v168, v160, v161
	v_cvt_pk_f16_f32 v169, v162, v163
	v_cvt_pk_f16_f32 v170, v164, v165
	v_cvt_pk_f16_f32 v171, v166, v167
	global_store_dwordx4 v23, v[168:171], s[32:33]
	v_mul_f32_e32 v160, s50, v88
	v_mul_f32_e32 v161, s50, v89
	v_mul_f32_e32 v162, s50, v90
	v_mul_f32_e32 v163, s50, v91
	v_mul_f32_e32 v164, s50, v92
	v_mul_f32_e32 v165, s50, v93
	v_mul_f32_e32 v166, s50, v94
	v_mul_f32_e32 v167, s50, v95
	v_mul_f32_e32 v176, 0xbfb8aa3b, v160
	v_mul_f32_e32 v177, 0xbfb8aa3b, v161
	v_mul_f32_e32 v178, 0xbfb8aa3b, v162
	v_mul_f32_e32 v179, 0xbfb8aa3b, v163
	v_mul_f32_e32 v180, 0xbfb8aa3b, v164
	v_mul_f32_e32 v181, 0xbfb8aa3b, v165
	v_mul_f32_e32 v182, 0xbfb8aa3b, v166
	v_mul_f32_e32 v183, 0xbfb8aa3b, v167
	v_exp_f32_e32 v176, v176
	v_exp_f32_e32 v177, v177
	v_exp_f32_e32 v178, v178
	v_exp_f32_e32 v179, v179
	v_exp_f32_e32 v180, v180
	v_exp_f32_e32 v181, v181
	v_exp_f32_e32 v182, v182
	v_exp_f32_e32 v183, v183
	v_add_f32_e32 v176, 1.0, v176
	v_add_f32_e32 v177, 1.0, v177
	v_add_f32_e32 v178, 1.0, v178
	v_add_f32_e32 v179, 1.0, v179
	v_add_f32_e32 v180, 1.0, v180
	v_add_f32_e32 v181, 1.0, v181
	v_add_f32_e32 v182, 1.0, v182
	v_add_f32_e32 v183, 1.0, v183
	v_rcp_f32_e32 v176, v176
	v_rcp_f32_e32 v177, v177
	v_rcp_f32_e32 v178, v178
	v_rcp_f32_e32 v179, v179
	v_rcp_f32_e32 v180, v180
	v_rcp_f32_e32 v181, v181
	v_rcp_f32_e32 v182, v182
	v_rcp_f32_e32 v183, v183
	v_mul_f32_e32 v160, v160, v176
	v_mul_f32_e32 v161, v161, v177
	v_mul_f32_e32 v162, v162, v178
	v_mul_f32_e32 v163, v163, v179
	v_mul_f32_e32 v164, v164, v180
	v_mul_f32_e32 v165, v165, v181
	v_mul_f32_e32 v166, v166, v182
	v_mul_f32_e32 v167, v167, v183
	v_cvt_pk_f16_f32 v172, v160, v161
	v_cvt_pk_f16_f32 v173, v162, v163
	v_cvt_pk_f16_f32 v174, v164, v165
	v_cvt_pk_f16_f32 v175, v166, v167
	global_store_dwordx4 v23, v[172:175], s[32:33] offset:64
	s_waitcnt lgkmcnt(0)
	v_mfma_f32_16x16x32_f16 v[32:35], v[112:115], v[96:99], 0
	ds_read_b128 v[128:131], v14
	v_mfma_f32_16x16x32_f16 v[36:39], v[116:119], v[96:99], 0
	ds_read_b128 v[144:147], v15 offset:32768
	v_mfma_f32_16x16x32_f16 v[40:43], v[120:123], v[96:99], 0
	ds_read_b128 v[148:151], v15 offset:34816
	v_mfma_f32_16x16x32_f16 v[44:47], v[124:127], v[96:99], 0
	ds_read_b128 v[152:155], v15 offset:36864
	v_mfma_f32_16x16x32_f16 v[48:51], v[112:115], v[100:103], 0
	ds_read_b128 v[156:159], v15 offset:38912
	v_mfma_f32_16x16x32_f16 v[52:55], v[116:119], v[100:103], 0
	ds_read_b128 v[132:135], v14 offset:2048
	v_mfma_f32_16x16x32_f16 v[56:59], v[120:123], v[100:103], 0
	ds_read_b128 v[136:139], v14 offset:4096
	v_mfma_f32_16x16x32_f16 v[60:63], v[124:127], v[100:103], 0
	ds_read_b128 v[140:143], v14 offset:6144
	v_mfma_f32_16x16x32_f16 v[64:67], v[112:115], v[104:107], 0
	v_mfma_f32_16x16x32_f16 v[68:71], v[116:119], v[104:107], 0
	v_mfma_f32_16x16x32_f16 v[72:75], v[120:123], v[104:107], 0
	s_add_u32 m0, s14, 0x6000
	s_nop 0
	global_load_lds_dwordx4 v5, s[28:29]
	v_mfma_f32_16x16x32_f16 v[76:79], v[124:127], v[104:107], 0
	v_mfma_f32_16x16x32_f16 v[80:83], v[112:115], v[108:111], 0
	s_add_u32 m0, s14, 0x8000
	s_nop 0
	global_load_lds_dwordx4 v6, s[30:31]
	v_mfma_f32_16x16x32_f16 v[84:87], v[116:119], v[108:111], 0
	v_mfma_f32_16x16x32_f16 v[88:91], v[120:123], v[108:111], 0
	s_add_u32 m0, s14, 0xa000
	s_nop 0
	global_load_lds_dwordx4 v7, s[30:31]
	v_mfma_f32_16x16x32_f16 v[92:95], v[124:127], v[108:111], 0
	s_waitcnt vmcnt(14) lgkmcnt(0)
	s_barrier
	s_add_u32 s28, s28, 0x80
	s_addc_u32 s29, s29, 0
	s_add_u32 s30, s30, 0x80
	s_addc_u32 s31, s31, 0
	s_waitcnt lgkmcnt(0)
	v_mfma_f32_16x16x32_f16 v[32:35], v[144:147], v[128:131], v[32:35]
	ds_read_b128 v[96:99], v16
	v_mfma_f32_16x16x32_f16 v[36:39], v[148:151], v[128:131], v[36:39]
	ds_read_b128 v[112:115], v17 offset:32768
	v_mfma_f32_16x16x32_f16 v[40:43], v[152:155], v[128:131], v[40:43]
	ds_read_b128 v[116:119], v17 offset:34816
	v_mfma_f32_16x16x32_f16 v[44:47], v[156:159], v[128:131], v[44:47]
	ds_read_b128 v[120:123], v17 offset:36864
	v_mfma_f32_16x16x32_f16 v[48:51], v[144:147], v[132:135], v[48:51]
	ds_read_b128 v[124:127], v17 offset:38912
	v_mfma_f32_16x16x32_f16 v[52:55], v[148:151], v[132:135], v[52:55]
	ds_read_b128 v[100:103], v16 offset:2048
	v_mfma_f32_16x16x32_f16 v[56:59], v[152:155], v[132:135], v[56:59]
	ds_read_b128 v[104:107], v16 offset:4096
	v_mfma_f32_16x16x32_f16 v[60:63], v[156:159], v[132:135], v[60:63]
	ds_read_b128 v[108:111], v16 offset:6144
	v_mfma_f32_16x16x32_f16 v[64:67], v[144:147], v[136:139], v[64:67]
	v_mfma_f32_16x16x32_f16 v[68:71], v[148:151], v[136:139], v[68:71]
	v_mfma_f32_16x16x32_f16 v[72:75], v[152:155], v[136:139], v[72:75]
	s_add_u32 m0, s14, 0xc000
	s_nop 0
	global_load_lds_dwordx4 v2, s[28:29]
	v_mfma_f32_16x16x32_f16 v[76:79], v[156:159], v[136:139], v[76:79]
	v_mfma_f32_16x16x32_f16 v[80:83], v[144:147], v[140:143], v[80:83]
	s_add_u32 m0, s14, 0xe000
	s_nop 0
	global_load_lds_dwordx4 v3, s[28:29]
	v_mfma_f32_16x16x32_f16 v[84:87], v[148:151], v[140:143], v[84:87]
	v_mfma_f32_16x16x32_f16 v[88:91], v[152:155], v[140:143], v[88:91]
	s_add_u32 m0, s14, 0x10000
	s_nop 0
	global_load_lds_dwordx4 v4, s[28:29]
	v_mfma_f32_16x16x32_f16 v[92:95], v[156:159], v[140:143], v[92:95]
	s_waitcnt lgkmcnt(0)
	v_mfma_f32_16x16x32_f16 v[32:35], v[112:115], v[96:99], v[32:35]
	ds_read_b128 v[128:131], v18
	v_mfma_f32_16x16x32_f16 v[36:39], v[116:119], v[96:99], v[36:39]
	ds_read_b128 v[144:147], v19 offset:32768
	v_mfma_f32_16x16x32_f16 v[40:43], v[120:123], v[96:99], v[40:43]
	ds_read_b128 v[148:151], v19 offset:34816
	v_mfma_f32_16x16x32_f16 v[44:47], v[124:127], v[96:99], v[44:47]
	ds_read_b128 v[152:155], v19 offset:36864
	v_mfma_f32_16x16x32_f16 v[48:51], v[112:115], v[100:103], v[48:51]
	ds_read_b128 v[156:159], v19 offset:38912
	v_mfma_f32_16x16x32_f16 v[52:55], v[116:119], v[100:103], v[52:55]
	ds_read_b128 v[132:135], v18 offset:2048
	v_mfma_f32_16x16x32_f16 v[56:59], v[120:123], v[100:103], v[56:59]
	ds_read_b128 v[136:139], v18 offset:4096
	v_mfma_f32_16x16x32_f16 v[60:63], v[124:127], v[100:103], v[60:63]
	ds_read_b128 v[140:143], v18 offset:6144
	v_mfma_f32_16x16x32_f16 v[64:67], v[112:115], v[104:107], v[64:67]
	v_mfma_f32_16x16x32_f16 v[68:71], v[116:119], v[104:107], v[68:71]
	v_mfma_f32_16x16x32_f16 v[72:75], v[120:123], v[104:107], v[72:75]
	s_add_u32 m0, s14, 0x12000
	s_nop 0
	global_load_lds_dwordx4 v5, s[28:29]
	v_mfma_f32_16x16x32_f16 v[76:79], v[124:127], v[104:107], v[76:79]
	v_mfma_f32_16x16x32_f16 v[80:83], v[112:115], v[108:111], v[80:83]
	s_add_u32 m0, s14, 0x14000
	s_nop 0
	global_load_lds_dwordx4 v6, s[30:31]
	v_mfma_f32_16x16x32_f16 v[84:87], v[116:119], v[108:111], v[84:87]
	v_mfma_f32_16x16x32_f16 v[88:91], v[120:123], v[108:111], v[88:91]
	s_add_u32 m0, s14, 0x16000
	s_nop 0
	global_load_lds_dwordx4 v7, s[30:31]
	v_mfma_f32_16x16x32_f16 v[92:95], v[124:127], v[108:111], v[92:95]
	s_waitcnt vmcnt(6) lgkmcnt(0)
	s_barrier
	s_add_u32 s28, s28, 0x80
	s_addc_u32 s29, s29, 0
	s_add_u32 s30, s30, 0x80
	s_addc_u32 s31, s31, 0
	s_waitcnt lgkmcnt(0)
	v_mfma_f32_16x16x32_f16 v[32:35], v[144:147], v[128:131], v[32:35]
	ds_read_b128 v[96:99], v8
	v_mfma_f32_16x16x32_f16 v[36:39], v[148:151], v[128:131], v[36:39]
	ds_read_b128 v[112:115], v9 offset:32768
	v_mfma_f32_16x16x32_f16 v[40:43], v[152:155], v[128:131], v[40:43]
	ds_read_b128 v[116:119], v9 offset:34816
	v_mfma_f32_16x16x32_f16 v[44:47], v[156:159], v[128:131], v[44:47]
	ds_read_b128 v[120:123], v9 offset:36864
	v_mfma_f32_16x16x32_f16 v[48:51], v[144:147], v[132:135], v[48:51]
	ds_read_b128 v[124:127], v9 offset:38912
	v_mfma_f32_16x16x32_f16 v[52:55], v[148:151], v[132:135], v[52:55]
	ds_read_b128 v[100:103], v8 offset:2048
	v_mfma_f32_16x16x32_f16 v[56:59], v[152:155], v[132:135], v[56:59]
	ds_read_b128 v[104:107], v8 offset:4096
	v_mfma_f32_16x16x32_f16 v[60:63], v[156:159], v[132:135], v[60:63]
	ds_read_b128 v[108:111], v8 offset:6144
	v_mfma_f32_16x16x32_f16 v[64:67], v[144:147], v[136:139], v[64:67]
	v_mfma_f32_16x16x32_f16 v[68:71], v[148:151], v[136:139], v[68:71]
	v_mfma_f32_16x16x32_f16 v[72:75], v[152:155], v[136:139], v[72:75]
	s_add_u32 m0, s14, 0x18000
	s_nop 0
	global_load_lds_dwordx4 v2, s[28:29]
	v_mfma_f32_16x16x32_f16 v[76:79], v[156:159], v[136:139], v[76:79]
	v_mfma_f32_16x16x32_f16 v[80:83], v[144:147], v[140:143], v[80:83]
	s_add_u32 m0, s14, 0x1a000
	s_nop 0
	global_load_lds_dwordx4 v3, s[28:29]
	v_mfma_f32_16x16x32_f16 v[84:87], v[148:151], v[140:143], v[84:87]
	v_mfma_f32_16x16x32_f16 v[88:91], v[152:155], v[140:143], v[88:91]
	s_add_u32 m0, s14, 0x1c000
	s_nop 0
	global_load_lds_dwordx4 v4, s[28:29]
	v_mfma_f32_16x16x32_f16 v[92:95], v[156:159], v[140:143], v[92:95]
	s_waitcnt lgkmcnt(0)
	v_mfma_f32_16x16x32_f16 v[32:35], v[112:115], v[96:99], v[32:35]
	ds_read_b128 v[128:131], v10
	v_mfma_f32_16x16x32_f16 v[36:39], v[116:119], v[96:99], v[36:39]
	ds_read_b128 v[144:147], v11 offset:32768
	v_mfma_f32_16x16x32_f16 v[40:43], v[120:123], v[96:99], v[40:43]
	ds_read_b128 v[148:151], v11 offset:34816
	v_mfma_f32_16x16x32_f16 v[44:47], v[124:127], v[96:99], v[44:47]
	ds_read_b128 v[152:155], v11 offset:36864
	v_mfma_f32_16x16x32_f16 v[48:51], v[112:115], v[100:103], v[48:51]
	ds_read_b128 v[156:159], v11 offset:38912
	v_mfma_f32_16x16x32_f16 v[52:55], v[116:119], v[100:103], v[52:55]
	ds_read_b128 v[132:135], v10 offset:2048
	v_mfma_f32_16x16x32_f16 v[56:59], v[120:123], v[100:103], v[56:59]
	ds_read_b128 v[136:139], v10 offset:4096
	v_mfma_f32_16x16x32_f16 v[60:63], v[124:127], v[100:103], v[60:63]
	ds_read_b128 v[140:143], v10 offset:6144
	v_mfma_f32_16x16x32_f16 v[64:67], v[112:115], v[104:107], v[64:67]
	v_mfma_f32_16x16x32_f16 v[68:71], v[116:119], v[104:107], v[68:71]
	v_mfma_f32_16x16x32_f16 v[72:75], v[120:123], v[104:107], v[72:75]
	s_add_u32 m0, s14, 0x1e000
	s_nop 0
	global_load_lds_dwordx4 v5, s[28:29]
	v_mfma_f32_16x16x32_f16 v[76:79], v[124:127], v[104:107], v[76:79]
	v_mfma_f32_16x16x32_f16 v[80:83], v[112:115], v[108:111], v[80:83]
	s_add_u32 m0, s14, 0x20000
	s_nop 0
	global_load_lds_dwordx4 v6, s[30:31]
	v_mfma_f32_16x16x32_f16 v[84:87], v[116:119], v[108:111], v[84:87]
	v_mfma_f32_16x16x32_f16 v[88:91], v[120:123], v[108:111], v[88:91]
	s_add_u32 m0, s14, 0x22000
	s_nop 0
	global_load_lds_dwordx4 v7, s[30:31]
	v_mfma_f32_16x16x32_f16 v[92:95], v[124:127], v[108:111], v[92:95]
	s_waitcnt vmcnt(6) lgkmcnt(0)
	s_barrier
	s_add_u32 s28, s28, 0x80
	s_addc_u32 s29, s29, 0
	s_add_u32 s30, s30, 0x80
	s_addc_u32 s31, s31, 0
	s_waitcnt lgkmcnt(0)
	v_mfma_f32_16x16x32_f16 v[32:35], v[144:147], v[128:131], v[32:35]
	ds_read_b128 v[96:99], v12
	v_mfma_f32_16x16x32_f16 v[36:39], v[148:151], v[128:131], v[36:39]
	ds_read_b128 v[112:115], v13 offset:32768
	v_mfma_f32_16x16x32_f16 v[40:43], v[152:155], v[128:131], v[40:43]
	ds_read_b128 v[116:119], v13 offset:34816
	v_mfma_f32_16x16x32_f16 v[44:47], v[156:159], v[128:131], v[44:47]
	ds_read_b128 v[120:123], v13 offset:36864
	v_mfma_f32_16x16x32_f16 v[48:51], v[144:147], v[132:135], v[48:51]
	ds_read_b128 v[124:127], v13 offset:38912
	v_mfma_f32_16x16x32_f16 v[52:55], v[148:151], v[132:135], v[52:55]
	ds_read_b128 v[100:103], v12 offset:2048
	v_mfma_f32_16x16x32_f16 v[56:59], v[152:155], v[132:135], v[56:59]
	ds_read_b128 v[104:107], v12 offset:4096
	v_mfma_f32_16x16x32_f16 v[60:63], v[156:159], v[132:135], v[60:63]
	ds_read_b128 v[108:111], v12 offset:6144
	v_mfma_f32_16x16x32_f16 v[64:67], v[144:147], v[136:139], v[64:67]
	v_mfma_f32_16x16x32_f16 v[68:71], v[148:151], v[136:139], v[68:71]
	v_mfma_f32_16x16x32_f16 v[72:75], v[152:155], v[136:139], v[72:75]
	s_add_u32 m0, s14, 0x0
	s_nop 0
	global_load_lds_dwordx4 v2, s[28:29]
	v_mfma_f32_16x16x32_f16 v[76:79], v[156:159], v[136:139], v[76:79]
	v_mfma_f32_16x16x32_f16 v[80:83], v[144:147], v[140:143], v[80:83]
	s_add_u32 m0, s14, 0x2000
	s_nop 0
	global_load_lds_dwordx4 v3, s[28:29]
	v_mfma_f32_16x16x32_f16 v[84:87], v[148:151], v[140:143], v[84:87]
	v_mfma_f32_16x16x32_f16 v[88:91], v[152:155], v[140:143], v[88:91]
	s_add_u32 m0, s14, 0x4000
	s_nop 0
	global_load_lds_dwordx4 v4, s[28:29]
	v_mfma_f32_16x16x32_f16 v[92:95], v[156:159], v[140:143], v[92:95]
	s_waitcnt lgkmcnt(0)
	v_mfma_f32_16x16x32_f16 v[32:35], v[112:115], v[96:99], v[32:35]
	ds_read_b128 v[128:131], v14
	v_mfma_f32_16x16x32_f16 v[36:39], v[116:119], v[96:99], v[36:39]
	ds_read_b128 v[144:147], v15 offset:32768
	v_mfma_f32_16x16x32_f16 v[40:43], v[120:123], v[96:99], v[40:43]
	ds_read_b128 v[148:151], v15 offset:34816
	v_mfma_f32_16x16x32_f16 v[44:47], v[124:127], v[96:99], v[44:47]
	ds_read_b128 v[152:155], v15 offset:36864
	v_mfma_f32_16x16x32_f16 v[48:51], v[112:115], v[100:103], v[48:51]
	ds_read_b128 v[156:159], v15 offset:38912
	v_mfma_f32_16x16x32_f16 v[52:55], v[116:119], v[100:103], v[52:55]
	ds_read_b128 v[132:135], v14 offset:2048
	v_mfma_f32_16x16x32_f16 v[56:59], v[120:123], v[100:103], v[56:59]
	ds_read_b128 v[136:139], v14 offset:4096
	v_mfma_f32_16x16x32_f16 v[60:63], v[124:127], v[100:103], v[60:63]
	ds_read_b128 v[140:143], v14 offset:6144
	v_mfma_f32_16x16x32_f16 v[64:67], v[112:115], v[104:107], v[64:67]
	v_mfma_f32_16x16x32_f16 v[68:71], v[116:119], v[104:107], v[68:71]
	v_mfma_f32_16x16x32_f16 v[72:75], v[120:123], v[104:107], v[72:75]
	s_add_u32 m0, s14, 0x6000
	s_nop 0
	global_load_lds_dwordx4 v5, s[28:29]
	v_mfma_f32_16x16x32_f16 v[76:79], v[124:127], v[104:107], v[76:79]
	v_mfma_f32_16x16x32_f16 v[80:83], v[112:115], v[108:111], v[80:83]
	s_add_u32 m0, s14, 0x8000
	s_nop 0
	global_load_lds_dwordx4 v6, s[30:31]
	v_mfma_f32_16x16x32_f16 v[84:87], v[116:119], v[108:111], v[84:87]
	v_mfma_f32_16x16x32_f16 v[88:91], v[120:123], v[108:111], v[88:91]
	s_add_u32 m0, s14, 0xa000
	s_nop 0
	global_load_lds_dwordx4 v7, s[30:31]
	v_mfma_f32_16x16x32_f16 v[92:95], v[124:127], v[108:111], v[92:95]
	s_waitcnt vmcnt(6) lgkmcnt(0)
	s_barrier
	s_add_u32 s28, s28, 0x80
	s_addc_u32 s29, s29, 0
	s_add_u32 s30, s30, 0x80
	s_addc_u32 s31, s31, 0
	s_waitcnt lgkmcnt(0)
	v_mfma_f32_16x16x32_f16 v[32:35], v[144:147], v[128:131], v[32:35]
	ds_read_b128 v[96:99], v16
	v_mfma_f32_16x16x32_f16 v[36:39], v[148:151], v[128:131], v[36:39]
	ds_read_b128 v[112:115], v17 offset:32768
	v_mfma_f32_16x16x32_f16 v[40:43], v[152:155], v[128:131], v[40:43]
	ds_read_b128 v[116:119], v17 offset:34816
	v_mfma_f32_16x16x32_f16 v[44:47], v[156:159], v[128:131], v[44:47]
	ds_read_b128 v[120:123], v17 offset:36864
	v_mfma_f32_16x16x32_f16 v[48:51], v[144:147], v[132:135], v[48:51]
	ds_read_b128 v[124:127], v17 offset:38912
	v_mfma_f32_16x16x32_f16 v[52:55], v[148:151], v[132:135], v[52:55]
	ds_read_b128 v[100:103], v16 offset:2048
	v_mfma_f32_16x16x32_f16 v[56:59], v[152:155], v[132:135], v[56:59]
	ds_read_b128 v[104:107], v16 offset:4096
	v_mfma_f32_16x16x32_f16 v[60:63], v[156:159], v[132:135], v[60:63]
	ds_read_b128 v[108:111], v16 offset:6144
	v_mfma_f32_16x16x32_f16 v[64:67], v[144:147], v[136:139], v[64:67]
	v_mfma_f32_16x16x32_f16 v[68:71], v[148:151], v[136:139], v[68:71]
	v_mfma_f32_16x16x32_f16 v[72:75], v[152:155], v[136:139], v[72:75]
	s_add_u32 m0, s14, 0xc000
	s_nop 0
	global_load_lds_dwordx4 v2, s[28:29]
	v_mfma_f32_16x16x32_f16 v[76:79], v[156:159], v[136:139], v[76:79]
	v_mfma_f32_16x16x32_f16 v[80:83], v[144:147], v[140:143], v[80:83]
	s_add_u32 m0, s14, 0xe000
	s_nop 0
	global_load_lds_dwordx4 v3, s[28:29]
	v_mfma_f32_16x16x32_f16 v[84:87], v[148:151], v[140:143], v[84:87]
	v_mfma_f32_16x16x32_f16 v[88:91], v[152:155], v[140:143], v[88:91]
	s_add_u32 m0, s14, 0x10000
	s_nop 0
	global_load_lds_dwordx4 v4, s[28:29]
	v_mfma_f32_16x16x32_f16 v[92:95], v[156:159], v[140:143], v[92:95]
	s_waitcnt lgkmcnt(0)
	v_mfma_f32_16x16x32_f16 v[32:35], v[112:115], v[96:99], v[32:35]
	ds_read_b128 v[128:131], v18
	v_mfma_f32_16x16x32_f16 v[36:39], v[116:119], v[96:99], v[36:39]
	ds_read_b128 v[144:147], v19 offset:32768
	v_mfma_f32_16x16x32_f16 v[40:43], v[120:123], v[96:99], v[40:43]
	ds_read_b128 v[148:151], v19 offset:34816
	v_mfma_f32_16x16x32_f16 v[44:47], v[124:127], v[96:99], v[44:47]
	ds_read_b128 v[152:155], v19 offset:36864
	v_mfma_f32_16x16x32_f16 v[48:51], v[112:115], v[100:103], v[48:51]
	ds_read_b128 v[156:159], v19 offset:38912
	v_mfma_f32_16x16x32_f16 v[52:55], v[116:119], v[100:103], v[52:55]
	ds_read_b128 v[132:135], v18 offset:2048
	v_mfma_f32_16x16x32_f16 v[56:59], v[120:123], v[100:103], v[56:59]
	ds_read_b128 v[136:139], v18 offset:4096
	v_mfma_f32_16x16x32_f16 v[60:63], v[124:127], v[100:103], v[60:63]
	ds_read_b128 v[140:143], v18 offset:6144
	v_mfma_f32_16x16x32_f16 v[64:67], v[112:115], v[104:107], v[64:67]
	v_mfma_f32_16x16x32_f16 v[68:71], v[116:119], v[104:107], v[68:71]
	v_mfma_f32_16x16x32_f16 v[72:75], v[120:123], v[104:107], v[72:75]
	s_add_u32 m0, s14, 0x12000
	s_nop 0
	global_load_lds_dwordx4 v5, s[28:29]
	v_mfma_f32_16x16x32_f16 v[76:79], v[124:127], v[104:107], v[76:79]
	v_mfma_f32_16x16x32_f16 v[80:83], v[112:115], v[108:111], v[80:83]
	s_add_u32 m0, s14, 0x14000
	s_nop 0
	global_load_lds_dwordx4 v6, s[30:31]
	v_mfma_f32_16x16x32_f16 v[84:87], v[116:119], v[108:111], v[84:87]
	v_mfma_f32_16x16x32_f16 v[88:91], v[120:123], v[108:111], v[88:91]
	s_add_u32 m0, s14, 0x16000
	s_nop 0
	global_load_lds_dwordx4 v7, s[30:31]
	v_mfma_f32_16x16x32_f16 v[92:95], v[124:127], v[108:111], v[92:95]
	s_waitcnt vmcnt(6) lgkmcnt(0)
	s_barrier
	s_add_u32 s28, s28, 0x80
	s_addc_u32 s29, s29, 0
	s_add_u32 s30, s30, 0x80
	s_addc_u32 s31, s31, 0
	s_waitcnt lgkmcnt(0)
	v_mfma_f32_16x16x32_f16 v[32:35], v[144:147], v[128:131], v[32:35]
	ds_read_b128 v[96:99], v8
	v_mfma_f32_16x16x32_f16 v[36:39], v[148:151], v[128:131], v[36:39]
	ds_read_b128 v[112:115], v9 offset:32768
	v_mfma_f32_16x16x32_f16 v[40:43], v[152:155], v[128:131], v[40:43]
	ds_read_b128 v[116:119], v9 offset:34816
	v_mfma_f32_16x16x32_f16 v[44:47], v[156:159], v[128:131], v[44:47]
	ds_read_b128 v[120:123], v9 offset:36864
	v_mfma_f32_16x16x32_f16 v[48:51], v[144:147], v[132:135], v[48:51]
	ds_read_b128 v[124:127], v9 offset:38912
	v_mfma_f32_16x16x32_f16 v[52:55], v[148:151], v[132:135], v[52:55]
	ds_read_b128 v[100:103], v8 offset:2048
	v_mfma_f32_16x16x32_f16 v[56:59], v[152:155], v[132:135], v[56:59]
	ds_read_b128 v[104:107], v8 offset:4096
	v_mfma_f32_16x16x32_f16 v[60:63], v[156:159], v[132:135], v[60:63]
	ds_read_b128 v[108:111], v8 offset:6144
	v_mfma_f32_16x16x32_f16 v[64:67], v[144:147], v[136:139], v[64:67]
	v_mfma_f32_16x16x32_f16 v[68:71], v[148:151], v[136:139], v[68:71]
	v_mfma_f32_16x16x32_f16 v[72:75], v[152:155], v[136:139], v[72:75]
	s_add_u32 m0, s14, 0x18000
	s_nop 0
	global_load_lds_dwordx4 v2, s[28:29]
	v_mfma_f32_16x16x32_f16 v[76:79], v[156:159], v[136:139], v[76:79]
	v_mfma_f32_16x16x32_f16 v[80:83], v[144:147], v[140:143], v[80:83]
	s_add_u32 m0, s14, 0x1a000
	s_nop 0
	global_load_lds_dwordx4 v3, s[28:29]
	v_mfma_f32_16x16x32_f16 v[84:87], v[148:151], v[140:143], v[84:87]
	v_mfma_f32_16x16x32_f16 v[88:91], v[152:155], v[140:143], v[88:91]
	s_add_u32 m0, s14, 0x1c000
	s_nop 0
	global_load_lds_dwordx4 v4, s[28:29]
	v_mfma_f32_16x16x32_f16 v[92:95], v[156:159], v[140:143], v[92:95]
	s_waitcnt lgkmcnt(0)
	v_mfma_f32_16x16x32_f16 v[32:35], v[112:115], v[96:99], v[32:35]
	ds_read_b128 v[128:131], v10
	v_mfma_f32_16x16x32_f16 v[36:39], v[116:119], v[96:99], v[36:39]
	ds_read_b128 v[144:147], v11 offset:32768
	v_mfma_f32_16x16x32_f16 v[40:43], v[120:123], v[96:99], v[40:43]
	ds_read_b128 v[148:151], v11 offset:34816
	v_mfma_f32_16x16x32_f16 v[44:47], v[124:127], v[96:99], v[44:47]
	ds_read_b128 v[152:155], v11 offset:36864
	v_mfma_f32_16x16x32_f16 v[48:51], v[112:115], v[100:103], v[48:51]
	ds_read_b128 v[156:159], v11 offset:38912
	v_mfma_f32_16x16x32_f16 v[52:55], v[116:119], v[100:103], v[52:55]
	ds_read_b128 v[132:135], v10 offset:2048
	v_mfma_f32_16x16x32_f16 v[56:59], v[120:123], v[100:103], v[56:59]
	ds_read_b128 v[136:139], v10 offset:4096
	v_mfma_f32_16x16x32_f16 v[60:63], v[124:127], v[100:103], v[60:63]
	ds_read_b128 v[140:143], v10 offset:6144
	v_mfma_f32_16x16x32_f16 v[64:67], v[112:115], v[104:107], v[64:67]
	v_mfma_f32_16x16x32_f16 v[68:71], v[116:119], v[104:107], v[68:71]
	v_mfma_f32_16x16x32_f16 v[72:75], v[120:123], v[104:107], v[72:75]
	s_add_u32 m0, s14, 0x1e000
	s_nop 0
	global_load_lds_dwordx4 v5, s[28:29]
	v_mfma_f32_16x16x32_f16 v[76:79], v[124:127], v[104:107], v[76:79]
	v_mfma_f32_16x16x32_f16 v[80:83], v[112:115], v[108:111], v[80:83]
	s_add_u32 m0, s14, 0x20000
	s_nop 0
	global_load_lds_dwordx4 v6, s[30:31]
	v_mfma_f32_16x16x32_f16 v[84:87], v[116:119], v[108:111], v[84:87]
	v_mfma_f32_16x16x32_f16 v[88:91], v[120:123], v[108:111], v[88:91]
	s_add_u32 m0, s14, 0x22000
	s_nop 0
	global_load_lds_dwordx4 v7, s[30:31]
	v_mfma_f32_16x16x32_f16 v[92:95], v[124:127], v[108:111], v[92:95]
	s_waitcnt vmcnt(6) lgkmcnt(0)
	s_barrier
	s_add_u32 s28, s28, 0x80
	s_addc_u32 s29, s29, 0
	s_add_u32 s30, s30, 0x80
	s_addc_u32 s31, s31, 0
	s_waitcnt lgkmcnt(0)
	v_mfma_f32_16x16x32_f16 v[32:35], v[144:147], v[128:131], v[32:35]
	ds_read_b128 v[96:99], v12
	v_mfma_f32_16x16x32_f16 v[36:39], v[148:151], v[128:131], v[36:39]
	ds_read_b128 v[112:115], v13 offset:32768
	v_mfma_f32_16x16x32_f16 v[40:43], v[152:155], v[128:131], v[40:43]
	ds_read_b128 v[116:119], v13 offset:34816
	v_mfma_f32_16x16x32_f16 v[44:47], v[156:159], v[128:131], v[44:47]
	ds_read_b128 v[120:123], v13 offset:36864
	v_mfma_f32_16x16x32_f16 v[48:51], v[144:147], v[132:135], v[48:51]
	ds_read_b128 v[124:127], v13 offset:38912
	v_mfma_f32_16x16x32_f16 v[52:55], v[148:151], v[132:135], v[52:55]
	ds_read_b128 v[100:103], v12 offset:2048
	v_mfma_f32_16x16x32_f16 v[56:59], v[152:155], v[132:135], v[56:59]
	ds_read_b128 v[104:107], v12 offset:4096
	v_mfma_f32_16x16x32_f16 v[60:63], v[156:159], v[132:135], v[60:63]
	ds_read_b128 v[108:111], v12 offset:6144
	v_mfma_f32_16x16x32_f16 v[64:67], v[144:147], v[136:139], v[64:67]
	v_mfma_f32_16x16x32_f16 v[68:71], v[148:151], v[136:139], v[68:71]
	v_mfma_f32_16x16x32_f16 v[72:75], v[152:155], v[136:139], v[72:75]
	s_add_u32 m0, s14, 0x0
	s_nop 0
	global_load_lds_dwordx4 v2, s[28:29]
	v_mfma_f32_16x16x32_f16 v[76:79], v[156:159], v[136:139], v[76:79]
	v_mfma_f32_16x16x32_f16 v[80:83], v[144:147], v[140:143], v[80:83]
	s_add_u32 m0, s14, 0x2000
	s_nop 0
	global_load_lds_dwordx4 v3, s[28:29]
	v_mfma_f32_16x16x32_f16 v[84:87], v[148:151], v[140:143], v[84:87]
	v_mfma_f32_16x16x32_f16 v[88:91], v[152:155], v[140:143], v[88:91]
	s_add_u32 m0, s14, 0x4000
	s_nop 0
	global_load_lds_dwordx4 v4, s[28:29]
	v_mfma_f32_16x16x32_f16 v[92:95], v[156:159], v[140:143], v[92:95]
	s_waitcnt lgkmcnt(0)
	v_mfma_f32_16x16x32_f16 v[32:35], v[112:115], v[96:99], v[32:35]
	ds_read_b128 v[128:131], v14
	v_mfma_f32_16x16x32_f16 v[36:39], v[116:119], v[96:99], v[36:39]
	ds_read_b128 v[144:147], v15 offset:32768
	v_mfma_f32_16x16x32_f16 v[40:43], v[120:123], v[96:99], v[40:43]
	ds_read_b128 v[148:151], v15 offset:34816
	v_mfma_f32_16x16x32_f16 v[44:47], v[124:127], v[96:99], v[44:47]
	ds_read_b128 v[152:155], v15 offset:36864
	v_mfma_f32_16x16x32_f16 v[48:51], v[112:115], v[100:103], v[48:51]
	ds_read_b128 v[156:159], v15 offset:38912
	v_mfma_f32_16x16x32_f16 v[52:55], v[116:119], v[100:103], v[52:55]
	ds_read_b128 v[132:135], v14 offset:2048
	v_mfma_f32_16x16x32_f16 v[56:59], v[120:123], v[100:103], v[56:59]
	ds_read_b128 v[136:139], v14 offset:4096
	v_mfma_f32_16x16x32_f16 v[60:63], v[124:127], v[100:103], v[60:63]
	ds_read_b128 v[140:143], v14 offset:6144
	v_mfma_f32_16x16x32_f16 v[64:67], v[112:115], v[104:107], v[64:67]
	v_mfma_f32_16x16x32_f16 v[68:71], v[116:119], v[104:107], v[68:71]
	v_mfma_f32_16x16x32_f16 v[72:75], v[120:123], v[104:107], v[72:75]
	s_add_u32 m0, s14, 0x6000
	s_nop 0
	global_load_lds_dwordx4 v5, s[28:29]
	v_mfma_f32_16x16x32_f16 v[76:79], v[124:127], v[104:107], v[76:79]
	v_mfma_f32_16x16x32_f16 v[80:83], v[112:115], v[108:111], v[80:83]
	s_add_u32 m0, s14, 0x8000
	s_nop 0
	global_load_lds_dwordx4 v6, s[30:31]
	v_mfma_f32_16x16x32_f16 v[84:87], v[116:119], v[108:111], v[84:87]
	v_mfma_f32_16x16x32_f16 v[88:91], v[120:123], v[108:111], v[88:91]
	s_add_u32 m0, s14, 0xa000
	s_nop 0
	global_load_lds_dwordx4 v7, s[30:31]
	v_mfma_f32_16x16x32_f16 v[92:95], v[124:127], v[108:111], v[92:95]
	s_waitcnt vmcnt(6) lgkmcnt(0)
	s_barrier
	s_add_u32 s28, s28, 0x80
	s_addc_u32 s29, s29, 0
	s_add_u32 s30, s30, 0x80
	s_addc_u32 s31, s31, 0
	s_waitcnt lgkmcnt(0)
	v_mfma_f32_16x16x32_f16 v[32:35], v[144:147], v[128:131], v[32:35]
	ds_read_b128 v[96:99], v16
	v_mfma_f32_16x16x32_f16 v[36:39], v[148:151], v[128:131], v[36:39]
	ds_read_b128 v[112:115], v17 offset:32768
	v_mfma_f32_16x16x32_f16 v[40:43], v[152:155], v[128:131], v[40:43]
	ds_read_b128 v[116:119], v17 offset:34816
	v_mfma_f32_16x16x32_f16 v[44:47], v[156:159], v[128:131], v[44:47]
	ds_read_b128 v[120:123], v17 offset:36864
	v_mfma_f32_16x16x32_f16 v[48:51], v[144:147], v[132:135], v[48:51]
	ds_read_b128 v[124:127], v17 offset:38912
	v_mfma_f32_16x16x32_f16 v[52:55], v[148:151], v[132:135], v[52:55]
	ds_read_b128 v[100:103], v16 offset:2048
	v_mfma_f32_16x16x32_f16 v[56:59], v[152:155], v[132:135], v[56:59]
	ds_read_b128 v[104:107], v16 offset:4096
	v_mfma_f32_16x16x32_f16 v[60:63], v[156:159], v[132:135], v[60:63]
	ds_read_b128 v[108:111], v16 offset:6144
	v_mfma_f32_16x16x32_f16 v[64:67], v[144:147], v[136:139], v[64:67]
	v_mfma_f32_16x16x32_f16 v[68:71], v[148:151], v[136:139], v[68:71]
	v_mfma_f32_16x16x32_f16 v[72:75], v[152:155], v[136:139], v[72:75]
	s_add_u32 m0, s14, 0xc000
	s_nop 0
	global_load_lds_dwordx4 v2, s[28:29]
	v_mfma_f32_16x16x32_f16 v[76:79], v[156:159], v[136:139], v[76:79]
	v_mfma_f32_16x16x32_f16 v[80:83], v[144:147], v[140:143], v[80:83]
	s_add_u32 m0, s14, 0xe000
	s_nop 0
	global_load_lds_dwordx4 v3, s[28:29]
	v_mfma_f32_16x16x32_f16 v[84:87], v[148:151], v[140:143], v[84:87]
	v_mfma_f32_16x16x32_f16 v[88:91], v[152:155], v[140:143], v[88:91]
	s_add_u32 m0, s14, 0x10000
	s_nop 0
	global_load_lds_dwordx4 v4, s[28:29]
	v_mfma_f32_16x16x32_f16 v[92:95], v[156:159], v[140:143], v[92:95]
	s_waitcnt lgkmcnt(0)
	v_mfma_f32_16x16x32_f16 v[32:35], v[112:115], v[96:99], v[32:35]
	ds_read_b128 v[128:131], v18
	v_mfma_f32_16x16x32_f16 v[36:39], v[116:119], v[96:99], v[36:39]
	ds_read_b128 v[144:147], v19 offset:32768
	v_mfma_f32_16x16x32_f16 v[40:43], v[120:123], v[96:99], v[40:43]
	ds_read_b128 v[148:151], v19 offset:34816
	v_mfma_f32_16x16x32_f16 v[44:47], v[124:127], v[96:99], v[44:47]
	ds_read_b128 v[152:155], v19 offset:36864
	v_mfma_f32_16x16x32_f16 v[48:51], v[112:115], v[100:103], v[48:51]
	ds_read_b128 v[156:159], v19 offset:38912
	v_mfma_f32_16x16x32_f16 v[52:55], v[116:119], v[100:103], v[52:55]
	ds_read_b128 v[132:135], v18 offset:2048
	v_mfma_f32_16x16x32_f16 v[56:59], v[120:123], v[100:103], v[56:59]
	ds_read_b128 v[136:139], v18 offset:4096
	v_mfma_f32_16x16x32_f16 v[60:63], v[124:127], v[100:103], v[60:63]
	ds_read_b128 v[140:143], v18 offset:6144
	v_mfma_f32_16x16x32_f16 v[64:67], v[112:115], v[104:107], v[64:67]
	v_mfma_f32_16x16x32_f16 v[68:71], v[116:119], v[104:107], v[68:71]
	v_mfma_f32_16x16x32_f16 v[72:75], v[120:123], v[104:107], v[72:75]
	s_add_u32 m0, s14, 0x12000
	s_nop 0
	global_load_lds_dwordx4 v5, s[28:29]
	v_mfma_f32_16x16x32_f16 v[76:79], v[124:127], v[104:107], v[76:79]
	v_mfma_f32_16x16x32_f16 v[80:83], v[112:115], v[108:111], v[80:83]
	s_add_u32 m0, s14, 0x14000
	s_nop 0
	global_load_lds_dwordx4 v6, s[30:31]
	v_mfma_f32_16x16x32_f16 v[84:87], v[116:119], v[108:111], v[84:87]
	v_mfma_f32_16x16x32_f16 v[88:91], v[120:123], v[108:111], v[88:91]
	s_add_u32 m0, s14, 0x16000
	s_nop 0
	global_load_lds_dwordx4 v7, s[30:31]
	v_mfma_f32_16x16x32_f16 v[92:95], v[124:127], v[108:111], v[92:95]
	s_waitcnt vmcnt(6) lgkmcnt(0)
	s_barrier
	s_add_u32 s28, s28, 0x80
	s_addc_u32 s29, s29, 0
	s_add_u32 s30, s30, 0x80
	s_addc_u32 s31, s31, 0
	s_waitcnt lgkmcnt(0)
	v_mfma_f32_16x16x32_f16 v[32:35], v[144:147], v[128:131], v[32:35]
	ds_read_b128 v[96:99], v8
	v_mfma_f32_16x16x32_f16 v[36:39], v[148:151], v[128:131], v[36:39]
	ds_read_b128 v[112:115], v9 offset:32768
	v_mfma_f32_16x16x32_f16 v[40:43], v[152:155], v[128:131], v[40:43]
	ds_read_b128 v[116:119], v9 offset:34816
	v_mfma_f32_16x16x32_f16 v[44:47], v[156:159], v[128:131], v[44:47]
	ds_read_b128 v[120:123], v9 offset:36864
	v_mfma_f32_16x16x32_f16 v[48:51], v[144:147], v[132:135], v[48:51]
	ds_read_b128 v[124:127], v9 offset:38912
	v_mfma_f32_16x16x32_f16 v[52:55], v[148:151], v[132:135], v[52:55]
	ds_read_b128 v[100:103], v8 offset:2048
	v_mfma_f32_16x16x32_f16 v[56:59], v[152:155], v[132:135], v[56:59]
	ds_read_b128 v[104:107], v8 offset:4096
	v_mfma_f32_16x16x32_f16 v[60:63], v[156:159], v[132:135], v[60:63]
	ds_read_b128 v[108:111], v8 offset:6144
	v_mfma_f32_16x16x32_f16 v[64:67], v[144:147], v[136:139], v[64:67]
	v_mfma_f32_16x16x32_f16 v[68:71], v[148:151], v[136:139], v[68:71]
	v_mfma_f32_16x16x32_f16 v[72:75], v[152:155], v[136:139], v[72:75]
	s_add_u32 m0, s14, 0x18000
	s_nop 0
	global_load_lds_dwordx4 v2, s[28:29]
	v_mfma_f32_16x16x32_f16 v[76:79], v[156:159], v[136:139], v[76:79]
	v_mfma_f32_16x16x32_f16 v[80:83], v[144:147], v[140:143], v[80:83]
	s_add_u32 m0, s14, 0x1a000
	s_nop 0
	global_load_lds_dwordx4 v3, s[28:29]
	v_mfma_f32_16x16x32_f16 v[84:87], v[148:151], v[140:143], v[84:87]
	v_mfma_f32_16x16x32_f16 v[88:91], v[152:155], v[140:143], v[88:91]
	s_add_u32 m0, s14, 0x1c000
	s_nop 0
	global_load_lds_dwordx4 v4, s[28:29]
	v_mfma_f32_16x16x32_f16 v[92:95], v[156:159], v[140:143], v[92:95]
	s_waitcnt lgkmcnt(0)
	v_mfma_f32_16x16x32_f16 v[32:35], v[112:115], v[96:99], v[32:35]
	ds_read_b128 v[128:131], v10
	v_mfma_f32_16x16x32_f16 v[36:39], v[116:119], v[96:99], v[36:39]
	ds_read_b128 v[144:147], v11 offset:32768
	v_mfma_f32_16x16x32_f16 v[40:43], v[120:123], v[96:99], v[40:43]
	ds_read_b128 v[148:151], v11 offset:34816
	v_mfma_f32_16x16x32_f16 v[44:47], v[124:127], v[96:99], v[44:47]
	ds_read_b128 v[152:155], v11 offset:36864
	v_mfma_f32_16x16x32_f16 v[48:51], v[112:115], v[100:103], v[48:51]
	ds_read_b128 v[156:159], v11 offset:38912
	v_mfma_f32_16x16x32_f16 v[52:55], v[116:119], v[100:103], v[52:55]
	ds_read_b128 v[132:135], v10 offset:2048
	v_mfma_f32_16x16x32_f16 v[56:59], v[120:123], v[100:103], v[56:59]
	ds_read_b128 v[136:139], v10 offset:4096
	v_mfma_f32_16x16x32_f16 v[60:63], v[124:127], v[100:103], v[60:63]
	ds_read_b128 v[140:143], v10 offset:6144
	v_mfma_f32_16x16x32_f16 v[64:67], v[112:115], v[104:107], v[64:67]
	v_mfma_f32_16x16x32_f16 v[68:71], v[116:119], v[104:107], v[68:71]
	v_mfma_f32_16x16x32_f16 v[72:75], v[120:123], v[104:107], v[72:75]
	s_add_u32 m0, s14, 0x1e000
	s_nop 0
	global_load_lds_dwordx4 v5, s[28:29]
	v_mfma_f32_16x16x32_f16 v[76:79], v[124:127], v[104:107], v[76:79]
	v_mfma_f32_16x16x32_f16 v[80:83], v[112:115], v[108:111], v[80:83]
	s_add_u32 m0, s14, 0x20000
	s_nop 0
	global_load_lds_dwordx4 v6, s[30:31]
	v_mfma_f32_16x16x32_f16 v[84:87], v[116:119], v[108:111], v[84:87]
	v_mfma_f32_16x16x32_f16 v[88:91], v[120:123], v[108:111], v[88:91]
	s_add_u32 m0, s14, 0x22000
	s_nop 0
	global_load_lds_dwordx4 v7, s[30:31]
	v_mfma_f32_16x16x32_f16 v[92:95], v[124:127], v[108:111], v[92:95]
	s_waitcnt vmcnt(6) lgkmcnt(0)
	s_barrier
	s_add_u32 s28, s28, 0x80
	s_addc_u32 s29, s29, 0
	s_add_u32 s30, s30, 0x80
	s_addc_u32 s31, s31, 0
	s_waitcnt lgkmcnt(0)
	v_mfma_f32_16x16x32_f16 v[32:35], v[144:147], v[128:131], v[32:35]
	ds_read_b128 v[96:99], v12
	v_mfma_f32_16x16x32_f16 v[36:39], v[148:151], v[128:131], v[36:39]
	ds_read_b128 v[112:115], v13 offset:32768
	v_mfma_f32_16x16x32_f16 v[40:43], v[152:155], v[128:131], v[40:43]
	ds_read_b128 v[116:119], v13 offset:34816
	v_mfma_f32_16x16x32_f16 v[44:47], v[156:159], v[128:131], v[44:47]
	ds_read_b128 v[120:123], v13 offset:36864
	v_mfma_f32_16x16x32_f16 v[48:51], v[144:147], v[132:135], v[48:51]
	ds_read_b128 v[124:127], v13 offset:38912
	v_mfma_f32_16x16x32_f16 v[52:55], v[148:151], v[132:135], v[52:55]
	ds_read_b128 v[100:103], v12 offset:2048
	v_mfma_f32_16x16x32_f16 v[56:59], v[152:155], v[132:135], v[56:59]
	ds_read_b128 v[104:107], v12 offset:4096
	v_mfma_f32_16x16x32_f16 v[60:63], v[156:159], v[132:135], v[60:63]
	ds_read_b128 v[108:111], v12 offset:6144
	v_mfma_f32_16x16x32_f16 v[64:67], v[144:147], v[136:139], v[64:67]
	v_mfma_f32_16x16x32_f16 v[68:71], v[148:151], v[136:139], v[68:71]
	v_mfma_f32_16x16x32_f16 v[72:75], v[152:155], v[136:139], v[72:75]
	s_add_u32 m0, s14, 0x0
	s_nop 0
	global_load_lds_dwordx4 v2, s[28:29]
	v_mfma_f32_16x16x32_f16 v[76:79], v[156:159], v[136:139], v[76:79]
	v_mfma_f32_16x16x32_f16 v[80:83], v[144:147], v[140:143], v[80:83]
	s_add_u32 m0, s14, 0x2000
	s_nop 0
	global_load_lds_dwordx4 v3, s[28:29]
	v_mfma_f32_16x16x32_f16 v[84:87], v[148:151], v[140:143], v[84:87]
	v_mfma_f32_16x16x32_f16 v[88:91], v[152:155], v[140:143], v[88:91]
	s_add_u32 m0, s14, 0x4000
	s_nop 0
	global_load_lds_dwordx4 v4, s[28:29]
	v_mfma_f32_16x16x32_f16 v[92:95], v[156:159], v[140:143], v[92:95]
	s_waitcnt lgkmcnt(0)
	v_mfma_f32_16x16x32_f16 v[32:35], v[112:115], v[96:99], v[32:35]
	ds_read_b128 v[128:131], v14
	v_mfma_f32_16x16x32_f16 v[36:39], v[116:119], v[96:99], v[36:39]
	ds_read_b128 v[144:147], v15 offset:32768
	v_mfma_f32_16x16x32_f16 v[40:43], v[120:123], v[96:99], v[40:43]
	ds_read_b128 v[148:151], v15 offset:34816
	v_mfma_f32_16x16x32_f16 v[44:47], v[124:127], v[96:99], v[44:47]
	ds_read_b128 v[152:155], v15 offset:36864
	v_mfma_f32_16x16x32_f16 v[48:51], v[112:115], v[100:103], v[48:51]
	ds_read_b128 v[156:159], v15 offset:38912
	v_mfma_f32_16x16x32_f16 v[52:55], v[116:119], v[100:103], v[52:55]
	ds_read_b128 v[132:135], v14 offset:2048
	v_mfma_f32_16x16x32_f16 v[56:59], v[120:123], v[100:103], v[56:59]
	ds_read_b128 v[136:139], v14 offset:4096
	v_mfma_f32_16x16x32_f16 v[60:63], v[124:127], v[100:103], v[60:63]
	ds_read_b128 v[140:143], v14 offset:6144
	v_mfma_f32_16x16x32_f16 v[64:67], v[112:115], v[104:107], v[64:67]
	v_mfma_f32_16x16x32_f16 v[68:71], v[116:119], v[104:107], v[68:71]
	v_mfma_f32_16x16x32_f16 v[72:75], v[120:123], v[104:107], v[72:75]
	s_add_u32 m0, s14, 0x6000
	s_nop 0
	global_load_lds_dwordx4 v5, s[28:29]
	v_mfma_f32_16x16x32_f16 v[76:79], v[124:127], v[104:107], v[76:79]
	v_mfma_f32_16x16x32_f16 v[80:83], v[112:115], v[108:111], v[80:83]
	s_add_u32 m0, s14, 0x8000
	s_nop 0
	global_load_lds_dwordx4 v6, s[30:31]
	v_mfma_f32_16x16x32_f16 v[84:87], v[116:119], v[108:111], v[84:87]
	v_mfma_f32_16x16x32_f16 v[88:91], v[120:123], v[108:111], v[88:91]
	s_add_u32 m0, s14, 0xa000
	s_nop 0
	global_load_lds_dwordx4 v7, s[30:31]
	v_mfma_f32_16x16x32_f16 v[92:95], v[124:127], v[108:111], v[92:95]
	s_waitcnt vmcnt(6) lgkmcnt(0)
	s_barrier
	s_add_u32 s28, s28, 0x80
	s_addc_u32 s29, s29, 0
	s_add_u32 s30, s30, 0x80
	s_addc_u32 s31, s31, 0
	s_waitcnt lgkmcnt(0)
	v_mfma_f32_16x16x32_f16 v[32:35], v[144:147], v[128:131], v[32:35]
	ds_read_b128 v[96:99], v16
	v_mfma_f32_16x16x32_f16 v[36:39], v[148:151], v[128:131], v[36:39]
	ds_read_b128 v[112:115], v17 offset:32768
	v_mfma_f32_16x16x32_f16 v[40:43], v[152:155], v[128:131], v[40:43]
	ds_read_b128 v[116:119], v17 offset:34816
	v_mfma_f32_16x16x32_f16 v[44:47], v[156:159], v[128:131], v[44:47]
	ds_read_b128 v[120:123], v17 offset:36864
	v_mfma_f32_16x16x32_f16 v[48:51], v[144:147], v[132:135], v[48:51]
	ds_read_b128 v[124:127], v17 offset:38912
	v_mfma_f32_16x16x32_f16 v[52:55], v[148:151], v[132:135], v[52:55]
	ds_read_b128 v[100:103], v16 offset:2048
	v_mfma_f32_16x16x32_f16 v[56:59], v[152:155], v[132:135], v[56:59]
	ds_read_b128 v[104:107], v16 offset:4096
	v_mfma_f32_16x16x32_f16 v[60:63], v[156:159], v[132:135], v[60:63]
	ds_read_b128 v[108:111], v16 offset:6144
	v_mfma_f32_16x16x32_f16 v[64:67], v[144:147], v[136:139], v[64:67]
	v_mfma_f32_16x16x32_f16 v[68:71], v[148:151], v[136:139], v[68:71]
	v_mfma_f32_16x16x32_f16 v[72:75], v[152:155], v[136:139], v[72:75]
	s_add_u32 m0, s14, 0xc000
	s_nop 0
	global_load_lds_dwordx4 v2, s[28:29]
	v_mfma_f32_16x16x32_f16 v[76:79], v[156:159], v[136:139], v[76:79]
	v_mfma_f32_16x16x32_f16 v[80:83], v[144:147], v[140:143], v[80:83]
	s_add_u32 m0, s14, 0xe000
	s_nop 0
	global_load_lds_dwordx4 v3, s[28:29]
	v_mfma_f32_16x16x32_f16 v[84:87], v[148:151], v[140:143], v[84:87]
	v_mfma_f32_16x16x32_f16 v[88:91], v[152:155], v[140:143], v[88:91]
	s_add_u32 m0, s14, 0x10000
	s_nop 0
	global_load_lds_dwordx4 v4, s[28:29]
	v_mfma_f32_16x16x32_f16 v[92:95], v[156:159], v[140:143], v[92:95]
	s_waitcnt lgkmcnt(0)
	v_mfma_f32_16x16x32_f16 v[32:35], v[112:115], v[96:99], v[32:35]
	ds_read_b128 v[128:131], v18
	v_mfma_f32_16x16x32_f16 v[36:39], v[116:119], v[96:99], v[36:39]
	ds_read_b128 v[144:147], v19 offset:32768
	v_mfma_f32_16x16x32_f16 v[40:43], v[120:123], v[96:99], v[40:43]
	ds_read_b128 v[148:151], v19 offset:34816
	v_mfma_f32_16x16x32_f16 v[44:47], v[124:127], v[96:99], v[44:47]
	ds_read_b128 v[152:155], v19 offset:36864
	v_mfma_f32_16x16x32_f16 v[48:51], v[112:115], v[100:103], v[48:51]
	ds_read_b128 v[156:159], v19 offset:38912
	v_mfma_f32_16x16x32_f16 v[52:55], v[116:119], v[100:103], v[52:55]
	ds_read_b128 v[132:135], v18 offset:2048
	v_mfma_f32_16x16x32_f16 v[56:59], v[120:123], v[100:103], v[56:59]
	ds_read_b128 v[136:139], v18 offset:4096
	v_mfma_f32_16x16x32_f16 v[60:63], v[124:127], v[100:103], v[60:63]
	ds_read_b128 v[140:143], v18 offset:6144
	v_mfma_f32_16x16x32_f16 v[64:67], v[112:115], v[104:107], v[64:67]
	v_mfma_f32_16x16x32_f16 v[68:71], v[116:119], v[104:107], v[68:71]
	v_mfma_f32_16x16x32_f16 v[72:75], v[120:123], v[104:107], v[72:75]
	s_add_u32 m0, s14, 0x12000
	s_nop 0
	global_load_lds_dwordx4 v5, s[28:29]
	v_mfma_f32_16x16x32_f16 v[76:79], v[124:127], v[104:107], v[76:79]
	v_mfma_f32_16x16x32_f16 v[80:83], v[112:115], v[108:111], v[80:83]
	s_add_u32 m0, s14, 0x14000
	s_nop 0
	global_load_lds_dwordx4 v6, s[30:31]
	v_mfma_f32_16x16x32_f16 v[84:87], v[116:119], v[108:111], v[84:87]
	v_mfma_f32_16x16x32_f16 v[88:91], v[120:123], v[108:111], v[88:91]
	s_add_u32 m0, s14, 0x16000
	s_nop 0
	global_load_lds_dwordx4 v7, s[30:31]
	v_mfma_f32_16x16x32_f16 v[92:95], v[124:127], v[108:111], v[92:95]
	s_waitcnt vmcnt(6) lgkmcnt(0)
	s_barrier
	s_add_u32 s28, s28, 0x80
	s_addc_u32 s29, s29, 0
	s_add_u32 s30, s30, 0x80
	s_addc_u32 s31, s31, 0
	s_waitcnt lgkmcnt(0)
	v_mfma_f32_16x16x32_f16 v[32:35], v[144:147], v[128:131], v[32:35]
	ds_read_b128 v[96:99], v8
	v_mfma_f32_16x16x32_f16 v[36:39], v[148:151], v[128:131], v[36:39]
	ds_read_b128 v[112:115], v9 offset:32768
	v_mfma_f32_16x16x32_f16 v[40:43], v[152:155], v[128:131], v[40:43]
	ds_read_b128 v[116:119], v9 offset:34816
	v_mfma_f32_16x16x32_f16 v[44:47], v[156:159], v[128:131], v[44:47]
	ds_read_b128 v[120:123], v9 offset:36864
	v_mfma_f32_16x16x32_f16 v[48:51], v[144:147], v[132:135], v[48:51]
	ds_read_b128 v[124:127], v9 offset:38912
	v_mfma_f32_16x16x32_f16 v[52:55], v[148:151], v[132:135], v[52:55]
	ds_read_b128 v[100:103], v8 offset:2048
	v_mfma_f32_16x16x32_f16 v[56:59], v[152:155], v[132:135], v[56:59]
	ds_read_b128 v[104:107], v8 offset:4096
	v_mfma_f32_16x16x32_f16 v[60:63], v[156:159], v[132:135], v[60:63]
	ds_read_b128 v[108:111], v8 offset:6144
	v_mfma_f32_16x16x32_f16 v[64:67], v[144:147], v[136:139], v[64:67]
	v_mfma_f32_16x16x32_f16 v[68:71], v[148:151], v[136:139], v[68:71]
	v_mfma_f32_16x16x32_f16 v[72:75], v[152:155], v[136:139], v[72:75]
	s_add_u32 m0, s14, 0x18000
	s_nop 0
	global_load_lds_dwordx4 v2, s[28:29]
	v_mfma_f32_16x16x32_f16 v[76:79], v[156:159], v[136:139], v[76:79]
	v_mfma_f32_16x16x32_f16 v[80:83], v[144:147], v[140:143], v[80:83]
	s_add_u32 m0, s14, 0x1a000
	s_nop 0
	global_load_lds_dwordx4 v3, s[28:29]
	v_mfma_f32_16x16x32_f16 v[84:87], v[148:151], v[140:143], v[84:87]
	v_mfma_f32_16x16x32_f16 v[88:91], v[152:155], v[140:143], v[88:91]
	s_add_u32 m0, s14, 0x1c000
	s_nop 0
	global_load_lds_dwordx4 v4, s[28:29]
	v_mfma_f32_16x16x32_f16 v[92:95], v[156:159], v[140:143], v[92:95]
	s_waitcnt lgkmcnt(0)
	v_mfma_f32_16x16x32_f16 v[32:35], v[112:115], v[96:99], v[32:35]
	ds_read_b128 v[128:131], v10
	v_mfma_f32_16x16x32_f16 v[36:39], v[116:119], v[96:99], v[36:39]
	ds_read_b128 v[144:147], v11 offset:32768
	v_mfma_f32_16x16x32_f16 v[40:43], v[120:123], v[96:99], v[40:43]
	ds_read_b128 v[148:151], v11 offset:34816
	v_mfma_f32_16x16x32_f16 v[44:47], v[124:127], v[96:99], v[44:47]
	ds_read_b128 v[152:155], v11 offset:36864
	v_mfma_f32_16x16x32_f16 v[48:51], v[112:115], v[100:103], v[48:51]
	ds_read_b128 v[156:159], v11 offset:38912
	v_mfma_f32_16x16x32_f16 v[52:55], v[116:119], v[100:103], v[52:55]
	ds_read_b128 v[132:135], v10 offset:2048
	v_mfma_f32_16x16x32_f16 v[56:59], v[120:123], v[100:103], v[56:59]
	ds_read_b128 v[136:139], v10 offset:4096
	v_mfma_f32_16x16x32_f16 v[60:63], v[124:127], v[100:103], v[60:63]
	ds_read_b128 v[140:143], v10 offset:6144
	v_mfma_f32_16x16x32_f16 v[64:67], v[112:115], v[104:107], v[64:67]
	v_mfma_f32_16x16x32_f16 v[68:71], v[116:119], v[104:107], v[68:71]
	v_mfma_f32_16x16x32_f16 v[72:75], v[120:123], v[104:107], v[72:75]
	s_add_u32 m0, s14, 0x1e000
	s_nop 0
	global_load_lds_dwordx4 v5, s[28:29]
	v_mfma_f32_16x16x32_f16 v[76:79], v[124:127], v[104:107], v[76:79]
	v_mfma_f32_16x16x32_f16 v[80:83], v[112:115], v[108:111], v[80:83]
	s_add_u32 m0, s14, 0x20000
	s_nop 0
	global_load_lds_dwordx4 v6, s[30:31]
	v_mfma_f32_16x16x32_f16 v[84:87], v[116:119], v[108:111], v[84:87]
	v_mfma_f32_16x16x32_f16 v[88:91], v[120:123], v[108:111], v[88:91]
	s_add_u32 m0, s14, 0x22000
	s_nop 0
	global_load_lds_dwordx4 v7, s[30:31]
	v_mfma_f32_16x16x32_f16 v[92:95], v[124:127], v[108:111], v[92:95]
	s_waitcnt vmcnt(6) lgkmcnt(0)
	s_barrier
	s_add_u32 s28, s28, 0x80
	s_addc_u32 s29, s29, 0
	s_add_u32 s30, s30, 0x80
	s_addc_u32 s31, s31, 0
	s_waitcnt lgkmcnt(0)
	v_mfma_f32_16x16x32_f16 v[32:35], v[144:147], v[128:131], v[32:35]
	ds_read_b128 v[96:99], v12
	v_mfma_f32_16x16x32_f16 v[36:39], v[148:151], v[128:131], v[36:39]
	ds_read_b128 v[112:115], v13 offset:32768
	v_mfma_f32_16x16x32_f16 v[40:43], v[152:155], v[128:131], v[40:43]
	ds_read_b128 v[116:119], v13 offset:34816
	v_mfma_f32_16x16x32_f16 v[44:47], v[156:159], v[128:131], v[44:47]
	ds_read_b128 v[120:123], v13 offset:36864
	v_mfma_f32_16x16x32_f16 v[48:51], v[144:147], v[132:135], v[48:51]
	ds_read_b128 v[124:127], v13 offset:38912
	v_mfma_f32_16x16x32_f16 v[52:55], v[148:151], v[132:135], v[52:55]
	ds_read_b128 v[100:103], v12 offset:2048
	v_mfma_f32_16x16x32_f16 v[56:59], v[152:155], v[132:135], v[56:59]
	ds_read_b128 v[104:107], v12 offset:4096
	v_mfma_f32_16x16x32_f16 v[60:63], v[156:159], v[132:135], v[60:63]
	ds_read_b128 v[108:111], v12 offset:6144
	v_mfma_f32_16x16x32_f16 v[64:67], v[144:147], v[136:139], v[64:67]
	v_mfma_f32_16x16x32_f16 v[68:71], v[148:151], v[136:139], v[68:71]
	v_mfma_f32_16x16x32_f16 v[72:75], v[152:155], v[136:139], v[72:75]
	s_add_u32 m0, s14, 0x0
	s_nop 0
	global_load_lds_dwordx4 v2, s[28:29]
	v_mfma_f32_16x16x32_f16 v[76:79], v[156:159], v[136:139], v[76:79]
	v_mfma_f32_16x16x32_f16 v[80:83], v[144:147], v[140:143], v[80:83]
	s_add_u32 m0, s14, 0x2000
	s_nop 0
	global_load_lds_dwordx4 v3, s[28:29]
	v_mfma_f32_16x16x32_f16 v[84:87], v[148:151], v[140:143], v[84:87]
	v_mfma_f32_16x16x32_f16 v[88:91], v[152:155], v[140:143], v[88:91]
	s_add_u32 m0, s14, 0x4000
	s_nop 0
	global_load_lds_dwordx4 v4, s[28:29]
	v_mfma_f32_16x16x32_f16 v[92:95], v[156:159], v[140:143], v[92:95]
	s_waitcnt lgkmcnt(0)
	v_mfma_f32_16x16x32_f16 v[32:35], v[112:115], v[96:99], v[32:35]
	ds_read_b128 v[128:131], v14
	v_mfma_f32_16x16x32_f16 v[36:39], v[116:119], v[96:99], v[36:39]
	ds_read_b128 v[144:147], v15 offset:32768
	v_mfma_f32_16x16x32_f16 v[40:43], v[120:123], v[96:99], v[40:43]
	ds_read_b128 v[148:151], v15 offset:34816
	v_mfma_f32_16x16x32_f16 v[44:47], v[124:127], v[96:99], v[44:47]
	ds_read_b128 v[152:155], v15 offset:36864
	v_mfma_f32_16x16x32_f16 v[48:51], v[112:115], v[100:103], v[48:51]
	ds_read_b128 v[156:159], v15 offset:38912
	v_mfma_f32_16x16x32_f16 v[52:55], v[116:119], v[100:103], v[52:55]
	ds_read_b128 v[132:135], v14 offset:2048
	v_mfma_f32_16x16x32_f16 v[56:59], v[120:123], v[100:103], v[56:59]
	ds_read_b128 v[136:139], v14 offset:4096
	v_mfma_f32_16x16x32_f16 v[60:63], v[124:127], v[100:103], v[60:63]
	ds_read_b128 v[140:143], v14 offset:6144
	v_mfma_f32_16x16x32_f16 v[64:67], v[112:115], v[104:107], v[64:67]
	v_mfma_f32_16x16x32_f16 v[68:71], v[116:119], v[104:107], v[68:71]
	v_mfma_f32_16x16x32_f16 v[72:75], v[120:123], v[104:107], v[72:75]
	s_add_u32 m0, s14, 0x6000
	s_nop 0
	global_load_lds_dwordx4 v5, s[28:29]
	v_mfma_f32_16x16x32_f16 v[76:79], v[124:127], v[104:107], v[76:79]
	v_mfma_f32_16x16x32_f16 v[80:83], v[112:115], v[108:111], v[80:83]
	s_add_u32 m0, s14, 0x8000
	s_nop 0
	global_load_lds_dwordx4 v6, s[30:31]
	v_mfma_f32_16x16x32_f16 v[84:87], v[116:119], v[108:111], v[84:87]
	v_mfma_f32_16x16x32_f16 v[88:91], v[120:123], v[108:111], v[88:91]
	s_add_u32 m0, s14, 0xa000
	s_nop 0
	global_load_lds_dwordx4 v7, s[30:31]
	v_mfma_f32_16x16x32_f16 v[92:95], v[124:127], v[108:111], v[92:95]
	s_waitcnt vmcnt(6) lgkmcnt(0)
	s_barrier
	s_add_u32 s28, s28, 0x80
	s_addc_u32 s29, s29, 0
	s_add_u32 s30, s30, 0x80
	s_addc_u32 s31, s31, 0
	s_waitcnt lgkmcnt(0)
	v_mfma_f32_16x16x32_f16 v[32:35], v[144:147], v[128:131], v[32:35]
	ds_read_b128 v[96:99], v16
	v_mfma_f32_16x16x32_f16 v[36:39], v[148:151], v[128:131], v[36:39]
	ds_read_b128 v[112:115], v17 offset:32768
	v_mfma_f32_16x16x32_f16 v[40:43], v[152:155], v[128:131], v[40:43]
	ds_read_b128 v[116:119], v17 offset:34816
	v_mfma_f32_16x16x32_f16 v[44:47], v[156:159], v[128:131], v[44:47]
	ds_read_b128 v[120:123], v17 offset:36864
	v_mfma_f32_16x16x32_f16 v[48:51], v[144:147], v[132:135], v[48:51]
	ds_read_b128 v[124:127], v17 offset:38912
	v_mfma_f32_16x16x32_f16 v[52:55], v[148:151], v[132:135], v[52:55]
	ds_read_b128 v[100:103], v16 offset:2048
	v_mfma_f32_16x16x32_f16 v[56:59], v[152:155], v[132:135], v[56:59]
	ds_read_b128 v[104:107], v16 offset:4096
	v_mfma_f32_16x16x32_f16 v[60:63], v[156:159], v[132:135], v[60:63]
	ds_read_b128 v[108:111], v16 offset:6144
	v_mfma_f32_16x16x32_f16 v[64:67], v[144:147], v[136:139], v[64:67]
	v_mfma_f32_16x16x32_f16 v[68:71], v[148:151], v[136:139], v[68:71]
	v_mfma_f32_16x16x32_f16 v[72:75], v[152:155], v[136:139], v[72:75]
	s_add_u32 m0, s14, 0xc000
	s_nop 0
	global_load_lds_dwordx4 v2, s[28:29]
	v_mfma_f32_16x16x32_f16 v[76:79], v[156:159], v[136:139], v[76:79]
	v_mfma_f32_16x16x32_f16 v[80:83], v[144:147], v[140:143], v[80:83]
	s_add_u32 m0, s14, 0xe000
	s_nop 0
	global_load_lds_dwordx4 v3, s[28:29]
	v_mfma_f32_16x16x32_f16 v[84:87], v[148:151], v[140:143], v[84:87]
	v_mfma_f32_16x16x32_f16 v[88:91], v[152:155], v[140:143], v[88:91]
	s_add_u32 m0, s14, 0x10000
	s_nop 0
	global_load_lds_dwordx4 v4, s[28:29]
	v_mfma_f32_16x16x32_f16 v[92:95], v[156:159], v[140:143], v[92:95]
	s_waitcnt lgkmcnt(0)
	v_mfma_f32_16x16x32_f16 v[32:35], v[112:115], v[96:99], v[32:35]
	ds_read_b128 v[128:131], v18
	v_mfma_f32_16x16x32_f16 v[36:39], v[116:119], v[96:99], v[36:39]
	ds_read_b128 v[144:147], v19 offset:32768
	v_mfma_f32_16x16x32_f16 v[40:43], v[120:123], v[96:99], v[40:43]
	ds_read_b128 v[148:151], v19 offset:34816
	v_mfma_f32_16x16x32_f16 v[44:47], v[124:127], v[96:99], v[44:47]
	ds_read_b128 v[152:155], v19 offset:36864
	v_mfma_f32_16x16x32_f16 v[48:51], v[112:115], v[100:103], v[48:51]
	ds_read_b128 v[156:159], v19 offset:38912
	v_mfma_f32_16x16x32_f16 v[52:55], v[116:119], v[100:103], v[52:55]
	ds_read_b128 v[132:135], v18 offset:2048
	v_mfma_f32_16x16x32_f16 v[56:59], v[120:123], v[100:103], v[56:59]
	ds_read_b128 v[136:139], v18 offset:4096
	v_mfma_f32_16x16x32_f16 v[60:63], v[124:127], v[100:103], v[60:63]
	ds_read_b128 v[140:143], v18 offset:6144
	v_mfma_f32_16x16x32_f16 v[64:67], v[112:115], v[104:107], v[64:67]
	v_mfma_f32_16x16x32_f16 v[68:71], v[116:119], v[104:107], v[68:71]
	v_mfma_f32_16x16x32_f16 v[72:75], v[120:123], v[104:107], v[72:75]
	s_add_u32 m0, s14, 0x12000
	s_nop 0
	global_load_lds_dwordx4 v5, s[28:29]
	v_mfma_f32_16x16x32_f16 v[76:79], v[124:127], v[104:107], v[76:79]
	v_mfma_f32_16x16x32_f16 v[80:83], v[112:115], v[108:111], v[80:83]
	s_add_u32 m0, s14, 0x14000
	s_nop 0
	global_load_lds_dwordx4 v6, s[30:31]
	v_mfma_f32_16x16x32_f16 v[84:87], v[116:119], v[108:111], v[84:87]
	v_mfma_f32_16x16x32_f16 v[88:91], v[120:123], v[108:111], v[88:91]
	s_add_u32 m0, s14, 0x16000
	s_nop 0
	global_load_lds_dwordx4 v7, s[30:31]
	v_mfma_f32_16x16x32_f16 v[92:95], v[124:127], v[108:111], v[92:95]
	s_waitcnt vmcnt(6) lgkmcnt(0)
	s_barrier
	s_mov_b64 s[28:29], s[18:19]
	s_mov_b64 s[30:31], s[24:25]
	s_waitcnt lgkmcnt(0)
	v_mfma_f32_16x16x32_f16 v[32:35], v[144:147], v[128:131], v[32:35]
	ds_read_b128 v[96:99], v8
	v_mfma_f32_16x16x32_f16 v[36:39], v[148:151], v[128:131], v[36:39]
	ds_read_b128 v[112:115], v9 offset:32768
	v_mfma_f32_16x16x32_f16 v[40:43], v[152:155], v[128:131], v[40:43]
	ds_read_b128 v[116:119], v9 offset:34816
	v_mfma_f32_16x16x32_f16 v[44:47], v[156:159], v[128:131], v[44:47]
	ds_read_b128 v[120:123], v9 offset:36864
	v_mfma_f32_16x16x32_f16 v[48:51], v[144:147], v[132:135], v[48:51]
	ds_read_b128 v[124:127], v9 offset:38912
	v_mfma_f32_16x16x32_f16 v[52:55], v[148:151], v[132:135], v[52:55]
	ds_read_b128 v[100:103], v8 offset:2048
	v_mfma_f32_16x16x32_f16 v[56:59], v[152:155], v[132:135], v[56:59]
	ds_read_b128 v[104:107], v8 offset:4096
	v_mfma_f32_16x16x32_f16 v[60:63], v[156:159], v[132:135], v[60:63]
	ds_read_b128 v[108:111], v8 offset:6144
	v_mfma_f32_16x16x32_f16 v[64:67], v[144:147], v[136:139], v[64:67]
	v_mfma_f32_16x16x32_f16 v[68:71], v[148:151], v[136:139], v[68:71]
	v_mfma_f32_16x16x32_f16 v[72:75], v[152:155], v[136:139], v[72:75]
	s_add_u32 m0, s14, 0x18000
	s_nop 0
	global_load_lds_dwordx4 v2, s[28:29]
	v_mfma_f32_16x16x32_f16 v[76:79], v[156:159], v[136:139], v[76:79]
	v_mfma_f32_16x16x32_f16 v[80:83], v[144:147], v[140:143], v[80:83]
	s_add_u32 m0, s14, 0x1a000
	s_nop 0
	global_load_lds_dwordx4 v3, s[28:29]
	v_mfma_f32_16x16x32_f16 v[84:87], v[148:151], v[140:143], v[84:87]
	v_mfma_f32_16x16x32_f16 v[88:91], v[152:155], v[140:143], v[88:91]
	s_add_u32 m0, s14, 0x1c000
	s_nop 0
	global_load_lds_dwordx4 v4, s[28:29]
	v_mfma_f32_16x16x32_f16 v[92:95], v[156:159], v[140:143], v[92:95]
	s_waitcnt lgkmcnt(0)
	v_mfma_f32_16x16x32_f16 v[32:35], v[112:115], v[96:99], v[32:35]
	ds_read_b128 v[128:131], v10
	v_mfma_f32_16x16x32_f16 v[36:39], v[116:119], v[96:99], v[36:39]
	ds_read_b128 v[144:147], v11 offset:32768
	v_mfma_f32_16x16x32_f16 v[40:43], v[120:123], v[96:99], v[40:43]
	ds_read_b128 v[148:151], v11 offset:34816
	v_mfma_f32_16x16x32_f16 v[44:47], v[124:127], v[96:99], v[44:47]
	ds_read_b128 v[152:155], v11 offset:36864
	v_mfma_f32_16x16x32_f16 v[48:51], v[112:115], v[100:103], v[48:51]
	ds_read_b128 v[156:159], v11 offset:38912
	v_mfma_f32_16x16x32_f16 v[52:55], v[116:119], v[100:103], v[52:55]
	ds_read_b128 v[132:135], v10 offset:2048
	v_mfma_f32_16x16x32_f16 v[56:59], v[120:123], v[100:103], v[56:59]
	ds_read_b128 v[136:139], v10 offset:4096
	v_mfma_f32_16x16x32_f16 v[60:63], v[124:127], v[100:103], v[60:63]
	ds_read_b128 v[140:143], v10 offset:6144
	v_mfma_f32_16x16x32_f16 v[64:67], v[112:115], v[104:107], v[64:67]
	v_mfma_f32_16x16x32_f16 v[68:71], v[116:119], v[104:107], v[68:71]
	v_mfma_f32_16x16x32_f16 v[72:75], v[120:123], v[104:107], v[72:75]
	s_add_u32 m0, s14, 0x1e000
	s_nop 0
	global_load_lds_dwordx4 v5, s[28:29]
	v_mfma_f32_16x16x32_f16 v[76:79], v[124:127], v[104:107], v[76:79]
	v_mfma_f32_16x16x32_f16 v[80:83], v[112:115], v[108:111], v[80:83]
	s_add_u32 m0, s14, 0x20000
	s_nop 0
	global_load_lds_dwordx4 v6, s[30:31]
	v_mfma_f32_16x16x32_f16 v[84:87], v[116:119], v[108:111], v[84:87]
	v_mfma_f32_16x16x32_f16 v[88:91], v[120:123], v[108:111], v[88:91]
	s_add_u32 m0, s14, 0x22000
	s_nop 0
	global_load_lds_dwordx4 v7, s[30:31]
	v_mfma_f32_16x16x32_f16 v[92:95], v[124:127], v[108:111], v[92:95]
	s_waitcnt vmcnt(6) lgkmcnt(0)
	s_barrier
	s_add_u32 s28, s28, 0x80
	s_addc_u32 s29, s29, 0
	s_add_u32 s30, s30, 0x80
	s_addc_u32 s31, s31, 0
	s_waitcnt lgkmcnt(0)
	v_mfma_f32_16x16x32_f16 v[32:35], v[144:147], v[128:131], v[32:35]
	ds_read_b128 v[96:99], v12
	v_mfma_f32_16x16x32_f16 v[36:39], v[148:151], v[128:131], v[36:39]
	ds_read_b128 v[112:115], v13 offset:32768
	v_mfma_f32_16x16x32_f16 v[40:43], v[152:155], v[128:131], v[40:43]
	ds_read_b128 v[116:119], v13 offset:34816
	v_mfma_f32_16x16x32_f16 v[44:47], v[156:159], v[128:131], v[44:47]
	ds_read_b128 v[120:123], v13 offset:36864
	v_mfma_f32_16x16x32_f16 v[48:51], v[144:147], v[132:135], v[48:51]
	ds_read_b128 v[124:127], v13 offset:38912
	v_mfma_f32_16x16x32_f16 v[52:55], v[148:151], v[132:135], v[52:55]
	ds_read_b128 v[100:103], v12 offset:2048
	v_mfma_f32_16x16x32_f16 v[56:59], v[152:155], v[132:135], v[56:59]
	ds_read_b128 v[104:107], v12 offset:4096
	v_mfma_f32_16x16x32_f16 v[60:63], v[156:159], v[132:135], v[60:63]
	ds_read_b128 v[108:111], v12 offset:6144
	v_mfma_f32_16x16x32_f16 v[64:67], v[144:147], v[136:139], v[64:67]
	v_mfma_f32_16x16x32_f16 v[68:71], v[148:151], v[136:139], v[68:71]
	v_mfma_f32_16x16x32_f16 v[72:75], v[152:155], v[136:139], v[72:75]
	s_add_u32 m0, s14, 0x0
	s_nop 0
	global_load_lds_dwordx4 v2, s[28:29]
	v_mfma_f32_16x16x32_f16 v[76:79], v[156:159], v[136:139], v[76:79]
	v_mfma_f32_16x16x32_f16 v[80:83], v[144:147], v[140:143], v[80:83]
	s_add_u32 m0, s14, 0x2000
	s_nop 0
	global_load_lds_dwordx4 v3, s[28:29]
	v_mfma_f32_16x16x32_f16 v[84:87], v[148:151], v[140:143], v[84:87]
	v_mfma_f32_16x16x32_f16 v[88:91], v[152:155], v[140:143], v[88:91]
	s_add_u32 m0, s14, 0x4000
	s_nop 0
	global_load_lds_dwordx4 v4, s[28:29]
	v_mfma_f32_16x16x32_f16 v[92:95], v[156:159], v[140:143], v[92:95]
	s_waitcnt lgkmcnt(0)
	v_mfma_f32_16x16x32_f16 v[32:35], v[112:115], v[96:99], v[32:35]
	ds_read_b128 v[128:131], v14
	v_mfma_f32_16x16x32_f16 v[36:39], v[116:119], v[96:99], v[36:39]
	ds_read_b128 v[144:147], v15 offset:32768
	v_mfma_f32_16x16x32_f16 v[40:43], v[120:123], v[96:99], v[40:43]
	ds_read_b128 v[148:151], v15 offset:34816
	v_mfma_f32_16x16x32_f16 v[44:47], v[124:127], v[96:99], v[44:47]
	ds_read_b128 v[152:155], v15 offset:36864
	v_mfma_f32_16x16x32_f16 v[48:51], v[112:115], v[100:103], v[48:51]
	ds_read_b128 v[156:159], v15 offset:38912
	v_mfma_f32_16x16x32_f16 v[52:55], v[116:119], v[100:103], v[52:55]
	ds_read_b128 v[132:135], v14 offset:2048
	v_mfma_f32_16x16x32_f16 v[56:59], v[120:123], v[100:103], v[56:59]
	ds_read_b128 v[136:139], v14 offset:4096
	v_mfma_f32_16x16x32_f16 v[60:63], v[124:127], v[100:103], v[60:63]
	ds_read_b128 v[140:143], v14 offset:6144
	v_mfma_f32_16x16x32_f16 v[64:67], v[112:115], v[104:107], v[64:67]
	v_mfma_f32_16x16x32_f16 v[68:71], v[116:119], v[104:107], v[68:71]
	v_mfma_f32_16x16x32_f16 v[72:75], v[120:123], v[104:107], v[72:75]
	s_add_u32 m0, s14, 0x6000
	s_nop 0
	global_load_lds_dwordx4 v5, s[28:29]
	v_mfma_f32_16x16x32_f16 v[76:79], v[124:127], v[104:107], v[76:79]
	v_mfma_f32_16x16x32_f16 v[80:83], v[112:115], v[108:111], v[80:83]
	s_add_u32 m0, s14, 0x8000
	s_nop 0
	global_load_lds_dwordx4 v6, s[30:31]
	v_mfma_f32_16x16x32_f16 v[84:87], v[116:119], v[108:111], v[84:87]
	v_mfma_f32_16x16x32_f16 v[88:91], v[120:123], v[108:111], v[88:91]
	s_add_u32 m0, s14, 0xa000
	s_nop 0
	global_load_lds_dwordx4 v7, s[30:31]
	v_mfma_f32_16x16x32_f16 v[92:95], v[124:127], v[108:111], v[92:95]
	s_waitcnt vmcnt(6) lgkmcnt(0)
	s_barrier
	s_add_u32 s28, s28, 0x80
	s_addc_u32 s29, s29, 0
	s_add_u32 s30, s30, 0x80
	s_addc_u32 s31, s31, 0
	s_waitcnt lgkmcnt(0)
	v_mfma_f32_16x16x32_f16 v[32:35], v[144:147], v[128:131], v[32:35]
	ds_read_b128 v[96:99], v16
	v_mfma_f32_16x16x32_f16 v[36:39], v[148:151], v[128:131], v[36:39]
	ds_read_b128 v[112:115], v17 offset:32768
	v_mfma_f32_16x16x32_f16 v[40:43], v[152:155], v[128:131], v[40:43]
	ds_read_b128 v[116:119], v17 offset:34816
	v_mfma_f32_16x16x32_f16 v[44:47], v[156:159], v[128:131], v[44:47]
	ds_read_b128 v[120:123], v17 offset:36864
	v_mfma_f32_16x16x32_f16 v[48:51], v[144:147], v[132:135], v[48:51]
	ds_read_b128 v[124:127], v17 offset:38912
	v_mfma_f32_16x16x32_f16 v[52:55], v[148:151], v[132:135], v[52:55]
	ds_read_b128 v[100:103], v16 offset:2048
	v_mfma_f32_16x16x32_f16 v[56:59], v[152:155], v[132:135], v[56:59]
	ds_read_b128 v[104:107], v16 offset:4096
	v_mfma_f32_16x16x32_f16 v[60:63], v[156:159], v[132:135], v[60:63]
	ds_read_b128 v[108:111], v16 offset:6144
	v_mfma_f32_16x16x32_f16 v[64:67], v[144:147], v[136:139], v[64:67]
	v_mfma_f32_16x16x32_f16 v[68:71], v[148:151], v[136:139], v[68:71]
	v_mfma_f32_16x16x32_f16 v[72:75], v[152:155], v[136:139], v[72:75]
	s_add_u32 m0, s14, 0xc000
	s_nop 0
	global_load_lds_dwordx4 v2, s[28:29]
	v_mfma_f32_16x16x32_f16 v[76:79], v[156:159], v[136:139], v[76:79]
	v_mfma_f32_16x16x32_f16 v[80:83], v[144:147], v[140:143], v[80:83]
	s_add_u32 m0, s14, 0xe000
	s_nop 0
	global_load_lds_dwordx4 v3, s[28:29]
	v_mfma_f32_16x16x32_f16 v[84:87], v[148:151], v[140:143], v[84:87]
	v_mfma_f32_16x16x32_f16 v[88:91], v[152:155], v[140:143], v[88:91]
	s_add_u32 m0, s14, 0x10000
	s_nop 0
	global_load_lds_dwordx4 v4, s[28:29]
	v_mfma_f32_16x16x32_f16 v[92:95], v[156:159], v[140:143], v[92:95]
	s_nop 7
	s_nop 1
	v_mul_f32_e32 v160, s50, v32
	v_mul_f32_e32 v161, s50, v33
	v_mul_f32_e32 v162, s50, v34
	v_mul_f32_e32 v163, s50, v35
	v_mul_f32_e32 v164, s50, v36
	v_mul_f32_e32 v165, s50, v37
	v_mul_f32_e32 v166, s50, v38
	v_mul_f32_e32 v167, s50, v39
	v_mul_f32_e32 v176, 0xbfb8aa3b, v160
	v_mul_f32_e32 v177, 0xbfb8aa3b, v161
	v_mul_f32_e32 v178, 0xbfb8aa3b, v162
	v_mul_f32_e32 v179, 0xbfb8aa3b, v163
	v_mul_f32_e32 v180, 0xbfb8aa3b, v164
	v_mul_f32_e32 v181, 0xbfb8aa3b, v165
	v_mul_f32_e32 v182, 0xbfb8aa3b, v166
	v_mul_f32_e32 v183, 0xbfb8aa3b, v167
	v_exp_f32_e32 v176, v176
	v_exp_f32_e32 v177, v177
	v_exp_f32_e32 v178, v178
	v_exp_f32_e32 v179, v179
	v_exp_f32_e32 v180, v180
	v_exp_f32_e32 v181, v181
	v_exp_f32_e32 v182, v182
	v_exp_f32_e32 v183, v183
	v_add_f32_e32 v176, 1.0, v176
	v_add_f32_e32 v177, 1.0, v177
	v_add_f32_e32 v178, 1.0, v178
	v_add_f32_e32 v179, 1.0, v179
	v_add_f32_e32 v180, 1.0, v180
	v_add_f32_e32 v181, 1.0, v181
	v_add_f32_e32 v182, 1.0, v182
	v_add_f32_e32 v183, 1.0, v183
	v_rcp_f32_e32 v176, v176
	v_rcp_f32_e32 v177, v177
	v_rcp_f32_e32 v178, v178
	v_rcp_f32_e32 v179, v179
	v_rcp_f32_e32 v180, v180
	v_rcp_f32_e32 v181, v181
	v_rcp_f32_e32 v182, v182
	v_rcp_f32_e32 v183, v183
	v_mul_f32_e32 v160, v160, v176
	v_mul_f32_e32 v161, v161, v177
	v_mul_f32_e32 v162, v162, v178
	v_mul_f32_e32 v163, v163, v179
	v_mul_f32_e32 v164, v164, v180
	v_mul_f32_e32 v165, v165, v181
	v_mul_f32_e32 v166, v166, v182
	v_mul_f32_e32 v167, v167, v183
	v_cvt_pk_f16_f32 v168, v160, v161
	v_cvt_pk_f16_f32 v169, v162, v163
	v_cvt_pk_f16_f32 v170, v164, v165
	v_cvt_pk_f16_f32 v171, v166, v167
	global_store_dwordx4 v20, v[168:171], s[32:33] offset:256
	v_mul_f32_e32 v160, s50, v40
	v_mul_f32_e32 v161, s50, v41
	v_mul_f32_e32 v162, s50, v42
	v_mul_f32_e32 v163, s50, v43
	v_mul_f32_e32 v164, s50, v44
	v_mul_f32_e32 v165, s50, v45
	v_mul_f32_e32 v166, s50, v46
	v_mul_f32_e32 v167, s50, v47
	v_mul_f32_e32 v176, 0xbfb8aa3b, v160
	v_mul_f32_e32 v177, 0xbfb8aa3b, v161
	v_mul_f32_e32 v178, 0xbfb8aa3b, v162
	v_mul_f32_e32 v179, 0xbfb8aa3b, v163
	v_mul_f32_e32 v180, 0xbfb8aa3b, v164
	v_mul_f32_e32 v181, 0xbfb8aa3b, v165
	v_mul_f32_e32 v182, 0xbfb8aa3b, v166
	v_mul_f32_e32 v183, 0xbfb8aa3b, v167
	v_exp_f32_e32 v176, v176
	v_exp_f32_e32 v177, v177
	v_exp_f32_e32 v178, v178
	v_exp_f32_e32 v179, v179
	v_exp_f32_e32 v180, v180
	v_exp_f32_e32 v181, v181
	v_exp_f32_e32 v182, v182
	v_exp_f32_e32 v183, v183
	v_add_f32_e32 v176, 1.0, v176
	v_add_f32_e32 v177, 1.0, v177
	v_add_f32_e32 v178, 1.0, v178
	v_add_f32_e32 v179, 1.0, v179
	v_add_f32_e32 v180, 1.0, v180
	v_add_f32_e32 v181, 1.0, v181
	v_add_f32_e32 v182, 1.0, v182
	v_add_f32_e32 v183, 1.0, v183
	v_rcp_f32_e32 v176, v176
	v_rcp_f32_e32 v177, v177
	v_rcp_f32_e32 v178, v178
	v_rcp_f32_e32 v179, v179
	v_rcp_f32_e32 v180, v180
	v_rcp_f32_e32 v181, v181
	v_rcp_f32_e32 v182, v182
	v_rcp_f32_e32 v183, v183
	v_mul_f32_e32 v160, v160, v176
	v_mul_f32_e32 v161, v161, v177
	v_mul_f32_e32 v162, v162, v178
	v_mul_f32_e32 v163, v163, v179
	v_mul_f32_e32 v164, v164, v180
	v_mul_f32_e32 v165, v165, v181
	v_mul_f32_e32 v166, v166, v182
	v_mul_f32_e32 v167, v167, v183
	v_cvt_pk_f16_f32 v172, v160, v161
	v_cvt_pk_f16_f32 v173, v162, v163
	v_cvt_pk_f16_f32 v174, v164, v165
	v_cvt_pk_f16_f32 v175, v166, v167
	global_store_dwordx4 v20, v[172:175], s[32:33] offset:320
	v_mul_f32_e32 v160, s50, v48
	v_mul_f32_e32 v161, s50, v49
	v_mul_f32_e32 v162, s50, v50
	v_mul_f32_e32 v163, s50, v51
	v_mul_f32_e32 v164, s50, v52
	v_mul_f32_e32 v165, s50, v53
	v_mul_f32_e32 v166, s50, v54
	v_mul_f32_e32 v167, s50, v55
	v_mul_f32_e32 v176, 0xbfb8aa3b, v160
	v_mul_f32_e32 v177, 0xbfb8aa3b, v161
	v_mul_f32_e32 v178, 0xbfb8aa3b, v162
	v_mul_f32_e32 v179, 0xbfb8aa3b, v163
	v_mul_f32_e32 v180, 0xbfb8aa3b, v164
	v_mul_f32_e32 v181, 0xbfb8aa3b, v165
	v_mul_f32_e32 v182, 0xbfb8aa3b, v166
	v_mul_f32_e32 v183, 0xbfb8aa3b, v167
	v_exp_f32_e32 v176, v176
	v_exp_f32_e32 v177, v177
	v_exp_f32_e32 v178, v178
	v_exp_f32_e32 v179, v179
	v_exp_f32_e32 v180, v180
	v_exp_f32_e32 v181, v181
	v_exp_f32_e32 v182, v182
	v_exp_f32_e32 v183, v183
	v_add_f32_e32 v176, 1.0, v176
	v_add_f32_e32 v177, 1.0, v177
	v_add_f32_e32 v178, 1.0, v178
	v_add_f32_e32 v179, 1.0, v179
	v_add_f32_e32 v180, 1.0, v180
	v_add_f32_e32 v181, 1.0, v181
	v_add_f32_e32 v182, 1.0, v182
	v_add_f32_e32 v183, 1.0, v183
	v_rcp_f32_e32 v176, v176
	v_rcp_f32_e32 v177, v177
	v_rcp_f32_e32 v178, v178
	v_rcp_f32_e32 v179, v179
	v_rcp_f32_e32 v180, v180
	v_rcp_f32_e32 v181, v181
	v_rcp_f32_e32 v182, v182
	v_rcp_f32_e32 v183, v183
	v_mul_f32_e32 v160, v160, v176
	v_mul_f32_e32 v161, v161, v177
	v_mul_f32_e32 v162, v162, v178
	v_mul_f32_e32 v163, v163, v179
	v_mul_f32_e32 v164, v164, v180
	v_mul_f32_e32 v165, v165, v181
	v_mul_f32_e32 v166, v166, v182
	v_mul_f32_e32 v167, v167, v183
	v_cvt_pk_f16_f32 v168, v160, v161
	v_cvt_pk_f16_f32 v169, v162, v163
	v_cvt_pk_f16_f32 v170, v164, v165
	v_cvt_pk_f16_f32 v171, v166, v167
	global_store_dwordx4 v21, v[168:171], s[32:33] offset:256
	v_mul_f32_e32 v160, s50, v56
	v_mul_f32_e32 v161, s50, v57
	v_mul_f32_e32 v162, s50, v58
	v_mul_f32_e32 v163, s50, v59
	v_mul_f32_e32 v164, s50, v60
	v_mul_f32_e32 v165, s50, v61
	v_mul_f32_e32 v166, s50, v62
	v_mul_f32_e32 v167, s50, v63
	v_mul_f32_e32 v176, 0xbfb8aa3b, v160
	v_mul_f32_e32 v177, 0xbfb8aa3b, v161
	v_mul_f32_e32 v178, 0xbfb8aa3b, v162
	v_mul_f32_e32 v179, 0xbfb8aa3b, v163
	v_mul_f32_e32 v180, 0xbfb8aa3b, v164
	v_mul_f32_e32 v181, 0xbfb8aa3b, v165
	v_mul_f32_e32 v182, 0xbfb8aa3b, v166
	v_mul_f32_e32 v183, 0xbfb8aa3b, v167
	v_exp_f32_e32 v176, v176
	v_exp_f32_e32 v177, v177
	v_exp_f32_e32 v178, v178
	v_exp_f32_e32 v179, v179
	v_exp_f32_e32 v180, v180
	v_exp_f32_e32 v181, v181
	v_exp_f32_e32 v182, v182
	v_exp_f32_e32 v183, v183
	v_add_f32_e32 v176, 1.0, v176
	v_add_f32_e32 v177, 1.0, v177
	v_add_f32_e32 v178, 1.0, v178
	v_add_f32_e32 v179, 1.0, v179
	v_add_f32_e32 v180, 1.0, v180
	v_add_f32_e32 v181, 1.0, v181
	v_add_f32_e32 v182, 1.0, v182
	v_add_f32_e32 v183, 1.0, v183
	v_rcp_f32_e32 v176, v176
	v_rcp_f32_e32 v177, v177
	v_rcp_f32_e32 v178, v178
	v_rcp_f32_e32 v179, v179
	v_rcp_f32_e32 v180, v180
	v_rcp_f32_e32 v181, v181
	v_rcp_f32_e32 v182, v182
	v_rcp_f32_e32 v183, v183
	v_mul_f32_e32 v160, v160, v176
	v_mul_f32_e32 v161, v161, v177
	v_mul_f32_e32 v162, v162, v178
	v_mul_f32_e32 v163, v163, v179
	v_mul_f32_e32 v164, v164, v180
	v_mul_f32_e32 v165, v165, v181
	v_mul_f32_e32 v166, v166, v182
	v_mul_f32_e32 v167, v167, v183
	v_cvt_pk_f16_f32 v172, v160, v161
	v_cvt_pk_f16_f32 v173, v162, v163
	v_cvt_pk_f16_f32 v174, v164, v165
	v_cvt_pk_f16_f32 v175, v166, v167
	global_store_dwordx4 v21, v[172:175], s[32:33] offset:320
	v_mul_f32_e32 v160, s50, v64
	v_mul_f32_e32 v161, s50, v65
	v_mul_f32_e32 v162, s50, v66
	v_mul_f32_e32 v163, s50, v67
	v_mul_f32_e32 v164, s50, v68
	v_mul_f32_e32 v165, s50, v69
	v_mul_f32_e32 v166, s50, v70
	v_mul_f32_e32 v167, s50, v71
	v_mul_f32_e32 v176, 0xbfb8aa3b, v160
	v_mul_f32_e32 v177, 0xbfb8aa3b, v161
	v_mul_f32_e32 v178, 0xbfb8aa3b, v162
	v_mul_f32_e32 v179, 0xbfb8aa3b, v163
	v_mul_f32_e32 v180, 0xbfb8aa3b, v164
	v_mul_f32_e32 v181, 0xbfb8aa3b, v165
	v_mul_f32_e32 v182, 0xbfb8aa3b, v166
	v_mul_f32_e32 v183, 0xbfb8aa3b, v167
	v_exp_f32_e32 v176, v176
	v_exp_f32_e32 v177, v177
	v_exp_f32_e32 v178, v178
	v_exp_f32_e32 v179, v179
	v_exp_f32_e32 v180, v180
	v_exp_f32_e32 v181, v181
	v_exp_f32_e32 v182, v182
	v_exp_f32_e32 v183, v183
	v_add_f32_e32 v176, 1.0, v176
	v_add_f32_e32 v177, 1.0, v177
	v_add_f32_e32 v178, 1.0, v178
	v_add_f32_e32 v179, 1.0, v179
	v_add_f32_e32 v180, 1.0, v180
	v_add_f32_e32 v181, 1.0, v181
	v_add_f32_e32 v182, 1.0, v182
	v_add_f32_e32 v183, 1.0, v183
	v_rcp_f32_e32 v176, v176
	v_rcp_f32_e32 v177, v177
	v_rcp_f32_e32 v178, v178
	v_rcp_f32_e32 v179, v179
	v_rcp_f32_e32 v180, v180
	v_rcp_f32_e32 v181, v181
	v_rcp_f32_e32 v182, v182
	v_rcp_f32_e32 v183, v183
	v_mul_f32_e32 v160, v160, v176
	v_mul_f32_e32 v161, v161, v177
	v_mul_f32_e32 v162, v162, v178
	v_mul_f32_e32 v163, v163, v179
	v_mul_f32_e32 v164, v164, v180
	v_mul_f32_e32 v165, v165, v181
	v_mul_f32_e32 v166, v166, v182
	v_mul_f32_e32 v167, v167, v183
	v_cvt_pk_f16_f32 v168, v160, v161
	v_cvt_pk_f16_f32 v169, v162, v163
	v_cvt_pk_f16_f32 v170, v164, v165
	v_cvt_pk_f16_f32 v171, v166, v167
	global_store_dwordx4 v22, v[168:171], s[32:33] offset:256
	v_mul_f32_e32 v160, s50, v72
	v_mul_f32_e32 v161, s50, v73
	v_mul_f32_e32 v162, s50, v74
	v_mul_f32_e32 v163, s50, v75
	v_mul_f32_e32 v164, s50, v76
	v_mul_f32_e32 v165, s50, v77
	v_mul_f32_e32 v166, s50, v78
	v_mul_f32_e32 v167, s50, v79
	v_mul_f32_e32 v176, 0xbfb8aa3b, v160
	v_mul_f32_e32 v177, 0xbfb8aa3b, v161
	v_mul_f32_e32 v178, 0xbfb8aa3b, v162
	v_mul_f32_e32 v179, 0xbfb8aa3b, v163
	v_mul_f32_e32 v180, 0xbfb8aa3b, v164
	v_mul_f32_e32 v181, 0xbfb8aa3b, v165
	v_mul_f32_e32 v182, 0xbfb8aa3b, v166
	v_mul_f32_e32 v183, 0xbfb8aa3b, v167
	v_exp_f32_e32 v176, v176
	v_exp_f32_e32 v177, v177
	v_exp_f32_e32 v178, v178
	v_exp_f32_e32 v179, v179
	v_exp_f32_e32 v180, v180
	v_exp_f32_e32 v181, v181
	v_exp_f32_e32 v182, v182
	v_exp_f32_e32 v183, v183
	v_add_f32_e32 v176, 1.0, v176
	v_add_f32_e32 v177, 1.0, v177
	v_add_f32_e32 v178, 1.0, v178
	v_add_f32_e32 v179, 1.0, v179
	v_add_f32_e32 v180, 1.0, v180
	v_add_f32_e32 v181, 1.0, v181
	v_add_f32_e32 v182, 1.0, v182
	v_add_f32_e32 v183, 1.0, v183
	v_rcp_f32_e32 v176, v176
	v_rcp_f32_e32 v177, v177
	v_rcp_f32_e32 v178, v178
	v_rcp_f32_e32 v179, v179
	v_rcp_f32_e32 v180, v180
	v_rcp_f32_e32 v181, v181
	v_rcp_f32_e32 v182, v182
	v_rcp_f32_e32 v183, v183
	v_mul_f32_e32 v160, v160, v176
	v_mul_f32_e32 v161, v161, v177
	v_mul_f32_e32 v162, v162, v178
	v_mul_f32_e32 v163, v163, v179
	v_mul_f32_e32 v164, v164, v180
	v_mul_f32_e32 v165, v165, v181
	v_mul_f32_e32 v166, v166, v182
	v_mul_f32_e32 v167, v167, v183
	v_cvt_pk_f16_f32 v172, v160, v161
	v_cvt_pk_f16_f32 v173, v162, v163
	v_cvt_pk_f16_f32 v174, v164, v165
	v_cvt_pk_f16_f32 v175, v166, v167
	global_store_dwordx4 v22, v[172:175], s[32:33] offset:320
	v_mul_f32_e32 v160, s50, v80
	v_mul_f32_e32 v161, s50, v81
	v_mul_f32_e32 v162, s50, v82
	v_mul_f32_e32 v163, s50, v83
	v_mul_f32_e32 v164, s50, v84
	v_mul_f32_e32 v165, s50, v85
	v_mul_f32_e32 v166, s50, v86
	v_mul_f32_e32 v167, s50, v87
	v_mul_f32_e32 v176, 0xbfb8aa3b, v160
	v_mul_f32_e32 v177, 0xbfb8aa3b, v161
	v_mul_f32_e32 v178, 0xbfb8aa3b, v162
	v_mul_f32_e32 v179, 0xbfb8aa3b, v163
	v_mul_f32_e32 v180, 0xbfb8aa3b, v164
	v_mul_f32_e32 v181, 0xbfb8aa3b, v165
	v_mul_f32_e32 v182, 0xbfb8aa3b, v166
	v_mul_f32_e32 v183, 0xbfb8aa3b, v167
	v_exp_f32_e32 v176, v176
	v_exp_f32_e32 v177, v177
	v_exp_f32_e32 v178, v178
	v_exp_f32_e32 v179, v179
	v_exp_f32_e32 v180, v180
	v_exp_f32_e32 v181, v181
	v_exp_f32_e32 v182, v182
	v_exp_f32_e32 v183, v183
	v_add_f32_e32 v176, 1.0, v176
	v_add_f32_e32 v177, 1.0, v177
	v_add_f32_e32 v178, 1.0, v178
	v_add_f32_e32 v179, 1.0, v179
	v_add_f32_e32 v180, 1.0, v180
	v_add_f32_e32 v181, 1.0, v181
	v_add_f32_e32 v182, 1.0, v182
	v_add_f32_e32 v183, 1.0, v183
	v_rcp_f32_e32 v176, v176
	v_rcp_f32_e32 v177, v177
	v_rcp_f32_e32 v178, v178
	v_rcp_f32_e32 v179, v179
	v_rcp_f32_e32 v180, v180
	v_rcp_f32_e32 v181, v181
	v_rcp_f32_e32 v182, v182
	v_rcp_f32_e32 v183, v183
	v_mul_f32_e32 v160, v160, v176
	v_mul_f32_e32 v161, v161, v177
	v_mul_f32_e32 v162, v162, v178
	v_mul_f32_e32 v163, v163, v179
	v_mul_f32_e32 v164, v164, v180
	v_mul_f32_e32 v165, v165, v181
	v_mul_f32_e32 v166, v166, v182
	v_mul_f32_e32 v167, v167, v183
	v_cvt_pk_f16_f32 v168, v160, v161
	v_cvt_pk_f16_f32 v169, v162, v163
	v_cvt_pk_f16_f32 v170, v164, v165
	v_cvt_pk_f16_f32 v171, v166, v167
	global_store_dwordx4 v23, v[168:171], s[32:33] offset:256
	v_mul_f32_e32 v160, s50, v88
	v_mul_f32_e32 v161, s50, v89
	v_mul_f32_e32 v162, s50, v90
	v_mul_f32_e32 v163, s50, v91
	v_mul_f32_e32 v164, s50, v92
	v_mul_f32_e32 v165, s50, v93
	v_mul_f32_e32 v166, s50, v94
	v_mul_f32_e32 v167, s50, v95
	v_mul_f32_e32 v176, 0xbfb8aa3b, v160
	v_mul_f32_e32 v177, 0xbfb8aa3b, v161
	v_mul_f32_e32 v178, 0xbfb8aa3b, v162
	v_mul_f32_e32 v179, 0xbfb8aa3b, v163
	v_mul_f32_e32 v180, 0xbfb8aa3b, v164
	v_mul_f32_e32 v181, 0xbfb8aa3b, v165
	v_mul_f32_e32 v182, 0xbfb8aa3b, v166
	v_mul_f32_e32 v183, 0xbfb8aa3b, v167
	v_exp_f32_e32 v176, v176
	v_exp_f32_e32 v177, v177
	v_exp_f32_e32 v178, v178
	v_exp_f32_e32 v179, v179
	v_exp_f32_e32 v180, v180
	v_exp_f32_e32 v181, v181
	v_exp_f32_e32 v182, v182
	v_exp_f32_e32 v183, v183
	v_add_f32_e32 v176, 1.0, v176
	v_add_f32_e32 v177, 1.0, v177
	v_add_f32_e32 v178, 1.0, v178
	v_add_f32_e32 v179, 1.0, v179
	v_add_f32_e32 v180, 1.0, v180
	v_add_f32_e32 v181, 1.0, v181
	v_add_f32_e32 v182, 1.0, v182
	v_add_f32_e32 v183, 1.0, v183
	v_rcp_f32_e32 v176, v176
	v_rcp_f32_e32 v177, v177
	v_rcp_f32_e32 v178, v178
	v_rcp_f32_e32 v179, v179
	v_rcp_f32_e32 v180, v180
	v_rcp_f32_e32 v181, v181
	v_rcp_f32_e32 v182, v182
	v_rcp_f32_e32 v183, v183
	v_mul_f32_e32 v160, v160, v176
	v_mul_f32_e32 v161, v161, v177
	v_mul_f32_e32 v162, v162, v178
	v_mul_f32_e32 v163, v163, v179
	v_mul_f32_e32 v164, v164, v180
	v_mul_f32_e32 v165, v165, v181
	v_mul_f32_e32 v166, v166, v182
	v_mul_f32_e32 v167, v167, v183
	v_cvt_pk_f16_f32 v172, v160, v161
	v_cvt_pk_f16_f32 v173, v162, v163
	v_cvt_pk_f16_f32 v174, v164, v165
	v_cvt_pk_f16_f32 v175, v166, v167
	global_store_dwordx4 v23, v[172:175], s[32:33] offset:320
	s_waitcnt lgkmcnt(0)
	v_mfma_f32_16x16x32_f16 v[32:35], v[112:115], v[96:99], 0
	ds_read_b128 v[128:131], v18
	v_mfma_f32_16x16x32_f16 v[36:39], v[116:119], v[96:99], 0
	ds_read_b128 v[144:147], v19 offset:32768
	v_mfma_f32_16x16x32_f16 v[40:43], v[120:123], v[96:99], 0
	ds_read_b128 v[148:151], v19 offset:34816
	v_mfma_f32_16x16x32_f16 v[44:47], v[124:127], v[96:99], 0
	ds_read_b128 v[152:155], v19 offset:36864
	v_mfma_f32_16x16x32_f16 v[48:51], v[112:115], v[100:103], 0
	ds_read_b128 v[156:159], v19 offset:38912
	v_mfma_f32_16x16x32_f16 v[52:55], v[116:119], v[100:103], 0
	ds_read_b128 v[132:135], v18 offset:2048
	v_mfma_f32_16x16x32_f16 v[56:59], v[120:123], v[100:103], 0
	ds_read_b128 v[136:139], v18 offset:4096
	v_mfma_f32_16x16x32_f16 v[60:63], v[124:127], v[100:103], 0
	ds_read_b128 v[140:143], v18 offset:6144
	v_mfma_f32_16x16x32_f16 v[64:67], v[112:115], v[104:107], 0
	v_mfma_f32_16x16x32_f16 v[68:71], v[116:119], v[104:107], 0
	v_mfma_f32_16x16x32_f16 v[72:75], v[120:123], v[104:107], 0
	s_add_u32 m0, s14, 0x12000
	s_nop 0
	global_load_lds_dwordx4 v5, s[28:29]
	v_mfma_f32_16x16x32_f16 v[76:79], v[124:127], v[104:107], 0
	v_mfma_f32_16x16x32_f16 v[80:83], v[112:115], v[108:111], 0
	s_add_u32 m0, s14, 0x14000
	s_nop 0
	global_load_lds_dwordx4 v6, s[30:31]
	v_mfma_f32_16x16x32_f16 v[84:87], v[116:119], v[108:111], 0
	v_mfma_f32_16x16x32_f16 v[88:91], v[120:123], v[108:111], 0
	s_add_u32 m0, s14, 0x16000
	s_nop 0
	global_load_lds_dwordx4 v7, s[30:31]
	v_mfma_f32_16x16x32_f16 v[92:95], v[124:127], v[108:111], 0
	s_waitcnt vmcnt(14) lgkmcnt(0)
	s_barrier
	s_add_u32 s28, s28, 0x80
	s_addc_u32 s29, s29, 0
	s_add_u32 s30, s30, 0x80
	s_addc_u32 s31, s31, 0
	s_waitcnt lgkmcnt(0)
	v_mfma_f32_16x16x32_f16 v[32:35], v[144:147], v[128:131], v[32:35]
	ds_read_b128 v[96:99], v8
	v_mfma_f32_16x16x32_f16 v[36:39], v[148:151], v[128:131], v[36:39]
	ds_read_b128 v[112:115], v9 offset:32768
	v_mfma_f32_16x16x32_f16 v[40:43], v[152:155], v[128:131], v[40:43]
	ds_read_b128 v[116:119], v9 offset:34816
	v_mfma_f32_16x16x32_f16 v[44:47], v[156:159], v[128:131], v[44:47]
	ds_read_b128 v[120:123], v9 offset:36864
	v_mfma_f32_16x16x32_f16 v[48:51], v[144:147], v[132:135], v[48:51]
	ds_read_b128 v[124:127], v9 offset:38912
	v_mfma_f32_16x16x32_f16 v[52:55], v[148:151], v[132:135], v[52:55]
	ds_read_b128 v[100:103], v8 offset:2048
	v_mfma_f32_16x16x32_f16 v[56:59], v[152:155], v[132:135], v[56:59]
	ds_read_b128 v[104:107], v8 offset:4096
	v_mfma_f32_16x16x32_f16 v[60:63], v[156:159], v[132:135], v[60:63]
	ds_read_b128 v[108:111], v8 offset:6144
	v_mfma_f32_16x16x32_f16 v[64:67], v[144:147], v[136:139], v[64:67]
	v_mfma_f32_16x16x32_f16 v[68:71], v[148:151], v[136:139], v[68:71]
	v_mfma_f32_16x16x32_f16 v[72:75], v[152:155], v[136:139], v[72:75]
	s_add_u32 m0, s14, 0x18000
	s_nop 0
	global_load_lds_dwordx4 v2, s[28:29]
	v_mfma_f32_16x16x32_f16 v[76:79], v[156:159], v[136:139], v[76:79]
	v_mfma_f32_16x16x32_f16 v[80:83], v[144:147], v[140:143], v[80:83]
	s_add_u32 m0, s14, 0x1a000
	s_nop 0
	global_load_lds_dwordx4 v3, s[28:29]
	v_mfma_f32_16x16x32_f16 v[84:87], v[148:151], v[140:143], v[84:87]
	v_mfma_f32_16x16x32_f16 v[88:91], v[152:155], v[140:143], v[88:91]
	s_add_u32 m0, s14, 0x1c000
	s_nop 0
	global_load_lds_dwordx4 v4, s[28:29]
	v_mfma_f32_16x16x32_f16 v[92:95], v[156:159], v[140:143], v[92:95]
	s_waitcnt lgkmcnt(0)
	v_mfma_f32_16x16x32_f16 v[32:35], v[112:115], v[96:99], v[32:35]
	ds_read_b128 v[128:131], v10
	v_mfma_f32_16x16x32_f16 v[36:39], v[116:119], v[96:99], v[36:39]
	ds_read_b128 v[144:147], v11 offset:32768
	v_mfma_f32_16x16x32_f16 v[40:43], v[120:123], v[96:99], v[40:43]
	ds_read_b128 v[148:151], v11 offset:34816
	v_mfma_f32_16x16x32_f16 v[44:47], v[124:127], v[96:99], v[44:47]
	ds_read_b128 v[152:155], v11 offset:36864
	v_mfma_f32_16x16x32_f16 v[48:51], v[112:115], v[100:103], v[48:51]
	ds_read_b128 v[156:159], v11 offset:38912
	v_mfma_f32_16x16x32_f16 v[52:55], v[116:119], v[100:103], v[52:55]
	ds_read_b128 v[132:135], v10 offset:2048
	v_mfma_f32_16x16x32_f16 v[56:59], v[120:123], v[100:103], v[56:59]
	ds_read_b128 v[136:139], v10 offset:4096
	v_mfma_f32_16x16x32_f16 v[60:63], v[124:127], v[100:103], v[60:63]
	ds_read_b128 v[140:143], v10 offset:6144
	v_mfma_f32_16x16x32_f16 v[64:67], v[112:115], v[104:107], v[64:67]
	v_mfma_f32_16x16x32_f16 v[68:71], v[116:119], v[104:107], v[68:71]
	v_mfma_f32_16x16x32_f16 v[72:75], v[120:123], v[104:107], v[72:75]
	s_add_u32 m0, s14, 0x1e000
	s_nop 0
	global_load_lds_dwordx4 v5, s[28:29]
	v_mfma_f32_16x16x32_f16 v[76:79], v[124:127], v[104:107], v[76:79]
	v_mfma_f32_16x16x32_f16 v[80:83], v[112:115], v[108:111], v[80:83]
	s_add_u32 m0, s14, 0x20000
	s_nop 0
	global_load_lds_dwordx4 v6, s[30:31]
	v_mfma_f32_16x16x32_f16 v[84:87], v[116:119], v[108:111], v[84:87]
	v_mfma_f32_16x16x32_f16 v[88:91], v[120:123], v[108:111], v[88:91]
	s_add_u32 m0, s14, 0x22000
	s_nop 0
	global_load_lds_dwordx4 v7, s[30:31]
	v_mfma_f32_16x16x32_f16 v[92:95], v[124:127], v[108:111], v[92:95]
	s_waitcnt vmcnt(6) lgkmcnt(0)
	s_barrier
	s_add_u32 s28, s28, 0x80
	s_addc_u32 s29, s29, 0
	s_add_u32 s30, s30, 0x80
	s_addc_u32 s31, s31, 0
	s_waitcnt lgkmcnt(0)
	v_mfma_f32_16x16x32_f16 v[32:35], v[144:147], v[128:131], v[32:35]
	ds_read_b128 v[96:99], v12
	v_mfma_f32_16x16x32_f16 v[36:39], v[148:151], v[128:131], v[36:39]
	ds_read_b128 v[112:115], v13 offset:32768
	v_mfma_f32_16x16x32_f16 v[40:43], v[152:155], v[128:131], v[40:43]
	ds_read_b128 v[116:119], v13 offset:34816
	v_mfma_f32_16x16x32_f16 v[44:47], v[156:159], v[128:131], v[44:47]
	ds_read_b128 v[120:123], v13 offset:36864
	v_mfma_f32_16x16x32_f16 v[48:51], v[144:147], v[132:135], v[48:51]
	ds_read_b128 v[124:127], v13 offset:38912
	v_mfma_f32_16x16x32_f16 v[52:55], v[148:151], v[132:135], v[52:55]
	ds_read_b128 v[100:103], v12 offset:2048
	v_mfma_f32_16x16x32_f16 v[56:59], v[152:155], v[132:135], v[56:59]
	ds_read_b128 v[104:107], v12 offset:4096
	v_mfma_f32_16x16x32_f16 v[60:63], v[156:159], v[132:135], v[60:63]
	ds_read_b128 v[108:111], v12 offset:6144
	v_mfma_f32_16x16x32_f16 v[64:67], v[144:147], v[136:139], v[64:67]
	v_mfma_f32_16x16x32_f16 v[68:71], v[148:151], v[136:139], v[68:71]
	v_mfma_f32_16x16x32_f16 v[72:75], v[152:155], v[136:139], v[72:75]
	s_add_u32 m0, s14, 0x0
	s_nop 0
	global_load_lds_dwordx4 v2, s[28:29]
	v_mfma_f32_16x16x32_f16 v[76:79], v[156:159], v[136:139], v[76:79]
	v_mfma_f32_16x16x32_f16 v[80:83], v[144:147], v[140:143], v[80:83]
	s_add_u32 m0, s14, 0x2000
	s_nop 0
	global_load_lds_dwordx4 v3, s[28:29]
	v_mfma_f32_16x16x32_f16 v[84:87], v[148:151], v[140:143], v[84:87]
	v_mfma_f32_16x16x32_f16 v[88:91], v[152:155], v[140:143], v[88:91]
	s_add_u32 m0, s14, 0x4000
	s_nop 0
	global_load_lds_dwordx4 v4, s[28:29]
	v_mfma_f32_16x16x32_f16 v[92:95], v[156:159], v[140:143], v[92:95]
	s_waitcnt lgkmcnt(0)
	v_mfma_f32_16x16x32_f16 v[32:35], v[112:115], v[96:99], v[32:35]
	ds_read_b128 v[128:131], v14
	v_mfma_f32_16x16x32_f16 v[36:39], v[116:119], v[96:99], v[36:39]
	ds_read_b128 v[144:147], v15 offset:32768
	v_mfma_f32_16x16x32_f16 v[40:43], v[120:123], v[96:99], v[40:43]
	ds_read_b128 v[148:151], v15 offset:34816
	v_mfma_f32_16x16x32_f16 v[44:47], v[124:127], v[96:99], v[44:47]
	ds_read_b128 v[152:155], v15 offset:36864
	v_mfma_f32_16x16x32_f16 v[48:51], v[112:115], v[100:103], v[48:51]
	ds_read_b128 v[156:159], v15 offset:38912
	v_mfma_f32_16x16x32_f16 v[52:55], v[116:119], v[100:103], v[52:55]
	ds_read_b128 v[132:135], v14 offset:2048
	v_mfma_f32_16x16x32_f16 v[56:59], v[120:123], v[100:103], v[56:59]
	ds_read_b128 v[136:139], v14 offset:4096
	v_mfma_f32_16x16x32_f16 v[60:63], v[124:127], v[100:103], v[60:63]
	ds_read_b128 v[140:143], v14 offset:6144
	v_mfma_f32_16x16x32_f16 v[64:67], v[112:115], v[104:107], v[64:67]
	v_mfma_f32_16x16x32_f16 v[68:71], v[116:119], v[104:107], v[68:71]
	v_mfma_f32_16x16x32_f16 v[72:75], v[120:123], v[104:107], v[72:75]
	s_add_u32 m0, s14, 0x6000
	s_nop 0
	global_load_lds_dwordx4 v5, s[28:29]
	v_mfma_f32_16x16x32_f16 v[76:79], v[124:127], v[104:107], v[76:79]
	v_mfma_f32_16x16x32_f16 v[80:83], v[112:115], v[108:111], v[80:83]
	s_add_u32 m0, s14, 0x8000
	s_nop 0
	global_load_lds_dwordx4 v6, s[30:31]
	v_mfma_f32_16x16x32_f16 v[84:87], v[116:119], v[108:111], v[84:87]
	v_mfma_f32_16x16x32_f16 v[88:91], v[120:123], v[108:111], v[88:91]
	s_add_u32 m0, s14, 0xa000
	s_nop 0
	global_load_lds_dwordx4 v7, s[30:31]
	v_mfma_f32_16x16x32_f16 v[92:95], v[124:127], v[108:111], v[92:95]
	s_waitcnt vmcnt(6) lgkmcnt(0)
	s_barrier
	s_add_u32 s28, s28, 0x80
	s_addc_u32 s29, s29, 0
	s_add_u32 s30, s30, 0x80
	s_addc_u32 s31, s31, 0
	s_waitcnt lgkmcnt(0)
	v_mfma_f32_16x16x32_f16 v[32:35], v[144:147], v[128:131], v[32:35]
	ds_read_b128 v[96:99], v16
	v_mfma_f32_16x16x32_f16 v[36:39], v[148:151], v[128:131], v[36:39]
	ds_read_b128 v[112:115], v17 offset:32768
	v_mfma_f32_16x16x32_f16 v[40:43], v[152:155], v[128:131], v[40:43]
	ds_read_b128 v[116:119], v17 offset:34816
	v_mfma_f32_16x16x32_f16 v[44:47], v[156:159], v[128:131], v[44:47]
	ds_read_b128 v[120:123], v17 offset:36864
	v_mfma_f32_16x16x32_f16 v[48:51], v[144:147], v[132:135], v[48:51]
	ds_read_b128 v[124:127], v17 offset:38912
	v_mfma_f32_16x16x32_f16 v[52:55], v[148:151], v[132:135], v[52:55]
	ds_read_b128 v[100:103], v16 offset:2048
	v_mfma_f32_16x16x32_f16 v[56:59], v[152:155], v[132:135], v[56:59]
	ds_read_b128 v[104:107], v16 offset:4096
	v_mfma_f32_16x16x32_f16 v[60:63], v[156:159], v[132:135], v[60:63]
	ds_read_b128 v[108:111], v16 offset:6144
	v_mfma_f32_16x16x32_f16 v[64:67], v[144:147], v[136:139], v[64:67]
	v_mfma_f32_16x16x32_f16 v[68:71], v[148:151], v[136:139], v[68:71]
	v_mfma_f32_16x16x32_f16 v[72:75], v[152:155], v[136:139], v[72:75]
	s_add_u32 m0, s14, 0xc000
	s_nop 0
	global_load_lds_dwordx4 v2, s[28:29]
	v_mfma_f32_16x16x32_f16 v[76:79], v[156:159], v[136:139], v[76:79]
	v_mfma_f32_16x16x32_f16 v[80:83], v[144:147], v[140:143], v[80:83]
	s_add_u32 m0, s14, 0xe000
	s_nop 0
	global_load_lds_dwordx4 v3, s[28:29]
	v_mfma_f32_16x16x32_f16 v[84:87], v[148:151], v[140:143], v[84:87]
	v_mfma_f32_16x16x32_f16 v[88:91], v[152:155], v[140:143], v[88:91]
	s_add_u32 m0, s14, 0x10000
	s_nop 0
	global_load_lds_dwordx4 v4, s[28:29]
	v_mfma_f32_16x16x32_f16 v[92:95], v[156:159], v[140:143], v[92:95]
	s_waitcnt lgkmcnt(0)
	v_mfma_f32_16x16x32_f16 v[32:35], v[112:115], v[96:99], v[32:35]
	ds_read_b128 v[128:131], v18
	v_mfma_f32_16x16x32_f16 v[36:39], v[116:119], v[96:99], v[36:39]
	ds_read_b128 v[144:147], v19 offset:32768
	v_mfma_f32_16x16x32_f16 v[40:43], v[120:123], v[96:99], v[40:43]
	ds_read_b128 v[148:151], v19 offset:34816
	v_mfma_f32_16x16x32_f16 v[44:47], v[124:127], v[96:99], v[44:47]
	ds_read_b128 v[152:155], v19 offset:36864
	v_mfma_f32_16x16x32_f16 v[48:51], v[112:115], v[100:103], v[48:51]
	ds_read_b128 v[156:159], v19 offset:38912
	v_mfma_f32_16x16x32_f16 v[52:55], v[116:119], v[100:103], v[52:55]
	ds_read_b128 v[132:135], v18 offset:2048
	v_mfma_f32_16x16x32_f16 v[56:59], v[120:123], v[100:103], v[56:59]
	ds_read_b128 v[136:139], v18 offset:4096
	v_mfma_f32_16x16x32_f16 v[60:63], v[124:127], v[100:103], v[60:63]
	ds_read_b128 v[140:143], v18 offset:6144
	v_mfma_f32_16x16x32_f16 v[64:67], v[112:115], v[104:107], v[64:67]
	v_mfma_f32_16x16x32_f16 v[68:71], v[116:119], v[104:107], v[68:71]
	v_mfma_f32_16x16x32_f16 v[72:75], v[120:123], v[104:107], v[72:75]
	s_add_u32 m0, s14, 0x12000
	s_nop 0
	global_load_lds_dwordx4 v5, s[28:29]
	v_mfma_f32_16x16x32_f16 v[76:79], v[124:127], v[104:107], v[76:79]
	v_mfma_f32_16x16x32_f16 v[80:83], v[112:115], v[108:111], v[80:83]
	s_add_u32 m0, s14, 0x14000
	s_nop 0
	global_load_lds_dwordx4 v6, s[30:31]
	v_mfma_f32_16x16x32_f16 v[84:87], v[116:119], v[108:111], v[84:87]
	v_mfma_f32_16x16x32_f16 v[88:91], v[120:123], v[108:111], v[88:91]
	s_add_u32 m0, s14, 0x16000
	s_nop 0
	global_load_lds_dwordx4 v7, s[30:31]
	v_mfma_f32_16x16x32_f16 v[92:95], v[124:127], v[108:111], v[92:95]
	s_waitcnt vmcnt(6) lgkmcnt(0)
	s_barrier
	s_add_u32 s28, s28, 0x80
	s_addc_u32 s29, s29, 0
	s_add_u32 s30, s30, 0x80
	s_addc_u32 s31, s31, 0
	s_waitcnt lgkmcnt(0)
	v_mfma_f32_16x16x32_f16 v[32:35], v[144:147], v[128:131], v[32:35]
	ds_read_b128 v[96:99], v8
	v_mfma_f32_16x16x32_f16 v[36:39], v[148:151], v[128:131], v[36:39]
	ds_read_b128 v[112:115], v9 offset:32768
	v_mfma_f32_16x16x32_f16 v[40:43], v[152:155], v[128:131], v[40:43]
	ds_read_b128 v[116:119], v9 offset:34816
	v_mfma_f32_16x16x32_f16 v[44:47], v[156:159], v[128:131], v[44:47]
	ds_read_b128 v[120:123], v9 offset:36864
	v_mfma_f32_16x16x32_f16 v[48:51], v[144:147], v[132:135], v[48:51]
	ds_read_b128 v[124:127], v9 offset:38912
	v_mfma_f32_16x16x32_f16 v[52:55], v[148:151], v[132:135], v[52:55]
	ds_read_b128 v[100:103], v8 offset:2048
	v_mfma_f32_16x16x32_f16 v[56:59], v[152:155], v[132:135], v[56:59]
	ds_read_b128 v[104:107], v8 offset:4096
	v_mfma_f32_16x16x32_f16 v[60:63], v[156:159], v[132:135], v[60:63]
	ds_read_b128 v[108:111], v8 offset:6144
	v_mfma_f32_16x16x32_f16 v[64:67], v[144:147], v[136:139], v[64:67]
	v_mfma_f32_16x16x32_f16 v[68:71], v[148:151], v[136:139], v[68:71]
	v_mfma_f32_16x16x32_f16 v[72:75], v[152:155], v[136:139], v[72:75]
	s_add_u32 m0, s14, 0x18000
	s_nop 0
	global_load_lds_dwordx4 v2, s[28:29]
	v_mfma_f32_16x16x32_f16 v[76:79], v[156:159], v[136:139], v[76:79]
	v_mfma_f32_16x16x32_f16 v[80:83], v[144:147], v[140:143], v[80:83]
	s_add_u32 m0, s14, 0x1a000
	s_nop 0
	global_load_lds_dwordx4 v3, s[28:29]
	v_mfma_f32_16x16x32_f16 v[84:87], v[148:151], v[140:143], v[84:87]
	v_mfma_f32_16x16x32_f16 v[88:91], v[152:155], v[140:143], v[88:91]
	s_add_u32 m0, s14, 0x1c000
	s_nop 0
	global_load_lds_dwordx4 v4, s[28:29]
	v_mfma_f32_16x16x32_f16 v[92:95], v[156:159], v[140:143], v[92:95]
	s_waitcnt lgkmcnt(0)
	v_mfma_f32_16x16x32_f16 v[32:35], v[112:115], v[96:99], v[32:35]
	ds_read_b128 v[128:131], v10
	v_mfma_f32_16x16x32_f16 v[36:39], v[116:119], v[96:99], v[36:39]
	ds_read_b128 v[144:147], v11 offset:32768
	v_mfma_f32_16x16x32_f16 v[40:43], v[120:123], v[96:99], v[40:43]
	ds_read_b128 v[148:151], v11 offset:34816
	v_mfma_f32_16x16x32_f16 v[44:47], v[124:127], v[96:99], v[44:47]
	ds_read_b128 v[152:155], v11 offset:36864
	v_mfma_f32_16x16x32_f16 v[48:51], v[112:115], v[100:103], v[48:51]
	ds_read_b128 v[156:159], v11 offset:38912
	v_mfma_f32_16x16x32_f16 v[52:55], v[116:119], v[100:103], v[52:55]
	ds_read_b128 v[132:135], v10 offset:2048
	v_mfma_f32_16x16x32_f16 v[56:59], v[120:123], v[100:103], v[56:59]
	ds_read_b128 v[136:139], v10 offset:4096
	v_mfma_f32_16x16x32_f16 v[60:63], v[124:127], v[100:103], v[60:63]
	ds_read_b128 v[140:143], v10 offset:6144
	v_mfma_f32_16x16x32_f16 v[64:67], v[112:115], v[104:107], v[64:67]
	v_mfma_f32_16x16x32_f16 v[68:71], v[116:119], v[104:107], v[68:71]
	v_mfma_f32_16x16x32_f16 v[72:75], v[120:123], v[104:107], v[72:75]
	s_add_u32 m0, s14, 0x1e000
	s_nop 0
	global_load_lds_dwordx4 v5, s[28:29]
	v_mfma_f32_16x16x32_f16 v[76:79], v[124:127], v[104:107], v[76:79]
	v_mfma_f32_16x16x32_f16 v[80:83], v[112:115], v[108:111], v[80:83]
	s_add_u32 m0, s14, 0x20000
	s_nop 0
	global_load_lds_dwordx4 v6, s[30:31]
	v_mfma_f32_16x16x32_f16 v[84:87], v[116:119], v[108:111], v[84:87]
	v_mfma_f32_16x16x32_f16 v[88:91], v[120:123], v[108:111], v[88:91]
	s_add_u32 m0, s14, 0x22000
	s_nop 0
	global_load_lds_dwordx4 v7, s[30:31]
	v_mfma_f32_16x16x32_f16 v[92:95], v[124:127], v[108:111], v[92:95]
	s_waitcnt vmcnt(6) lgkmcnt(0)
	s_barrier
	s_add_u32 s28, s28, 0x80
	s_addc_u32 s29, s29, 0
	s_add_u32 s30, s30, 0x80
	s_addc_u32 s31, s31, 0
	s_waitcnt lgkmcnt(0)
	v_mfma_f32_16x16x32_f16 v[32:35], v[144:147], v[128:131], v[32:35]
	ds_read_b128 v[96:99], v12
	v_mfma_f32_16x16x32_f16 v[36:39], v[148:151], v[128:131], v[36:39]
	ds_read_b128 v[112:115], v13 offset:32768
	v_mfma_f32_16x16x32_f16 v[40:43], v[152:155], v[128:131], v[40:43]
	ds_read_b128 v[116:119], v13 offset:34816
	v_mfma_f32_16x16x32_f16 v[44:47], v[156:159], v[128:131], v[44:47]
	ds_read_b128 v[120:123], v13 offset:36864
	v_mfma_f32_16x16x32_f16 v[48:51], v[144:147], v[132:135], v[48:51]
	ds_read_b128 v[124:127], v13 offset:38912
	v_mfma_f32_16x16x32_f16 v[52:55], v[148:151], v[132:135], v[52:55]
	ds_read_b128 v[100:103], v12 offset:2048
	v_mfma_f32_16x16x32_f16 v[56:59], v[152:155], v[132:135], v[56:59]
	ds_read_b128 v[104:107], v12 offset:4096
	v_mfma_f32_16x16x32_f16 v[60:63], v[156:159], v[132:135], v[60:63]
	ds_read_b128 v[108:111], v12 offset:6144
	v_mfma_f32_16x16x32_f16 v[64:67], v[144:147], v[136:139], v[64:67]
	v_mfma_f32_16x16x32_f16 v[68:71], v[148:151], v[136:139], v[68:71]
	v_mfma_f32_16x16x32_f16 v[72:75], v[152:155], v[136:139], v[72:75]
	s_add_u32 m0, s14, 0x0
	s_nop 0
	global_load_lds_dwordx4 v2, s[28:29]
	v_mfma_f32_16x16x32_f16 v[76:79], v[156:159], v[136:139], v[76:79]
	v_mfma_f32_16x16x32_f16 v[80:83], v[144:147], v[140:143], v[80:83]
	s_add_u32 m0, s14, 0x2000
	s_nop 0
	global_load_lds_dwordx4 v3, s[28:29]
	v_mfma_f32_16x16x32_f16 v[84:87], v[148:151], v[140:143], v[84:87]
	v_mfma_f32_16x16x32_f16 v[88:91], v[152:155], v[140:143], v[88:91]
	s_add_u32 m0, s14, 0x4000
	s_nop 0
	global_load_lds_dwordx4 v4, s[28:29]
	v_mfma_f32_16x16x32_f16 v[92:95], v[156:159], v[140:143], v[92:95]
	s_waitcnt lgkmcnt(0)
	v_mfma_f32_16x16x32_f16 v[32:35], v[112:115], v[96:99], v[32:35]
	ds_read_b128 v[128:131], v14
	v_mfma_f32_16x16x32_f16 v[36:39], v[116:119], v[96:99], v[36:39]
	ds_read_b128 v[144:147], v15 offset:32768
	v_mfma_f32_16x16x32_f16 v[40:43], v[120:123], v[96:99], v[40:43]
	ds_read_b128 v[148:151], v15 offset:34816
	v_mfma_f32_16x16x32_f16 v[44:47], v[124:127], v[96:99], v[44:47]
	ds_read_b128 v[152:155], v15 offset:36864
	v_mfma_f32_16x16x32_f16 v[48:51], v[112:115], v[100:103], v[48:51]
	ds_read_b128 v[156:159], v15 offset:38912
	v_mfma_f32_16x16x32_f16 v[52:55], v[116:119], v[100:103], v[52:55]
	ds_read_b128 v[132:135], v14 offset:2048
	v_mfma_f32_16x16x32_f16 v[56:59], v[120:123], v[100:103], v[56:59]
	ds_read_b128 v[136:139], v14 offset:4096
	v_mfma_f32_16x16x32_f16 v[60:63], v[124:127], v[100:103], v[60:63]
	ds_read_b128 v[140:143], v14 offset:6144
	v_mfma_f32_16x16x32_f16 v[64:67], v[112:115], v[104:107], v[64:67]
	v_mfma_f32_16x16x32_f16 v[68:71], v[116:119], v[104:107], v[68:71]
	v_mfma_f32_16x16x32_f16 v[72:75], v[120:123], v[104:107], v[72:75]
	s_add_u32 m0, s14, 0x6000
	s_nop 0
	global_load_lds_dwordx4 v5, s[28:29]
	v_mfma_f32_16x16x32_f16 v[76:79], v[124:127], v[104:107], v[76:79]
	v_mfma_f32_16x16x32_f16 v[80:83], v[112:115], v[108:111], v[80:83]
	s_add_u32 m0, s14, 0x8000
	s_nop 0
	global_load_lds_dwordx4 v6, s[30:31]
	v_mfma_f32_16x16x32_f16 v[84:87], v[116:119], v[108:111], v[84:87]
	v_mfma_f32_16x16x32_f16 v[88:91], v[120:123], v[108:111], v[88:91]
	s_add_u32 m0, s14, 0xa000
	s_nop 0
	global_load_lds_dwordx4 v7, s[30:31]
	v_mfma_f32_16x16x32_f16 v[92:95], v[124:127], v[108:111], v[92:95]
	s_waitcnt vmcnt(6) lgkmcnt(0)
	s_barrier
	s_add_u32 s28, s28, 0x80
	s_addc_u32 s29, s29, 0
	s_add_u32 s30, s30, 0x80
	s_addc_u32 s31, s31, 0
	s_waitcnt lgkmcnt(0)
	v_mfma_f32_16x16x32_f16 v[32:35], v[144:147], v[128:131], v[32:35]
	ds_read_b128 v[96:99], v16
	v_mfma_f32_16x16x32_f16 v[36:39], v[148:151], v[128:131], v[36:39]
	ds_read_b128 v[112:115], v17 offset:32768
	v_mfma_f32_16x16x32_f16 v[40:43], v[152:155], v[128:131], v[40:43]
	ds_read_b128 v[116:119], v17 offset:34816
	v_mfma_f32_16x16x32_f16 v[44:47], v[156:159], v[128:131], v[44:47]
	ds_read_b128 v[120:123], v17 offset:36864
	v_mfma_f32_16x16x32_f16 v[48:51], v[144:147], v[132:135], v[48:51]
	ds_read_b128 v[124:127], v17 offset:38912
	v_mfma_f32_16x16x32_f16 v[52:55], v[148:151], v[132:135], v[52:55]
	ds_read_b128 v[100:103], v16 offset:2048
	v_mfma_f32_16x16x32_f16 v[56:59], v[152:155], v[132:135], v[56:59]
	ds_read_b128 v[104:107], v16 offset:4096
	v_mfma_f32_16x16x32_f16 v[60:63], v[156:159], v[132:135], v[60:63]
	ds_read_b128 v[108:111], v16 offset:6144
	v_mfma_f32_16x16x32_f16 v[64:67], v[144:147], v[136:139], v[64:67]
	v_mfma_f32_16x16x32_f16 v[68:71], v[148:151], v[136:139], v[68:71]
	v_mfma_f32_16x16x32_f16 v[72:75], v[152:155], v[136:139], v[72:75]
	s_add_u32 m0, s14, 0xc000
	s_nop 0
	global_load_lds_dwordx4 v2, s[28:29]
	v_mfma_f32_16x16x32_f16 v[76:79], v[156:159], v[136:139], v[76:79]
	v_mfma_f32_16x16x32_f16 v[80:83], v[144:147], v[140:143], v[80:83]
	s_add_u32 m0, s14, 0xe000
	s_nop 0
	global_load_lds_dwordx4 v3, s[28:29]
	v_mfma_f32_16x16x32_f16 v[84:87], v[148:151], v[140:143], v[84:87]
	v_mfma_f32_16x16x32_f16 v[88:91], v[152:155], v[140:143], v[88:91]
	s_add_u32 m0, s14, 0x10000
	s_nop 0
	global_load_lds_dwordx4 v4, s[28:29]
	v_mfma_f32_16x16x32_f16 v[92:95], v[156:159], v[140:143], v[92:95]
	s_waitcnt lgkmcnt(0)
	v_mfma_f32_16x16x32_f16 v[32:35], v[112:115], v[96:99], v[32:35]
	ds_read_b128 v[128:131], v18
	v_mfma_f32_16x16x32_f16 v[36:39], v[116:119], v[96:99], v[36:39]
	ds_read_b128 v[144:147], v19 offset:32768
	v_mfma_f32_16x16x32_f16 v[40:43], v[120:123], v[96:99], v[40:43]
	ds_read_b128 v[148:151], v19 offset:34816
	v_mfma_f32_16x16x32_f16 v[44:47], v[124:127], v[96:99], v[44:47]
	ds_read_b128 v[152:155], v19 offset:36864
	v_mfma_f32_16x16x32_f16 v[48:51], v[112:115], v[100:103], v[48:51]
	ds_read_b128 v[156:159], v19 offset:38912
	v_mfma_f32_16x16x32_f16 v[52:55], v[116:119], v[100:103], v[52:55]
	ds_read_b128 v[132:135], v18 offset:2048
	v_mfma_f32_16x16x32_f16 v[56:59], v[120:123], v[100:103], v[56:59]
	ds_read_b128 v[136:139], v18 offset:4096
	v_mfma_f32_16x16x32_f16 v[60:63], v[124:127], v[100:103], v[60:63]
	ds_read_b128 v[140:143], v18 offset:6144
	v_mfma_f32_16x16x32_f16 v[64:67], v[112:115], v[104:107], v[64:67]
	v_mfma_f32_16x16x32_f16 v[68:71], v[116:119], v[104:107], v[68:71]
	v_mfma_f32_16x16x32_f16 v[72:75], v[120:123], v[104:107], v[72:75]
	s_add_u32 m0, s14, 0x12000
	s_nop 0
	global_load_lds_dwordx4 v5, s[28:29]
	v_mfma_f32_16x16x32_f16 v[76:79], v[124:127], v[104:107], v[76:79]
	v_mfma_f32_16x16x32_f16 v[80:83], v[112:115], v[108:111], v[80:83]
	s_add_u32 m0, s14, 0x14000
	s_nop 0
	global_load_lds_dwordx4 v6, s[30:31]
	v_mfma_f32_16x16x32_f16 v[84:87], v[116:119], v[108:111], v[84:87]
	v_mfma_f32_16x16x32_f16 v[88:91], v[120:123], v[108:111], v[88:91]
	s_add_u32 m0, s14, 0x16000
	s_nop 0
	global_load_lds_dwordx4 v7, s[30:31]
	v_mfma_f32_16x16x32_f16 v[92:95], v[124:127], v[108:111], v[92:95]
	s_waitcnt vmcnt(6) lgkmcnt(0)
	s_barrier
	s_add_u32 s28, s28, 0x80
	s_addc_u32 s29, s29, 0
	s_add_u32 s30, s30, 0x80
	s_addc_u32 s31, s31, 0
	s_waitcnt lgkmcnt(0)
	v_mfma_f32_16x16x32_f16 v[32:35], v[144:147], v[128:131], v[32:35]
	ds_read_b128 v[96:99], v8
	v_mfma_f32_16x16x32_f16 v[36:39], v[148:151], v[128:131], v[36:39]
	ds_read_b128 v[112:115], v9 offset:32768
	v_mfma_f32_16x16x32_f16 v[40:43], v[152:155], v[128:131], v[40:43]
	ds_read_b128 v[116:119], v9 offset:34816
	v_mfma_f32_16x16x32_f16 v[44:47], v[156:159], v[128:131], v[44:47]
	ds_read_b128 v[120:123], v9 offset:36864
	v_mfma_f32_16x16x32_f16 v[48:51], v[144:147], v[132:135], v[48:51]
	ds_read_b128 v[124:127], v9 offset:38912
	v_mfma_f32_16x16x32_f16 v[52:55], v[148:151], v[132:135], v[52:55]
	ds_read_b128 v[100:103], v8 offset:2048
	v_mfma_f32_16x16x32_f16 v[56:59], v[152:155], v[132:135], v[56:59]
	ds_read_b128 v[104:107], v8 offset:4096
	v_mfma_f32_16x16x32_f16 v[60:63], v[156:159], v[132:135], v[60:63]
	ds_read_b128 v[108:111], v8 offset:6144
	v_mfma_f32_16x16x32_f16 v[64:67], v[144:147], v[136:139], v[64:67]
	v_mfma_f32_16x16x32_f16 v[68:71], v[148:151], v[136:139], v[68:71]
	v_mfma_f32_16x16x32_f16 v[72:75], v[152:155], v[136:139], v[72:75]
	s_add_u32 m0, s14, 0x18000
	s_nop 0
	global_load_lds_dwordx4 v2, s[28:29]
	v_mfma_f32_16x16x32_f16 v[76:79], v[156:159], v[136:139], v[76:79]
	v_mfma_f32_16x16x32_f16 v[80:83], v[144:147], v[140:143], v[80:83]
	s_add_u32 m0, s14, 0x1a000
	s_nop 0
	global_load_lds_dwordx4 v3, s[28:29]
	v_mfma_f32_16x16x32_f16 v[84:87], v[148:151], v[140:143], v[84:87]
	v_mfma_f32_16x16x32_f16 v[88:91], v[152:155], v[140:143], v[88:91]
	s_add_u32 m0, s14, 0x1c000
	s_nop 0
	global_load_lds_dwordx4 v4, s[28:29]
	v_mfma_f32_16x16x32_f16 v[92:95], v[156:159], v[140:143], v[92:95]
	s_waitcnt lgkmcnt(0)
	v_mfma_f32_16x16x32_f16 v[32:35], v[112:115], v[96:99], v[32:35]
	ds_read_b128 v[128:131], v10
	v_mfma_f32_16x16x32_f16 v[36:39], v[116:119], v[96:99], v[36:39]
	ds_read_b128 v[144:147], v11 offset:32768
	v_mfma_f32_16x16x32_f16 v[40:43], v[120:123], v[96:99], v[40:43]
	ds_read_b128 v[148:151], v11 offset:34816
	v_mfma_f32_16x16x32_f16 v[44:47], v[124:127], v[96:99], v[44:47]
	ds_read_b128 v[152:155], v11 offset:36864
	v_mfma_f32_16x16x32_f16 v[48:51], v[112:115], v[100:103], v[48:51]
	ds_read_b128 v[156:159], v11 offset:38912
	v_mfma_f32_16x16x32_f16 v[52:55], v[116:119], v[100:103], v[52:55]
	ds_read_b128 v[132:135], v10 offset:2048
	v_mfma_f32_16x16x32_f16 v[56:59], v[120:123], v[100:103], v[56:59]
	ds_read_b128 v[136:139], v10 offset:4096
	v_mfma_f32_16x16x32_f16 v[60:63], v[124:127], v[100:103], v[60:63]
	ds_read_b128 v[140:143], v10 offset:6144
	v_mfma_f32_16x16x32_f16 v[64:67], v[112:115], v[104:107], v[64:67]
	v_mfma_f32_16x16x32_f16 v[68:71], v[116:119], v[104:107], v[68:71]
	v_mfma_f32_16x16x32_f16 v[72:75], v[120:123], v[104:107], v[72:75]
	s_add_u32 m0, s14, 0x1e000
	s_nop 0
	global_load_lds_dwordx4 v5, s[28:29]
	v_mfma_f32_16x16x32_f16 v[76:79], v[124:127], v[104:107], v[76:79]
	v_mfma_f32_16x16x32_f16 v[80:83], v[112:115], v[108:111], v[80:83]
	s_add_u32 m0, s14, 0x20000
	s_nop 0
	global_load_lds_dwordx4 v6, s[30:31]
	v_mfma_f32_16x16x32_f16 v[84:87], v[116:119], v[108:111], v[84:87]
	v_mfma_f32_16x16x32_f16 v[88:91], v[120:123], v[108:111], v[88:91]
	s_add_u32 m0, s14, 0x22000
	s_nop 0
	global_load_lds_dwordx4 v7, s[30:31]
	v_mfma_f32_16x16x32_f16 v[92:95], v[124:127], v[108:111], v[92:95]
	s_waitcnt vmcnt(6) lgkmcnt(0)
	s_barrier
	s_add_u32 s28, s28, 0x80
	s_addc_u32 s29, s29, 0
	s_add_u32 s30, s30, 0x80
	s_addc_u32 s31, s31, 0
	s_waitcnt lgkmcnt(0)
	v_mfma_f32_16x16x32_f16 v[32:35], v[144:147], v[128:131], v[32:35]
	ds_read_b128 v[96:99], v12
	v_mfma_f32_16x16x32_f16 v[36:39], v[148:151], v[128:131], v[36:39]
	ds_read_b128 v[112:115], v13 offset:32768
	v_mfma_f32_16x16x32_f16 v[40:43], v[152:155], v[128:131], v[40:43]
	ds_read_b128 v[116:119], v13 offset:34816
	v_mfma_f32_16x16x32_f16 v[44:47], v[156:159], v[128:131], v[44:47]
	ds_read_b128 v[120:123], v13 offset:36864
	v_mfma_f32_16x16x32_f16 v[48:51], v[144:147], v[132:135], v[48:51]
	ds_read_b128 v[124:127], v13 offset:38912
	v_mfma_f32_16x16x32_f16 v[52:55], v[148:151], v[132:135], v[52:55]
	ds_read_b128 v[100:103], v12 offset:2048
	v_mfma_f32_16x16x32_f16 v[56:59], v[152:155], v[132:135], v[56:59]
	ds_read_b128 v[104:107], v12 offset:4096
	v_mfma_f32_16x16x32_f16 v[60:63], v[156:159], v[132:135], v[60:63]
	ds_read_b128 v[108:111], v12 offset:6144
	v_mfma_f32_16x16x32_f16 v[64:67], v[144:147], v[136:139], v[64:67]
	v_mfma_f32_16x16x32_f16 v[68:71], v[148:151], v[136:139], v[68:71]
	v_mfma_f32_16x16x32_f16 v[72:75], v[152:155], v[136:139], v[72:75]
	s_add_u32 m0, s14, 0x0
	s_nop 0
	global_load_lds_dwordx4 v2, s[28:29]
	v_mfma_f32_16x16x32_f16 v[76:79], v[156:159], v[136:139], v[76:79]
	v_mfma_f32_16x16x32_f16 v[80:83], v[144:147], v[140:143], v[80:83]
	s_add_u32 m0, s14, 0x2000
	s_nop 0
	global_load_lds_dwordx4 v3, s[28:29]
	v_mfma_f32_16x16x32_f16 v[84:87], v[148:151], v[140:143], v[84:87]
	v_mfma_f32_16x16x32_f16 v[88:91], v[152:155], v[140:143], v[88:91]
	s_add_u32 m0, s14, 0x4000
	s_nop 0
	global_load_lds_dwordx4 v4, s[28:29]
	v_mfma_f32_16x16x32_f16 v[92:95], v[156:159], v[140:143], v[92:95]
	s_waitcnt lgkmcnt(0)
	v_mfma_f32_16x16x32_f16 v[32:35], v[112:115], v[96:99], v[32:35]
	ds_read_b128 v[128:131], v14
	v_mfma_f32_16x16x32_f16 v[36:39], v[116:119], v[96:99], v[36:39]
	ds_read_b128 v[144:147], v15 offset:32768
	v_mfma_f32_16x16x32_f16 v[40:43], v[120:123], v[96:99], v[40:43]
	ds_read_b128 v[148:151], v15 offset:34816
	v_mfma_f32_16x16x32_f16 v[44:47], v[124:127], v[96:99], v[44:47]
	ds_read_b128 v[152:155], v15 offset:36864
	v_mfma_f32_16x16x32_f16 v[48:51], v[112:115], v[100:103], v[48:51]
	ds_read_b128 v[156:159], v15 offset:38912
	v_mfma_f32_16x16x32_f16 v[52:55], v[116:119], v[100:103], v[52:55]
	ds_read_b128 v[132:135], v14 offset:2048
	v_mfma_f32_16x16x32_f16 v[56:59], v[120:123], v[100:103], v[56:59]
	ds_read_b128 v[136:139], v14 offset:4096
	v_mfma_f32_16x16x32_f16 v[60:63], v[124:127], v[100:103], v[60:63]
	ds_read_b128 v[140:143], v14 offset:6144
	v_mfma_f32_16x16x32_f16 v[64:67], v[112:115], v[104:107], v[64:67]
	v_mfma_f32_16x16x32_f16 v[68:71], v[116:119], v[104:107], v[68:71]
	v_mfma_f32_16x16x32_f16 v[72:75], v[120:123], v[104:107], v[72:75]
	s_add_u32 m0, s14, 0x6000
	s_nop 0
	global_load_lds_dwordx4 v5, s[28:29]
	v_mfma_f32_16x16x32_f16 v[76:79], v[124:127], v[104:107], v[76:79]
	v_mfma_f32_16x16x32_f16 v[80:83], v[112:115], v[108:111], v[80:83]
	s_add_u32 m0, s14, 0x8000
	s_nop 0
	global_load_lds_dwordx4 v6, s[30:31]
	v_mfma_f32_16x16x32_f16 v[84:87], v[116:119], v[108:111], v[84:87]
	v_mfma_f32_16x16x32_f16 v[88:91], v[120:123], v[108:111], v[88:91]
	s_add_u32 m0, s14, 0xa000
	s_nop 0
	global_load_lds_dwordx4 v7, s[30:31]
	v_mfma_f32_16x16x32_f16 v[92:95], v[124:127], v[108:111], v[92:95]
	s_waitcnt vmcnt(6) lgkmcnt(0)
	s_barrier
	s_add_u32 s28, s28, 0x80
	s_addc_u32 s29, s29, 0
	s_add_u32 s30, s30, 0x80
	s_addc_u32 s31, s31, 0
	s_waitcnt lgkmcnt(0)
	v_mfma_f32_16x16x32_f16 v[32:35], v[144:147], v[128:131], v[32:35]
	ds_read_b128 v[96:99], v16
	v_mfma_f32_16x16x32_f16 v[36:39], v[148:151], v[128:131], v[36:39]
	ds_read_b128 v[112:115], v17 offset:32768
	v_mfma_f32_16x16x32_f16 v[40:43], v[152:155], v[128:131], v[40:43]
	ds_read_b128 v[116:119], v17 offset:34816
	v_mfma_f32_16x16x32_f16 v[44:47], v[156:159], v[128:131], v[44:47]
	ds_read_b128 v[120:123], v17 offset:36864
	v_mfma_f32_16x16x32_f16 v[48:51], v[144:147], v[132:135], v[48:51]
	ds_read_b128 v[124:127], v17 offset:38912
	v_mfma_f32_16x16x32_f16 v[52:55], v[148:151], v[132:135], v[52:55]
	ds_read_b128 v[100:103], v16 offset:2048
	v_mfma_f32_16x16x32_f16 v[56:59], v[152:155], v[132:135], v[56:59]
	ds_read_b128 v[104:107], v16 offset:4096
	v_mfma_f32_16x16x32_f16 v[60:63], v[156:159], v[132:135], v[60:63]
	ds_read_b128 v[108:111], v16 offset:6144
	v_mfma_f32_16x16x32_f16 v[64:67], v[144:147], v[136:139], v[64:67]
	v_mfma_f32_16x16x32_f16 v[68:71], v[148:151], v[136:139], v[68:71]
	v_mfma_f32_16x16x32_f16 v[72:75], v[152:155], v[136:139], v[72:75]
	s_add_u32 m0, s14, 0xc000
	s_nop 0
	global_load_lds_dwordx4 v2, s[28:29]
	v_mfma_f32_16x16x32_f16 v[76:79], v[156:159], v[136:139], v[76:79]
	v_mfma_f32_16x16x32_f16 v[80:83], v[144:147], v[140:143], v[80:83]
	s_add_u32 m0, s14, 0xe000
	s_nop 0
	global_load_lds_dwordx4 v3, s[28:29]
	v_mfma_f32_16x16x32_f16 v[84:87], v[148:151], v[140:143], v[84:87]
	v_mfma_f32_16x16x32_f16 v[88:91], v[152:155], v[140:143], v[88:91]
	s_add_u32 m0, s14, 0x10000
	s_nop 0
	global_load_lds_dwordx4 v4, s[28:29]
	v_mfma_f32_16x16x32_f16 v[92:95], v[156:159], v[140:143], v[92:95]
	s_waitcnt lgkmcnt(0)
	v_mfma_f32_16x16x32_f16 v[32:35], v[112:115], v[96:99], v[32:35]
	ds_read_b128 v[128:131], v18
	v_mfma_f32_16x16x32_f16 v[36:39], v[116:119], v[96:99], v[36:39]
	ds_read_b128 v[144:147], v19 offset:32768
	v_mfma_f32_16x16x32_f16 v[40:43], v[120:123], v[96:99], v[40:43]
	ds_read_b128 v[148:151], v19 offset:34816
	v_mfma_f32_16x16x32_f16 v[44:47], v[124:127], v[96:99], v[44:47]
	ds_read_b128 v[152:155], v19 offset:36864
	v_mfma_f32_16x16x32_f16 v[48:51], v[112:115], v[100:103], v[48:51]
	ds_read_b128 v[156:159], v19 offset:38912
	v_mfma_f32_16x16x32_f16 v[52:55], v[116:119], v[100:103], v[52:55]
	ds_read_b128 v[132:135], v18 offset:2048
	v_mfma_f32_16x16x32_f16 v[56:59], v[120:123], v[100:103], v[56:59]
	ds_read_b128 v[136:139], v18 offset:4096
	v_mfma_f32_16x16x32_f16 v[60:63], v[124:127], v[100:103], v[60:63]
	ds_read_b128 v[140:143], v18 offset:6144
	v_mfma_f32_16x16x32_f16 v[64:67], v[112:115], v[104:107], v[64:67]
	v_mfma_f32_16x16x32_f16 v[68:71], v[116:119], v[104:107], v[68:71]
	v_mfma_f32_16x16x32_f16 v[72:75], v[120:123], v[104:107], v[72:75]
	s_add_u32 m0, s14, 0x12000
	s_nop 0
	global_load_lds_dwordx4 v5, s[28:29]
	v_mfma_f32_16x16x32_f16 v[76:79], v[124:127], v[104:107], v[76:79]
	v_mfma_f32_16x16x32_f16 v[80:83], v[112:115], v[108:111], v[80:83]
	s_add_u32 m0, s14, 0x14000
	s_nop 0
	global_load_lds_dwordx4 v6, s[30:31]
	v_mfma_f32_16x16x32_f16 v[84:87], v[116:119], v[108:111], v[84:87]
	v_mfma_f32_16x16x32_f16 v[88:91], v[120:123], v[108:111], v[88:91]
	s_add_u32 m0, s14, 0x16000
	s_nop 0
	global_load_lds_dwordx4 v7, s[30:31]
	v_mfma_f32_16x16x32_f16 v[92:95], v[124:127], v[108:111], v[92:95]
	s_waitcnt vmcnt(6) lgkmcnt(0)
	s_barrier
	s_add_u32 s28, s28, 0x80
	s_addc_u32 s29, s29, 0
	s_add_u32 s30, s30, 0x80
	s_addc_u32 s31, s31, 0
	s_waitcnt lgkmcnt(0)
	v_mfma_f32_16x16x32_f16 v[32:35], v[144:147], v[128:131], v[32:35]
	ds_read_b128 v[96:99], v8
	v_mfma_f32_16x16x32_f16 v[36:39], v[148:151], v[128:131], v[36:39]
	ds_read_b128 v[112:115], v9 offset:32768
	v_mfma_f32_16x16x32_f16 v[40:43], v[152:155], v[128:131], v[40:43]
	ds_read_b128 v[116:119], v9 offset:34816
	v_mfma_f32_16x16x32_f16 v[44:47], v[156:159], v[128:131], v[44:47]
	ds_read_b128 v[120:123], v9 offset:36864
	v_mfma_f32_16x16x32_f16 v[48:51], v[144:147], v[132:135], v[48:51]
	ds_read_b128 v[124:127], v9 offset:38912
	v_mfma_f32_16x16x32_f16 v[52:55], v[148:151], v[132:135], v[52:55]
	ds_read_b128 v[100:103], v8 offset:2048
	v_mfma_f32_16x16x32_f16 v[56:59], v[152:155], v[132:135], v[56:59]
	ds_read_b128 v[104:107], v8 offset:4096
	v_mfma_f32_16x16x32_f16 v[60:63], v[156:159], v[132:135], v[60:63]
	ds_read_b128 v[108:111], v8 offset:6144
	v_mfma_f32_16x16x32_f16 v[64:67], v[144:147], v[136:139], v[64:67]
	v_mfma_f32_16x16x32_f16 v[68:71], v[148:151], v[136:139], v[68:71]
	v_mfma_f32_16x16x32_f16 v[72:75], v[152:155], v[136:139], v[72:75]
	s_add_u32 m0, s14, 0x18000
	s_nop 0
	global_load_lds_dwordx4 v2, s[28:29]
	v_mfma_f32_16x16x32_f16 v[76:79], v[156:159], v[136:139], v[76:79]
	v_mfma_f32_16x16x32_f16 v[80:83], v[144:147], v[140:143], v[80:83]
	s_add_u32 m0, s14, 0x1a000
	s_nop 0
	global_load_lds_dwordx4 v3, s[28:29]
	v_mfma_f32_16x16x32_f16 v[84:87], v[148:151], v[140:143], v[84:87]
	v_mfma_f32_16x16x32_f16 v[88:91], v[152:155], v[140:143], v[88:91]
	s_add_u32 m0, s14, 0x1c000
	s_nop 0
	global_load_lds_dwordx4 v4, s[28:29]
	v_mfma_f32_16x16x32_f16 v[92:95], v[156:159], v[140:143], v[92:95]
	s_waitcnt lgkmcnt(0)
	v_mfma_f32_16x16x32_f16 v[32:35], v[112:115], v[96:99], v[32:35]
	ds_read_b128 v[128:131], v10
	v_mfma_f32_16x16x32_f16 v[36:39], v[116:119], v[96:99], v[36:39]
	ds_read_b128 v[144:147], v11 offset:32768
	v_mfma_f32_16x16x32_f16 v[40:43], v[120:123], v[96:99], v[40:43]
	ds_read_b128 v[148:151], v11 offset:34816
	v_mfma_f32_16x16x32_f16 v[44:47], v[124:127], v[96:99], v[44:47]
	ds_read_b128 v[152:155], v11 offset:36864
	v_mfma_f32_16x16x32_f16 v[48:51], v[112:115], v[100:103], v[48:51]
	ds_read_b128 v[156:159], v11 offset:38912
	v_mfma_f32_16x16x32_f16 v[52:55], v[116:119], v[100:103], v[52:55]
	ds_read_b128 v[132:135], v10 offset:2048
	v_mfma_f32_16x16x32_f16 v[56:59], v[120:123], v[100:103], v[56:59]
	ds_read_b128 v[136:139], v10 offset:4096
	v_mfma_f32_16x16x32_f16 v[60:63], v[124:127], v[100:103], v[60:63]
	ds_read_b128 v[140:143], v10 offset:6144
	v_mfma_f32_16x16x32_f16 v[64:67], v[112:115], v[104:107], v[64:67]
	v_mfma_f32_16x16x32_f16 v[68:71], v[116:119], v[104:107], v[68:71]
	v_mfma_f32_16x16x32_f16 v[72:75], v[120:123], v[104:107], v[72:75]
	s_add_u32 m0, s14, 0x1e000
	s_nop 0
	global_load_lds_dwordx4 v5, s[28:29]
	v_mfma_f32_16x16x32_f16 v[76:79], v[124:127], v[104:107], v[76:79]
	v_mfma_f32_16x16x32_f16 v[80:83], v[112:115], v[108:111], v[80:83]
	s_add_u32 m0, s14, 0x20000
	s_nop 0
	global_load_lds_dwordx4 v6, s[30:31]
	v_mfma_f32_16x16x32_f16 v[84:87], v[116:119], v[108:111], v[84:87]
	v_mfma_f32_16x16x32_f16 v[88:91], v[120:123], v[108:111], v[88:91]
	s_add_u32 m0, s14, 0x22000
	s_nop 0
	global_load_lds_dwordx4 v7, s[30:31]
	v_mfma_f32_16x16x32_f16 v[92:95], v[124:127], v[108:111], v[92:95]
	s_waitcnt vmcnt(6) lgkmcnt(0)
	s_barrier
	s_add_u32 s28, s28, 0x80
	s_addc_u32 s29, s29, 0
	s_add_u32 s30, s30, 0x80
	s_addc_u32 s31, s31, 0
	s_waitcnt lgkmcnt(0)
	v_mfma_f32_16x16x32_f16 v[32:35], v[144:147], v[128:131], v[32:35]
	ds_read_b128 v[96:99], v12
	v_mfma_f32_16x16x32_f16 v[36:39], v[148:151], v[128:131], v[36:39]
	ds_read_b128 v[112:115], v13 offset:32768
	v_mfma_f32_16x16x32_f16 v[40:43], v[152:155], v[128:131], v[40:43]
	ds_read_b128 v[116:119], v13 offset:34816
	v_mfma_f32_16x16x32_f16 v[44:47], v[156:159], v[128:131], v[44:47]
	ds_read_b128 v[120:123], v13 offset:36864
	v_mfma_f32_16x16x32_f16 v[48:51], v[144:147], v[132:135], v[48:51]
	ds_read_b128 v[124:127], v13 offset:38912
	v_mfma_f32_16x16x32_f16 v[52:55], v[148:151], v[132:135], v[52:55]
	ds_read_b128 v[100:103], v12 offset:2048
	v_mfma_f32_16x16x32_f16 v[56:59], v[152:155], v[132:135], v[56:59]
	ds_read_b128 v[104:107], v12 offset:4096
	v_mfma_f32_16x16x32_f16 v[60:63], v[156:159], v[132:135], v[60:63]
	ds_read_b128 v[108:111], v12 offset:6144
	v_mfma_f32_16x16x32_f16 v[64:67], v[144:147], v[136:139], v[64:67]
	v_mfma_f32_16x16x32_f16 v[68:71], v[148:151], v[136:139], v[68:71]
	v_mfma_f32_16x16x32_f16 v[72:75], v[152:155], v[136:139], v[72:75]
	s_add_u32 m0, s14, 0x0
	s_nop 0
	global_load_lds_dwordx4 v2, s[28:29]
	v_mfma_f32_16x16x32_f16 v[76:79], v[156:159], v[136:139], v[76:79]
	v_mfma_f32_16x16x32_f16 v[80:83], v[144:147], v[140:143], v[80:83]
	s_add_u32 m0, s14, 0x2000
	s_nop 0
	global_load_lds_dwordx4 v3, s[28:29]
	v_mfma_f32_16x16x32_f16 v[84:87], v[148:151], v[140:143], v[84:87]
	v_mfma_f32_16x16x32_f16 v[88:91], v[152:155], v[140:143], v[88:91]
	s_add_u32 m0, s14, 0x4000
	s_nop 0
	global_load_lds_dwordx4 v4, s[28:29]
	v_mfma_f32_16x16x32_f16 v[92:95], v[156:159], v[140:143], v[92:95]
	s_waitcnt lgkmcnt(0)
	v_mfma_f32_16x16x32_f16 v[32:35], v[112:115], v[96:99], v[32:35]
	ds_read_b128 v[128:131], v14
	v_mfma_f32_16x16x32_f16 v[36:39], v[116:119], v[96:99], v[36:39]
	ds_read_b128 v[144:147], v15 offset:32768
	v_mfma_f32_16x16x32_f16 v[40:43], v[120:123], v[96:99], v[40:43]
	ds_read_b128 v[148:151], v15 offset:34816
	v_mfma_f32_16x16x32_f16 v[44:47], v[124:127], v[96:99], v[44:47]
	ds_read_b128 v[152:155], v15 offset:36864
	v_mfma_f32_16x16x32_f16 v[48:51], v[112:115], v[100:103], v[48:51]
	ds_read_b128 v[156:159], v15 offset:38912
	v_mfma_f32_16x16x32_f16 v[52:55], v[116:119], v[100:103], v[52:55]
	ds_read_b128 v[132:135], v14 offset:2048
	v_mfma_f32_16x16x32_f16 v[56:59], v[120:123], v[100:103], v[56:59]
	ds_read_b128 v[136:139], v14 offset:4096
	v_mfma_f32_16x16x32_f16 v[60:63], v[124:127], v[100:103], v[60:63]
	ds_read_b128 v[140:143], v14 offset:6144
	v_mfma_f32_16x16x32_f16 v[64:67], v[112:115], v[104:107], v[64:67]
	v_mfma_f32_16x16x32_f16 v[68:71], v[116:119], v[104:107], v[68:71]
	v_mfma_f32_16x16x32_f16 v[72:75], v[120:123], v[104:107], v[72:75]
	s_add_u32 m0, s14, 0x6000
	s_nop 0
	global_load_lds_dwordx4 v5, s[28:29]
	v_mfma_f32_16x16x32_f16 v[76:79], v[124:127], v[104:107], v[76:79]
	v_mfma_f32_16x16x32_f16 v[80:83], v[112:115], v[108:111], v[80:83]
	s_add_u32 m0, s14, 0x8000
	s_nop 0
	global_load_lds_dwordx4 v6, s[30:31]
	v_mfma_f32_16x16x32_f16 v[84:87], v[116:119], v[108:111], v[84:87]
	v_mfma_f32_16x16x32_f16 v[88:91], v[120:123], v[108:111], v[88:91]
	s_add_u32 m0, s14, 0xa000
	s_nop 0
	global_load_lds_dwordx4 v7, s[30:31]
	v_mfma_f32_16x16x32_f16 v[92:95], v[124:127], v[108:111], v[92:95]
	s_waitcnt vmcnt(6) lgkmcnt(0)
	s_barrier
	s_add_u32 s28, s28, 0x80
	s_addc_u32 s29, s29, 0
	s_add_u32 s30, s30, 0x80
	s_addc_u32 s31, s31, 0
	s_waitcnt lgkmcnt(0)
	v_mfma_f32_16x16x32_f16 v[32:35], v[144:147], v[128:131], v[32:35]
	ds_read_b128 v[96:99], v16
	v_mfma_f32_16x16x32_f16 v[36:39], v[148:151], v[128:131], v[36:39]
	ds_read_b128 v[112:115], v17 offset:32768
	v_mfma_f32_16x16x32_f16 v[40:43], v[152:155], v[128:131], v[40:43]
	ds_read_b128 v[116:119], v17 offset:34816
	v_mfma_f32_16x16x32_f16 v[44:47], v[156:159], v[128:131], v[44:47]
	ds_read_b128 v[120:123], v17 offset:36864
	v_mfma_f32_16x16x32_f16 v[48:51], v[144:147], v[132:135], v[48:51]
	ds_read_b128 v[124:127], v17 offset:38912
	v_mfma_f32_16x16x32_f16 v[52:55], v[148:151], v[132:135], v[52:55]
	ds_read_b128 v[100:103], v16 offset:2048
	v_mfma_f32_16x16x32_f16 v[56:59], v[152:155], v[132:135], v[56:59]
	ds_read_b128 v[104:107], v16 offset:4096
	v_mfma_f32_16x16x32_f16 v[60:63], v[156:159], v[132:135], v[60:63]
	ds_read_b128 v[108:111], v16 offset:6144
	v_mfma_f32_16x16x32_f16 v[64:67], v[144:147], v[136:139], v[64:67]
	v_mfma_f32_16x16x32_f16 v[68:71], v[148:151], v[136:139], v[68:71]
	v_mfma_f32_16x16x32_f16 v[72:75], v[152:155], v[136:139], v[72:75]
	s_add_u32 m0, s14, 0xc000
	s_nop 0
	global_load_lds_dwordx4 v2, s[28:29]
	v_mfma_f32_16x16x32_f16 v[76:79], v[156:159], v[136:139], v[76:79]
	v_mfma_f32_16x16x32_f16 v[80:83], v[144:147], v[140:143], v[80:83]
	s_add_u32 m0, s14, 0xe000
	s_nop 0
	global_load_lds_dwordx4 v3, s[28:29]
	v_mfma_f32_16x16x32_f16 v[84:87], v[148:151], v[140:143], v[84:87]
	v_mfma_f32_16x16x32_f16 v[88:91], v[152:155], v[140:143], v[88:91]
	s_add_u32 m0, s14, 0x10000
	s_nop 0
	global_load_lds_dwordx4 v4, s[28:29]
	v_mfma_f32_16x16x32_f16 v[92:95], v[156:159], v[140:143], v[92:95]
	s_waitcnt lgkmcnt(0)
	v_mfma_f32_16x16x32_f16 v[32:35], v[112:115], v[96:99], v[32:35]
	ds_read_b128 v[128:131], v18
	v_mfma_f32_16x16x32_f16 v[36:39], v[116:119], v[96:99], v[36:39]
	ds_read_b128 v[144:147], v19 offset:32768
	v_mfma_f32_16x16x32_f16 v[40:43], v[120:123], v[96:99], v[40:43]
	ds_read_b128 v[148:151], v19 offset:34816
	v_mfma_f32_16x16x32_f16 v[44:47], v[124:127], v[96:99], v[44:47]
	ds_read_b128 v[152:155], v19 offset:36864
	v_mfma_f32_16x16x32_f16 v[48:51], v[112:115], v[100:103], v[48:51]
	ds_read_b128 v[156:159], v19 offset:38912
	v_mfma_f32_16x16x32_f16 v[52:55], v[116:119], v[100:103], v[52:55]
	ds_read_b128 v[132:135], v18 offset:2048
	v_mfma_f32_16x16x32_f16 v[56:59], v[120:123], v[100:103], v[56:59]
	ds_read_b128 v[136:139], v18 offset:4096
	v_mfma_f32_16x16x32_f16 v[60:63], v[124:127], v[100:103], v[60:63]
	ds_read_b128 v[140:143], v18 offset:6144
	v_mfma_f32_16x16x32_f16 v[64:67], v[112:115], v[104:107], v[64:67]
	v_mfma_f32_16x16x32_f16 v[68:71], v[116:119], v[104:107], v[68:71]
	v_mfma_f32_16x16x32_f16 v[72:75], v[120:123], v[104:107], v[72:75]
	s_add_u32 m0, s14, 0x12000
	s_nop 0
	global_load_lds_dwordx4 v5, s[28:29]
	v_mfma_f32_16x16x32_f16 v[76:79], v[124:127], v[104:107], v[76:79]
	v_mfma_f32_16x16x32_f16 v[80:83], v[112:115], v[108:111], v[80:83]
	s_add_u32 m0, s14, 0x14000
	s_nop 0
	global_load_lds_dwordx4 v6, s[30:31]
	v_mfma_f32_16x16x32_f16 v[84:87], v[116:119], v[108:111], v[84:87]
	v_mfma_f32_16x16x32_f16 v[88:91], v[120:123], v[108:111], v[88:91]
	s_add_u32 m0, s14, 0x16000
	s_nop 0
	global_load_lds_dwordx4 v7, s[30:31]
	v_mfma_f32_16x16x32_f16 v[92:95], v[124:127], v[108:111], v[92:95]
	s_waitcnt vmcnt(6) lgkmcnt(0)
	s_barrier
	s_add_u32 s28, s28, 0x80
	s_addc_u32 s29, s29, 0
	s_add_u32 s30, s30, 0x80
	s_addc_u32 s31, s31, 0
	s_waitcnt lgkmcnt(0)
	v_mfma_f32_16x16x32_f16 v[32:35], v[144:147], v[128:131], v[32:35]
	ds_read_b128 v[96:99], v8
	v_mfma_f32_16x16x32_f16 v[36:39], v[148:151], v[128:131], v[36:39]
	ds_read_b128 v[112:115], v9 offset:32768
	v_mfma_f32_16x16x32_f16 v[40:43], v[152:155], v[128:131], v[40:43]
	ds_read_b128 v[116:119], v9 offset:34816
	v_mfma_f32_16x16x32_f16 v[44:47], v[156:159], v[128:131], v[44:47]
	ds_read_b128 v[120:123], v9 offset:36864
	v_mfma_f32_16x16x32_f16 v[48:51], v[144:147], v[132:135], v[48:51]
	ds_read_b128 v[124:127], v9 offset:38912
	v_mfma_f32_16x16x32_f16 v[52:55], v[148:151], v[132:135], v[52:55]
	ds_read_b128 v[100:103], v8 offset:2048
	v_mfma_f32_16x16x32_f16 v[56:59], v[152:155], v[132:135], v[56:59]
	ds_read_b128 v[104:107], v8 offset:4096
	v_mfma_f32_16x16x32_f16 v[60:63], v[156:159], v[132:135], v[60:63]
	ds_read_b128 v[108:111], v8 offset:6144
	v_mfma_f32_16x16x32_f16 v[64:67], v[144:147], v[136:139], v[64:67]
	v_mfma_f32_16x16x32_f16 v[68:71], v[148:151], v[136:139], v[68:71]
	v_mfma_f32_16x16x32_f16 v[72:75], v[152:155], v[136:139], v[72:75]
	s_add_u32 m0, s14, 0x18000
	s_nop 0
	global_load_lds_dwordx4 v2, s[28:29]
	v_mfma_f32_16x16x32_f16 v[76:79], v[156:159], v[136:139], v[76:79]
	v_mfma_f32_16x16x32_f16 v[80:83], v[144:147], v[140:143], v[80:83]
	s_add_u32 m0, s14, 0x1a000
	s_nop 0
	global_load_lds_dwordx4 v3, s[28:29]
	v_mfma_f32_16x16x32_f16 v[84:87], v[148:151], v[140:143], v[84:87]
	v_mfma_f32_16x16x32_f16 v[88:91], v[152:155], v[140:143], v[88:91]
	s_add_u32 m0, s14, 0x1c000
	s_nop 0
	global_load_lds_dwordx4 v4, s[28:29]
	v_mfma_f32_16x16x32_f16 v[92:95], v[156:159], v[140:143], v[92:95]
	s_waitcnt lgkmcnt(0)
	v_mfma_f32_16x16x32_f16 v[32:35], v[112:115], v[96:99], v[32:35]
	ds_read_b128 v[128:131], v10
	v_mfma_f32_16x16x32_f16 v[36:39], v[116:119], v[96:99], v[36:39]
	ds_read_b128 v[144:147], v11 offset:32768
	v_mfma_f32_16x16x32_f16 v[40:43], v[120:123], v[96:99], v[40:43]
	ds_read_b128 v[148:151], v11 offset:34816
	v_mfma_f32_16x16x32_f16 v[44:47], v[124:127], v[96:99], v[44:47]
	ds_read_b128 v[152:155], v11 offset:36864
	v_mfma_f32_16x16x32_f16 v[48:51], v[112:115], v[100:103], v[48:51]
	ds_read_b128 v[156:159], v11 offset:38912
	v_mfma_f32_16x16x32_f16 v[52:55], v[116:119], v[100:103], v[52:55]
	ds_read_b128 v[132:135], v10 offset:2048
	v_mfma_f32_16x16x32_f16 v[56:59], v[120:123], v[100:103], v[56:59]
	ds_read_b128 v[136:139], v10 offset:4096
	v_mfma_f32_16x16x32_f16 v[60:63], v[124:127], v[100:103], v[60:63]
	ds_read_b128 v[140:143], v10 offset:6144
	v_mfma_f32_16x16x32_f16 v[64:67], v[112:115], v[104:107], v[64:67]
	v_mfma_f32_16x16x32_f16 v[68:71], v[116:119], v[104:107], v[68:71]
	v_mfma_f32_16x16x32_f16 v[72:75], v[120:123], v[104:107], v[72:75]
	s_add_u32 m0, s14, 0x1e000
	s_nop 0
	global_load_lds_dwordx4 v5, s[28:29]
	v_mfma_f32_16x16x32_f16 v[76:79], v[124:127], v[104:107], v[76:79]
	v_mfma_f32_16x16x32_f16 v[80:83], v[112:115], v[108:111], v[80:83]
	s_add_u32 m0, s14, 0x20000
	s_nop 0
	global_load_lds_dwordx4 v6, s[30:31]
	v_mfma_f32_16x16x32_f16 v[84:87], v[116:119], v[108:111], v[84:87]
	v_mfma_f32_16x16x32_f16 v[88:91], v[120:123], v[108:111], v[88:91]
	s_add_u32 m0, s14, 0x22000
	s_nop 0
	global_load_lds_dwordx4 v7, s[30:31]
	v_mfma_f32_16x16x32_f16 v[92:95], v[124:127], v[108:111], v[92:95]
	s_waitcnt vmcnt(6) lgkmcnt(0)
	s_barrier
	s_mov_b64 s[28:29], s[18:19]
	s_mov_b64 s[30:31], s[26:27]
	s_waitcnt lgkmcnt(0)
	v_mfma_f32_16x16x32_f16 v[32:35], v[144:147], v[128:131], v[32:35]
	ds_read_b128 v[96:99], v12
	v_mfma_f32_16x16x32_f16 v[36:39], v[148:151], v[128:131], v[36:39]
	ds_read_b128 v[112:115], v13 offset:32768
	v_mfma_f32_16x16x32_f16 v[40:43], v[152:155], v[128:131], v[40:43]
	ds_read_b128 v[116:119], v13 offset:34816
	v_mfma_f32_16x16x32_f16 v[44:47], v[156:159], v[128:131], v[44:47]
	ds_read_b128 v[120:123], v13 offset:36864
	v_mfma_f32_16x16x32_f16 v[48:51], v[144:147], v[132:135], v[48:51]
	ds_read_b128 v[124:127], v13 offset:38912
	v_mfma_f32_16x16x32_f16 v[52:55], v[148:151], v[132:135], v[52:55]
	ds_read_b128 v[100:103], v12 offset:2048
	v_mfma_f32_16x16x32_f16 v[56:59], v[152:155], v[132:135], v[56:59]
	ds_read_b128 v[104:107], v12 offset:4096
	v_mfma_f32_16x16x32_f16 v[60:63], v[156:159], v[132:135], v[60:63]
	ds_read_b128 v[108:111], v12 offset:6144
	v_mfma_f32_16x16x32_f16 v[64:67], v[144:147], v[136:139], v[64:67]
	v_mfma_f32_16x16x32_f16 v[68:71], v[148:151], v[136:139], v[68:71]
	v_mfma_f32_16x16x32_f16 v[72:75], v[152:155], v[136:139], v[72:75]
	s_add_u32 m0, s14, 0x0
	s_nop 0
	global_load_lds_dwordx4 v2, s[28:29]
	v_mfma_f32_16x16x32_f16 v[76:79], v[156:159], v[136:139], v[76:79]
	v_mfma_f32_16x16x32_f16 v[80:83], v[144:147], v[140:143], v[80:83]
	s_add_u32 m0, s14, 0x2000
	s_nop 0
	global_load_lds_dwordx4 v3, s[28:29]
	v_mfma_f32_16x16x32_f16 v[84:87], v[148:151], v[140:143], v[84:87]
	v_mfma_f32_16x16x32_f16 v[88:91], v[152:155], v[140:143], v[88:91]
	s_add_u32 m0, s14, 0x4000
	s_nop 0
	global_load_lds_dwordx4 v4, s[28:29]
	v_mfma_f32_16x16x32_f16 v[92:95], v[156:159], v[140:143], v[92:95]
	s_waitcnt lgkmcnt(0)
	v_mfma_f32_16x16x32_f16 v[32:35], v[112:115], v[96:99], v[32:35]
	ds_read_b128 v[128:131], v14
	v_mfma_f32_16x16x32_f16 v[36:39], v[116:119], v[96:99], v[36:39]
	ds_read_b128 v[144:147], v15 offset:32768
	v_mfma_f32_16x16x32_f16 v[40:43], v[120:123], v[96:99], v[40:43]
	ds_read_b128 v[148:151], v15 offset:34816
	v_mfma_f32_16x16x32_f16 v[44:47], v[124:127], v[96:99], v[44:47]
	ds_read_b128 v[152:155], v15 offset:36864
	v_mfma_f32_16x16x32_f16 v[48:51], v[112:115], v[100:103], v[48:51]
	ds_read_b128 v[156:159], v15 offset:38912
	v_mfma_f32_16x16x32_f16 v[52:55], v[116:119], v[100:103], v[52:55]
	ds_read_b128 v[132:135], v14 offset:2048
	v_mfma_f32_16x16x32_f16 v[56:59], v[120:123], v[100:103], v[56:59]
	ds_read_b128 v[136:139], v14 offset:4096
	v_mfma_f32_16x16x32_f16 v[60:63], v[124:127], v[100:103], v[60:63]
	ds_read_b128 v[140:143], v14 offset:6144
	v_mfma_f32_16x16x32_f16 v[64:67], v[112:115], v[104:107], v[64:67]
	v_mfma_f32_16x16x32_f16 v[68:71], v[116:119], v[104:107], v[68:71]
	v_mfma_f32_16x16x32_f16 v[72:75], v[120:123], v[104:107], v[72:75]
	s_add_u32 m0, s14, 0x6000
	s_nop 0
	global_load_lds_dwordx4 v5, s[28:29]
	v_mfma_f32_16x16x32_f16 v[76:79], v[124:127], v[104:107], v[76:79]
	v_mfma_f32_16x16x32_f16 v[80:83], v[112:115], v[108:111], v[80:83]
	s_add_u32 m0, s14, 0x8000
	s_nop 0
	global_load_lds_dwordx4 v6, s[30:31]
	v_mfma_f32_16x16x32_f16 v[84:87], v[116:119], v[108:111], v[84:87]
	v_mfma_f32_16x16x32_f16 v[88:91], v[120:123], v[108:111], v[88:91]
	s_add_u32 m0, s14, 0xa000
	s_nop 0
	global_load_lds_dwordx4 v7, s[30:31]
	v_mfma_f32_16x16x32_f16 v[92:95], v[124:127], v[108:111], v[92:95]
	s_waitcnt vmcnt(6) lgkmcnt(0)
	s_barrier
	s_add_u32 s28, s28, 0x80
	s_addc_u32 s29, s29, 0
	s_add_u32 s30, s30, 0x80
	s_addc_u32 s31, s31, 0
	s_waitcnt lgkmcnt(0)
	v_mfma_f32_16x16x32_f16 v[32:35], v[144:147], v[128:131], v[32:35]
	ds_read_b128 v[96:99], v16
	v_mfma_f32_16x16x32_f16 v[36:39], v[148:151], v[128:131], v[36:39]
	ds_read_b128 v[112:115], v17 offset:32768
	v_mfma_f32_16x16x32_f16 v[40:43], v[152:155], v[128:131], v[40:43]
	ds_read_b128 v[116:119], v17 offset:34816
	v_mfma_f32_16x16x32_f16 v[44:47], v[156:159], v[128:131], v[44:47]
	ds_read_b128 v[120:123], v17 offset:36864
	v_mfma_f32_16x16x32_f16 v[48:51], v[144:147], v[132:135], v[48:51]
	ds_read_b128 v[124:127], v17 offset:38912
	v_mfma_f32_16x16x32_f16 v[52:55], v[148:151], v[132:135], v[52:55]
	ds_read_b128 v[100:103], v16 offset:2048
	v_mfma_f32_16x16x32_f16 v[56:59], v[152:155], v[132:135], v[56:59]
	ds_read_b128 v[104:107], v16 offset:4096
	v_mfma_f32_16x16x32_f16 v[60:63], v[156:159], v[132:135], v[60:63]
	ds_read_b128 v[108:111], v16 offset:6144
	v_mfma_f32_16x16x32_f16 v[64:67], v[144:147], v[136:139], v[64:67]
	v_mfma_f32_16x16x32_f16 v[68:71], v[148:151], v[136:139], v[68:71]
	v_mfma_f32_16x16x32_f16 v[72:75], v[152:155], v[136:139], v[72:75]
	s_add_u32 m0, s14, 0xc000
	s_nop 0
	global_load_lds_dwordx4 v2, s[28:29]
	v_mfma_f32_16x16x32_f16 v[76:79], v[156:159], v[136:139], v[76:79]
	v_mfma_f32_16x16x32_f16 v[80:83], v[144:147], v[140:143], v[80:83]
	s_add_u32 m0, s14, 0xe000
	s_nop 0
	global_load_lds_dwordx4 v3, s[28:29]
	v_mfma_f32_16x16x32_f16 v[84:87], v[148:151], v[140:143], v[84:87]
	v_mfma_f32_16x16x32_f16 v[88:91], v[152:155], v[140:143], v[88:91]
	s_add_u32 m0, s14, 0x10000
	s_nop 0
	global_load_lds_dwordx4 v4, s[28:29]
	v_mfma_f32_16x16x32_f16 v[92:95], v[156:159], v[140:143], v[92:95]
	s_waitcnt lgkmcnt(0)
	v_mfma_f32_16x16x32_f16 v[32:35], v[112:115], v[96:99], v[32:35]
	ds_read_b128 v[128:131], v18
	v_mfma_f32_16x16x32_f16 v[36:39], v[116:119], v[96:99], v[36:39]
	ds_read_b128 v[144:147], v19 offset:32768
	v_mfma_f32_16x16x32_f16 v[40:43], v[120:123], v[96:99], v[40:43]
	ds_read_b128 v[148:151], v19 offset:34816
	v_mfma_f32_16x16x32_f16 v[44:47], v[124:127], v[96:99], v[44:47]
	ds_read_b128 v[152:155], v19 offset:36864
	v_mfma_f32_16x16x32_f16 v[48:51], v[112:115], v[100:103], v[48:51]
	ds_read_b128 v[156:159], v19 offset:38912
	v_mfma_f32_16x16x32_f16 v[52:55], v[116:119], v[100:103], v[52:55]
	ds_read_b128 v[132:135], v18 offset:2048
	v_mfma_f32_16x16x32_f16 v[56:59], v[120:123], v[100:103], v[56:59]
	ds_read_b128 v[136:139], v18 offset:4096
	v_mfma_f32_16x16x32_f16 v[60:63], v[124:127], v[100:103], v[60:63]
	ds_read_b128 v[140:143], v18 offset:6144
	v_mfma_f32_16x16x32_f16 v[64:67], v[112:115], v[104:107], v[64:67]
	v_mfma_f32_16x16x32_f16 v[68:71], v[116:119], v[104:107], v[68:71]
	v_mfma_f32_16x16x32_f16 v[72:75], v[120:123], v[104:107], v[72:75]
	s_add_u32 m0, s14, 0x12000
	s_nop 0
	global_load_lds_dwordx4 v5, s[28:29]
	v_mfma_f32_16x16x32_f16 v[76:79], v[124:127], v[104:107], v[76:79]
	v_mfma_f32_16x16x32_f16 v[80:83], v[112:115], v[108:111], v[80:83]
	s_add_u32 m0, s14, 0x14000
	s_nop 0
	global_load_lds_dwordx4 v6, s[30:31]
	v_mfma_f32_16x16x32_f16 v[84:87], v[116:119], v[108:111], v[84:87]
	v_mfma_f32_16x16x32_f16 v[88:91], v[120:123], v[108:111], v[88:91]
	s_add_u32 m0, s14, 0x16000
	s_nop 0
	global_load_lds_dwordx4 v7, s[30:31]
	v_mfma_f32_16x16x32_f16 v[92:95], v[124:127], v[108:111], v[92:95]
	s_waitcnt vmcnt(6) lgkmcnt(0)
	s_barrier
	s_add_u32 s28, s28, 0x80
	s_addc_u32 s29, s29, 0
	s_add_u32 s30, s30, 0x80
	s_addc_u32 s31, s31, 0
	s_waitcnt lgkmcnt(0)
	v_mfma_f32_16x16x32_f16 v[32:35], v[144:147], v[128:131], v[32:35]
	ds_read_b128 v[96:99], v8
	v_mfma_f32_16x16x32_f16 v[36:39], v[148:151], v[128:131], v[36:39]
	ds_read_b128 v[112:115], v9 offset:32768
	v_mfma_f32_16x16x32_f16 v[40:43], v[152:155], v[128:131], v[40:43]
	ds_read_b128 v[116:119], v9 offset:34816
	v_mfma_f32_16x16x32_f16 v[44:47], v[156:159], v[128:131], v[44:47]
	ds_read_b128 v[120:123], v9 offset:36864
	v_mfma_f32_16x16x32_f16 v[48:51], v[144:147], v[132:135], v[48:51]
	ds_read_b128 v[124:127], v9 offset:38912
	v_mfma_f32_16x16x32_f16 v[52:55], v[148:151], v[132:135], v[52:55]
	ds_read_b128 v[100:103], v8 offset:2048
	v_mfma_f32_16x16x32_f16 v[56:59], v[152:155], v[132:135], v[56:59]
	ds_read_b128 v[104:107], v8 offset:4096
	v_mfma_f32_16x16x32_f16 v[60:63], v[156:159], v[132:135], v[60:63]
	ds_read_b128 v[108:111], v8 offset:6144
	v_mfma_f32_16x16x32_f16 v[64:67], v[144:147], v[136:139], v[64:67]
	v_mfma_f32_16x16x32_f16 v[68:71], v[148:151], v[136:139], v[68:71]
	v_mfma_f32_16x16x32_f16 v[72:75], v[152:155], v[136:139], v[72:75]
	s_add_u32 m0, s14, 0x18000
	s_nop 0
	global_load_lds_dwordx4 v2, s[28:29]
	v_mfma_f32_16x16x32_f16 v[76:79], v[156:159], v[136:139], v[76:79]
	v_mfma_f32_16x16x32_f16 v[80:83], v[144:147], v[140:143], v[80:83]
	s_add_u32 m0, s14, 0x1a000
	s_nop 0
	global_load_lds_dwordx4 v3, s[28:29]
	v_mfma_f32_16x16x32_f16 v[84:87], v[148:151], v[140:143], v[84:87]
	v_mfma_f32_16x16x32_f16 v[88:91], v[152:155], v[140:143], v[88:91]
	s_add_u32 m0, s14, 0x1c000
	s_nop 0
	global_load_lds_dwordx4 v4, s[28:29]
	v_mfma_f32_16x16x32_f16 v[92:95], v[156:159], v[140:143], v[92:95]
	s_nop 7
	s_nop 1
	v_mul_f32_e32 v160, s50, v32
	v_mul_f32_e32 v161, s50, v33
	v_mul_f32_e32 v162, s50, v34
	v_mul_f32_e32 v163, s50, v35
	v_mul_f32_e32 v164, s50, v36
	v_mul_f32_e32 v165, s50, v37
	v_mul_f32_e32 v166, s50, v38
	v_mul_f32_e32 v167, s50, v39
	v_cvt_pk_f16_f32 v168, v160, v161
	v_cvt_pk_f16_f32 v169, v162, v163
	v_cvt_pk_f16_f32 v170, v164, v165
	v_cvt_pk_f16_f32 v171, v166, v167
	global_store_dwordx4 v24, v[168:171], s[34:35]
	v_mul_f32_e32 v160, s50, v40
	v_mul_f32_e32 v161, s50, v41
	v_mul_f32_e32 v162, s50, v42
	v_mul_f32_e32 v163, s50, v43
	v_mul_f32_e32 v164, s50, v44
	v_mul_f32_e32 v165, s50, v45
	v_mul_f32_e32 v166, s50, v46
	v_mul_f32_e32 v167, s50, v47
	v_cvt_pk_f16_f32 v172, v160, v161
	v_cvt_pk_f16_f32 v173, v162, v163
	v_cvt_pk_f16_f32 v174, v164, v165
	v_cvt_pk_f16_f32 v175, v166, v167
	global_store_dwordx4 v24, v[172:175], s[34:35] offset:64
	v_mul_f32_e32 v160, s50, v48
	v_mul_f32_e32 v161, s50, v49
	v_mul_f32_e32 v162, s50, v50
	v_mul_f32_e32 v163, s50, v51
	v_mul_f32_e32 v164, s50, v52
	v_mul_f32_e32 v165, s50, v53
	v_mul_f32_e32 v166, s50, v54
	v_mul_f32_e32 v167, s50, v55
	v_cvt_pk_f16_f32 v168, v160, v161
	v_cvt_pk_f16_f32 v169, v162, v163
	v_cvt_pk_f16_f32 v170, v164, v165
	v_cvt_pk_f16_f32 v171, v166, v167
	global_store_dwordx4 v25, v[168:171], s[34:35]
	v_mul_f32_e32 v160, s50, v56
	v_mul_f32_e32 v161, s50, v57
	v_mul_f32_e32 v162, s50, v58
	v_mul_f32_e32 v163, s50, v59
	v_mul_f32_e32 v164, s50, v60
	v_mul_f32_e32 v165, s50, v61
	v_mul_f32_e32 v166, s50, v62
	v_mul_f32_e32 v167, s50, v63
	v_cvt_pk_f16_f32 v172, v160, v161
	v_cvt_pk_f16_f32 v173, v162, v163
	v_cvt_pk_f16_f32 v174, v164, v165
	v_cvt_pk_f16_f32 v175, v166, v167
	global_store_dwordx4 v25, v[172:175], s[34:35] offset:64
	v_mul_f32_e32 v160, s50, v64
	v_mul_f32_e32 v161, s50, v65
	v_mul_f32_e32 v162, s50, v66
	v_mul_f32_e32 v163, s50, v67
	v_mul_f32_e32 v164, s50, v68
	v_mul_f32_e32 v165, s50, v69
	v_mul_f32_e32 v166, s50, v70
	v_mul_f32_e32 v167, s50, v71
	v_cvt_pk_f16_f32 v168, v160, v161
	v_cvt_pk_f16_f32 v169, v162, v163
	v_cvt_pk_f16_f32 v170, v164, v165
	v_cvt_pk_f16_f32 v171, v166, v167
	global_store_dwordx4 v26, v[168:171], s[34:35]
	v_mul_f32_e32 v160, s50, v72
	v_mul_f32_e32 v161, s50, v73
	v_mul_f32_e32 v162, s50, v74
	v_mul_f32_e32 v163, s50, v75
	v_mul_f32_e32 v164, s50, v76
	v_mul_f32_e32 v165, s50, v77
	v_mul_f32_e32 v166, s50, v78
	v_mul_f32_e32 v167, s50, v79
	v_cvt_pk_f16_f32 v172, v160, v161
	v_cvt_pk_f16_f32 v173, v162, v163
	v_cvt_pk_f16_f32 v174, v164, v165
	v_cvt_pk_f16_f32 v175, v166, v167
	global_store_dwordx4 v26, v[172:175], s[34:35] offset:64
	v_mul_f32_e32 v160, s50, v80
	v_mul_f32_e32 v161, s50, v81
	v_mul_f32_e32 v162, s50, v82
	v_mul_f32_e32 v163, s50, v83
	v_mul_f32_e32 v164, s50, v84
	v_mul_f32_e32 v165, s50, v85
	v_mul_f32_e32 v166, s50, v86
	v_mul_f32_e32 v167, s50, v87
	v_cvt_pk_f16_f32 v168, v160, v161
	v_cvt_pk_f16_f32 v169, v162, v163
	v_cvt_pk_f16_f32 v170, v164, v165
	v_cvt_pk_f16_f32 v171, v166, v167
	global_store_dwordx4 v27, v[168:171], s[34:35]
	v_mul_f32_e32 v160, s50, v88
	v_mul_f32_e32 v161, s50, v89
	v_mul_f32_e32 v162, s50, v90
	v_mul_f32_e32 v163, s50, v91
	v_mul_f32_e32 v164, s50, v92
	v_mul_f32_e32 v165, s50, v93
	v_mul_f32_e32 v166, s50, v94
	v_mul_f32_e32 v167, s50, v95
	v_cvt_pk_f16_f32 v172, v160, v161
	v_cvt_pk_f16_f32 v173, v162, v163
	v_cvt_pk_f16_f32 v174, v164, v165
	v_cvt_pk_f16_f32 v175, v166, v167
	global_store_dwordx4 v27, v[172:175], s[34:35] offset:64
	s_waitcnt lgkmcnt(0)
	v_mfma_f32_16x16x32_f16 v[32:35], v[112:115], v[96:99], 0
	ds_read_b128 v[128:131], v10
	v_mfma_f32_16x16x32_f16 v[36:39], v[116:119], v[96:99], 0
	ds_read_b128 v[144:147], v11 offset:32768
	v_mfma_f32_16x16x32_f16 v[40:43], v[120:123], v[96:99], 0
	ds_read_b128 v[148:151], v11 offset:34816
	v_mfma_f32_16x16x32_f16 v[44:47], v[124:127], v[96:99], 0
	ds_read_b128 v[152:155], v11 offset:36864
	v_mfma_f32_16x16x32_f16 v[48:51], v[112:115], v[100:103], 0
	ds_read_b128 v[156:159], v11 offset:38912
	v_mfma_f32_16x16x32_f16 v[52:55], v[116:119], v[100:103], 0
	ds_read_b128 v[132:135], v10 offset:2048
	v_mfma_f32_16x16x32_f16 v[56:59], v[120:123], v[100:103], 0
	ds_read_b128 v[136:139], v10 offset:4096
	v_mfma_f32_16x16x32_f16 v[60:63], v[124:127], v[100:103], 0
	ds_read_b128 v[140:143], v10 offset:6144
	v_mfma_f32_16x16x32_f16 v[64:67], v[112:115], v[104:107], 0
	v_mfma_f32_16x16x32_f16 v[68:71], v[116:119], v[104:107], 0
	v_mfma_f32_16x16x32_f16 v[72:75], v[120:123], v[104:107], 0
	s_add_u32 m0, s14, 0x1e000
	s_nop 0
	global_load_lds_dwordx4 v5, s[28:29]
	v_mfma_f32_16x16x32_f16 v[76:79], v[124:127], v[104:107], 0
	v_mfma_f32_16x16x32_f16 v[80:83], v[112:115], v[108:111], 0
	s_add_u32 m0, s14, 0x20000
	s_nop 0
	global_load_lds_dwordx4 v6, s[30:31]
	v_mfma_f32_16x16x32_f16 v[84:87], v[116:119], v[108:111], 0
	v_mfma_f32_16x16x32_f16 v[88:91], v[120:123], v[108:111], 0
	s_add_u32 m0, s14, 0x22000
	s_nop 0
	global_load_lds_dwordx4 v7, s[30:31]
	v_mfma_f32_16x16x32_f16 v[92:95], v[124:127], v[108:111], 0
	s_waitcnt vmcnt(14) lgkmcnt(0)
	s_barrier
	s_add_u32 s28, s28, 0x80
	s_addc_u32 s29, s29, 0
	s_add_u32 s30, s30, 0x80
	s_addc_u32 s31, s31, 0
	s_waitcnt lgkmcnt(0)
	v_mfma_f32_16x16x32_f16 v[32:35], v[144:147], v[128:131], v[32:35]
	ds_read_b128 v[96:99], v12
	v_mfma_f32_16x16x32_f16 v[36:39], v[148:151], v[128:131], v[36:39]
	ds_read_b128 v[112:115], v13 offset:32768
	v_mfma_f32_16x16x32_f16 v[40:43], v[152:155], v[128:131], v[40:43]
	ds_read_b128 v[116:119], v13 offset:34816
	v_mfma_f32_16x16x32_f16 v[44:47], v[156:159], v[128:131], v[44:47]
	ds_read_b128 v[120:123], v13 offset:36864
	v_mfma_f32_16x16x32_f16 v[48:51], v[144:147], v[132:135], v[48:51]
	ds_read_b128 v[124:127], v13 offset:38912
	v_mfma_f32_16x16x32_f16 v[52:55], v[148:151], v[132:135], v[52:55]
	ds_read_b128 v[100:103], v12 offset:2048
	v_mfma_f32_16x16x32_f16 v[56:59], v[152:155], v[132:135], v[56:59]
	ds_read_b128 v[104:107], v12 offset:4096
	v_mfma_f32_16x16x32_f16 v[60:63], v[156:159], v[132:135], v[60:63]
	ds_read_b128 v[108:111], v12 offset:6144
	v_mfma_f32_16x16x32_f16 v[64:67], v[144:147], v[136:139], v[64:67]
	v_mfma_f32_16x16x32_f16 v[68:71], v[148:151], v[136:139], v[68:71]
	v_mfma_f32_16x16x32_f16 v[72:75], v[152:155], v[136:139], v[72:75]
	s_add_u32 m0, s14, 0x0
	s_nop 0
	global_load_lds_dwordx4 v2, s[28:29]
	v_mfma_f32_16x16x32_f16 v[76:79], v[156:159], v[136:139], v[76:79]
	v_mfma_f32_16x16x32_f16 v[80:83], v[144:147], v[140:143], v[80:83]
	s_add_u32 m0, s14, 0x2000
	s_nop 0
	global_load_lds_dwordx4 v3, s[28:29]
	v_mfma_f32_16x16x32_f16 v[84:87], v[148:151], v[140:143], v[84:87]
	v_mfma_f32_16x16x32_f16 v[88:91], v[152:155], v[140:143], v[88:91]
	s_add_u32 m0, s14, 0x4000
	s_nop 0
	global_load_lds_dwordx4 v4, s[28:29]
	v_mfma_f32_16x16x32_f16 v[92:95], v[156:159], v[140:143], v[92:95]
	s_waitcnt lgkmcnt(0)
	v_mfma_f32_16x16x32_f16 v[32:35], v[112:115], v[96:99], v[32:35]
	ds_read_b128 v[128:131], v14
	v_mfma_f32_16x16x32_f16 v[36:39], v[116:119], v[96:99], v[36:39]
	ds_read_b128 v[144:147], v15 offset:32768
	v_mfma_f32_16x16x32_f16 v[40:43], v[120:123], v[96:99], v[40:43]
	ds_read_b128 v[148:151], v15 offset:34816
	v_mfma_f32_16x16x32_f16 v[44:47], v[124:127], v[96:99], v[44:47]
	ds_read_b128 v[152:155], v15 offset:36864
	v_mfma_f32_16x16x32_f16 v[48:51], v[112:115], v[100:103], v[48:51]
	ds_read_b128 v[156:159], v15 offset:38912
	v_mfma_f32_16x16x32_f16 v[52:55], v[116:119], v[100:103], v[52:55]
	ds_read_b128 v[132:135], v14 offset:2048
	v_mfma_f32_16x16x32_f16 v[56:59], v[120:123], v[100:103], v[56:59]
	ds_read_b128 v[136:139], v14 offset:4096
	v_mfma_f32_16x16x32_f16 v[60:63], v[124:127], v[100:103], v[60:63]
	ds_read_b128 v[140:143], v14 offset:6144
	v_mfma_f32_16x16x32_f16 v[64:67], v[112:115], v[104:107], v[64:67]
	v_mfma_f32_16x16x32_f16 v[68:71], v[116:119], v[104:107], v[68:71]
	v_mfma_f32_16x16x32_f16 v[72:75], v[120:123], v[104:107], v[72:75]
	s_add_u32 m0, s14, 0x6000
	s_nop 0
	global_load_lds_dwordx4 v5, s[28:29]
	v_mfma_f32_16x16x32_f16 v[76:79], v[124:127], v[104:107], v[76:79]
	v_mfma_f32_16x16x32_f16 v[80:83], v[112:115], v[108:111], v[80:83]
	s_add_u32 m0, s14, 0x8000
	s_nop 0
	global_load_lds_dwordx4 v6, s[30:31]
	v_mfma_f32_16x16x32_f16 v[84:87], v[116:119], v[108:111], v[84:87]
	v_mfma_f32_16x16x32_f16 v[88:91], v[120:123], v[108:111], v[88:91]
	s_add_u32 m0, s14, 0xa000
	s_nop 0
	global_load_lds_dwordx4 v7, s[30:31]
	v_mfma_f32_16x16x32_f16 v[92:95], v[124:127], v[108:111], v[92:95]
	s_waitcnt vmcnt(6) lgkmcnt(0)
	s_barrier
	s_add_u32 s28, s28, 0x80
	s_addc_u32 s29, s29, 0
	s_add_u32 s30, s30, 0x80
	s_addc_u32 s31, s31, 0
	s_waitcnt lgkmcnt(0)
	v_mfma_f32_16x16x32_f16 v[32:35], v[144:147], v[128:131], v[32:35]
	ds_read_b128 v[96:99], v16
	v_mfma_f32_16x16x32_f16 v[36:39], v[148:151], v[128:131], v[36:39]
	ds_read_b128 v[112:115], v17 offset:32768
	v_mfma_f32_16x16x32_f16 v[40:43], v[152:155], v[128:131], v[40:43]
	ds_read_b128 v[116:119], v17 offset:34816
	v_mfma_f32_16x16x32_f16 v[44:47], v[156:159], v[128:131], v[44:47]
	ds_read_b128 v[120:123], v17 offset:36864
	v_mfma_f32_16x16x32_f16 v[48:51], v[144:147], v[132:135], v[48:51]
	ds_read_b128 v[124:127], v17 offset:38912
	v_mfma_f32_16x16x32_f16 v[52:55], v[148:151], v[132:135], v[52:55]
	ds_read_b128 v[100:103], v16 offset:2048
	v_mfma_f32_16x16x32_f16 v[56:59], v[152:155], v[132:135], v[56:59]
	ds_read_b128 v[104:107], v16 offset:4096
	v_mfma_f32_16x16x32_f16 v[60:63], v[156:159], v[132:135], v[60:63]
	ds_read_b128 v[108:111], v16 offset:6144
	v_mfma_f32_16x16x32_f16 v[64:67], v[144:147], v[136:139], v[64:67]
	v_mfma_f32_16x16x32_f16 v[68:71], v[148:151], v[136:139], v[68:71]
	v_mfma_f32_16x16x32_f16 v[72:75], v[152:155], v[136:139], v[72:75]
	s_add_u32 m0, s14, 0xc000
	s_nop 0
	global_load_lds_dwordx4 v2, s[28:29]
	v_mfma_f32_16x16x32_f16 v[76:79], v[156:159], v[136:139], v[76:79]
	v_mfma_f32_16x16x32_f16 v[80:83], v[144:147], v[140:143], v[80:83]
	s_add_u32 m0, s14, 0xe000
	s_nop 0
	global_load_lds_dwordx4 v3, s[28:29]
	v_mfma_f32_16x16x32_f16 v[84:87], v[148:151], v[140:143], v[84:87]
	v_mfma_f32_16x16x32_f16 v[88:91], v[152:155], v[140:143], v[88:91]
	s_add_u32 m0, s14, 0x10000
	s_nop 0
	global_load_lds_dwordx4 v4, s[28:29]
	v_mfma_f32_16x16x32_f16 v[92:95], v[156:159], v[140:143], v[92:95]
	s_waitcnt lgkmcnt(0)
	v_mfma_f32_16x16x32_f16 v[32:35], v[112:115], v[96:99], v[32:35]
	ds_read_b128 v[128:131], v18
	v_mfma_f32_16x16x32_f16 v[36:39], v[116:119], v[96:99], v[36:39]
	ds_read_b128 v[144:147], v19 offset:32768
	v_mfma_f32_16x16x32_f16 v[40:43], v[120:123], v[96:99], v[40:43]
	ds_read_b128 v[148:151], v19 offset:34816
	v_mfma_f32_16x16x32_f16 v[44:47], v[124:127], v[96:99], v[44:47]
	ds_read_b128 v[152:155], v19 offset:36864
	v_mfma_f32_16x16x32_f16 v[48:51], v[112:115], v[100:103], v[48:51]
	ds_read_b128 v[156:159], v19 offset:38912
	v_mfma_f32_16x16x32_f16 v[52:55], v[116:119], v[100:103], v[52:55]
	ds_read_b128 v[132:135], v18 offset:2048
	v_mfma_f32_16x16x32_f16 v[56:59], v[120:123], v[100:103], v[56:59]
	ds_read_b128 v[136:139], v18 offset:4096
	v_mfma_f32_16x16x32_f16 v[60:63], v[124:127], v[100:103], v[60:63]
	ds_read_b128 v[140:143], v18 offset:6144
	v_mfma_f32_16x16x32_f16 v[64:67], v[112:115], v[104:107], v[64:67]
	v_mfma_f32_16x16x32_f16 v[68:71], v[116:119], v[104:107], v[68:71]
	v_mfma_f32_16x16x32_f16 v[72:75], v[120:123], v[104:107], v[72:75]
	s_add_u32 m0, s14, 0x12000
	s_nop 0
	global_load_lds_dwordx4 v5, s[28:29]
	v_mfma_f32_16x16x32_f16 v[76:79], v[124:127], v[104:107], v[76:79]
	v_mfma_f32_16x16x32_f16 v[80:83], v[112:115], v[108:111], v[80:83]
	s_add_u32 m0, s14, 0x14000
	s_nop 0
	global_load_lds_dwordx4 v6, s[30:31]
	v_mfma_f32_16x16x32_f16 v[84:87], v[116:119], v[108:111], v[84:87]
	v_mfma_f32_16x16x32_f16 v[88:91], v[120:123], v[108:111], v[88:91]
	s_add_u32 m0, s14, 0x16000
	s_nop 0
	global_load_lds_dwordx4 v7, s[30:31]
	v_mfma_f32_16x16x32_f16 v[92:95], v[124:127], v[108:111], v[92:95]
	s_waitcnt vmcnt(6) lgkmcnt(0)
	s_barrier
	s_add_u32 s28, s28, 0x80
	s_addc_u32 s29, s29, 0
	s_add_u32 s30, s30, 0x80
	s_addc_u32 s31, s31, 0
	s_waitcnt lgkmcnt(0)
	v_mfma_f32_16x16x32_f16 v[32:35], v[144:147], v[128:131], v[32:35]
	ds_read_b128 v[96:99], v8
	v_mfma_f32_16x16x32_f16 v[36:39], v[148:151], v[128:131], v[36:39]
	ds_read_b128 v[112:115], v9 offset:32768
	v_mfma_f32_16x16x32_f16 v[40:43], v[152:155], v[128:131], v[40:43]
	ds_read_b128 v[116:119], v9 offset:34816
	v_mfma_f32_16x16x32_f16 v[44:47], v[156:159], v[128:131], v[44:47]
	ds_read_b128 v[120:123], v9 offset:36864
	v_mfma_f32_16x16x32_f16 v[48:51], v[144:147], v[132:135], v[48:51]
	ds_read_b128 v[124:127], v9 offset:38912
	v_mfma_f32_16x16x32_f16 v[52:55], v[148:151], v[132:135], v[52:55]
	ds_read_b128 v[100:103], v8 offset:2048
	v_mfma_f32_16x16x32_f16 v[56:59], v[152:155], v[132:135], v[56:59]
	ds_read_b128 v[104:107], v8 offset:4096
	v_mfma_f32_16x16x32_f16 v[60:63], v[156:159], v[132:135], v[60:63]
	ds_read_b128 v[108:111], v8 offset:6144
	v_mfma_f32_16x16x32_f16 v[64:67], v[144:147], v[136:139], v[64:67]
	v_mfma_f32_16x16x32_f16 v[68:71], v[148:151], v[136:139], v[68:71]
	v_mfma_f32_16x16x32_f16 v[72:75], v[152:155], v[136:139], v[72:75]
	s_add_u32 m0, s14, 0x18000
	s_nop 0
	global_load_lds_dwordx4 v2, s[28:29]
	v_mfma_f32_16x16x32_f16 v[76:79], v[156:159], v[136:139], v[76:79]
	v_mfma_f32_16x16x32_f16 v[80:83], v[144:147], v[140:143], v[80:83]
	s_add_u32 m0, s14, 0x1a000
	s_nop 0
	global_load_lds_dwordx4 v3, s[28:29]
	v_mfma_f32_16x16x32_f16 v[84:87], v[148:151], v[140:143], v[84:87]
	v_mfma_f32_16x16x32_f16 v[88:91], v[152:155], v[140:143], v[88:91]
	s_add_u32 m0, s14, 0x1c000
	s_nop 0
	global_load_lds_dwordx4 v4, s[28:29]
	v_mfma_f32_16x16x32_f16 v[92:95], v[156:159], v[140:143], v[92:95]
	s_waitcnt lgkmcnt(0)
	v_mfma_f32_16x16x32_f16 v[32:35], v[112:115], v[96:99], v[32:35]
	ds_read_b128 v[128:131], v10
	v_mfma_f32_16x16x32_f16 v[36:39], v[116:119], v[96:99], v[36:39]
	ds_read_b128 v[144:147], v11 offset:32768
	v_mfma_f32_16x16x32_f16 v[40:43], v[120:123], v[96:99], v[40:43]
	ds_read_b128 v[148:151], v11 offset:34816
	v_mfma_f32_16x16x32_f16 v[44:47], v[124:127], v[96:99], v[44:47]
	ds_read_b128 v[152:155], v11 offset:36864
	v_mfma_f32_16x16x32_f16 v[48:51], v[112:115], v[100:103], v[48:51]
	ds_read_b128 v[156:159], v11 offset:38912
	v_mfma_f32_16x16x32_f16 v[52:55], v[116:119], v[100:103], v[52:55]
	ds_read_b128 v[132:135], v10 offset:2048
	v_mfma_f32_16x16x32_f16 v[56:59], v[120:123], v[100:103], v[56:59]
	ds_read_b128 v[136:139], v10 offset:4096
	v_mfma_f32_16x16x32_f16 v[60:63], v[124:127], v[100:103], v[60:63]
	ds_read_b128 v[140:143], v10 offset:6144
	v_mfma_f32_16x16x32_f16 v[64:67], v[112:115], v[104:107], v[64:67]
	v_mfma_f32_16x16x32_f16 v[68:71], v[116:119], v[104:107], v[68:71]
	v_mfma_f32_16x16x32_f16 v[72:75], v[120:123], v[104:107], v[72:75]
	s_add_u32 m0, s14, 0x1e000
	s_nop 0
	global_load_lds_dwordx4 v5, s[28:29]
	v_mfma_f32_16x16x32_f16 v[76:79], v[124:127], v[104:107], v[76:79]
	v_mfma_f32_16x16x32_f16 v[80:83], v[112:115], v[108:111], v[80:83]
	s_add_u32 m0, s14, 0x20000
	s_nop 0
	global_load_lds_dwordx4 v6, s[30:31]
	v_mfma_f32_16x16x32_f16 v[84:87], v[116:119], v[108:111], v[84:87]
	v_mfma_f32_16x16x32_f16 v[88:91], v[120:123], v[108:111], v[88:91]
	s_add_u32 m0, s14, 0x22000
	s_nop 0
	global_load_lds_dwordx4 v7, s[30:31]
	v_mfma_f32_16x16x32_f16 v[92:95], v[124:127], v[108:111], v[92:95]
	s_waitcnt vmcnt(6) lgkmcnt(0)
	s_barrier
	s_add_u32 s28, s28, 0x80
	s_addc_u32 s29, s29, 0
	s_add_u32 s30, s30, 0x80
	s_addc_u32 s31, s31, 0
	s_waitcnt lgkmcnt(0)
	v_mfma_f32_16x16x32_f16 v[32:35], v[144:147], v[128:131], v[32:35]
	ds_read_b128 v[96:99], v12
	v_mfma_f32_16x16x32_f16 v[36:39], v[148:151], v[128:131], v[36:39]
	ds_read_b128 v[112:115], v13 offset:32768
	v_mfma_f32_16x16x32_f16 v[40:43], v[152:155], v[128:131], v[40:43]
	ds_read_b128 v[116:119], v13 offset:34816
	v_mfma_f32_16x16x32_f16 v[44:47], v[156:159], v[128:131], v[44:47]
	ds_read_b128 v[120:123], v13 offset:36864
	v_mfma_f32_16x16x32_f16 v[48:51], v[144:147], v[132:135], v[48:51]
	ds_read_b128 v[124:127], v13 offset:38912
	v_mfma_f32_16x16x32_f16 v[52:55], v[148:151], v[132:135], v[52:55]
	ds_read_b128 v[100:103], v12 offset:2048
	v_mfma_f32_16x16x32_f16 v[56:59], v[152:155], v[132:135], v[56:59]
	ds_read_b128 v[104:107], v12 offset:4096
	v_mfma_f32_16x16x32_f16 v[60:63], v[156:159], v[132:135], v[60:63]
	ds_read_b128 v[108:111], v12 offset:6144
	v_mfma_f32_16x16x32_f16 v[64:67], v[144:147], v[136:139], v[64:67]
	v_mfma_f32_16x16x32_f16 v[68:71], v[148:151], v[136:139], v[68:71]
	v_mfma_f32_16x16x32_f16 v[72:75], v[152:155], v[136:139], v[72:75]
	s_add_u32 m0, s14, 0x0
	s_nop 0
	global_load_lds_dwordx4 v2, s[28:29]
	v_mfma_f32_16x16x32_f16 v[76:79], v[156:159], v[136:139], v[76:79]
	v_mfma_f32_16x16x32_f16 v[80:83], v[144:147], v[140:143], v[80:83]
	s_add_u32 m0, s14, 0x2000
	s_nop 0
	global_load_lds_dwordx4 v3, s[28:29]
	v_mfma_f32_16x16x32_f16 v[84:87], v[148:151], v[140:143], v[84:87]
	v_mfma_f32_16x16x32_f16 v[88:91], v[152:155], v[140:143], v[88:91]
	s_add_u32 m0, s14, 0x4000
	s_nop 0
	global_load_lds_dwordx4 v4, s[28:29]
	v_mfma_f32_16x16x32_f16 v[92:95], v[156:159], v[140:143], v[92:95]
	s_waitcnt lgkmcnt(0)
	v_mfma_f32_16x16x32_f16 v[32:35], v[112:115], v[96:99], v[32:35]
	ds_read_b128 v[128:131], v14
	v_mfma_f32_16x16x32_f16 v[36:39], v[116:119], v[96:99], v[36:39]
	ds_read_b128 v[144:147], v15 offset:32768
	v_mfma_f32_16x16x32_f16 v[40:43], v[120:123], v[96:99], v[40:43]
	ds_read_b128 v[148:151], v15 offset:34816
	v_mfma_f32_16x16x32_f16 v[44:47], v[124:127], v[96:99], v[44:47]
	ds_read_b128 v[152:155], v15 offset:36864
	v_mfma_f32_16x16x32_f16 v[48:51], v[112:115], v[100:103], v[48:51]
	ds_read_b128 v[156:159], v15 offset:38912
	v_mfma_f32_16x16x32_f16 v[52:55], v[116:119], v[100:103], v[52:55]
	ds_read_b128 v[132:135], v14 offset:2048
	v_mfma_f32_16x16x32_f16 v[56:59], v[120:123], v[100:103], v[56:59]
	ds_read_b128 v[136:139], v14 offset:4096
	v_mfma_f32_16x16x32_f16 v[60:63], v[124:127], v[100:103], v[60:63]
	ds_read_b128 v[140:143], v14 offset:6144
	v_mfma_f32_16x16x32_f16 v[64:67], v[112:115], v[104:107], v[64:67]
	v_mfma_f32_16x16x32_f16 v[68:71], v[116:119], v[104:107], v[68:71]
	v_mfma_f32_16x16x32_f16 v[72:75], v[120:123], v[104:107], v[72:75]
	s_add_u32 m0, s14, 0x6000
	s_nop 0
	global_load_lds_dwordx4 v5, s[28:29]
	v_mfma_f32_16x16x32_f16 v[76:79], v[124:127], v[104:107], v[76:79]
	v_mfma_f32_16x16x32_f16 v[80:83], v[112:115], v[108:111], v[80:83]
	s_add_u32 m0, s14, 0x8000
	s_nop 0
	global_load_lds_dwordx4 v6, s[30:31]
	v_mfma_f32_16x16x32_f16 v[84:87], v[116:119], v[108:111], v[84:87]
	v_mfma_f32_16x16x32_f16 v[88:91], v[120:123], v[108:111], v[88:91]
	s_add_u32 m0, s14, 0xa000
	s_nop 0
	global_load_lds_dwordx4 v7, s[30:31]
	v_mfma_f32_16x16x32_f16 v[92:95], v[124:127], v[108:111], v[92:95]
	s_waitcnt vmcnt(6) lgkmcnt(0)
	s_barrier
	s_add_u32 s28, s28, 0x80
	s_addc_u32 s29, s29, 0
	s_add_u32 s30, s30, 0x80
	s_addc_u32 s31, s31, 0
	s_waitcnt lgkmcnt(0)
	v_mfma_f32_16x16x32_f16 v[32:35], v[144:147], v[128:131], v[32:35]
	ds_read_b128 v[96:99], v16
	v_mfma_f32_16x16x32_f16 v[36:39], v[148:151], v[128:131], v[36:39]
	ds_read_b128 v[112:115], v17 offset:32768
	v_mfma_f32_16x16x32_f16 v[40:43], v[152:155], v[128:131], v[40:43]
	ds_read_b128 v[116:119], v17 offset:34816
	v_mfma_f32_16x16x32_f16 v[44:47], v[156:159], v[128:131], v[44:47]
	ds_read_b128 v[120:123], v17 offset:36864
	v_mfma_f32_16x16x32_f16 v[48:51], v[144:147], v[132:135], v[48:51]
	ds_read_b128 v[124:127], v17 offset:38912
	v_mfma_f32_16x16x32_f16 v[52:55], v[148:151], v[132:135], v[52:55]
	ds_read_b128 v[100:103], v16 offset:2048
	v_mfma_f32_16x16x32_f16 v[56:59], v[152:155], v[132:135], v[56:59]
	ds_read_b128 v[104:107], v16 offset:4096
	v_mfma_f32_16x16x32_f16 v[60:63], v[156:159], v[132:135], v[60:63]
	ds_read_b128 v[108:111], v16 offset:6144
	v_mfma_f32_16x16x32_f16 v[64:67], v[144:147], v[136:139], v[64:67]
	v_mfma_f32_16x16x32_f16 v[68:71], v[148:151], v[136:139], v[68:71]
	v_mfma_f32_16x16x32_f16 v[72:75], v[152:155], v[136:139], v[72:75]
	s_add_u32 m0, s14, 0xc000
	s_nop 0
	global_load_lds_dwordx4 v2, s[28:29]
	v_mfma_f32_16x16x32_f16 v[76:79], v[156:159], v[136:139], v[76:79]
	v_mfma_f32_16x16x32_f16 v[80:83], v[144:147], v[140:143], v[80:83]
	s_add_u32 m0, s14, 0xe000
	s_nop 0
	global_load_lds_dwordx4 v3, s[28:29]
	v_mfma_f32_16x16x32_f16 v[84:87], v[148:151], v[140:143], v[84:87]
	v_mfma_f32_16x16x32_f16 v[88:91], v[152:155], v[140:143], v[88:91]
	s_add_u32 m0, s14, 0x10000
	s_nop 0
	global_load_lds_dwordx4 v4, s[28:29]
	v_mfma_f32_16x16x32_f16 v[92:95], v[156:159], v[140:143], v[92:95]
	s_waitcnt lgkmcnt(0)
	v_mfma_f32_16x16x32_f16 v[32:35], v[112:115], v[96:99], v[32:35]
	ds_read_b128 v[128:131], v18
	v_mfma_f32_16x16x32_f16 v[36:39], v[116:119], v[96:99], v[36:39]
	ds_read_b128 v[144:147], v19 offset:32768
	v_mfma_f32_16x16x32_f16 v[40:43], v[120:123], v[96:99], v[40:43]
	ds_read_b128 v[148:151], v19 offset:34816
	v_mfma_f32_16x16x32_f16 v[44:47], v[124:127], v[96:99], v[44:47]
	ds_read_b128 v[152:155], v19 offset:36864
	v_mfma_f32_16x16x32_f16 v[48:51], v[112:115], v[100:103], v[48:51]
	ds_read_b128 v[156:159], v19 offset:38912
	v_mfma_f32_16x16x32_f16 v[52:55], v[116:119], v[100:103], v[52:55]
	ds_read_b128 v[132:135], v18 offset:2048
	v_mfma_f32_16x16x32_f16 v[56:59], v[120:123], v[100:103], v[56:59]
	ds_read_b128 v[136:139], v18 offset:4096
	v_mfma_f32_16x16x32_f16 v[60:63], v[124:127], v[100:103], v[60:63]
	ds_read_b128 v[140:143], v18 offset:6144
	v_mfma_f32_16x16x32_f16 v[64:67], v[112:115], v[104:107], v[64:67]
	v_mfma_f32_16x16x32_f16 v[68:71], v[116:119], v[104:107], v[68:71]
	v_mfma_f32_16x16x32_f16 v[72:75], v[120:123], v[104:107], v[72:75]
	s_add_u32 m0, s14, 0x12000
	s_nop 0
	global_load_lds_dwordx4 v5, s[28:29]
	v_mfma_f32_16x16x32_f16 v[76:79], v[124:127], v[104:107], v[76:79]
	v_mfma_f32_16x16x32_f16 v[80:83], v[112:115], v[108:111], v[80:83]
	s_add_u32 m0, s14, 0x14000
	s_nop 0
	global_load_lds_dwordx4 v6, s[30:31]
	v_mfma_f32_16x16x32_f16 v[84:87], v[116:119], v[108:111], v[84:87]
	v_mfma_f32_16x16x32_f16 v[88:91], v[120:123], v[108:111], v[88:91]
	s_add_u32 m0, s14, 0x16000
	s_nop 0
	global_load_lds_dwordx4 v7, s[30:31]
	v_mfma_f32_16x16x32_f16 v[92:95], v[124:127], v[108:111], v[92:95]
	s_waitcnt vmcnt(6) lgkmcnt(0)
	s_barrier
	s_add_u32 s28, s28, 0x80
	s_addc_u32 s29, s29, 0
	s_add_u32 s30, s30, 0x80
	s_addc_u32 s31, s31, 0
	s_waitcnt lgkmcnt(0)
	v_mfma_f32_16x16x32_f16 v[32:35], v[144:147], v[128:131], v[32:35]
	ds_read_b128 v[96:99], v8
	v_mfma_f32_16x16x32_f16 v[36:39], v[148:151], v[128:131], v[36:39]
	ds_read_b128 v[112:115], v9 offset:32768
	v_mfma_f32_16x16x32_f16 v[40:43], v[152:155], v[128:131], v[40:43]
	ds_read_b128 v[116:119], v9 offset:34816
	v_mfma_f32_16x16x32_f16 v[44:47], v[156:159], v[128:131], v[44:47]
	ds_read_b128 v[120:123], v9 offset:36864
	v_mfma_f32_16x16x32_f16 v[48:51], v[144:147], v[132:135], v[48:51]
	ds_read_b128 v[124:127], v9 offset:38912
	v_mfma_f32_16x16x32_f16 v[52:55], v[148:151], v[132:135], v[52:55]
	ds_read_b128 v[100:103], v8 offset:2048
	v_mfma_f32_16x16x32_f16 v[56:59], v[152:155], v[132:135], v[56:59]
	ds_read_b128 v[104:107], v8 offset:4096
	v_mfma_f32_16x16x32_f16 v[60:63], v[156:159], v[132:135], v[60:63]
	ds_read_b128 v[108:111], v8 offset:6144
	v_mfma_f32_16x16x32_f16 v[64:67], v[144:147], v[136:139], v[64:67]
	v_mfma_f32_16x16x32_f16 v[68:71], v[148:151], v[136:139], v[68:71]
	v_mfma_f32_16x16x32_f16 v[72:75], v[152:155], v[136:139], v[72:75]
	s_add_u32 m0, s14, 0x18000
	s_nop 0
	global_load_lds_dwordx4 v2, s[28:29]
	v_mfma_f32_16x16x32_f16 v[76:79], v[156:159], v[136:139], v[76:79]
	v_mfma_f32_16x16x32_f16 v[80:83], v[144:147], v[140:143], v[80:83]
	s_add_u32 m0, s14, 0x1a000
	s_nop 0
	global_load_lds_dwordx4 v3, s[28:29]
	v_mfma_f32_16x16x32_f16 v[84:87], v[148:151], v[140:143], v[84:87]
	v_mfma_f32_16x16x32_f16 v[88:91], v[152:155], v[140:143], v[88:91]
	s_add_u32 m0, s14, 0x1c000
	s_nop 0
	global_load_lds_dwordx4 v4, s[28:29]
	v_mfma_f32_16x16x32_f16 v[92:95], v[156:159], v[140:143], v[92:95]
	s_waitcnt lgkmcnt(0)
	v_mfma_f32_16x16x32_f16 v[32:35], v[112:115], v[96:99], v[32:35]
	ds_read_b128 v[128:131], v10
	v_mfma_f32_16x16x32_f16 v[36:39], v[116:119], v[96:99], v[36:39]
	ds_read_b128 v[144:147], v11 offset:32768
	v_mfma_f32_16x16x32_f16 v[40:43], v[120:123], v[96:99], v[40:43]
	ds_read_b128 v[148:151], v11 offset:34816
	v_mfma_f32_16x16x32_f16 v[44:47], v[124:127], v[96:99], v[44:47]
	ds_read_b128 v[152:155], v11 offset:36864
	v_mfma_f32_16x16x32_f16 v[48:51], v[112:115], v[100:103], v[48:51]
	ds_read_b128 v[156:159], v11 offset:38912
	v_mfma_f32_16x16x32_f16 v[52:55], v[116:119], v[100:103], v[52:55]
	ds_read_b128 v[132:135], v10 offset:2048
	v_mfma_f32_16x16x32_f16 v[56:59], v[120:123], v[100:103], v[56:59]
	ds_read_b128 v[136:139], v10 offset:4096
	v_mfma_f32_16x16x32_f16 v[60:63], v[124:127], v[100:103], v[60:63]
	ds_read_b128 v[140:143], v10 offset:6144
	v_mfma_f32_16x16x32_f16 v[64:67], v[112:115], v[104:107], v[64:67]
	v_mfma_f32_16x16x32_f16 v[68:71], v[116:119], v[104:107], v[68:71]
	v_mfma_f32_16x16x32_f16 v[72:75], v[120:123], v[104:107], v[72:75]
	s_add_u32 m0, s14, 0x1e000
	s_nop 0
	global_load_lds_dwordx4 v5, s[28:29]
	v_mfma_f32_16x16x32_f16 v[76:79], v[124:127], v[104:107], v[76:79]
	v_mfma_f32_16x16x32_f16 v[80:83], v[112:115], v[108:111], v[80:83]
	s_add_u32 m0, s14, 0x20000
	s_nop 0
	global_load_lds_dwordx4 v6, s[30:31]
	v_mfma_f32_16x16x32_f16 v[84:87], v[116:119], v[108:111], v[84:87]
	v_mfma_f32_16x16x32_f16 v[88:91], v[120:123], v[108:111], v[88:91]
	s_add_u32 m0, s14, 0x22000
	s_nop 0
	global_load_lds_dwordx4 v7, s[30:31]
	v_mfma_f32_16x16x32_f16 v[92:95], v[124:127], v[108:111], v[92:95]
	s_waitcnt vmcnt(6) lgkmcnt(0)
	s_barrier
	s_add_u32 s28, s28, 0x80
	s_addc_u32 s29, s29, 0
	s_add_u32 s30, s30, 0x80
	s_addc_u32 s31, s31, 0
	s_waitcnt lgkmcnt(0)
	v_mfma_f32_16x16x32_f16 v[32:35], v[144:147], v[128:131], v[32:35]
	ds_read_b128 v[96:99], v12
	v_mfma_f32_16x16x32_f16 v[36:39], v[148:151], v[128:131], v[36:39]
	ds_read_b128 v[112:115], v13 offset:32768
	v_mfma_f32_16x16x32_f16 v[40:43], v[152:155], v[128:131], v[40:43]
	ds_read_b128 v[116:119], v13 offset:34816
	v_mfma_f32_16x16x32_f16 v[44:47], v[156:159], v[128:131], v[44:47]
	ds_read_b128 v[120:123], v13 offset:36864
	v_mfma_f32_16x16x32_f16 v[48:51], v[144:147], v[132:135], v[48:51]
	ds_read_b128 v[124:127], v13 offset:38912
	v_mfma_f32_16x16x32_f16 v[52:55], v[148:151], v[132:135], v[52:55]
	ds_read_b128 v[100:103], v12 offset:2048
	v_mfma_f32_16x16x32_f16 v[56:59], v[152:155], v[132:135], v[56:59]
	ds_read_b128 v[104:107], v12 offset:4096
	v_mfma_f32_16x16x32_f16 v[60:63], v[156:159], v[132:135], v[60:63]
	ds_read_b128 v[108:111], v12 offset:6144
	v_mfma_f32_16x16x32_f16 v[64:67], v[144:147], v[136:139], v[64:67]
	v_mfma_f32_16x16x32_f16 v[68:71], v[148:151], v[136:139], v[68:71]
	v_mfma_f32_16x16x32_f16 v[72:75], v[152:155], v[136:139], v[72:75]
	s_add_u32 m0, s14, 0x0
	s_nop 0
	global_load_lds_dwordx4 v2, s[28:29]
	v_mfma_f32_16x16x32_f16 v[76:79], v[156:159], v[136:139], v[76:79]
	v_mfma_f32_16x16x32_f16 v[80:83], v[144:147], v[140:143], v[80:83]
	s_add_u32 m0, s14, 0x2000
	s_nop 0
	global_load_lds_dwordx4 v3, s[28:29]
	v_mfma_f32_16x16x32_f16 v[84:87], v[148:151], v[140:143], v[84:87]
	v_mfma_f32_16x16x32_f16 v[88:91], v[152:155], v[140:143], v[88:91]
	s_add_u32 m0, s14, 0x4000
	s_nop 0
	global_load_lds_dwordx4 v4, s[28:29]
	v_mfma_f32_16x16x32_f16 v[92:95], v[156:159], v[140:143], v[92:95]
	s_waitcnt lgkmcnt(0)
	v_mfma_f32_16x16x32_f16 v[32:35], v[112:115], v[96:99], v[32:35]
	ds_read_b128 v[128:131], v14
	v_mfma_f32_16x16x32_f16 v[36:39], v[116:119], v[96:99], v[36:39]
	ds_read_b128 v[144:147], v15 offset:32768
	v_mfma_f32_16x16x32_f16 v[40:43], v[120:123], v[96:99], v[40:43]
	ds_read_b128 v[148:151], v15 offset:34816
	v_mfma_f32_16x16x32_f16 v[44:47], v[124:127], v[96:99], v[44:47]
	ds_read_b128 v[152:155], v15 offset:36864
	v_mfma_f32_16x16x32_f16 v[48:51], v[112:115], v[100:103], v[48:51]
	ds_read_b128 v[156:159], v15 offset:38912
	v_mfma_f32_16x16x32_f16 v[52:55], v[116:119], v[100:103], v[52:55]
	ds_read_b128 v[132:135], v14 offset:2048
	v_mfma_f32_16x16x32_f16 v[56:59], v[120:123], v[100:103], v[56:59]
	ds_read_b128 v[136:139], v14 offset:4096
	v_mfma_f32_16x16x32_f16 v[60:63], v[124:127], v[100:103], v[60:63]
	ds_read_b128 v[140:143], v14 offset:6144
	v_mfma_f32_16x16x32_f16 v[64:67], v[112:115], v[104:107], v[64:67]
	v_mfma_f32_16x16x32_f16 v[68:71], v[116:119], v[104:107], v[68:71]
	v_mfma_f32_16x16x32_f16 v[72:75], v[120:123], v[104:107], v[72:75]
	s_add_u32 m0, s14, 0x6000
	s_nop 0
	global_load_lds_dwordx4 v5, s[28:29]
	v_mfma_f32_16x16x32_f16 v[76:79], v[124:127], v[104:107], v[76:79]
	v_mfma_f32_16x16x32_f16 v[80:83], v[112:115], v[108:111], v[80:83]
	s_add_u32 m0, s14, 0x8000
	s_nop 0
	global_load_lds_dwordx4 v6, s[30:31]
	v_mfma_f32_16x16x32_f16 v[84:87], v[116:119], v[108:111], v[84:87]
	v_mfma_f32_16x16x32_f16 v[88:91], v[120:123], v[108:111], v[88:91]
	s_add_u32 m0, s14, 0xa000
	s_nop 0
	global_load_lds_dwordx4 v7, s[30:31]
	v_mfma_f32_16x16x32_f16 v[92:95], v[124:127], v[108:111], v[92:95]
	s_waitcnt vmcnt(6) lgkmcnt(0)
	s_barrier
	s_add_u32 s28, s28, 0x80
	s_addc_u32 s29, s29, 0
	s_add_u32 s30, s30, 0x80
	s_addc_u32 s31, s31, 0
	s_waitcnt lgkmcnt(0)
	v_mfma_f32_16x16x32_f16 v[32:35], v[144:147], v[128:131], v[32:35]
	ds_read_b128 v[96:99], v16
	v_mfma_f32_16x16x32_f16 v[36:39], v[148:151], v[128:131], v[36:39]
	ds_read_b128 v[112:115], v17 offset:32768
	v_mfma_f32_16x16x32_f16 v[40:43], v[152:155], v[128:131], v[40:43]
	ds_read_b128 v[116:119], v17 offset:34816
	v_mfma_f32_16x16x32_f16 v[44:47], v[156:159], v[128:131], v[44:47]
	ds_read_b128 v[120:123], v17 offset:36864
	v_mfma_f32_16x16x32_f16 v[48:51], v[144:147], v[132:135], v[48:51]
	ds_read_b128 v[124:127], v17 offset:38912
	v_mfma_f32_16x16x32_f16 v[52:55], v[148:151], v[132:135], v[52:55]
	ds_read_b128 v[100:103], v16 offset:2048
	v_mfma_f32_16x16x32_f16 v[56:59], v[152:155], v[132:135], v[56:59]
	ds_read_b128 v[104:107], v16 offset:4096
	v_mfma_f32_16x16x32_f16 v[60:63], v[156:159], v[132:135], v[60:63]
	ds_read_b128 v[108:111], v16 offset:6144
	v_mfma_f32_16x16x32_f16 v[64:67], v[144:147], v[136:139], v[64:67]
	v_mfma_f32_16x16x32_f16 v[68:71], v[148:151], v[136:139], v[68:71]
	v_mfma_f32_16x16x32_f16 v[72:75], v[152:155], v[136:139], v[72:75]
	s_add_u32 m0, s14, 0xc000
	s_nop 0
	global_load_lds_dwordx4 v2, s[28:29]
	v_mfma_f32_16x16x32_f16 v[76:79], v[156:159], v[136:139], v[76:79]
	v_mfma_f32_16x16x32_f16 v[80:83], v[144:147], v[140:143], v[80:83]
	s_add_u32 m0, s14, 0xe000
	s_nop 0
	global_load_lds_dwordx4 v3, s[28:29]
	v_mfma_f32_16x16x32_f16 v[84:87], v[148:151], v[140:143], v[84:87]
	v_mfma_f32_16x16x32_f16 v[88:91], v[152:155], v[140:143], v[88:91]
	s_add_u32 m0, s14, 0x10000
	s_nop 0
	global_load_lds_dwordx4 v4, s[28:29]
	v_mfma_f32_16x16x32_f16 v[92:95], v[156:159], v[140:143], v[92:95]
	s_waitcnt lgkmcnt(0)
	v_mfma_f32_16x16x32_f16 v[32:35], v[112:115], v[96:99], v[32:35]
	ds_read_b128 v[128:131], v18
	v_mfma_f32_16x16x32_f16 v[36:39], v[116:119], v[96:99], v[36:39]
	ds_read_b128 v[144:147], v19 offset:32768
	v_mfma_f32_16x16x32_f16 v[40:43], v[120:123], v[96:99], v[40:43]
	ds_read_b128 v[148:151], v19 offset:34816
	v_mfma_f32_16x16x32_f16 v[44:47], v[124:127], v[96:99], v[44:47]
	ds_read_b128 v[152:155], v19 offset:36864
	v_mfma_f32_16x16x32_f16 v[48:51], v[112:115], v[100:103], v[48:51]
	ds_read_b128 v[156:159], v19 offset:38912
	v_mfma_f32_16x16x32_f16 v[52:55], v[116:119], v[100:103], v[52:55]
	ds_read_b128 v[132:135], v18 offset:2048
	v_mfma_f32_16x16x32_f16 v[56:59], v[120:123], v[100:103], v[56:59]
	ds_read_b128 v[136:139], v18 offset:4096
	v_mfma_f32_16x16x32_f16 v[60:63], v[124:127], v[100:103], v[60:63]
	ds_read_b128 v[140:143], v18 offset:6144
	v_mfma_f32_16x16x32_f16 v[64:67], v[112:115], v[104:107], v[64:67]
	v_mfma_f32_16x16x32_f16 v[68:71], v[116:119], v[104:107], v[68:71]
	v_mfma_f32_16x16x32_f16 v[72:75], v[120:123], v[104:107], v[72:75]
	s_add_u32 m0, s14, 0x12000
	s_nop 0
	global_load_lds_dwordx4 v5, s[28:29]
	v_mfma_f32_16x16x32_f16 v[76:79], v[124:127], v[104:107], v[76:79]
	v_mfma_f32_16x16x32_f16 v[80:83], v[112:115], v[108:111], v[80:83]
	s_add_u32 m0, s14, 0x14000
	s_nop 0
	global_load_lds_dwordx4 v6, s[30:31]
	v_mfma_f32_16x16x32_f16 v[84:87], v[116:119], v[108:111], v[84:87]
	v_mfma_f32_16x16x32_f16 v[88:91], v[120:123], v[108:111], v[88:91]
	s_add_u32 m0, s14, 0x16000
	s_nop 0
	global_load_lds_dwordx4 v7, s[30:31]
	v_mfma_f32_16x16x32_f16 v[92:95], v[124:127], v[108:111], v[92:95]
	s_waitcnt vmcnt(6) lgkmcnt(0)
	s_barrier
	s_add_u32 s28, s28, 0x80
	s_addc_u32 s29, s29, 0
	s_add_u32 s30, s30, 0x80
	s_addc_u32 s31, s31, 0
	s_waitcnt lgkmcnt(0)
	v_mfma_f32_16x16x32_f16 v[32:35], v[144:147], v[128:131], v[32:35]
	ds_read_b128 v[96:99], v8
	v_mfma_f32_16x16x32_f16 v[36:39], v[148:151], v[128:131], v[36:39]
	ds_read_b128 v[112:115], v9 offset:32768
	v_mfma_f32_16x16x32_f16 v[40:43], v[152:155], v[128:131], v[40:43]
	ds_read_b128 v[116:119], v9 offset:34816
	v_mfma_f32_16x16x32_f16 v[44:47], v[156:159], v[128:131], v[44:47]
	ds_read_b128 v[120:123], v9 offset:36864
	v_mfma_f32_16x16x32_f16 v[48:51], v[144:147], v[132:135], v[48:51]
	ds_read_b128 v[124:127], v9 offset:38912
	v_mfma_f32_16x16x32_f16 v[52:55], v[148:151], v[132:135], v[52:55]
	ds_read_b128 v[100:103], v8 offset:2048
	v_mfma_f32_16x16x32_f16 v[56:59], v[152:155], v[132:135], v[56:59]
	ds_read_b128 v[104:107], v8 offset:4096
	v_mfma_f32_16x16x32_f16 v[60:63], v[156:159], v[132:135], v[60:63]
	ds_read_b128 v[108:111], v8 offset:6144
	v_mfma_f32_16x16x32_f16 v[64:67], v[144:147], v[136:139], v[64:67]
	v_mfma_f32_16x16x32_f16 v[68:71], v[148:151], v[136:139], v[68:71]
	v_mfma_f32_16x16x32_f16 v[72:75], v[152:155], v[136:139], v[72:75]
	s_add_u32 m0, s14, 0x18000
	s_nop 0
	global_load_lds_dwordx4 v2, s[28:29]
	v_mfma_f32_16x16x32_f16 v[76:79], v[156:159], v[136:139], v[76:79]
	v_mfma_f32_16x16x32_f16 v[80:83], v[144:147], v[140:143], v[80:83]
	s_add_u32 m0, s14, 0x1a000
	s_nop 0
	global_load_lds_dwordx4 v3, s[28:29]
	v_mfma_f32_16x16x32_f16 v[84:87], v[148:151], v[140:143], v[84:87]
	v_mfma_f32_16x16x32_f16 v[88:91], v[152:155], v[140:143], v[88:91]
	s_add_u32 m0, s14, 0x1c000
	s_nop 0
	global_load_lds_dwordx4 v4, s[28:29]
	v_mfma_f32_16x16x32_f16 v[92:95], v[156:159], v[140:143], v[92:95]
	s_waitcnt lgkmcnt(0)
	v_mfma_f32_16x16x32_f16 v[32:35], v[112:115], v[96:99], v[32:35]
	ds_read_b128 v[128:131], v10
	v_mfma_f32_16x16x32_f16 v[36:39], v[116:119], v[96:99], v[36:39]
	ds_read_b128 v[144:147], v11 offset:32768
	v_mfma_f32_16x16x32_f16 v[40:43], v[120:123], v[96:99], v[40:43]
	ds_read_b128 v[148:151], v11 offset:34816
	v_mfma_f32_16x16x32_f16 v[44:47], v[124:127], v[96:99], v[44:47]
	ds_read_b128 v[152:155], v11 offset:36864
	v_mfma_f32_16x16x32_f16 v[48:51], v[112:115], v[100:103], v[48:51]
	ds_read_b128 v[156:159], v11 offset:38912
	v_mfma_f32_16x16x32_f16 v[52:55], v[116:119], v[100:103], v[52:55]
	ds_read_b128 v[132:135], v10 offset:2048
	v_mfma_f32_16x16x32_f16 v[56:59], v[120:123], v[100:103], v[56:59]
	ds_read_b128 v[136:139], v10 offset:4096
	v_mfma_f32_16x16x32_f16 v[60:63], v[124:127], v[100:103], v[60:63]
	ds_read_b128 v[140:143], v10 offset:6144
	v_mfma_f32_16x16x32_f16 v[64:67], v[112:115], v[104:107], v[64:67]
	v_mfma_f32_16x16x32_f16 v[68:71], v[116:119], v[104:107], v[68:71]
	v_mfma_f32_16x16x32_f16 v[72:75], v[120:123], v[104:107], v[72:75]
	s_add_u32 m0, s14, 0x1e000
	s_nop 0
	global_load_lds_dwordx4 v5, s[28:29]
	v_mfma_f32_16x16x32_f16 v[76:79], v[124:127], v[104:107], v[76:79]
	v_mfma_f32_16x16x32_f16 v[80:83], v[112:115], v[108:111], v[80:83]
	s_add_u32 m0, s14, 0x20000
	s_nop 0
	global_load_lds_dwordx4 v6, s[30:31]
	v_mfma_f32_16x16x32_f16 v[84:87], v[116:119], v[108:111], v[84:87]
	v_mfma_f32_16x16x32_f16 v[88:91], v[120:123], v[108:111], v[88:91]
	s_add_u32 m0, s14, 0x22000
	s_nop 0
	global_load_lds_dwordx4 v7, s[30:31]
	v_mfma_f32_16x16x32_f16 v[92:95], v[124:127], v[108:111], v[92:95]
	s_waitcnt vmcnt(6) lgkmcnt(0)
	s_barrier
	s_add_u32 s28, s28, 0x80
	s_addc_u32 s29, s29, 0
	s_add_u32 s30, s30, 0x80
	s_addc_u32 s31, s31, 0
	s_waitcnt lgkmcnt(0)
	v_mfma_f32_16x16x32_f16 v[32:35], v[144:147], v[128:131], v[32:35]
	ds_read_b128 v[96:99], v12
	v_mfma_f32_16x16x32_f16 v[36:39], v[148:151], v[128:131], v[36:39]
	ds_read_b128 v[112:115], v13 offset:32768
	v_mfma_f32_16x16x32_f16 v[40:43], v[152:155], v[128:131], v[40:43]
	ds_read_b128 v[116:119], v13 offset:34816
	v_mfma_f32_16x16x32_f16 v[44:47], v[156:159], v[128:131], v[44:47]
	ds_read_b128 v[120:123], v13 offset:36864
	v_mfma_f32_16x16x32_f16 v[48:51], v[144:147], v[132:135], v[48:51]
	ds_read_b128 v[124:127], v13 offset:38912
	v_mfma_f32_16x16x32_f16 v[52:55], v[148:151], v[132:135], v[52:55]
	ds_read_b128 v[100:103], v12 offset:2048
	v_mfma_f32_16x16x32_f16 v[56:59], v[152:155], v[132:135], v[56:59]
	ds_read_b128 v[104:107], v12 offset:4096
	v_mfma_f32_16x16x32_f16 v[60:63], v[156:159], v[132:135], v[60:63]
	ds_read_b128 v[108:111], v12 offset:6144
	v_mfma_f32_16x16x32_f16 v[64:67], v[144:147], v[136:139], v[64:67]
	v_mfma_f32_16x16x32_f16 v[68:71], v[148:151], v[136:139], v[68:71]
	v_mfma_f32_16x16x32_f16 v[72:75], v[152:155], v[136:139], v[72:75]
	s_add_u32 m0, s14, 0x0
	s_nop 0
	global_load_lds_dwordx4 v2, s[28:29]
	v_mfma_f32_16x16x32_f16 v[76:79], v[156:159], v[136:139], v[76:79]
	v_mfma_f32_16x16x32_f16 v[80:83], v[144:147], v[140:143], v[80:83]
	s_add_u32 m0, s14, 0x2000
	s_nop 0
	global_load_lds_dwordx4 v3, s[28:29]
	v_mfma_f32_16x16x32_f16 v[84:87], v[148:151], v[140:143], v[84:87]
	v_mfma_f32_16x16x32_f16 v[88:91], v[152:155], v[140:143], v[88:91]
	s_add_u32 m0, s14, 0x4000
	s_nop 0
	global_load_lds_dwordx4 v4, s[28:29]
	v_mfma_f32_16x16x32_f16 v[92:95], v[156:159], v[140:143], v[92:95]
	s_waitcnt lgkmcnt(0)
	v_mfma_f32_16x16x32_f16 v[32:35], v[112:115], v[96:99], v[32:35]
	ds_read_b128 v[128:131], v14
	v_mfma_f32_16x16x32_f16 v[36:39], v[116:119], v[96:99], v[36:39]
	ds_read_b128 v[144:147], v15 offset:32768
	v_mfma_f32_16x16x32_f16 v[40:43], v[120:123], v[96:99], v[40:43]
	ds_read_b128 v[148:151], v15 offset:34816
	v_mfma_f32_16x16x32_f16 v[44:47], v[124:127], v[96:99], v[44:47]
	ds_read_b128 v[152:155], v15 offset:36864
	v_mfma_f32_16x16x32_f16 v[48:51], v[112:115], v[100:103], v[48:51]
	ds_read_b128 v[156:159], v15 offset:38912
	v_mfma_f32_16x16x32_f16 v[52:55], v[116:119], v[100:103], v[52:55]
	ds_read_b128 v[132:135], v14 offset:2048
	v_mfma_f32_16x16x32_f16 v[56:59], v[120:123], v[100:103], v[56:59]
	ds_read_b128 v[136:139], v14 offset:4096
	v_mfma_f32_16x16x32_f16 v[60:63], v[124:127], v[100:103], v[60:63]
	ds_read_b128 v[140:143], v14 offset:6144
	v_mfma_f32_16x16x32_f16 v[64:67], v[112:115], v[104:107], v[64:67]
	v_mfma_f32_16x16x32_f16 v[68:71], v[116:119], v[104:107], v[68:71]
	v_mfma_f32_16x16x32_f16 v[72:75], v[120:123], v[104:107], v[72:75]
	s_add_u32 m0, s14, 0x6000
	s_nop 0
	global_load_lds_dwordx4 v5, s[28:29]
	v_mfma_f32_16x16x32_f16 v[76:79], v[124:127], v[104:107], v[76:79]
	v_mfma_f32_16x16x32_f16 v[80:83], v[112:115], v[108:111], v[80:83]
	s_add_u32 m0, s14, 0x8000
	s_nop 0
	global_load_lds_dwordx4 v6, s[30:31]
	v_mfma_f32_16x16x32_f16 v[84:87], v[116:119], v[108:111], v[84:87]
	v_mfma_f32_16x16x32_f16 v[88:91], v[120:123], v[108:111], v[88:91]
	s_add_u32 m0, s14, 0xa000
	s_nop 0
	global_load_lds_dwordx4 v7, s[30:31]
	v_mfma_f32_16x16x32_f16 v[92:95], v[124:127], v[108:111], v[92:95]
	s_waitcnt vmcnt(6) lgkmcnt(0)
	s_barrier
	s_add_u32 s28, s28, 0x80
	s_addc_u32 s29, s29, 0
	s_add_u32 s30, s30, 0x80
	s_addc_u32 s31, s31, 0
	s_waitcnt lgkmcnt(0)
	v_mfma_f32_16x16x32_f16 v[32:35], v[144:147], v[128:131], v[32:35]
	ds_read_b128 v[96:99], v16
	v_mfma_f32_16x16x32_f16 v[36:39], v[148:151], v[128:131], v[36:39]
	ds_read_b128 v[112:115], v17 offset:32768
	v_mfma_f32_16x16x32_f16 v[40:43], v[152:155], v[128:131], v[40:43]
	ds_read_b128 v[116:119], v17 offset:34816
	v_mfma_f32_16x16x32_f16 v[44:47], v[156:159], v[128:131], v[44:47]
	ds_read_b128 v[120:123], v17 offset:36864
	v_mfma_f32_16x16x32_f16 v[48:51], v[144:147], v[132:135], v[48:51]
	ds_read_b128 v[124:127], v17 offset:38912
	v_mfma_f32_16x16x32_f16 v[52:55], v[148:151], v[132:135], v[52:55]
	ds_read_b128 v[100:103], v16 offset:2048
	v_mfma_f32_16x16x32_f16 v[56:59], v[152:155], v[132:135], v[56:59]
	ds_read_b128 v[104:107], v16 offset:4096
	v_mfma_f32_16x16x32_f16 v[60:63], v[156:159], v[132:135], v[60:63]
	ds_read_b128 v[108:111], v16 offset:6144
	v_mfma_f32_16x16x32_f16 v[64:67], v[144:147], v[136:139], v[64:67]
	v_mfma_f32_16x16x32_f16 v[68:71], v[148:151], v[136:139], v[68:71]
	v_mfma_f32_16x16x32_f16 v[72:75], v[152:155], v[136:139], v[72:75]
	s_add_u32 m0, s14, 0xc000
	s_nop 0
	global_load_lds_dwordx4 v2, s[28:29]
	v_mfma_f32_16x16x32_f16 v[76:79], v[156:159], v[136:139], v[76:79]
	v_mfma_f32_16x16x32_f16 v[80:83], v[144:147], v[140:143], v[80:83]
	s_add_u32 m0, s14, 0xe000
	s_nop 0
	global_load_lds_dwordx4 v3, s[28:29]
	v_mfma_f32_16x16x32_f16 v[84:87], v[148:151], v[140:143], v[84:87]
	v_mfma_f32_16x16x32_f16 v[88:91], v[152:155], v[140:143], v[88:91]
	s_add_u32 m0, s14, 0x10000
	s_nop 0
	global_load_lds_dwordx4 v4, s[28:29]
	v_mfma_f32_16x16x32_f16 v[92:95], v[156:159], v[140:143], v[92:95]
	s_waitcnt lgkmcnt(0)
	v_mfma_f32_16x16x32_f16 v[32:35], v[112:115], v[96:99], v[32:35]
	ds_read_b128 v[128:131], v18
	v_mfma_f32_16x16x32_f16 v[36:39], v[116:119], v[96:99], v[36:39]
	ds_read_b128 v[144:147], v19 offset:32768
	v_mfma_f32_16x16x32_f16 v[40:43], v[120:123], v[96:99], v[40:43]
	ds_read_b128 v[148:151], v19 offset:34816
	v_mfma_f32_16x16x32_f16 v[44:47], v[124:127], v[96:99], v[44:47]
	ds_read_b128 v[152:155], v19 offset:36864
	v_mfma_f32_16x16x32_f16 v[48:51], v[112:115], v[100:103], v[48:51]
	ds_read_b128 v[156:159], v19 offset:38912
	v_mfma_f32_16x16x32_f16 v[52:55], v[116:119], v[100:103], v[52:55]
	ds_read_b128 v[132:135], v18 offset:2048
	v_mfma_f32_16x16x32_f16 v[56:59], v[120:123], v[100:103], v[56:59]
	ds_read_b128 v[136:139], v18 offset:4096
	v_mfma_f32_16x16x32_f16 v[60:63], v[124:127], v[100:103], v[60:63]
	ds_read_b128 v[140:143], v18 offset:6144
	v_mfma_f32_16x16x32_f16 v[64:67], v[112:115], v[104:107], v[64:67]
	v_mfma_f32_16x16x32_f16 v[68:71], v[116:119], v[104:107], v[68:71]
	v_mfma_f32_16x16x32_f16 v[72:75], v[120:123], v[104:107], v[72:75]
	s_add_u32 m0, s14, 0x12000
	s_nop 0
	global_load_lds_dwordx4 v5, s[28:29]
	v_mfma_f32_16x16x32_f16 v[76:79], v[124:127], v[104:107], v[76:79]
	v_mfma_f32_16x16x32_f16 v[80:83], v[112:115], v[108:111], v[80:83]
	s_add_u32 m0, s14, 0x14000
	s_nop 0
	global_load_lds_dwordx4 v6, s[30:31]
	v_mfma_f32_16x16x32_f16 v[84:87], v[116:119], v[108:111], v[84:87]
	v_mfma_f32_16x16x32_f16 v[88:91], v[120:123], v[108:111], v[88:91]
	s_add_u32 m0, s14, 0x16000
	s_nop 0
	global_load_lds_dwordx4 v7, s[30:31]
	v_mfma_f32_16x16x32_f16 v[92:95], v[124:127], v[108:111], v[92:95]
	s_waitcnt vmcnt(6) lgkmcnt(0)
	s_barrier
	s_add_u32 s28, s28, 0x80
	s_addc_u32 s29, s29, 0
	s_add_u32 s30, s30, 0x80
	s_addc_u32 s31, s31, 0
	s_waitcnt lgkmcnt(0)
	v_mfma_f32_16x16x32_f16 v[32:35], v[144:147], v[128:131], v[32:35]
	ds_read_b128 v[96:99], v8
	v_mfma_f32_16x16x32_f16 v[36:39], v[148:151], v[128:131], v[36:39]
	ds_read_b128 v[112:115], v9 offset:32768
	v_mfma_f32_16x16x32_f16 v[40:43], v[152:155], v[128:131], v[40:43]
	ds_read_b128 v[116:119], v9 offset:34816
	v_mfma_f32_16x16x32_f16 v[44:47], v[156:159], v[128:131], v[44:47]
	ds_read_b128 v[120:123], v9 offset:36864
	v_mfma_f32_16x16x32_f16 v[48:51], v[144:147], v[132:135], v[48:51]
	ds_read_b128 v[124:127], v9 offset:38912
	v_mfma_f32_16x16x32_f16 v[52:55], v[148:151], v[132:135], v[52:55]
	ds_read_b128 v[100:103], v8 offset:2048
	v_mfma_f32_16x16x32_f16 v[56:59], v[152:155], v[132:135], v[56:59]
	ds_read_b128 v[104:107], v8 offset:4096
	v_mfma_f32_16x16x32_f16 v[60:63], v[156:159], v[132:135], v[60:63]
	ds_read_b128 v[108:111], v8 offset:6144
	v_mfma_f32_16x16x32_f16 v[64:67], v[144:147], v[136:139], v[64:67]
	v_mfma_f32_16x16x32_f16 v[68:71], v[148:151], v[136:139], v[68:71]
	v_mfma_f32_16x16x32_f16 v[72:75], v[152:155], v[136:139], v[72:75]
	s_add_u32 m0, s14, 0x18000
	s_nop 0
	global_load_lds_dwordx4 v2, s[28:29]
	v_mfma_f32_16x16x32_f16 v[76:79], v[156:159], v[136:139], v[76:79]
	v_mfma_f32_16x16x32_f16 v[80:83], v[144:147], v[140:143], v[80:83]
	s_add_u32 m0, s14, 0x1a000
	s_nop 0
	global_load_lds_dwordx4 v3, s[28:29]
	v_mfma_f32_16x16x32_f16 v[84:87], v[148:151], v[140:143], v[84:87]
	v_mfma_f32_16x16x32_f16 v[88:91], v[152:155], v[140:143], v[88:91]
	s_add_u32 m0, s14, 0x1c000
	s_nop 0
	global_load_lds_dwordx4 v4, s[28:29]
	v_mfma_f32_16x16x32_f16 v[92:95], v[156:159], v[140:143], v[92:95]
	s_waitcnt lgkmcnt(0)
	v_mfma_f32_16x16x32_f16 v[32:35], v[112:115], v[96:99], v[32:35]
	ds_read_b128 v[128:131], v10
	v_mfma_f32_16x16x32_f16 v[36:39], v[116:119], v[96:99], v[36:39]
	ds_read_b128 v[144:147], v11 offset:32768
	v_mfma_f32_16x16x32_f16 v[40:43], v[120:123], v[96:99], v[40:43]
	ds_read_b128 v[148:151], v11 offset:34816
	v_mfma_f32_16x16x32_f16 v[44:47], v[124:127], v[96:99], v[44:47]
	ds_read_b128 v[152:155], v11 offset:36864
	v_mfma_f32_16x16x32_f16 v[48:51], v[112:115], v[100:103], v[48:51]
	ds_read_b128 v[156:159], v11 offset:38912
	v_mfma_f32_16x16x32_f16 v[52:55], v[116:119], v[100:103], v[52:55]
	ds_read_b128 v[132:135], v10 offset:2048
	v_mfma_f32_16x16x32_f16 v[56:59], v[120:123], v[100:103], v[56:59]
	ds_read_b128 v[136:139], v10 offset:4096
	v_mfma_f32_16x16x32_f16 v[60:63], v[124:127], v[100:103], v[60:63]
	ds_read_b128 v[140:143], v10 offset:6144
	v_mfma_f32_16x16x32_f16 v[64:67], v[112:115], v[104:107], v[64:67]
	v_mfma_f32_16x16x32_f16 v[68:71], v[116:119], v[104:107], v[68:71]
	v_mfma_f32_16x16x32_f16 v[72:75], v[120:123], v[104:107], v[72:75]
	s_add_u32 m0, s14, 0x1e000
	s_nop 0
	global_load_lds_dwordx4 v5, s[28:29]
	v_mfma_f32_16x16x32_f16 v[76:79], v[124:127], v[104:107], v[76:79]
	v_mfma_f32_16x16x32_f16 v[80:83], v[112:115], v[108:111], v[80:83]
	s_add_u32 m0, s14, 0x20000
	s_nop 0
	global_load_lds_dwordx4 v6, s[30:31]
	v_mfma_f32_16x16x32_f16 v[84:87], v[116:119], v[108:111], v[84:87]
	v_mfma_f32_16x16x32_f16 v[88:91], v[120:123], v[108:111], v[88:91]
	s_add_u32 m0, s14, 0x22000
	s_nop 0
	global_load_lds_dwordx4 v7, s[30:31]
	v_mfma_f32_16x16x32_f16 v[92:95], v[124:127], v[108:111], v[92:95]
	s_waitcnt vmcnt(6) lgkmcnt(0)
	s_barrier
	s_add_u32 s28, s28, 0x80
	s_addc_u32 s29, s29, 0
	s_add_u32 s30, s30, 0x80
	s_addc_u32 s31, s31, 0
	s_waitcnt lgkmcnt(0)
	v_mfma_f32_16x16x32_f16 v[32:35], v[144:147], v[128:131], v[32:35]
	ds_read_b128 v[96:99], v12
	v_mfma_f32_16x16x32_f16 v[36:39], v[148:151], v[128:131], v[36:39]
	ds_read_b128 v[112:115], v13 offset:32768
	v_mfma_f32_16x16x32_f16 v[40:43], v[152:155], v[128:131], v[40:43]
	ds_read_b128 v[116:119], v13 offset:34816
	v_mfma_f32_16x16x32_f16 v[44:47], v[156:159], v[128:131], v[44:47]
	ds_read_b128 v[120:123], v13 offset:36864
	v_mfma_f32_16x16x32_f16 v[48:51], v[144:147], v[132:135], v[48:51]
	ds_read_b128 v[124:127], v13 offset:38912
	v_mfma_f32_16x16x32_f16 v[52:55], v[148:151], v[132:135], v[52:55]
	ds_read_b128 v[100:103], v12 offset:2048
	v_mfma_f32_16x16x32_f16 v[56:59], v[152:155], v[132:135], v[56:59]
	ds_read_b128 v[104:107], v12 offset:4096
	v_mfma_f32_16x16x32_f16 v[60:63], v[156:159], v[132:135], v[60:63]
	ds_read_b128 v[108:111], v12 offset:6144
	v_mfma_f32_16x16x32_f16 v[64:67], v[144:147], v[136:139], v[64:67]
	v_mfma_f32_16x16x32_f16 v[68:71], v[148:151], v[136:139], v[68:71]
	v_mfma_f32_16x16x32_f16 v[72:75], v[152:155], v[136:139], v[72:75]
	s_add_u32 m0, s14, 0x0
	s_nop 0
	global_load_lds_dwordx4 v2, s[28:29]
	v_mfma_f32_16x16x32_f16 v[76:79], v[156:159], v[136:139], v[76:79]
	v_mfma_f32_16x16x32_f16 v[80:83], v[144:147], v[140:143], v[80:83]
	s_add_u32 m0, s14, 0x2000
	s_nop 0
	global_load_lds_dwordx4 v3, s[28:29]
	v_mfma_f32_16x16x32_f16 v[84:87], v[148:151], v[140:143], v[84:87]
	v_mfma_f32_16x16x32_f16 v[88:91], v[152:155], v[140:143], v[88:91]
	s_add_u32 m0, s14, 0x4000
	s_nop 0
	global_load_lds_dwordx4 v4, s[28:29]
	v_mfma_f32_16x16x32_f16 v[92:95], v[156:159], v[140:143], v[92:95]
	s_waitcnt lgkmcnt(0)
	v_mfma_f32_16x16x32_f16 v[32:35], v[112:115], v[96:99], v[32:35]
	ds_read_b128 v[128:131], v14
	v_mfma_f32_16x16x32_f16 v[36:39], v[116:119], v[96:99], v[36:39]
	ds_read_b128 v[144:147], v15 offset:32768
	v_mfma_f32_16x16x32_f16 v[40:43], v[120:123], v[96:99], v[40:43]
	ds_read_b128 v[148:151], v15 offset:34816
	v_mfma_f32_16x16x32_f16 v[44:47], v[124:127], v[96:99], v[44:47]
	ds_read_b128 v[152:155], v15 offset:36864
	v_mfma_f32_16x16x32_f16 v[48:51], v[112:115], v[100:103], v[48:51]
	ds_read_b128 v[156:159], v15 offset:38912
	v_mfma_f32_16x16x32_f16 v[52:55], v[116:119], v[100:103], v[52:55]
	ds_read_b128 v[132:135], v14 offset:2048
	v_mfma_f32_16x16x32_f16 v[56:59], v[120:123], v[100:103], v[56:59]
	ds_read_b128 v[136:139], v14 offset:4096
	v_mfma_f32_16x16x32_f16 v[60:63], v[124:127], v[100:103], v[60:63]
	ds_read_b128 v[140:143], v14 offset:6144
	v_mfma_f32_16x16x32_f16 v[64:67], v[112:115], v[104:107], v[64:67]
	v_mfma_f32_16x16x32_f16 v[68:71], v[116:119], v[104:107], v[68:71]
	v_mfma_f32_16x16x32_f16 v[72:75], v[120:123], v[104:107], v[72:75]
	s_add_u32 m0, s14, 0x6000
	s_nop 0
	global_load_lds_dwordx4 v5, s[28:29]
	v_mfma_f32_16x16x32_f16 v[76:79], v[124:127], v[104:107], v[76:79]
	v_mfma_f32_16x16x32_f16 v[80:83], v[112:115], v[108:111], v[80:83]
	s_add_u32 m0, s14, 0x8000
	s_nop 0
	global_load_lds_dwordx4 v6, s[30:31]
	v_mfma_f32_16x16x32_f16 v[84:87], v[116:119], v[108:111], v[84:87]
	v_mfma_f32_16x16x32_f16 v[88:91], v[120:123], v[108:111], v[88:91]
	s_add_u32 m0, s14, 0xa000
	s_nop 0
	global_load_lds_dwordx4 v7, s[30:31]
	v_mfma_f32_16x16x32_f16 v[92:95], v[124:127], v[108:111], v[92:95]
	s_waitcnt vmcnt(6) lgkmcnt(0)
	s_barrier
	s_waitcnt lgkmcnt(0)
	v_mfma_f32_16x16x32_f16 v[32:35], v[144:147], v[128:131], v[32:35]
	ds_read_b128 v[96:99], v16
	v_mfma_f32_16x16x32_f16 v[36:39], v[148:151], v[128:131], v[36:39]
	ds_read_b128 v[112:115], v17 offset:32768
	v_mfma_f32_16x16x32_f16 v[40:43], v[152:155], v[128:131], v[40:43]
	ds_read_b128 v[116:119], v17 offset:34816
	v_mfma_f32_16x16x32_f16 v[44:47], v[156:159], v[128:131], v[44:47]
	ds_read_b128 v[120:123], v17 offset:36864
	v_mfma_f32_16x16x32_f16 v[48:51], v[144:147], v[132:135], v[48:51]
	ds_read_b128 v[124:127], v17 offset:38912
	v_mfma_f32_16x16x32_f16 v[52:55], v[148:151], v[132:135], v[52:55]
	ds_read_b128 v[100:103], v16 offset:2048
	v_mfma_f32_16x16x32_f16 v[56:59], v[152:155], v[132:135], v[56:59]
	ds_read_b128 v[104:107], v16 offset:4096
	v_mfma_f32_16x16x32_f16 v[60:63], v[156:159], v[132:135], v[60:63]
	ds_read_b128 v[108:111], v16 offset:6144
	v_mfma_f32_16x16x32_f16 v[64:67], v[144:147], v[136:139], v[64:67]
	v_mfma_f32_16x16x32_f16 v[68:71], v[148:151], v[136:139], v[68:71]
	v_mfma_f32_16x16x32_f16 v[72:75], v[152:155], v[136:139], v[72:75]
	v_mfma_f32_16x16x32_f16 v[76:79], v[156:159], v[136:139], v[76:79]
	v_mfma_f32_16x16x32_f16 v[80:83], v[144:147], v[140:143], v[80:83]
	v_mfma_f32_16x16x32_f16 v[84:87], v[148:151], v[140:143], v[84:87]
	v_mfma_f32_16x16x32_f16 v[88:91], v[152:155], v[140:143], v[88:91]
	v_mfma_f32_16x16x32_f16 v[92:95], v[156:159], v[140:143], v[92:95]
	s_waitcnt lgkmcnt(0)
	v_mfma_f32_16x16x32_f16 v[32:35], v[112:115], v[96:99], v[32:35]
	ds_read_b128 v[128:131], v18
	v_mfma_f32_16x16x32_f16 v[36:39], v[116:119], v[96:99], v[36:39]
	ds_read_b128 v[144:147], v19 offset:32768
	v_mfma_f32_16x16x32_f16 v[40:43], v[120:123], v[96:99], v[40:43]
	ds_read_b128 v[148:151], v19 offset:34816
	v_mfma_f32_16x16x32_f16 v[44:47], v[124:127], v[96:99], v[44:47]
	ds_read_b128 v[152:155], v19 offset:36864
	v_mfma_f32_16x16x32_f16 v[48:51], v[112:115], v[100:103], v[48:51]
	ds_read_b128 v[156:159], v19 offset:38912
	v_mfma_f32_16x16x32_f16 v[52:55], v[116:119], v[100:103], v[52:55]
	ds_read_b128 v[132:135], v18 offset:2048
	v_mfma_f32_16x16x32_f16 v[56:59], v[120:123], v[100:103], v[56:59]
	ds_read_b128 v[136:139], v18 offset:4096
	v_mfma_f32_16x16x32_f16 v[60:63], v[124:127], v[100:103], v[60:63]
	ds_read_b128 v[140:143], v18 offset:6144
	v_mfma_f32_16x16x32_f16 v[64:67], v[112:115], v[104:107], v[64:67]
	v_mfma_f32_16x16x32_f16 v[68:71], v[116:119], v[104:107], v[68:71]
	v_mfma_f32_16x16x32_f16 v[72:75], v[120:123], v[104:107], v[72:75]
	v_mfma_f32_16x16x32_f16 v[76:79], v[124:127], v[104:107], v[76:79]
	v_mfma_f32_16x16x32_f16 v[80:83], v[112:115], v[108:111], v[80:83]
	v_mfma_f32_16x16x32_f16 v[84:87], v[116:119], v[108:111], v[84:87]
	v_mfma_f32_16x16x32_f16 v[88:91], v[120:123], v[108:111], v[88:91]
	v_mfma_f32_16x16x32_f16 v[92:95], v[124:127], v[108:111], v[92:95]
	s_waitcnt vmcnt(0) lgkmcnt(0)
	s_barrier
	s_waitcnt lgkmcnt(0)
	v_mfma_f32_16x16x32_f16 v[32:35], v[144:147], v[128:131], v[32:35]
	ds_read_b128 v[96:99], v8
	v_mfma_f32_16x16x32_f16 v[36:39], v[148:151], v[128:131], v[36:39]
	ds_read_b128 v[112:115], v9 offset:32768
	v_mfma_f32_16x16x32_f16 v[40:43], v[152:155], v[128:131], v[40:43]
	ds_read_b128 v[116:119], v9 offset:34816
	v_mfma_f32_16x16x32_f16 v[44:47], v[156:159], v[128:131], v[44:47]
	ds_read_b128 v[120:123], v9 offset:36864
	v_mfma_f32_16x16x32_f16 v[48:51], v[144:147], v[132:135], v[48:51]
	ds_read_b128 v[124:127], v9 offset:38912
	v_mfma_f32_16x16x32_f16 v[52:55], v[148:151], v[132:135], v[52:55]
	ds_read_b128 v[100:103], v8 offset:2048
	v_mfma_f32_16x16x32_f16 v[56:59], v[152:155], v[132:135], v[56:59]
	ds_read_b128 v[104:107], v8 offset:4096
	v_mfma_f32_16x16x32_f16 v[60:63], v[156:159], v[132:135], v[60:63]
	ds_read_b128 v[108:111], v8 offset:6144
	v_mfma_f32_16x16x32_f16 v[64:67], v[144:147], v[136:139], v[64:67]
	v_mfma_f32_16x16x32_f16 v[68:71], v[148:151], v[136:139], v[68:71]
	v_mfma_f32_16x16x32_f16 v[72:75], v[152:155], v[136:139], v[72:75]
	v_mfma_f32_16x16x32_f16 v[76:79], v[156:159], v[136:139], v[76:79]
	v_mfma_f32_16x16x32_f16 v[80:83], v[144:147], v[140:143], v[80:83]
	v_mfma_f32_16x16x32_f16 v[84:87], v[148:151], v[140:143], v[84:87]
	v_mfma_f32_16x16x32_f16 v[88:91], v[152:155], v[140:143], v[88:91]
	v_mfma_f32_16x16x32_f16 v[92:95], v[156:159], v[140:143], v[92:95]
	s_waitcnt lgkmcnt(0)
	v_mfma_f32_16x16x32_f16 v[32:35], v[112:115], v[96:99], v[32:35]
	ds_read_b128 v[128:131], v10
	v_mfma_f32_16x16x32_f16 v[36:39], v[116:119], v[96:99], v[36:39]
	ds_read_b128 v[144:147], v11 offset:32768
	v_mfma_f32_16x16x32_f16 v[40:43], v[120:123], v[96:99], v[40:43]
	ds_read_b128 v[148:151], v11 offset:34816
	v_mfma_f32_16x16x32_f16 v[44:47], v[124:127], v[96:99], v[44:47]
	ds_read_b128 v[152:155], v11 offset:36864
	v_mfma_f32_16x16x32_f16 v[48:51], v[112:115], v[100:103], v[48:51]
	ds_read_b128 v[156:159], v11 offset:38912
	v_mfma_f32_16x16x32_f16 v[52:55], v[116:119], v[100:103], v[52:55]
	ds_read_b128 v[132:135], v10 offset:2048
	v_mfma_f32_16x16x32_f16 v[56:59], v[120:123], v[100:103], v[56:59]
	ds_read_b128 v[136:139], v10 offset:4096
	v_mfma_f32_16x16x32_f16 v[60:63], v[124:127], v[100:103], v[60:63]
	ds_read_b128 v[140:143], v10 offset:6144
	v_mfma_f32_16x16x32_f16 v[64:67], v[112:115], v[104:107], v[64:67]
	v_mfma_f32_16x16x32_f16 v[68:71], v[116:119], v[104:107], v[68:71]
	v_mfma_f32_16x16x32_f16 v[72:75], v[120:123], v[104:107], v[72:75]
	v_mfma_f32_16x16x32_f16 v[76:79], v[124:127], v[104:107], v[76:79]
	v_mfma_f32_16x16x32_f16 v[80:83], v[112:115], v[108:111], v[80:83]
	v_mfma_f32_16x16x32_f16 v[84:87], v[116:119], v[108:111], v[84:87]
	v_mfma_f32_16x16x32_f16 v[88:91], v[120:123], v[108:111], v[88:91]
	v_mfma_f32_16x16x32_f16 v[92:95], v[124:127], v[108:111], v[92:95]
	s_waitcnt lgkmcnt(0)
	v_mfma_f32_16x16x32_f16 v[32:35], v[144:147], v[128:131], v[32:35]
	v_mfma_f32_16x16x32_f16 v[36:39], v[148:151], v[128:131], v[36:39]
	v_mfma_f32_16x16x32_f16 v[40:43], v[152:155], v[128:131], v[40:43]
	v_mfma_f32_16x16x32_f16 v[44:47], v[156:159], v[128:131], v[44:47]
	v_mfma_f32_16x16x32_f16 v[48:51], v[144:147], v[132:135], v[48:51]
	v_mfma_f32_16x16x32_f16 v[52:55], v[148:151], v[132:135], v[52:55]
	v_mfma_f32_16x16x32_f16 v[56:59], v[152:155], v[132:135], v[56:59]
	v_mfma_f32_16x16x32_f16 v[60:63], v[156:159], v[132:135], v[60:63]
	v_mfma_f32_16x16x32_f16 v[64:67], v[144:147], v[136:139], v[64:67]
	v_mfma_f32_16x16x32_f16 v[68:71], v[148:151], v[136:139], v[68:71]
	v_mfma_f32_16x16x32_f16 v[72:75], v[152:155], v[136:139], v[72:75]
	v_mfma_f32_16x16x32_f16 v[76:79], v[156:159], v[136:139], v[76:79]
	v_mfma_f32_16x16x32_f16 v[80:83], v[144:147], v[140:143], v[80:83]
	v_mfma_f32_16x16x32_f16 v[84:87], v[148:151], v[140:143], v[84:87]
	v_mfma_f32_16x16x32_f16 v[88:91], v[152:155], v[140:143], v[88:91]
	v_mfma_f32_16x16x32_f16 v[92:95], v[156:159], v[140:143], v[92:95]
	s_nop 7
	s_nop 1
	v_mul_f32_e32 v160, s50, v32
	v_mul_f32_e32 v161, s50, v33
	v_mul_f32_e32 v162, s50, v34
	v_mul_f32_e32 v163, s50, v35
	v_mul_f32_e32 v164, s50, v36
	v_mul_f32_e32 v165, s50, v37
	v_mul_f32_e32 v166, s50, v38
	v_mul_f32_e32 v167, s50, v39
	v_cvt_pk_f16_f32 v168, v160, v161
	v_cvt_pk_f16_f32 v169, v162, v163
	v_cvt_pk_f16_f32 v170, v164, v165
	v_cvt_pk_f16_f32 v171, v166, v167
	global_store_dwordx4 v24, v[168:171], s[34:35] offset:256
	v_mul_f32_e32 v160, s50, v40
	v_mul_f32_e32 v161, s50, v41
	v_mul_f32_e32 v162, s50, v42
	v_mul_f32_e32 v163, s50, v43
	v_mul_f32_e32 v164, s50, v44
	v_mul_f32_e32 v165, s50, v45
	v_mul_f32_e32 v166, s50, v46
	v_mul_f32_e32 v167, s50, v47
	v_cvt_pk_f16_f32 v172, v160, v161
	v_cvt_pk_f16_f32 v173, v162, v163
	v_cvt_pk_f16_f32 v174, v164, v165
	v_cvt_pk_f16_f32 v175, v166, v167
	global_store_dwordx4 v24, v[172:175], s[34:35] offset:320
	v_mul_f32_e32 v160, s50, v48
	v_mul_f32_e32 v161, s50, v49
	v_mul_f32_e32 v162, s50, v50
	v_mul_f32_e32 v163, s50, v51
	v_mul_f32_e32 v164, s50, v52
	v_mul_f32_e32 v165, s50, v53
	v_mul_f32_e32 v166, s50, v54
	v_mul_f32_e32 v167, s50, v55
	v_cvt_pk_f16_f32 v168, v160, v161
	v_cvt_pk_f16_f32 v169, v162, v163
	v_cvt_pk_f16_f32 v170, v164, v165
	v_cvt_pk_f16_f32 v171, v166, v167
	global_store_dwordx4 v25, v[168:171], s[34:35] offset:256
	v_mul_f32_e32 v160, s50, v56
	v_mul_f32_e32 v161, s50, v57
	v_mul_f32_e32 v162, s50, v58
	v_mul_f32_e32 v163, s50, v59
	v_mul_f32_e32 v164, s50, v60
	v_mul_f32_e32 v165, s50, v61
	v_mul_f32_e32 v166, s50, v62
	v_mul_f32_e32 v167, s50, v63
	v_cvt_pk_f16_f32 v172, v160, v161
	v_cvt_pk_f16_f32 v173, v162, v163
	v_cvt_pk_f16_f32 v174, v164, v165
	v_cvt_pk_f16_f32 v175, v166, v167
	global_store_dwordx4 v25, v[172:175], s[34:35] offset:320
	v_mul_f32_e32 v160, s50, v64
	v_mul_f32_e32 v161, s50, v65
	v_mul_f32_e32 v162, s50, v66
	v_mul_f32_e32 v163, s50, v67
	v_mul_f32_e32 v164, s50, v68
	v_mul_f32_e32 v165, s50, v69
	v_mul_f32_e32 v166, s50, v70
	v_mul_f32_e32 v167, s50, v71
	v_cvt_pk_f16_f32 v168, v160, v161
	v_cvt_pk_f16_f32 v169, v162, v163
	v_cvt_pk_f16_f32 v170, v164, v165
	v_cvt_pk_f16_f32 v171, v166, v167
	global_store_dwordx4 v26, v[168:171], s[34:35] offset:256
	v_mul_f32_e32 v160, s50, v72
	v_mul_f32_e32 v161, s50, v73
	v_mul_f32_e32 v162, s50, v74
	v_mul_f32_e32 v163, s50, v75
	v_mul_f32_e32 v164, s50, v76
	v_mul_f32_e32 v165, s50, v77
	v_mul_f32_e32 v166, s50, v78
	v_mul_f32_e32 v167, s50, v79
	v_cvt_pk_f16_f32 v172, v160, v161
	v_cvt_pk_f16_f32 v173, v162, v163
	v_cvt_pk_f16_f32 v174, v164, v165
	v_cvt_pk_f16_f32 v175, v166, v167
	global_store_dwordx4 v26, v[172:175], s[34:35] offset:320
	v_mul_f32_e32 v160, s50, v80
	v_mul_f32_e32 v161, s50, v81
	v_mul_f32_e32 v162, s50, v82
	v_mul_f32_e32 v163, s50, v83
	v_mul_f32_e32 v164, s50, v84
	v_mul_f32_e32 v165, s50, v85
	v_mul_f32_e32 v166, s50, v86
	v_mul_f32_e32 v167, s50, v87
	v_cvt_pk_f16_f32 v168, v160, v161
	v_cvt_pk_f16_f32 v169, v162, v163
	v_cvt_pk_f16_f32 v170, v164, v165
	v_cvt_pk_f16_f32 v171, v166, v167
	global_store_dwordx4 v27, v[168:171], s[34:35] offset:256
	v_mul_f32_e32 v160, s50, v88
	v_mul_f32_e32 v161, s50, v89
	v_mul_f32_e32 v162, s50, v90
	v_mul_f32_e32 v163, s50, v91
	v_mul_f32_e32 v164, s50, v92
	v_mul_f32_e32 v165, s50, v93
	v_mul_f32_e32 v166, s50, v94
	v_mul_f32_e32 v167, s50, v95
	v_cvt_pk_f16_f32 v172, v160, v161
	v_cvt_pk_f16_f32 v173, v162, v163
	v_cvt_pk_f16_f32 v174, v164, v165
	v_cvt_pk_f16_f32 v175, v166, v167
	global_store_dwordx4 v27, v[172:175], s[34:35] offset:320
	s_endpgm

	.amdhsa_kernel _Z12gemm8_kernelPKDF16_S0_PDF16_S1_
		.amdhsa_group_segment_fixed_size 16384
		.amdhsa_private_segment_fixed_size 0
		.amdhsa_kernarg_size 32
		.amdhsa_user_sgpr_count 2
		.amdhsa_user_sgpr_dispatch_ptr 0
		.amdhsa_user_sgpr_queue_ptr 0
		.amdhsa_user_sgpr_kernarg_segment_ptr 1
		.amdhsa_user_sgpr_dispatch_id 0
		.amdhsa_user_sgpr_kernarg_preload_length 0
		.amdhsa_user_sgpr_kernarg_preload_offset 0
		.amdhsa_user_sgpr_private_segment_size 0
		.amdhsa_uses_dynamic_stack 0
		.amdhsa_enable_private_segment 0
		.amdhsa_system_sgpr_workgroup_id_x 1
		.amdhsa_system_sgpr_workgroup_id_y 0
		.amdhsa_system_sgpr_workgroup_id_z 0
		.amdhsa_system_sgpr_workgroup_info 0
		.amdhsa_system_vgpr_workitem_id 0
		.amdhsa_next_free_vgpr 184
		.amdhsa_next_free_sgpr 52
		.amdhsa_accum_offset 184
		.amdhsa_reserve_vcc 1
		.amdhsa_float_round_mode_32 0
		.amdhsa_float_round_mode_16_64 0
		.amdhsa_float_denorm_mode_32 3
		.amdhsa_float_denorm_mode_16_64 3
		.amdhsa_dx10_clamp 1
		.amdhsa_ieee_mode 1
		.amdhsa_fp16_overflow 0
		.amdhsa_tg_split 0
		.amdhsa_exception_fp_ieee_invalid_op 0
		.amdhsa_exception_fp_denorm_src 0
		.amdhsa_exception_fp_ieee_div_zero 0
		.amdhsa_exception_fp_ieee_overflow 0
		.amdhsa_exception_fp_ieee_underflow 0
		.amdhsa_exception_fp_ieee_inexact 0
		.amdhsa_exception_int_div_zero 0
	.end_amdhsa_kernel

amdhsa.kernels:
  - .agpr_count:     0
    .args:
      - .actual_access:  read_only
        .address_space:  global
        .offset:         0
        .size:           8
        .value_kind:     global_buffer
      - .actual_access:  read_only
        .address_space:  global
        .offset:         8
        .size:           8
        .value_kind:     global_buffer
      - .actual_access:  read_only
        .address_space:  global
        .offset:         16
        .size:           8
        .value_kind:     global_buffer
      - .actual_access:  read_only
        .address_space:  global
        .offset:         24
        .size:           8
        .value_kind:     global_buffer
      - .actual_access:  write_only
        .address_space:  global
        .offset:         32
        .size:           8
        .value_kind:     global_buffer
      - .actual_access:  write_only
        .address_space:  global
        .offset:         40
        .size:           8
        .value_kind:     global_buffer
      - .actual_access:  write_only
        .address_space:  global
        .offset:         48
        .size:           8
        .value_kind:     global_buffer
      - .actual_access:  write_only
        .address_space:  global
        .offset:         56
        .size:           8
        .value_kind:     global_buffer
    .group_segment_fixed_size: 16640
    .kernarg_segment_align: 8
    .kernarg_segment_size: 64
    .language:       OpenCL C
    .language_version:
      - 2
      - 0
    .max_flat_workgroup_size: 256
    .name:           _Z11prep_kernelPKfS0_S0_S0_PDF16_S1_S1_Pf
    .private_segment_fixed_size: 0
    .sgpr_count:     18
    .sgpr_spill_count: 0
    .symbol:         _Z11prep_kernelPKfS0_S0_S0_PDF16_S1_S1_Pf.kd
    .uniform_work_group_size: 1
    .uses_dynamic_stack: false
    .vgpr_count:     42
    .vgpr_spill_count: 0
    .wavefront_size: 64
  - .agpr_count:     0
    .args:
      - .address_space:  global
        .offset:         0
        .size:           8
        .value_kind:     global_buffer
      - .address_space:  global
        .offset:         8
        .size:           8
        .value_kind:     global_buffer
      - .actual_access:  write_only
        .address_space:  global
        .offset:         16
        .size:           8
        .value_kind:     global_buffer
      - .actual_access:  read_only
        .address_space:  global
        .offset:         24
        .size:           8
        .value_kind:     global_buffer
    .group_segment_fixed_size: 49152
    .kernarg_segment_align: 8
    .kernarg_segment_size: 32
    .language:       OpenCL C
    .language_version:
      - 2
      - 0
    .max_flat_workgroup_size: 512
    .name:           _Z13gemm2b_kernelPKDF16_S0_PfPKf
    .private_segment_fixed_size: 0
    .sgpr_count:     24
    .sgpr_spill_count: 0
    .symbol:         _Z13gemm2b_kernelPKDF16_S0_PfPKf.kd
    .uniform_work_group_size: 1
    .uses_dynamic_stack: false
    .vgpr_count:     176
    .vgpr_spill_count: 0
    .wavefront_size: 64
  - .agpr_count:     0
    .args:
      - .address_space:  global
        .offset:         0
        .size:           8
        .value_kind:     global_buffer
      - .address_space:  global
        .offset:         8
        .size:           8
        .value_kind:     global_buffer
      - .actual_access:  write_only
        .address_space:  global
        .offset:         16
        .size:           8
        .value_kind:     global_buffer
      - .actual_access:  write_only
        .address_space:  global
        .offset:         24
        .size:           8
        .value_kind:     global_buffer
    .group_segment_fixed_size: 16384
    .kernarg_segment_align: 8
    .kernarg_segment_size: 32
    .language:       OpenCL C
    .language_version:
      - 2
      - 0
    .max_flat_workgroup_size: 512
    .name:           _Z12gemm8_kernelPKDF16_S0_PDF16_S1_
    .private_segment_fixed_size: 0
    .sgpr_count:     58
    .sgpr_spill_count: 0
    .symbol:         _Z12gemm8_kernelPKDF16_S0_PDF16_S1_.kd
    .uniform_work_group_size: 1
    .uses_dynamic_stack: false
    .vgpr_count:     184
    .vgpr_spill_count: 0
    .wavefront_size: 64
  - .agpr_count:     0
    .args:
      - .actual_access:  read_only
        .address_space:  global
        .offset:         0
        .size:           8
        .value_kind:     global_buffer
      - .actual_access:  read_only
        .address_space:  global
        .offset:         8
        .size:           8
        .value_kind:     global_buffer
      - .actual_access:  read_only
        .address_space:  global
        .offset:         16
        .size:           8
        .value_kind:     global_buffer
      - .actual_access:  read_only
        .address_space:  global
        .offset:         24
        .size:           8
        .value_kind:     global_buffer
      - .actual_access:  write_only
        .address_space:  global
        .offset:         32
        .size:           8
        .value_kind:     global_buffer
      - .actual_access:  write_only
        .address_space:  global
        .offset:         40
        .size:           8
        .value_kind:     global_buffer
      - .actual_access:  read_only
        .address_space:  global
        .offset:         48
        .size:           8
        .value_kind:     global_buffer
      - .actual_access:  read_only
        .address_space:  global
        .offset:         56
        .size:           8
        .value_kind:     global_buffer
      - .actual_access:  read_only
        .address_space:  global
        .offset:         64
        .size:           8
        .value_kind:     global_buffer
      - .actual_access:  write_only
        .address_space:  global
        .offset:         72
        .size:           8
        .value_kind:     global_buffer
      - .actual_access:  write_only
        .address_space:  global
        .offset:         80
        .size:           8
        .value_kind:     global_buffer
      - .actual_access:  write_only
        .address_space:  global
        .offset:         88
        .size:           8
        .value_kind:     global_buffer
      - .actual_access:  write_only
        .address_space:  global
        .offset:         96
        .size:           8
        .value_kind:     global_buffer
    .group_segment_fixed_size: 17952
    .kernarg_segment_align: 8
    .kernarg_segment_size: 104
    .language:       OpenCL C
    .language_version:
      - 2
      - 0
    .max_flat_workgroup_size: 256
    .name:           _Z13convdt_kernelPKDF16_S0_PKfS2_PDF16_S3_S2_S2_S2_PfS4_S4_S4_
    .private_segment_fixed_size: 0
    .sgpr_count:     26
    .sgpr_spill_count: 0
    .symbol:         _Z13convdt_kernelPKDF16_S0_PKfS2_PDF16_S3_S2_S2_S2_PfS4_S4_S4_.kd
    .uniform_work_group_size: 1
    .uses_dynamic_stack: false
    .vgpr_count:     88
    .vgpr_spill_count: 0
    .wavefront_size: 64
  - .agpr_count:     0
    .args:
      - .actual_access:  read_only
        .address_space:  global
        .offset:         0
        .size:           8
        .value_kind:     global_buffer
      - .actual_access:  read_only
        .address_space:  global
        .offset:         8
        .size:           8
        .value_kind:     global_buffer
      - .actual_access:  read_only
        .address_space:  global
        .offset:         16
        .size:           8
        .value_kind:     global_buffer
      - .actual_access:  write_only
        .address_space:  global
        .offset:         24
        .size:           8
        .value_kind:     global_buffer
    .group_segment_fixed_size: 34816
    .kernarg_segment_align: 8
    .kernarg_segment_size: 32
    .language:       OpenCL C
    .language_version:
      - 2
      - 0
    .max_flat_workgroup_size: 256
    .name:           _Z11sloc_kernelPKDF16_PKfS2_PDF16_
    .private_segment_fixed_size: 0
    .sgpr_count:     28
    .sgpr_spill_count: 0
    .symbol:         _Z11sloc_kernelPKDF16_PKfS2_PDF16_.kd
    .uniform_work_group_size: 1
    .uses_dynamic_stack: false
    .vgpr_count:     120
    .vgpr_spill_count: 0
    .wavefront_size: 64
  - .agpr_count:     64
    .args:
      - .actual_access:  read_only
        .address_space:  global
        .offset:         0
        .size:           8
        .value_kind:     global_buffer
      - .address_space:  global
        .offset:         8
        .size:           8
        .value_kind:     global_buffer
      - .actual_access:  read_only
        .address_space:  global
        .offset:         16
        .size:           8
        .value_kind:     global_buffer
      - .actual_access:  write_only
        .address_space:  global
        .offset:         24
        .size:           8
        .value_kind:     global_buffer
    .group_segment_fixed_size: 0
    .kernarg_segment_align: 8
    .kernarg_segment_size: 32
    .language:       OpenCL C
    .language_version:
      - 2
      - 0
    .max_flat_workgroup_size: 256
    .name:           _Z12spass_kernelPKfPDF16_PKDF16_S1_
    .private_segment_fixed_size: 0
    .sgpr_count:     21
    .sgpr_spill_count: 0
    .symbol:         _Z12spass_kernelPKfPDF16_PKDF16_S1_.kd
    .uniform_work_group_size: 1
    .uses_dynamic_stack: false
    .vgpr_count:     180
    .vgpr_spill_count: 0
    .wavefront_size: 64
  - .agpr_count:     0
    .args:
      - .actual_access:  read_only
        .address_space:  global
        .offset:         0
        .size:           8
        .value_kind:     global_buffer
      - .actual_access:  read_only
        .address_space:  global
        .offset:         8
        .size:           8
        .value_kind:     global_buffer
      - .actual_access:  read_only
        .address_space:  global
        .offset:         16
        .size:           8
        .value_kind:     global_buffer
      - .actual_access:  read_only
        .address_space:  global
        .offset:         24
        .size:           8
        .value_kind:     global_buffer
      - .actual_access:  read_only
        .address_space:  global
        .offset:         32
        .size:           8
        .value_kind:     global_buffer
      - .actual_access:  read_only
        .address_space:  global
        .offset:         40
        .size:           8
        .value_kind:     global_buffer
      - .actual_access:  read_only
        .address_space:  global
        .offset:         48
        .size:           8
        .value_kind:     global_buffer
      - .actual_access:  read_only
        .address_space:  global
        .offset:         56
        .size:           8
        .value_kind:     global_buffer
      - .actual_access:  read_only
        .address_space:  global
        .offset:         64
        .size:           8
        .value_kind:     global_buffer
      - .actual_access:  write_only
        .address_space:  global
        .offset:         72
        .size:           8
        .value_kind:     global_buffer
      - .address_space:  global
        .offset:         80
        .size:           8
        .value_kind:     global_buffer
      - .actual_access:  read_only
        .address_space:  global
        .offset:         88
        .size:           8
        .value_kind:     global_buffer
    .group_segment_fixed_size: 54272
    .kernarg_segment_align: 8
    .kernarg_segment_size: 96
    .language:       OpenCL C
    .language_version:
      - 2
      - 0
    .max_flat_workgroup_size: 256
    .name:           _Z11scan_kernelPKDF16_S0_S0_S0_S0_PKfS2_S2_S2_PDF16_PfS4_
    .private_segment_fixed_size: 0
    .sgpr_count:     106
    .sgpr_spill_count: 56
    .symbol:         _Z11scan_kernelPKDF16_S0_S0_S0_S0_PKfS2_S2_S2_PDF16_PfS4_.kd
    .uniform_work_group_size: 1
    .uses_dynamic_stack: false
    .vgpr_count:     243
    .vgpr_spill_count: 0
    .wavefront_size: 64
  - .agpr_count:     0
    .args:
      - .actual_access:  read_only
        .address_space:  global
        .offset:         0
        .size:           8
        .value_kind:     global_buffer
      - .address_space:  global
        .offset:         8
        .size:           8
        .value_kind:     global_buffer
      - .address_space:  global
        .offset:         16
        .size:           8
        .value_kind:     global_buffer
      - .actual_access:  read_only
        .address_space:  global
        .offset:         24
        .size:           8
        .value_kind:     global_buffer
      - .address_space:  global
        .offset:         32
        .size:           8
        .value_kind:     global_buffer
      - .address_space:  global
        .offset:         40
        .size:           8
        .value_kind:     global_buffer
      - .address_space:  global
        .offset:         48
        .size:           8
        .value_kind:     global_buffer
      - .actual_access:  read_only
        .address_space:  global
        .offset:         56
        .size:           8
        .value_kind:     global_buffer
      - .actual_access:  read_only
        .address_space:  global
        .offset:         64
        .size:           8
        .value_kind:     global_buffer
      - .actual_access:  write_only
        .address_space:  global
        .offset:         72
        .size:           8
        .value_kind:     global_buffer
      - .address_space:  global
        .offset:         80
        .size:           8
        .value_kind:     global_buffer
      - .actual_access:  read_only
        .address_space:  global
        .offset:         88
        .size:           8
        .value_kind:     global_buffer
    .group_segment_fixed_size: 0
    .kernarg_segment_align: 8
    .kernarg_segment_size: 96
    .language:       OpenCL C
    .language_version:
      - 2
      - 0
    .max_flat_workgroup_size: 512
    .name:           _Z12scan2_kernelPKDF16_S0_S0_S0_S0_PKfS2_S2_S2_PDF16_PfS4_
    .private_segment_fixed_size: 0
    .sgpr_count:     106
    .sgpr_spill_count: 53
    .symbol:         _Z12scan2_kernelPKDF16_S0_S0_S0_S0_PKfS2_S2_S2_PDF16_PfS4_.kd
    .uniform_work_group_size: 1
    .uses_dynamic_stack: false
    .vgpr_count:     240
    .vgpr_spill_count: 0
    .wavefront_size: 64
  - .agpr_count:     64
    .args:
      - .address_space:  global
        .offset:         0
        .size:           8
        .value_kind:     global_buffer
      - .address_space:  global
        .offset:         8
        .size:           8
        .value_kind:     global_buffer
      - .offset:         16
        .size:           4
        .value_kind:     by_value
      - .offset:         20
        .size:           4
        .value_kind:     by_value
      - .offset:         24
        .size:           4
        .value_kind:     by_value
      - .actual_access:  write_only
        .address_space:  global
        .offset:         32
        .size:           8
        .value_kind:     global_buffer
      - .actual_access:  write_only
        .address_space:  global
        .offset:         40
        .size:           8
        .value_kind:     global_buffer
      - .actual_access:  read_only
        .address_space:  global
        .offset:         48
        .size:           8
        .value_kind:     global_buffer
      - .offset:         56
        .size:           4
        .value_kind:     by_value
    .group_segment_fixed_size: 131072
    .kernarg_segment_align: 8
    .kernarg_segment_size: 60
    .language:       OpenCL C
    .language_version:
      - 2
      - 0
    .max_flat_workgroup_size: 256
    .name:           _Z11gemm_kernelILi1EEvPKDF16_S1_iiiPDF16_PfPKfi
    .private_segment_fixed_size: 0
    .sgpr_count:     27
    .sgpr_spill_count: 0
    .symbol:         _Z11gemm_kernelILi1EEvPKDF16_S1_iiiPDF16_PfPKfi.kd
    .uniform_work_group_size: 1
    .uses_dynamic_stack: false
    .vgpr_count:     208
    .vgpr_spill_count: 0
    .wavefront_size: 64
